# GEMM epilogues: residual/scale/gate loads hoisted one block ahead into free registers, counted vmcnt waits
# speedup vs baseline: 1.0068x; 1.0068x over previous
; __device__ __forceinline__ unsigned cvt_pk_bf16(float lo, float hi) { unsigned r; asm volatile("v_cvt_pk_bf16_f32 %0, %1, %2" : "=v"(r) : "v"(lo), "v"(hi)); return r; }
;     __device__ __forceinline__ void operator()(const f32x4 (&acc)[2][2][4][2], const Unit& u, int wr, int wc, int fr, int fq) const {
;         const int row0 = u.pm * BM + wr * 64 + fr; const int col0 = u.pn * BM + wc * 32 + 8 * fq;
;         float cs[2][8];
; #pragma unroll
;         for (int bj = 0; bj < 2; ++bj) { const u32x4 c0 = *(const u32x4*)(cmax + col0 + bj * HALF), c1 = *(const u32x4*)(cmax + col0 + bj * HALF + 4);
; #pragma unroll
;             for (int e = 0; e < 4; ++e) { cs[bj][e] = __uint_as_float(c0[e] << 16) * (1.0f / 127.0f); cs[bj][4 + e] = __uint_as_float(c1[e] << 16) * (1.0f / 127.0f); } }
; #pragma unroll
;         for (int ai = 0; ai < 2; ++ai)
; #pragma unroll
;             for (int m = 0; m < 4; ++m) { const int row = row0 + ai * HALF + m * 16; bf16_t* rowp = O + (size_t)row * ldc + col0; const float rs = xs[row];
; #pragma unroll
;                 for (int bj = 0; bj < 2; ++bj) { const i32x4 i0 = __builtin_bit_cast(i32x4, acc[ai][bj][m][0]), i1 = __builtin_bit_cast(i32x4, acc[ai][bj][m][1]);
;                     float v[8];
; #pragma unroll
;                     for (int e = 0; e < 4; ++e) { v[e] = (float)i0[e] * rs * cs[bj][e]; v[4 + e] = (float)i1[e] * rs * cs[bj][4 + e]; }
;                     u32x4 w; w.x = cvt_pk_bf16(v[0], v[1]); w.y = cvt_pk_bf16(v[2], v[3]); w.z = cvt_pk_bf16(v[4], v[5]); w.w = cvt_pk_bf16(v[6], v[7]);
;                     *(u32x4*)(rowp + bj * HALF) = w; } }
.LBB0_254:
	v_lshl_or_b32 v170, s36, 8, v173
	v_ashrrev_i32_e32 v171, 31, v170
	v_lshl_add_u64 v[148:149], v[170:171], 2, s[14:15]
	global_load_dwordx4 v[154:157], v[148:149], off
	global_load_dwordx4 v[158:161], v[148:149], off offset:16
	global_load_dwordx4 v[162:165], v[148:149], off offset:512
	global_load_dwordx4 v[166:169], v[148:149], off offset:528
	v_lshl_add_u32 v148, s30, 8, v1
	v_ashrrev_i32_e32 v149, 31, v148
	v_lshl_add_u64 v[152:153], v[148:149], 2, s[12:13]
	global_load_dword v147, v[152:153], off
	v_cvt_f32_i32_e32 v179, v126
	v_cvt_f32_i32_e32 v127, v127
	v_cvt_f32_i32_e32 v181, v122
	v_cvt_f32_i32_e32 v123, v123
	v_cvt_f32_i32_e32 v183, v128
	v_cvt_f32_i32_e32 v185, v124
	v_cvt_f32_i32_e32 v129, v129
	v_cvt_f32_i32_e32 v187, v125
	v_cvt_f32_i32_e32 v188, v118
	v_cvt_f32_i32_e32 v194, v119
	v_mov_b64_e32 v[150:151], s[10:11]
	v_cvt_f32_i32_e32 v192, v114
	v_cvt_f32_i32_e32 v196, v115
	v_cvt_f32_i32_e32 v198, v120
	v_cvt_f32_i32_e32 v200, v116
	v_cvt_f32_i32_e32 v202, v121
	v_cvt_f32_i32_e32 v204, v117
	v_mad_i64_i32 v[116:117], s[34:35], v148, s61, v[150:151]
	v_lshlrev_b64 v[114:115], 1, v[170:171]
	v_mov_b32_e32 v191, v146
	v_lshl_add_u64 v[206:207], v[116:117], 0, v[114:115]
	v_cvt_f32_i32_e32 v110, v110
	v_cvt_f32_i32_e32 v111, v111
	v_cvt_f32_i32_e32 v112, v112
	v_cvt_f32_i32_e32 v108, v108
	v_cvt_f32_i32_e32 v113, v113
	v_cvt_f32_i32_e32 v109, v109
	v_cvt_f32_i32_e32 v100, v100
	v_cvt_f32_i32_e32 v101, v101
	v_cvt_f32_i32_e32 v94, v94
	v_cvt_f32_i32_e32 v95, v95
	v_cvt_f32_i32_e32 v96, v96
	v_cvt_f32_i32_e32 v92, v92
	v_cvt_f32_i32_e32 v97, v97
	v_cvt_f32_i32_e32 v93, v93
	v_cvt_f32_i32_e32 v84, v84
	v_cvt_f32_i32_e32 v85, v85
	v_cvt_f32_i32_e32 v78, v78
	v_cvt_f32_i32_e32 v74, v74
	v_cvt_f32_i32_e32 v79, v79
	v_cvt_f32_i32_e32 v75, v75
	v_cvt_f32_i32_e32 v80, v80
	v_cvt_f32_i32_e32 v76, v76
	v_cvt_f32_i32_e32 v81, v81
	v_cvt_f32_i32_e32 v77, v77
	v_cvt_f32_i32_e32 v72, v72
	v_cvt_f32_i32_e32 v68, v68
	v_cvt_f32_i32_e32 v73, v73
	v_cvt_f32_i32_e32 v69, v69
	v_cvt_f32_i32_e32 v62, v62
	v_cvt_f32_i32_e32 v58, v58
	v_cvt_f32_i32_e32 v63, v63
	v_cvt_f32_i32_e32 v59, v59
	v_cvt_f32_i32_e32 v64, v64
	v_cvt_f32_i32_e32 v60, v60
	v_cvt_f32_i32_e32 v65, v65
	v_cvt_f32_i32_e32 v61, v61
	v_cvt_f32_i32_e32 v56, v56
	v_cvt_f32_i32_e32 v52, v52
	v_cvt_f32_i32_e32 v57, v57
	v_cvt_f32_i32_e32 v53, v53
	v_cvt_f32_i32_e32 v46, v46
	v_cvt_f32_i32_e32 v42, v42
	v_cvt_f32_i32_e32 v47, v47
	v_cvt_f32_i32_e32 v43, v43
	v_cvt_f32_i32_e32 v48, v48
	v_cvt_f32_i32_e32 v44, v44
	v_cvt_f32_i32_e32 v49, v49
	v_cvt_f32_i32_e32 v45, v45
	v_cvt_f32_i32_e32 v40, v40
	v_cvt_f32_i32_e32 v36, v36
	v_or_b32_e32 v230, 16, v148
	v_ashrrev_i32_e32 v231, 31, v230
	v_lshl_add_u64 v[252:253], v[230:231], 2, s[12:13]
	global_load_dword v250, v[252:253], off
	v_or_b32_e32 v254, 32, v148
	v_ashrrev_i32_e32 v255, 31, v254
	v_lshl_add_u64 v[248:249], v[254:255], 2, s[12:13]
	global_load_dword v244, v[248:249], off
	v_or_b32_e32 v230, 48, v148
	v_ashrrev_i32_e32 v231, 31, v230
	v_lshl_add_u64 v[252:253], v[230:231], 2, s[12:13]
	global_load_dword v246, v[252:253], off
	global_load_dword v240, v[152:153], off offset:512
	global_load_dword v242, v[152:153], off offset:576
	global_load_dword v236, v[152:153], off offset:640
	global_load_dword v238, v[152:153], off offset:704
	s_nop 0
	s_waitcnt vmcnt(11)
	v_lshlrev_b32_e32 v178, 16, v154
	v_lshlrev_b32_e32 v126, 16, v155
	s_waitcnt vmcnt(10)
	v_lshlrev_b32_e32 v180, 16, v158
	v_lshlrev_b32_e32 v122, 16, v159
	v_lshlrev_b32_e32 v182, 16, v156
	v_lshlrev_b32_e32 v184, 16, v160
	v_lshlrev_b32_e32 v128, 16, v157
	v_lshlrev_b32_e32 v186, 16, v161
	s_waitcnt vmcnt(9)
	v_lshlrev_b32_e32 v189, 16, v162
	v_lshlrev_b32_e32 v195, 16, v163
	s_waitcnt vmcnt(7)
	v_mov_b32_e32 v190, v147
	v_pk_mul_f32 v[116:117], v[146:147], v[178:179]
	v_pk_mul_f32 v[120:121], v[146:147], v[126:127]
	v_lshlrev_b32_e32 v193, 16, v166
	v_lshlrev_b32_e32 v197, 16, v167
	v_lshlrev_b32_e32 v199, 16, v164
	v_lshlrev_b32_e32 v201, 16, v168
	v_lshlrev_b32_e32 v203, 16, v165
	v_lshlrev_b32_e32 v205, 16, v169
	v_pk_mul_f32 v[118:119], v[146:147], v[180:181]
	v_pk_mul_f32 v[122:123], v[146:147], v[122:123]
	v_pk_mul_f32 v[124:125], v[146:147], v[182:183]
	v_pk_mul_f32 v[126:127], v[146:147], v[184:185]
	v_pk_mul_f32 v[128:129], v[146:147], v[128:129]
	v_pk_mul_f32 v[154:155], v[146:147], v[186:187]
	v_pk_mul_f32 v[156:157], v[190:191], v[188:189]
	v_pk_mul_f32 v[160:161], v[190:191], v[194:195]
	v_mul_f32_e32 v117, v116, v117
	v_mul_f32_e32 v121, v120, v121
	v_cvt_pk_bf16_f32 v178, v117, v121
	v_pk_mul_f32 v[158:159], v[190:191], v[192:193]
	v_pk_mul_f32 v[162:163], v[190:191], v[196:197]
	v_pk_mul_f32 v[164:165], v[190:191], v[198:199]
	v_pk_mul_f32 v[166:167], v[190:191], v[200:201]
	v_pk_mul_f32 v[168:169], v[190:191], v[202:203]
	v_pk_mul_f32 v[170:171], v[190:191], v[204:205]
	v_mul_f32_e32 v119, v118, v119
	v_mul_f32_e32 v123, v122, v123
	v_mul_f32_e32 v125, v124, v125
	v_mul_f32_e32 v127, v126, v127
	v_mul_f32_e32 v129, v128, v129
	v_mul_f32_e32 v147, v154, v155
	v_mul_f32_e32 v149, v156, v157
	v_mul_f32_e32 v156, v160, v161
	v_cvt_pk_bf16_f32 v179, v125, v129
	v_cvt_pk_bf16_f32 v180, v119, v123
	v_cvt_pk_bf16_f32 v181, v127, v147
	global_store_dwordx4 v[206:207], v[178:181], off
	v_mul_f32_e32 v155, v158, v159
	v_mul_f32_e32 v158, v162, v163
	v_cvt_pk_bf16_f32 v178, v149, v156
	v_mul_f32_e32 v160, v164, v165
	v_mul_f32_e32 v162, v166, v167
	v_mul_f32_e32 v164, v168, v169
	v_mul_f32_e32 v166, v170, v171
	v_cvt_pk_bf16_f32 v179, v160, v164
	v_cvt_pk_bf16_f32 v180, v155, v158
	v_cvt_pk_bf16_f32 v181, v162, v166
	global_store_dwordx4 v[206:207], v[178:181], off offset:256
; __device__ __forceinline__ unsigned cvt_pk_bf16(float lo, float hi) { unsigned r; asm volatile("v_cvt_pk_bf16_f32 %0, %1, %2" : "=v"(r) : "v"(lo), "v"(hi)); return r; }
;     __device__ __forceinline__ void operator()(const f32x4 (&acc)[2][2][4][2], const Unit& u, int wr, int wc, int fr, int fq) const {
;     ...
;             for (int m = 0; m < 4; ++m) { const int row = row0 + ai * HALF + m * 16; bf16_t* rowp = O + (size_t)row * ldc + col0; const float rs = xs[row];
; #pragma unroll
;                 for (int bj = 0; bj < 2; ++bj) { const i32x4 i0 = __builtin_bit_cast(i32x4, acc[ai][bj][m][0]), i1 = __builtin_bit_cast(i32x4, acc[ai][bj][m][1]);
;                     float v[8];
; #pragma unroll
;                     for (int e = 0; e < 4; ++e) { v[e] = (float)i0[e] * rs * cs[bj][e]; v[4 + e] = (float)i1[e] * rs * cs[bj][4 + e]; }
;                     u32x4 w; w.x = cvt_pk_bf16(v[0], v[1]); w.y = cvt_pk_bf16(v[2], v[3]); w.z = cvt_pk_bf16(v[4], v[5]); w.w = cvt_pk_bf16(v[6], v[7]);
;                     *(u32x4*)(rowp + bj * HALF) = w; } }
	v_cvt_f32_i32_e32 v119, v106
	v_cvt_f32_i32_e32 v121, v107
	v_or_b32_e32 v178, 16, v148
	v_ashrrev_i32_e32 v179, 31, v178
	v_lshl_add_u64 v[180:181], v[178:179], 2, s[12:13]
	s_nop 0
	v_cvt_f32_i32_e32 v123, v102
	v_cvt_f32_i32_e32 v125, v98
	v_cvt_f32_i32_e32 v127, v103
	v_cvt_f32_i32_e32 v129, v99
	v_cvt_f32_i32_e32 v147, v104
	v_cvt_f32_i32_e32 v149, v105
	v_or_b32_e32 v102, 32, v148
	v_mad_i64_i32 v[98:99], s[34:35], v178, s61, v[150:151]
	v_ashrrev_i32_e32 v103, 31, v102
	v_lshl_add_u64 v[104:105], v[98:99], 0, v[114:115]
	v_lshl_add_u64 v[106:107], v[102:103], 2, s[12:13]
	v_cvt_f32_i32_e32 v41, v41
	v_cvt_f32_i32_e32 v37, v37
	v_cvt_f32_i32_e32 v30, v30
	v_cvt_f32_i32_e32 v26, v26
	v_cvt_f32_i32_e32 v31, v31
	v_cvt_f32_i32_e32 v27, v27
	v_cvt_f32_i32_e32 v32, v32
	v_cvt_f32_i32_e32 v28, v28
	v_cvt_f32_i32_e32 v33, v33
	v_cvt_f32_i32_e32 v29, v29
	v_cvt_f32_i32_e32 v24, v24
	v_cvt_f32_i32_e32 v20, v20
	v_cvt_f32_i32_e32 v25, v25
	v_cvt_f32_i32_e32 v21, v21
	v_cvt_f32_i32_e32 v14, v14
	v_cvt_f32_i32_e32 v10, v10
	v_cvt_f32_i32_e32 v15, v15
	v_cvt_f32_i32_e32 v11, v11
	v_cvt_f32_i32_e32 v16, v16
	v_cvt_f32_i32_e32 v12, v12
	v_cvt_f32_i32_e32 v17, v17
	v_cvt_f32_i32_e32 v13, v13
	v_cvt_f32_i32_e32 v8, v8
	v_cvt_f32_i32_e32 v4, v4
	v_cvt_f32_i32_e32 v9, v9
	v_cvt_f32_i32_e32 v5, v5
	s_andn2_b64 vcc, exec, s[4:5]
	s_mov_b64 s[4:5], -1
	s_nop 0
	s_waitcnt vmcnt(8)
	v_mul_f32_e32 v98, v250, v110
	v_mul_f32_e32 v99, v250, v119
	v_mul_f32_e32 v103, v250, v111
	v_mul_f32_e32 v110, v250, v121
	v_mul_f32_e32 v111, v250, v112
	v_mul_f32_e32 v108, v250, v108
	v_mul_f32_e32 v112, v250, v113
	v_mul_f32_e32 v109, v250, v109
	v_mul_f32_e32 v113, v250, v123
	v_mul_f32_e32 v119, v250, v125
	v_mul_f32_e32 v121, v250, v127
	v_mul_f32_e32 v123, v250, v129
	v_mul_f32_e32 v125, v250, v147
	v_mul_f32_e32 v100, v250, v100
	v_mul_f32_e32 v127, v250, v149
	v_mul_f32_e32 v101, v250, v101
	v_mul_f32_e32 v98, v116, v98
	v_mul_f32_e32 v117, v118, v99
	v_mul_f32_e32 v99, v120, v103
	v_mul_f32_e32 v103, v122, v110
	v_mul_f32_e32 v110, v124, v111
	v_mul_f32_e32 v108, v126, v108
	v_mul_f32_e32 v111, v128, v112
	v_mul_f32_e32 v109, v154, v109
	v_mul_f32_e32 v112, v157, v113
	v_mul_f32_e32 v113, v159, v119
	v_mul_f32_e32 v119, v161, v121
	v_mul_f32_e32 v121, v163, v123
	v_mul_f32_e32 v123, v165, v125
	v_mul_f32_e32 v125, v167, v100
	v_mul_f32_e32 v129, v171, v101
	v_cvt_pk_bf16_f32 v98, v98, v99
	v_cvt_pk_bf16_f32 v99, v110, v111
	v_cvt_pk_bf16_f32 v100, v117, v103
	v_cvt_pk_bf16_f32 v101, v108, v109
	v_mul_f32_e32 v127, v169, v127
	global_store_dwordx4 v[104:105], v[98:101], off
	v_cvt_f32_i32_e32 v103, v82
	s_nop 0
	v_cvt_pk_bf16_f32 v98, v112, v119
	v_cvt_pk_bf16_f32 v99, v123, v127
	v_cvt_pk_bf16_f32 v100, v113, v121
	v_cvt_pk_bf16_f32 v101, v125, v129
	global_store_dwordx4 v[104:105], v[98:101], off offset:256
	s_nop 0
	v_cvt_f32_i32_e32 v104, v87
	v_cvt_f32_i32_e32 v99, v90
	v_cvt_f32_i32_e32 v100, v91
	v_cvt_f32_i32_e32 v101, v86
	v_cvt_f32_i32_e32 v105, v83
	v_cvt_f32_i32_e32 v106, v88
	v_cvt_f32_i32_e32 v107, v89
	v_or_b32_e32 v86, 48, v148
	v_mad_i64_i32 v[82:83], s[34:35], v102, s61, v[150:151]
	v_ashrrev_i32_e32 v87, 31, v86
	v_lshl_add_u64 v[88:89], v[82:83], 0, v[114:115]
	v_lshl_add_u64 v[90:91], v[86:87], 2, s[12:13]
	s_nop 0
	s_waitcnt vmcnt(9)
	v_mul_f32_e32 v82, v244, v94
	v_mul_f32_e32 v83, v244, v99
	v_mul_f32_e32 v87, v244, v95
	v_mul_f32_e32 v94, v244, v100
	v_mul_f32_e32 v95, v244, v96
	v_mul_f32_e32 v92, v244, v92
	v_mul_f32_e32 v96, v244, v97
	v_mul_f32_e32 v93, v244, v93
	v_mul_f32_e32 v97, v244, v101
	v_mul_f32_e32 v99, v244, v103
	v_mul_f32_e32 v100, v244, v104
	v_mul_f32_e32 v101, v244, v105
	v_mul_f32_e32 v102, v244, v106
	v_mul_f32_e32 v84, v244, v84
	v_mul_f32_e32 v103, v244, v107
	v_mul_f32_e32 v85, v244, v85
	v_mul_f32_e32 v82, v116, v82
	v_mul_f32_e32 v98, v118, v83
	v_mul_f32_e32 v83, v120, v87
	v_mul_f32_e32 v87, v122, v94
	v_mul_f32_e32 v94, v124, v95
	v_mul_f32_e32 v92, v126, v92
	v_mul_f32_e32 v95, v128, v96
	v_mul_f32_e32 v93, v154, v93
	v_mul_f32_e32 v96, v157, v97
	v_mul_f32_e32 v97, v159, v99
	v_mul_f32_e32 v99, v161, v100
	v_mul_f32_e32 v100, v163, v101
	v_mul_f32_e32 v101, v165, v102
	v_mul_f32_e32 v102, v167, v84
	v_mul_f32_e32 v104, v171, v85
	v_cvt_pk_bf16_f32 v82, v82, v83
	v_cvt_pk_bf16_f32 v83, v94, v95
	v_cvt_pk_bf16_f32 v84, v98, v87
	v_cvt_pk_bf16_f32 v85, v92, v93
	v_mul_f32_e32 v103, v169, v103
	global_store_dwordx4 v[88:89], v[82:85], off
	v_cvt_f32_i32_e32 v87, v67
	s_nop 0
	v_cvt_pk_bf16_f32 v82, v96, v99
	v_cvt_pk_bf16_f32 v83, v101, v103
	v_cvt_pk_bf16_f32 v84, v97, v100
	v_cvt_pk_bf16_f32 v85, v102, v104
	global_store_dwordx4 v[88:89], v[82:85], off offset:256
	s_nop 0
	s_nop 0
	s_waitcnt vmcnt(10)
	v_mul_f32_e32 v75, v246, v75
	v_cvt_f32_i32_e32 v83, v70
	v_cvt_f32_i32_e32 v84, v66
	v_cvt_f32_i32_e32 v85, v71
	v_mad_i64_i32 v[66:67], s[34:35], v86, s61, v[150:151]
	v_lshl_add_u64 v[70:71], v[66:67], 0, v[114:115]
	v_mul_f32_e32 v66, v246, v78
	v_mul_f32_e32 v67, v246, v74
	v_mul_f32_e32 v74, v246, v79
	v_mul_f32_e32 v78, v246, v80
	v_mul_f32_e32 v76, v246, v76
	v_mul_f32_e32 v79, v246, v81
	v_mul_f32_e32 v77, v246, v77
	v_mul_f32_e32 v80, v246, v83
	v_mul_f32_e32 v81, v246, v84
	v_mul_f32_e32 v83, v246, v85
	v_mul_f32_e32 v84, v246, v87
	v_mul_f32_e32 v72, v246, v72
	v_mul_f32_e32 v68, v246, v68
	v_mul_f32_e32 v73, v246, v73
	v_mul_f32_e32 v69, v246, v69
	v_mul_f32_e32 v66, v116, v66
	v_mul_f32_e32 v82, v118, v67
	v_mul_f32_e32 v67, v120, v74
	v_mul_f32_e32 v74, v122, v75
	v_mul_f32_e32 v75, v124, v78
	v_mul_f32_e32 v76, v126, v76
	v_mul_f32_e32 v78, v128, v79
	v_mul_f32_e32 v77, v154, v77
	v_mul_f32_e32 v79, v157, v80
	v_mul_f32_e32 v80, v159, v81
	v_mul_f32_e32 v81, v161, v83
	v_mul_f32_e32 v83, v163, v84
	v_mul_f32_e32 v84, v167, v68
	v_mul_f32_e32 v85, v171, v69
	v_cvt_pk_bf16_f32 v66, v66, v67
	v_cvt_pk_bf16_f32 v67, v75, v78
	v_cvt_pk_bf16_f32 v68, v82, v74
	v_cvt_pk_bf16_f32 v69, v76, v77
	v_mul_f32_e32 v72, v165, v72
	v_mul_f32_e32 v73, v169, v73
	global_store_dwordx4 v[70:71], v[66:69], off
	s_nop 1
	v_cvt_pk_bf16_f32 v66, v79, v81
	v_cvt_pk_bf16_f32 v67, v72, v73
	v_cvt_pk_bf16_f32 v68, v80, v83
	v_cvt_pk_bf16_f32 v69, v84, v85
	global_store_dwordx4 v[70:71], v[66:69], off offset:256
	s_nop 0
	v_cvt_f32_i32_e32 v70, v51
	v_cvt_f32_i32_e32 v67, v54
	v_cvt_f32_i32_e32 v68, v50
	v_cvt_f32_i32_e32 v69, v55
	v_add_u32_e32 v50, 0x80, v148
	v_mad_i64_i32 v[50:51], s[34:35], v50, s61, v[150:151]
	v_lshl_add_u64 v[54:55], v[50:51], 0, v[114:115]
	s_nop 0
	s_waitcnt vmcnt(11)
; __device__ __forceinline__ unsigned cvt_pk_bf16(float lo, float hi) { unsigned r; asm volatile("v_cvt_pk_bf16_f32 %0, %1, %2" : "=v"(r) : "v"(lo), "v"(hi)); return r; }
;     __device__ __forceinline__ void operator()(const f32x4 (&acc)[2][2][4][2], const Unit& u, int wr, int wc, int fr, int fq) const {
;     ...
;             for (int m = 0; m < 4; ++m) { const int row = row0 + ai * HALF + m * 16; bf16_t* rowp = O + (size_t)row * ldc + col0; const float rs = xs[row];
; #pragma unroll
;                 for (int bj = 0; bj < 2; ++bj) { const i32x4 i0 = __builtin_bit_cast(i32x4, acc[ai][bj][m][0]), i1 = __builtin_bit_cast(i32x4, acc[ai][bj][m][1]);
;                     float v[8];
; #pragma unroll
;                     for (int e = 0; e < 4; ++e) { v[e] = (float)i0[e] * rs * cs[bj][e]; v[4 + e] = (float)i1[e] * rs * cs[bj][4 + e]; }
;                     u32x4 w; w.x = cvt_pk_bf16(v[0], v[1]); w.y = cvt_pk_bf16(v[2], v[3]); w.z = cvt_pk_bf16(v[4], v[5]); w.w = cvt_pk_bf16(v[6], v[7]);
;                     *(u32x4*)(rowp + bj * HALF) = w; } }
	v_mul_f32_e32 v50, v240, v62
	v_mul_f32_e32 v51, v240, v58
	v_mul_f32_e32 v58, v240, v63
	v_mul_f32_e32 v59, v240, v59
	v_mul_f32_e32 v62, v240, v64
	v_mul_f32_e32 v60, v240, v60
	v_mul_f32_e32 v63, v240, v65
	v_mul_f32_e32 v61, v240, v61
	v_mul_f32_e32 v64, v240, v67
	v_mul_f32_e32 v65, v240, v68
	v_mul_f32_e32 v67, v240, v69
	v_mul_f32_e32 v68, v240, v70
	v_mul_f32_e32 v56, v240, v56
	v_mul_f32_e32 v52, v240, v52
	v_mul_f32_e32 v57, v240, v57
	v_mul_f32_e32 v53, v240, v53
	v_mul_f32_e32 v50, v116, v50
	v_mul_f32_e32 v66, v118, v51
	v_mul_f32_e32 v51, v120, v58
	v_mul_f32_e32 v58, v122, v59
	v_mul_f32_e32 v59, v124, v62
	v_mul_f32_e32 v60, v126, v60
	v_mul_f32_e32 v62, v128, v63
	v_mul_f32_e32 v61, v154, v61
	v_mul_f32_e32 v63, v157, v64
	v_mul_f32_e32 v64, v159, v65
	v_mul_f32_e32 v65, v161, v67
	v_mul_f32_e32 v67, v163, v68
	v_mul_f32_e32 v68, v167, v52
	v_mul_f32_e32 v69, v171, v53
	v_cvt_pk_bf16_f32 v50, v50, v51
	v_cvt_pk_bf16_f32 v51, v59, v62
	v_cvt_pk_bf16_f32 v52, v66, v58
	v_cvt_pk_bf16_f32 v53, v60, v61
	v_mul_f32_e32 v56, v165, v56
	v_mul_f32_e32 v57, v169, v57
	global_store_dwordx4 v[54:55], v[50:53], off
	s_nop 1
	v_cvt_pk_bf16_f32 v50, v63, v65
	v_cvt_pk_bf16_f32 v51, v56, v57
	v_cvt_pk_bf16_f32 v52, v64, v67
	v_cvt_pk_bf16_f32 v53, v68, v69
	global_store_dwordx4 v[54:55], v[50:53], off offset:256
	s_nop 0
	v_cvt_f32_i32_e32 v54, v35
	v_cvt_f32_i32_e32 v51, v38
	v_cvt_f32_i32_e32 v52, v34
	v_cvt_f32_i32_e32 v53, v39
	v_add_u32_e32 v34, 0x90, v148
	v_mad_i64_i32 v[34:35], s[34:35], v34, s61, v[150:151]
	v_lshl_add_u64 v[38:39], v[34:35], 0, v[114:115]
	s_nop 0
	s_waitcnt vmcnt(12)
	v_mul_f32_e32 v34, v242, v46
	v_mul_f32_e32 v35, v242, v42
	v_mul_f32_e32 v42, v242, v47
	v_mul_f32_e32 v43, v242, v43
	v_mul_f32_e32 v46, v242, v48
	v_mul_f32_e32 v44, v242, v44
	v_mul_f32_e32 v47, v242, v49
	v_mul_f32_e32 v45, v242, v45
	v_mul_f32_e32 v48, v242, v51
	v_mul_f32_e32 v49, v242, v52
	v_mul_f32_e32 v51, v242, v53
	v_mul_f32_e32 v52, v242, v54
	v_mul_f32_e32 v40, v242, v40
	v_mul_f32_e32 v36, v242, v36
	v_mul_f32_e32 v41, v242, v41
	v_mul_f32_e32 v37, v242, v37
	v_mul_f32_e32 v34, v116, v34
	v_mul_f32_e32 v50, v118, v35
	v_mul_f32_e32 v35, v120, v42
	v_mul_f32_e32 v42, v122, v43
	v_mul_f32_e32 v43, v124, v46
	v_mul_f32_e32 v44, v126, v44
	v_mul_f32_e32 v46, v128, v47
	v_mul_f32_e32 v45, v154, v45
	v_mul_f32_e32 v47, v157, v48
	v_mul_f32_e32 v48, v159, v49
	v_mul_f32_e32 v49, v161, v51
	v_mul_f32_e32 v51, v163, v52
	v_mul_f32_e32 v52, v167, v36
	v_mul_f32_e32 v53, v171, v37
	v_cvt_pk_bf16_f32 v34, v34, v35
	v_cvt_pk_bf16_f32 v35, v43, v46
	v_cvt_pk_bf16_f32 v36, v50, v42
	v_cvt_pk_bf16_f32 v37, v44, v45
	v_mul_f32_e32 v40, v165, v40
	v_mul_f32_e32 v41, v169, v41
	global_store_dwordx4 v[38:39], v[34:37], off
	s_nop 1
	v_cvt_pk_bf16_f32 v34, v47, v49
	v_cvt_pk_bf16_f32 v35, v40, v41
	v_cvt_pk_bf16_f32 v36, v48, v51
	v_cvt_pk_bf16_f32 v37, v52, v53
	global_store_dwordx4 v[38:39], v[34:37], off offset:256
	s_nop 0
	v_cvt_f32_i32_e32 v38, v19
	v_cvt_f32_i32_e32 v35, v22
	v_cvt_f32_i32_e32 v36, v18
	v_cvt_f32_i32_e32 v37, v23
	v_add_u32_e32 v18, 0xa0, v148
	v_mad_i64_i32 v[18:19], s[34:35], v18, s61, v[150:151]
	v_lshl_add_u64 v[22:23], v[18:19], 0, v[114:115]
	s_nop 0
	s_waitcnt vmcnt(13)
	v_mul_f32_e32 v18, v236, v30
	v_mul_f32_e32 v19, v236, v26
	v_mul_f32_e32 v26, v236, v31
	v_mul_f32_e32 v27, v236, v27
	v_mul_f32_e32 v30, v236, v32
	v_mul_f32_e32 v28, v236, v28
	v_mul_f32_e32 v31, v236, v33
	v_mul_f32_e32 v29, v236, v29
	v_mul_f32_e32 v32, v236, v35
	v_mul_f32_e32 v33, v236, v36
	v_mul_f32_e32 v35, v236, v37
	v_mul_f32_e32 v36, v236, v38
	v_mul_f32_e32 v24, v236, v24
	v_mul_f32_e32 v20, v236, v20
	v_mul_f32_e32 v25, v236, v25
	v_mul_f32_e32 v21, v236, v21
	v_mul_f32_e32 v18, v116, v18
	v_mul_f32_e32 v34, v118, v19
	v_mul_f32_e32 v19, v120, v26
	v_mul_f32_e32 v26, v122, v27
	v_mul_f32_e32 v27, v124, v30
	v_mul_f32_e32 v28, v126, v28
	v_mul_f32_e32 v30, v128, v31
	v_mul_f32_e32 v29, v154, v29
	v_mul_f32_e32 v31, v157, v32
	v_mul_f32_e32 v32, v159, v33
	v_mul_f32_e32 v33, v161, v35
	v_mul_f32_e32 v35, v163, v36
	v_mul_f32_e32 v36, v167, v20
	v_mul_f32_e32 v37, v171, v21
	v_cvt_pk_bf16_f32 v18, v18, v19
	v_cvt_pk_bf16_f32 v19, v27, v30
	v_cvt_pk_bf16_f32 v20, v34, v26
	v_cvt_pk_bf16_f32 v21, v28, v29
	v_mul_f32_e32 v24, v165, v24
	v_mul_f32_e32 v25, v169, v25
	global_store_dwordx4 v[22:23], v[18:21], off
	s_nop 1
	v_cvt_pk_bf16_f32 v18, v31, v33
	v_cvt_pk_bf16_f32 v19, v24, v25
	v_cvt_pk_bf16_f32 v20, v32, v35
	v_cvt_pk_bf16_f32 v21, v36, v37
	global_store_dwordx4 v[22:23], v[18:21], off offset:256
	s_nop 0
	v_cvt_f32_i32_e32 v22, v3
	v_cvt_f32_i32_e32 v19, v6
	v_cvt_f32_i32_e32 v20, v2
	v_cvt_f32_i32_e32 v21, v7
	v_add_u32_e32 v2, 0xb0, v148
	v_mad_i64_i32 v[2:3], s[34:35], v2, s61, v[150:151]
	v_lshl_add_u64 v[6:7], v[2:3], 0, v[114:115]
	s_nop 0
	s_waitcnt vmcnt(14)
	v_mul_f32_e32 v2, v238, v14
	v_mul_f32_e32 v3, v238, v10
	v_mul_f32_e32 v10, v238, v15
	v_mul_f32_e32 v11, v238, v11
	v_mul_f32_e32 v14, v238, v16
	v_mul_f32_e32 v12, v238, v12
	v_mul_f32_e32 v15, v238, v17
	v_mul_f32_e32 v13, v238, v13
	v_mul_f32_e32 v16, v238, v19
	v_mul_f32_e32 v17, v238, v20
	v_mul_f32_e32 v19, v238, v21
	v_mul_f32_e32 v20, v238, v22
	v_mul_f32_e32 v8, v238, v8
	v_mul_f32_e32 v4, v238, v4
	v_mul_f32_e32 v9, v238, v9
	v_mul_f32_e32 v5, v238, v5
	v_mul_f32_e32 v2, v116, v2
	v_mul_f32_e32 v18, v118, v3
	v_mul_f32_e32 v3, v120, v10
	v_mul_f32_e32 v10, v122, v11
	v_mul_f32_e32 v11, v124, v14
	v_mul_f32_e32 v12, v126, v12
	v_mul_f32_e32 v14, v128, v15
	v_mul_f32_e32 v13, v154, v13
	v_mul_f32_e32 v15, v157, v16
	v_mul_f32_e32 v16, v159, v17
	v_mul_f32_e32 v17, v161, v19
	v_mul_f32_e32 v19, v163, v20
	v_mul_f32_e32 v20, v167, v4
	v_mul_f32_e32 v21, v171, v5
	v_cvt_pk_bf16_f32 v2, v2, v3
	v_cvt_pk_bf16_f32 v3, v11, v14
	v_cvt_pk_bf16_f32 v4, v18, v10
	v_cvt_pk_bf16_f32 v5, v12, v13
	v_mul_f32_e32 v8, v165, v8
	v_mul_f32_e32 v9, v169, v9
	global_store_dwordx4 v[6:7], v[2:5], off
	s_nop 1
	v_cvt_pk_bf16_f32 v2, v15, v17
	v_cvt_pk_bf16_f32 v3, v8, v9
	v_cvt_pk_bf16_f32 v4, v16, v19
	v_cvt_pk_bf16_f32 v5, v20, v21
	global_store_dwordx4 v[6:7], v[2:5], off offset:256
	s_cbranch_vccnz .LBB0_247
	s_andn2_b64 vcc, exec, s[8:9]
	s_cbranch_vccnz .LBB0_246
	s_barrier
	s_branch .LBB0_246

; __device__ __forceinline__ unsigned cvt_pk_bf16(float lo, float hi) { unsigned r; asm volatile("v_cvt_pk_bf16_f32 %0, %1, %2" : "=v"(r) : "v"(lo), "v"(hi)); return r; }
; __device__ __forceinline__ float bflo(unsigned u) { return __uint_as_float(u << 16); }
; __device__ __forceinline__ float bfhi(unsigned u) { return __uint_as_float(u & 0xffff0000u); }
;     __device__ __forceinline__ void operator()(const f32x4 (&acc)[2][2][4][2], const Unit& u, int wr, int wc, int fr, int fq) const {
;         const int row0 = u.pm * BM + wr * 64 + fr, col0 = u.pn * BM + wc * 32 + 4 * fq;
; #pragma unroll
;         for (int ai = 0; ai < 2; ++ai)
; #pragma unroll
;             for (int m = 0; m < 4; ++m) { const size_t ro = (size_t)(row0 + ai * HALF + m * 16) * ldc + col0;
; #pragma unroll
;                 for (int bj = 0; bj < 2; ++bj)
; #pragma unroll
;                     for (int n = 0; n < 2; ++n) { const f32x4 a = acc[ai][bj][m][n]; const u32x2 yy = *(const u32x2*)(Y + ro + bj * HALF + n * 16);
;                         f32x4 v; v[0] = bflo(yy.x) / (1.0f + __expf(-a[0])); v[1] = bfhi(yy.x) / (1.0f + __expf(-a[1])); v[2] = bflo(yy.y) / (1.0f + __expf(-a[2])); v[3] = bfhi(yy.y) / (1.0f + __expf(-a[3]));
;                         u32x2 o; o.x = cvt_pk_bf16(v[0], v[1]); o.y = cvt_pk_bf16(v[2], v[3]); *(u32x2*)(C + ro + bj * HALF + n * 16) = o; } }
.LBB0_686:
	v_lshl_add_u32 v146, s6, 8, v1
	v_lshl_or_b32 v144, s7, 8, v151
	v_ashrrev_i32_e32 v147, 31, v146
	v_ashrrev_i32_e32 v145, 31, v144
	v_lshlrev_b64 v[142:143], 10, v[146:147]
	v_lshl_add_u64 v[142:143], v[142:143], 0, v[144:145]
	v_lshlrev_b64 v[142:143], 1, v[142:143]
	v_lshl_add_u64 v[148:149], s[24:25], 0, v[142:143]
	global_load_dwordx2 v[156:157], v[148:149], off
	v_mul_f32_e32 v126, 0xbfb8aa3b, v126
	v_mul_f32_e32 v127, 0xbfb8aa3b, v127
	v_exp_f32_e32 v126, v126
	v_mul_f32_e32 v128, 0xbfb8aa3b, v128
	v_exp_f32_e32 v127, v127
	v_mul_f32_e32 v129, 0xbfb8aa3b, v129
	v_exp_f32_e32 v128, v128
	v_exp_f32_e32 v129, v129
	v_add_f32_e32 v126, 1.0, v126
	v_add_f32_e32 v127, 1.0, v127
	v_add_f32_e32 v128, 1.0, v128
	v_add_f32_e32 v129, 1.0, v129
	v_mul_f32_e32 v122, 0xbfb8aa3b, v122
	v_mul_f32_e32 v123, 0xbfb8aa3b, v123
	v_mul_f32_e32 v124, 0xbfb8aa3b, v124
	v_mul_f32_e32 v125, 0xbfb8aa3b, v125
	v_exp_f32_e32 v124, v124
	v_exp_f32_e32 v125, v125
	v_mul_f32_e32 v118, 0xbfb8aa3b, v118
	v_mul_f32_e32 v119, 0xbfb8aa3b, v119
	v_add_f32_e32 v124, 1.0, v124
	v_add_f32_e32 v125, 1.0, v125
	v_exp_f32_e32 v118, v118
	v_mul_f32_e32 v120, 0xbfb8aa3b, v120
	v_exp_f32_e32 v119, v119
	v_mul_f32_e32 v121, 0xbfb8aa3b, v121
	v_exp_f32_e32 v120, v120
	v_exp_f32_e32 v121, v121
	v_add_f32_e32 v118, 1.0, v118
	v_add_f32_e32 v119, 1.0, v119
	v_add_f32_e32 v120, 1.0, v120
	v_add_f32_e32 v121, 1.0, v121
	v_mul_f32_e32 v114, 0xbfb8aa3b, v114
	v_mul_f32_e32 v115, 0xbfb8aa3b, v115
	v_mul_f32_e32 v116, 0xbfb8aa3b, v116
	v_mul_f32_e32 v117, 0xbfb8aa3b, v117
	v_exp_f32_e32 v116, v116
	v_exp_f32_e32 v117, v117
	v_mul_f32_e32 v110, 0xbfb8aa3b, v110
	v_mul_f32_e32 v111, 0xbfb8aa3b, v111
	v_exp_f32_e32 v110, v110
	v_mul_f32_e32 v112, 0xbfb8aa3b, v112
	v_exp_f32_e32 v111, v111
	v_mul_f32_e32 v113, 0xbfb8aa3b, v113
	v_exp_f32_e32 v112, v112
	v_exp_f32_e32 v113, v113
	v_add_f32_e32 v110, 1.0, v110
	v_add_f32_e32 v111, 1.0, v111
	v_add_f32_e32 v112, 1.0, v112
	v_add_f32_e32 v113, 1.0, v113
	v_mul_f32_e32 v106, 0xbfb8aa3b, v106
	v_mul_f32_e32 v107, 0xbfb8aa3b, v107
	v_exp_f32_e32 v106, v106
	v_exp_f32_e32 v107, v107
	v_mul_f32_e32 v108, 0xbfb8aa3b, v108
	v_mul_f32_e32 v109, 0xbfb8aa3b, v109
	v_exp_f32_e32 v108, v108
	v_exp_f32_e32 v109, v109
	v_mul_f32_e32 v102, 0xbfb8aa3b, v102
	v_mul_f32_e32 v103, 0xbfb8aa3b, v103
	v_add_f32_e32 v108, 1.0, v108
	v_add_f32_e32 v109, 1.0, v109
	v_exp_f32_e32 v102, v102
	v_mul_f32_e32 v104, 0xbfb8aa3b, v104
	v_exp_f32_e32 v103, v103
	v_mul_f32_e32 v105, 0xbfb8aa3b, v105
	v_exp_f32_e32 v104, v104
	v_exp_f32_e32 v105, v105
	v_add_f32_e32 v102, 1.0, v102
	v_add_f32_e32 v103, 1.0, v103
	v_add_f32_e32 v104, 1.0, v104
	v_add_f32_e32 v105, 1.0, v105
	v_mul_f32_e32 v98, 0xbfb8aa3b, v98
	v_mul_f32_e32 v99, 0xbfb8aa3b, v99
	v_mul_f32_e32 v100, 0xbfb8aa3b, v100
	v_mul_f32_e32 v101, 0xbfb8aa3b, v101
	v_exp_f32_e32 v100, v100
	v_exp_f32_e32 v101, v101
	v_mul_f32_e32 v94, 0xbfb8aa3b, v94
	global_load_dwordx2 v[248:249], v[148:149], off offset:32
	global_load_dwordx2 v[250:251], v[148:149], off offset:256
	global_load_dwordx2 v[244:245], v[148:149], off offset:288
	v_or_b32_e32 v178, 16, v146
	v_ashrrev_i32_e32 v179, 31, v178
	v_lshlrev_b64 v[178:179], 10, v[178:179]
	v_lshl_add_u64 v[178:179], v[178:179], 0, v[144:145]
	v_lshlrev_b64 v[230:231], 1, v[178:179]
	v_lshl_add_u64 v[178:179], s[24:25], 0, v[230:231]
	global_load_dwordx2 v[246:247], v[178:179], off
	global_load_dwordx2 v[240:241], v[178:179], off offset:32
	global_load_dwordx2 v[242:243], v[178:179], off offset:256
	global_load_dwordx2 v[236:237], v[178:179], off offset:288
	v_or_b32_e32 v252, 32, v146
	v_ashrrev_i32_e32 v253, 31, v252
	v_lshlrev_b64 v[252:253], 10, v[252:253]
	v_lshl_add_u64 v[252:253], v[252:253], 0, v[144:145]
	v_lshlrev_b64 v[254:255], 1, v[252:253]
	v_lshl_add_u64 v[252:253], s[24:25], 0, v[254:255]
	global_load_dwordx2 v[238:239], v[252:253], off
	v_or_b32_e32 v178, 32, v146
	v_ashrrev_i32_e32 v179, 31, v178
	v_lshlrev_b64 v[178:179], 10, v[178:179]
	v_lshl_add_u64 v[178:179], v[178:179], 0, v[144:145]
	v_lshlrev_b64 v[230:231], 1, v[178:179]
	v_lshl_add_u64 v[178:179], s[24:25], 0, v[230:231]
	global_load_dwordx2 v[232:233], v[178:179], off offset:32
	global_load_dwordx2 v[234:235], v[178:179], off offset:256
	global_load_dwordx2 v[224:225], v[178:179], off offset:288
	v_or_b32_e32 v252, 48, v146
	v_ashrrev_i32_e32 v253, 31, v252
	v_lshlrev_b64 v[252:253], 10, v[252:253]
	v_lshl_add_u64 v[252:253], v[252:253], 0, v[144:145]
	v_lshlrev_b64 v[254:255], 1, v[252:253]
	v_lshl_add_u64 v[252:253], s[24:25], 0, v[254:255]
	global_load_dwordx2 v[226:227], v[252:253], off
	global_load_dwordx2 v[220:221], v[252:253], off offset:32
	global_load_dwordx2 v[222:223], v[252:253], off offset:256
	global_load_dwordx2 v[216:217], v[252:253], off offset:288
	v_lshl_add_u64 v[178:179], v[142:143], 0, s[28:29]
	v_lshl_add_u64 v[230:231], s[24:25], 0, v[178:179]
	global_load_dwordx2 v[218:219], v[230:231], off
	s_nop 0
	s_waitcnt vmcnt(16)
; __device__ __forceinline__ unsigned cvt_pk_bf16(float lo, float hi) { unsigned r; asm volatile("v_cvt_pk_bf16_f32 %0, %1, %2" : "=v"(r) : "v"(lo), "v"(hi)); return r; }
; __device__ __forceinline__ float bflo(unsigned u) { return __uint_as_float(u << 16); }
; __device__ __forceinline__ float bfhi(unsigned u) { return __uint_as_float(u & 0xffff0000u); }
;     __device__ __forceinline__ void operator()(const f32x4 (&acc)[2][2][4][2], const Unit& u, int wr, int wc, int fr, int fq) const {
;         const int row0 = u.pm * BM + wr * 64 + fr, col0 = u.pn * BM + wc * 32 + 4 * fq;
; #pragma unroll
;         for (int ai = 0; ai < 2; ++ai)
; #pragma unroll
;             for (int m = 0; m < 4; ++m) { const size_t ro = (size_t)(row0 + ai * HALF + m * 16) * ldc + col0;
; #pragma unroll
;                 for (int bj = 0; bj < 2; ++bj)
; #pragma unroll
;                     for (int n = 0; n < 2; ++n) { const f32x4 a = acc[ai][bj][m][n]; const u32x2 yy = *(const u32x2*)(Y + ro + bj * HALF + n * 16);
;                         f32x4 v; v[0] = bflo(yy.x) / (1.0f + __expf(-a[0])); v[1] = bfhi(yy.x) / (1.0f + __expf(-a[1])); v[2] = bflo(yy.y) / (1.0f + __expf(-a[2])); v[3] = bfhi(yy.y) / (1.0f + __expf(-a[3]));
;                         u32x2 o; o.x = cvt_pk_bf16(v[0], v[1]); o.y = cvt_pk_bf16(v[2], v[3]); *(u32x2*)(C + ro + bj * HALF + n * 16) = o; } }
	v_lshlrev_b32_e32 v147, 16, v156
	v_and_b32_e32 v155, 0xffff0000, v156
	v_div_scale_f32 v158, s[6:7], v126, v126, v147
	v_lshlrev_b32_e32 v156, 16, v157
	v_div_scale_f32 v160, s[6:7], v127, v127, v155
	v_rcp_f32_e32 v166, v158
	v_and_b32_e32 v157, 0xffff0000, v157
	v_div_scale_f32 v162, s[8:9], v128, v128, v156
	v_rcp_f32_e32 v167, v160
	v_div_scale_f32 v164, s[10:11], v129, v129, v157
	v_rcp_f32_e32 v168, v162
	v_rcp_f32_e32 v169, v164
	v_fma_f32 v170, -v158, v166, 1.0
	v_div_scale_f32 v159, vcc, v147, v126, v147
	v_fma_f32 v171, -v160, v167, 1.0
	v_fmac_f32_e32 v166, v170, v166
	v_div_scale_f32 v161, s[6:7], v155, v127, v155
	v_fma_f32 v172, -v162, v168, 1.0
	v_fmac_f32_e32 v167, v171, v167
	v_mul_f32_e32 v170, v159, v166
	v_div_scale_f32 v163, s[8:9], v156, v128, v156
	v_fma_f32 v173, -v164, v169, 1.0
	v_fmac_f32_e32 v168, v172, v168
	v_mul_f32_e32 v171, v161, v167
	v_fma_f32 v174, -v158, v170, v159
	v_div_scale_f32 v165, s[10:11], v157, v129, v157
	v_fmac_f32_e32 v169, v173, v169
	v_mul_f32_e32 v172, v163, v168
	v_fma_f32 v175, -v160, v171, v161
	v_fmac_f32_e32 v170, v174, v166
	v_mul_f32_e32 v173, v165, v169
	v_fma_f32 v176, -v162, v172, v163
	v_fmac_f32_e32 v171, v175, v167
	v_fma_f32 v158, -v158, v170, v159
	v_fma_f32 v177, -v164, v173, v165
	v_fmac_f32_e32 v172, v176, v168
	v_fma_f32 v159, -v160, v171, v161
	v_div_fmas_f32 v158, v158, v166, v170
	s_mov_b64 vcc, s[6:7]
	v_fmac_f32_e32 v173, v177, v169
	v_fma_f32 v160, -v162, v172, v163
	v_div_fixup_f32 v126, v158, v126, v147
	v_div_fmas_f32 v147, v159, v167, v171
	s_mov_b64 vcc, s[8:9]
	v_fma_f32 v161, -v164, v173, v165
	v_div_fixup_f32 v127, v147, v127, v155
	v_div_fmas_f32 v147, v160, v168, v172
	s_mov_b64 vcc, s[10:11]
	v_div_fixup_f32 v128, v147, v128, v156
	v_div_fmas_f32 v147, v161, v169, v173
	v_cvt_pk_bf16_f32 v126, v126, v127
	v_div_fixup_f32 v127, v147, v129, v157
	v_cvt_pk_bf16_f32 v127, v128, v127
	s_nop 0
	v_exp_f32_e32 v147, v122
	v_exp_f32_e32 v155, v123
	v_lshl_add_u64 v[122:123], s[36:37], 0, v[142:143]
	global_store_dwordx2 v[122:123], v[126:127], off
	v_add_f32_e32 v147, 1.0, v147
	v_add_f32_e32 v155, 1.0, v155
	v_mul_f32_e32 v95, 0xbfb8aa3b, v95
	v_exp_f32_e32 v94, v94
	v_mul_f32_e32 v96, 0xbfb8aa3b, v96
	v_exp_f32_e32 v95, v95
	v_mul_f32_e32 v97, 0xbfb8aa3b, v97
	v_exp_f32_e32 v96, v96
	v_exp_f32_e32 v97, v97
	v_add_f32_e32 v94, 1.0, v94
	v_add_f32_e32 v95, 1.0, v95
	v_add_f32_e32 v96, 1.0, v96
	v_add_f32_e32 v97, 1.0, v97
	v_mul_f32_e32 v90, 0xbfb8aa3b, v90
	v_mul_f32_e32 v91, 0xbfb8aa3b, v91
	v_exp_f32_e32 v90, v90
	v_exp_f32_e32 v91, v91
	v_mul_f32_e32 v92, 0xbfb8aa3b, v92
	v_mul_f32_e32 v93, 0xbfb8aa3b, v93
	v_exp_f32_e32 v92, v92
	v_exp_f32_e32 v93, v93
	v_mul_f32_e32 v86, 0xbfb8aa3b, v86
	v_mul_f32_e32 v87, 0xbfb8aa3b, v87
	v_add_f32_e32 v92, 1.0, v92
	v_add_f32_e32 v93, 1.0, v93
	v_exp_f32_e32 v86, v86
	v_mul_f32_e32 v88, 0xbfb8aa3b, v88
	v_exp_f32_e32 v87, v87
	v_mul_f32_e32 v89, 0xbfb8aa3b, v89
	v_exp_f32_e32 v88, v88
	v_exp_f32_e32 v89, v89
	v_add_f32_e32 v86, 1.0, v86
	v_add_f32_e32 v87, 1.0, v87
	v_add_f32_e32 v88, 1.0, v88
	v_add_f32_e32 v89, 1.0, v89
	v_mul_f32_e32 v82, 0xbfb8aa3b, v82
	v_mul_f32_e32 v83, 0xbfb8aa3b, v83
	v_mul_f32_e32 v84, 0xbfb8aa3b, v84
	v_mul_f32_e32 v85, 0xbfb8aa3b, v85
	v_exp_f32_e32 v84, v84
	v_exp_f32_e32 v85, v85
	v_mul_f32_e32 v78, 0xbfb8aa3b, v78
	v_mul_f32_e32 v79, 0xbfb8aa3b, v79
	v_exp_f32_e32 v78, v78
	v_mul_f32_e32 v80, 0xbfb8aa3b, v80
	v_exp_f32_e32 v79, v79
	v_mul_f32_e32 v81, 0xbfb8aa3b, v81
	v_exp_f32_e32 v80, v80
	v_exp_f32_e32 v81, v81
	v_add_f32_e32 v78, 1.0, v78
	v_add_f32_e32 v79, 1.0, v79
	v_add_f32_e32 v80, 1.0, v80
	v_add_f32_e32 v81, 1.0, v81
	v_mul_f32_e32 v74, 0xbfb8aa3b, v74
	v_mul_f32_e32 v75, 0xbfb8aa3b, v75
	v_exp_f32_e32 v74, v74
	v_exp_f32_e32 v75, v75
	v_mul_f32_e32 v76, 0xbfb8aa3b, v76
	v_mul_f32_e32 v77, 0xbfb8aa3b, v77
	v_exp_f32_e32 v76, v76
	v_exp_f32_e32 v77, v77
	v_mul_f32_e32 v70, 0xbfb8aa3b, v70
	v_mul_f32_e32 v71, 0xbfb8aa3b, v71
	v_add_f32_e32 v76, 1.0, v76
	v_add_f32_e32 v77, 1.0, v77
	v_exp_f32_e32 v70, v70
	v_mul_f32_e32 v72, 0xbfb8aa3b, v72
	v_exp_f32_e32 v71, v71
	v_mul_f32_e32 v73, 0xbfb8aa3b, v73
	v_exp_f32_e32 v72, v72
	v_exp_f32_e32 v73, v73
	v_add_f32_e32 v70, 1.0, v70
	v_add_f32_e32 v71, 1.0, v71
	v_add_f32_e32 v72, 1.0, v72
	v_add_f32_e32 v73, 1.0, v73
	s_nop 0
	s_waitcnt vmcnt(16)
; __device__ __forceinline__ unsigned cvt_pk_bf16(float lo, float hi) { unsigned r; asm volatile("v_cvt_pk_bf16_f32 %0, %1, %2" : "=v"(r) : "v"(lo), "v"(hi)); return r; }
; __device__ __forceinline__ float bflo(unsigned u) { return __uint_as_float(u << 16); }
; __device__ __forceinline__ float bfhi(unsigned u) { return __uint_as_float(u & 0xffff0000u); }
;     __device__ __forceinline__ void operator()(const f32x4 (&acc)[2][2][4][2], const Unit& u, int wr, int wc, int fr, int fq) const {
;         const int row0 = u.pm * BM + wr * 64 + fr, col0 = u.pn * BM + wc * 32 + 4 * fq;
; #pragma unroll
;         for (int ai = 0; ai < 2; ++ai)
; #pragma unroll
;             for (int m = 0; m < 4; ++m) { const size_t ro = (size_t)(row0 + ai * HALF + m * 16) * ldc + col0;
; #pragma unroll
;                 for (int bj = 0; bj < 2; ++bj)
; #pragma unroll
;                     for (int n = 0; n < 2; ++n) { const f32x4 a = acc[ai][bj][m][n]; const u32x2 yy = *(const u32x2*)(Y + ro + bj * HALF + n * 16);
;                         f32x4 v; v[0] = bflo(yy.x) / (1.0f + __expf(-a[0])); v[1] = bfhi(yy.x) / (1.0f + __expf(-a[1])); v[2] = bflo(yy.y) / (1.0f + __expf(-a[2])); v[3] = bfhi(yy.y) / (1.0f + __expf(-a[3]));
;                         u32x2 o; o.x = cvt_pk_bf16(v[0], v[1]); o.y = cvt_pk_bf16(v[2], v[3]); *(u32x2*)(C + ro + bj * HALF + n * 16) = o; } }
	v_lshlrev_b32_e32 v126, 16, v248
	v_and_b32_e32 v127, 0xffff0000, v248
	v_div_scale_f32 v156, s[6:7], v147, v147, v126
	v_lshlrev_b32_e32 v128, 16, v249
	v_div_scale_f32 v158, s[6:7], v155, v155, v127
	v_rcp_f32_e32 v164, v156
	v_and_b32_e32 v129, 0xffff0000, v249
	v_div_scale_f32 v160, s[8:9], v124, v124, v128
	v_rcp_f32_e32 v165, v158
	v_div_scale_f32 v162, s[10:11], v125, v125, v129
	v_rcp_f32_e32 v166, v160
	v_rcp_f32_e32 v167, v162
	v_fma_f32 v168, -v156, v164, 1.0
	v_div_scale_f32 v157, vcc, v126, v147, v126
	v_fma_f32 v169, -v158, v165, 1.0
	v_fmac_f32_e32 v164, v168, v164
	v_div_scale_f32 v159, s[6:7], v127, v155, v127
	v_fma_f32 v170, -v160, v166, 1.0
	v_fmac_f32_e32 v165, v169, v165
	v_mul_f32_e32 v168, v157, v164
	v_div_scale_f32 v161, s[8:9], v128, v124, v128
	v_fma_f32 v171, -v162, v167, 1.0
	v_fmac_f32_e32 v166, v170, v166
	v_mul_f32_e32 v169, v159, v165
	v_fma_f32 v172, -v156, v168, v157
	v_div_scale_f32 v163, s[10:11], v129, v125, v129
	v_fmac_f32_e32 v167, v171, v167
	v_mul_f32_e32 v170, v161, v166
	v_fma_f32 v173, -v158, v169, v159
	v_fmac_f32_e32 v168, v172, v164
	v_mul_f32_e32 v171, v163, v167
	v_fma_f32 v174, -v160, v170, v161
	v_fmac_f32_e32 v169, v173, v165
	v_fma_f32 v156, -v156, v168, v157
	v_fma_f32 v175, -v162, v171, v163
	v_fmac_f32_e32 v170, v174, v166
	v_fma_f32 v157, -v158, v169, v159
	v_div_fmas_f32 v156, v156, v164, v168
	s_mov_b64 vcc, s[6:7]
	v_fmac_f32_e32 v171, v175, v167
	v_fma_f32 v158, -v160, v170, v161
	v_div_fixup_f32 v126, v156, v147, v126
	v_div_fmas_f32 v147, v157, v165, v169
	s_mov_b64 vcc, s[8:9]
	v_fma_f32 v159, -v162, v171, v163
	v_div_fixup_f32 v127, v147, v155, v127
	v_div_fmas_f32 v147, v158, v166, v170
	s_mov_b64 vcc, s[10:11]
	v_div_fixup_f32 v128, v147, v124, v128
	v_div_fmas_f32 v147, v159, v167, v171
	v_div_fixup_f32 v125, v147, v125, v129
	v_cvt_pk_bf16_f32 v124, v126, v127
	v_cvt_pk_bf16_f32 v125, v128, v125
	s_nop 0
	v_mul_f32_e32 v66, 0xbfb8aa3b, v66
	global_store_dwordx2 v[122:123], v[124:125], off offset:32
	v_mul_f32_e32 v67, 0xbfb8aa3b, v67
	v_exp_f32_e32 v66, v66
	v_mul_f32_e32 v68, 0xbfb8aa3b, v68
	v_exp_f32_e32 v67, v67
	v_mul_f32_e32 v69, 0xbfb8aa3b, v69
	v_exp_f32_e32 v68, v68
	v_exp_f32_e32 v69, v69
	v_mul_f32_e32 v62, 0xbfb8aa3b, v62
	v_mul_f32_e32 v63, 0xbfb8aa3b, v63
	v_exp_f32_e32 v62, v62
	v_mul_f32_e32 v64, 0xbfb8aa3b, v64
	v_exp_f32_e32 v63, v63
	v_mul_f32_e32 v65, 0xbfb8aa3b, v65
	v_exp_f32_e32 v64, v64
	v_exp_f32_e32 v65, v65
	v_add_f32_e32 v62, 1.0, v62
	v_add_f32_e32 v63, 1.0, v63
	v_add_f32_e32 v64, 1.0, v64
	v_add_f32_e32 v65, 1.0, v65
	v_mul_f32_e32 v58, 0xbfb8aa3b, v58
	v_mul_f32_e32 v59, 0xbfb8aa3b, v59
	v_exp_f32_e32 v58, v58
	v_exp_f32_e32 v59, v59
	v_mul_f32_e32 v60, 0xbfb8aa3b, v60
	v_mul_f32_e32 v61, 0xbfb8aa3b, v61
	v_exp_f32_e32 v60, v60
	v_exp_f32_e32 v61, v61
	v_mul_f32_e32 v54, 0xbfb8aa3b, v54
	v_mul_f32_e32 v55, 0xbfb8aa3b, v55
	v_add_f32_e32 v60, 1.0, v60
	v_add_f32_e32 v61, 1.0, v61
	v_exp_f32_e32 v54, v54
	v_mul_f32_e32 v56, 0xbfb8aa3b, v56
	v_exp_f32_e32 v55, v55
	v_mul_f32_e32 v57, 0xbfb8aa3b, v57
	v_exp_f32_e32 v56, v56
	v_exp_f32_e32 v57, v57
	v_add_f32_e32 v54, 1.0, v54
	v_add_f32_e32 v55, 1.0, v55
	v_add_f32_e32 v56, 1.0, v56
	v_add_f32_e32 v57, 1.0, v57
	v_mul_f32_e32 v50, 0xbfb8aa3b, v50
	v_mul_f32_e32 v51, 0xbfb8aa3b, v51
	v_exp_f32_e32 v50, v50
	v_mul_f32_e32 v52, 0xbfb8aa3b, v52
	v_exp_f32_e32 v51, v51
	v_mul_f32_e32 v53, 0xbfb8aa3b, v53
	v_exp_f32_e32 v52, v52
	v_exp_f32_e32 v53, v53
	v_mul_f32_e32 v46, 0xbfb8aa3b, v46
	v_mul_f32_e32 v47, 0xbfb8aa3b, v47
	v_exp_f32_e32 v46, v46
	v_mul_f32_e32 v48, 0xbfb8aa3b, v48
	v_exp_f32_e32 v47, v47
	v_mul_f32_e32 v49, 0xbfb8aa3b, v49
	v_exp_f32_e32 v48, v48
	v_exp_f32_e32 v49, v49
	v_add_f32_e32 v46, 1.0, v46
	v_add_f32_e32 v47, 1.0, v47
	v_add_f32_e32 v48, 1.0, v48
	v_add_f32_e32 v49, 1.0, v49
	v_mul_f32_e32 v42, 0xbfb8aa3b, v42
	v_mul_f32_e32 v43, 0xbfb8aa3b, v43
	v_exp_f32_e32 v42, v42
	v_exp_f32_e32 v43, v43
	v_mul_f32_e32 v44, 0xbfb8aa3b, v44
	v_mul_f32_e32 v45, 0xbfb8aa3b, v45
	v_exp_f32_e32 v44, v44
	v_exp_f32_e32 v45, v45
	v_mul_f32_e32 v38, 0xbfb8aa3b, v38
	v_mul_f32_e32 v39, 0xbfb8aa3b, v39
	v_add_f32_e32 v44, 1.0, v44
	v_add_f32_e32 v45, 1.0, v45
	v_exp_f32_e32 v38, v38
	v_mul_f32_e32 v40, 0xbfb8aa3b, v40
	v_exp_f32_e32 v39, v39
	v_mul_f32_e32 v41, 0xbfb8aa3b, v41
	s_nop 0
	s_waitcnt vmcnt(16)
; __device__ __forceinline__ unsigned cvt_pk_bf16(float lo, float hi) { unsigned r; asm volatile("v_cvt_pk_bf16_f32 %0, %1, %2" : "=v"(r) : "v"(lo), "v"(hi)); return r; }
; __device__ __forceinline__ float bflo(unsigned u) { return __uint_as_float(u << 16); }
; __device__ __forceinline__ float bfhi(unsigned u) { return __uint_as_float(u & 0xffff0000u); }
;     __device__ __forceinline__ void operator()(const f32x4 (&acc)[2][2][4][2], const Unit& u, int wr, int wc, int fr, int fq) const {
;         const int row0 = u.pm * BM + wr * 64 + fr, col0 = u.pn * BM + wc * 32 + 4 * fq;
; #pragma unroll
;         for (int ai = 0; ai < 2; ++ai)
; #pragma unroll
;             for (int m = 0; m < 4; ++m) { const size_t ro = (size_t)(row0 + ai * HALF + m * 16) * ldc + col0;
; #pragma unroll
;                 for (int bj = 0; bj < 2; ++bj)
; #pragma unroll
;                     for (int n = 0; n < 2; ++n) { const f32x4 a = acc[ai][bj][m][n]; const u32x2 yy = *(const u32x2*)(Y + ro + bj * HALF + n * 16);
;                         f32x4 v; v[0] = bflo(yy.x) / (1.0f + __expf(-a[0])); v[1] = bfhi(yy.x) / (1.0f + __expf(-a[1])); v[2] = bflo(yy.y) / (1.0f + __expf(-a[2])); v[3] = bfhi(yy.y) / (1.0f + __expf(-a[3]));
;                         u32x2 o; o.x = cvt_pk_bf16(v[0], v[1]); o.y = cvt_pk_bf16(v[2], v[3]); *(u32x2*)(C + ro + bj * HALF + n * 16) = o; } }
	v_lshlrev_b32_e32 v124, 16, v250
	v_and_b32_e32 v125, 0xffff0000, v250
	v_div_scale_f32 v128, s[6:7], v118, v118, v124
	v_lshlrev_b32_e32 v126, 16, v251
	v_div_scale_f32 v147, s[6:7], v119, v119, v125
	v_rcp_f32_e32 v160, v128
	v_and_b32_e32 v127, 0xffff0000, v251
	v_div_scale_f32 v156, s[8:9], v120, v120, v126
	v_rcp_f32_e32 v161, v147
	v_div_scale_f32 v158, s[10:11], v121, v121, v127
	v_rcp_f32_e32 v162, v156
	v_rcp_f32_e32 v163, v158
	v_fma_f32 v164, -v128, v160, 1.0
	v_div_scale_f32 v129, vcc, v124, v118, v124
	v_fma_f32 v165, -v147, v161, 1.0
	v_fmac_f32_e32 v160, v164, v160
	v_div_scale_f32 v155, s[6:7], v125, v119, v125
	v_fma_f32 v166, -v156, v162, 1.0
	v_fmac_f32_e32 v161, v165, v161
	v_mul_f32_e32 v164, v129, v160
	v_div_scale_f32 v157, s[8:9], v126, v120, v126
	v_fma_f32 v167, -v158, v163, 1.0
	v_fmac_f32_e32 v162, v166, v162
	v_mul_f32_e32 v165, v155, v161
	v_fma_f32 v168, -v128, v164, v129
	v_div_scale_f32 v159, s[10:11], v127, v121, v127
	v_fmac_f32_e32 v163, v167, v163
	v_mul_f32_e32 v166, v157, v162
	v_fma_f32 v169, -v147, v165, v155
	v_fmac_f32_e32 v164, v168, v160
	v_mul_f32_e32 v167, v159, v163
	v_fma_f32 v170, -v156, v166, v157
	v_fmac_f32_e32 v165, v169, v161
	v_fma_f32 v128, -v128, v164, v129
	v_fma_f32 v171, -v158, v167, v159
	v_fmac_f32_e32 v166, v170, v162
	v_fma_f32 v129, -v147, v165, v155
	v_div_fmas_f32 v128, v128, v160, v164
	s_mov_b64 vcc, s[6:7]
	v_fmac_f32_e32 v167, v171, v163
	v_fma_f32 v147, -v156, v166, v157
	v_div_fixup_f32 v118, v128, v118, v124
	v_div_fmas_f32 v124, v129, v161, v165
	s_mov_b64 vcc, s[8:9]
	v_fma_f32 v155, -v158, v167, v159
	v_div_fixup_f32 v119, v124, v119, v125
	v_div_fmas_f32 v124, v147, v162, v166
	s_mov_b64 vcc, s[10:11]
	v_div_fixup_f32 v120, v124, v120, v126
	v_div_fmas_f32 v124, v155, v163, v167
	v_cvt_pk_bf16_f32 v118, v118, v119
	v_div_fixup_f32 v119, v124, v121, v127
	v_cvt_pk_bf16_f32 v119, v120, v119
	s_nop 0
	v_exp_f32_e32 v124, v114
	v_exp_f32_e32 v125, v115
	global_store_dwordx2 v[122:123], v[118:119], off offset:256
	v_add_f32_e32 v126, 1.0, v116
	v_add_f32_e32 v124, 1.0, v124
	v_add_f32_e32 v125, 1.0, v125
	v_add_f32_e32 v127, 1.0, v117
	v_or_b32_e32 v114, 16, v146
	v_ashrrev_i32_e32 v115, 31, v114
	v_lshlrev_b64 v[114:115], 10, v[114:115]
	v_lshl_add_u64 v[114:115], v[114:115], 0, v[144:145]
	v_lshlrev_b64 v[116:117], 1, v[114:115]
	v_lshl_add_u64 v[114:115], s[24:25], 0, v[116:117]
	v_exp_f32_e32 v40, v40
	v_exp_f32_e32 v41, v41
	v_add_f32_e32 v38, 1.0, v38
	v_add_f32_e32 v39, 1.0, v39
	v_add_f32_e32 v40, 1.0, v40
	v_add_f32_e32 v41, 1.0, v41
	v_mul_f32_e32 v34, 0xbfb8aa3b, v34
	v_mul_f32_e32 v35, 0xbfb8aa3b, v35
	v_exp_f32_e32 v34, v34
	v_mul_f32_e32 v36, 0xbfb8aa3b, v36
	v_exp_f32_e32 v35, v35
	v_mul_f32_e32 v37, 0xbfb8aa3b, v37
	v_exp_f32_e32 v36, v36
	v_exp_f32_e32 v37, v37
	v_mul_f32_e32 v30, 0xbfb8aa3b, v30
	v_mul_f32_e32 v31, 0xbfb8aa3b, v31
	v_exp_f32_e32 v30, v30
	v_mul_f32_e32 v32, 0xbfb8aa3b, v32
	v_exp_f32_e32 v31, v31
	v_mul_f32_e32 v33, 0xbfb8aa3b, v33
	v_exp_f32_e32 v32, v32
	v_exp_f32_e32 v33, v33
	v_add_f32_e32 v30, 1.0, v30
	v_add_f32_e32 v31, 1.0, v31
	v_add_f32_e32 v32, 1.0, v32
	v_add_f32_e32 v33, 1.0, v33
	v_mul_f32_e32 v26, 0xbfb8aa3b, v26
	v_mul_f32_e32 v27, 0xbfb8aa3b, v27
	v_exp_f32_e32 v26, v26
	v_exp_f32_e32 v27, v27
	v_mul_f32_e32 v28, 0xbfb8aa3b, v28
	v_mul_f32_e32 v29, 0xbfb8aa3b, v29
	v_exp_f32_e32 v28, v28
	v_exp_f32_e32 v29, v29
	v_mul_f32_e32 v22, 0xbfb8aa3b, v22
	v_mul_f32_e32 v23, 0xbfb8aa3b, v23
	v_add_f32_e32 v28, 1.0, v28
	v_add_f32_e32 v29, 1.0, v29
	v_exp_f32_e32 v22, v22
	v_mul_f32_e32 v24, 0xbfb8aa3b, v24
	v_exp_f32_e32 v23, v23
	v_mul_f32_e32 v25, 0xbfb8aa3b, v25
	v_exp_f32_e32 v24, v24
	v_exp_f32_e32 v25, v25
	v_add_f32_e32 v22, 1.0, v22
	v_add_f32_e32 v23, 1.0, v23
	v_add_f32_e32 v24, 1.0, v24
	v_add_f32_e32 v25, 1.0, v25
	v_mul_f32_e32 v18, 0xbfb8aa3b, v18
	v_mul_f32_e32 v19, 0xbfb8aa3b, v19
	v_exp_f32_e32 v18, v18
	v_mul_f32_e32 v20, 0xbfb8aa3b, v20
	v_exp_f32_e32 v19, v19
	v_mul_f32_e32 v21, 0xbfb8aa3b, v21
	v_exp_f32_e32 v20, v20
	v_exp_f32_e32 v21, v21
	v_mul_f32_e32 v14, 0xbfb8aa3b, v14
	v_mul_f32_e32 v15, 0xbfb8aa3b, v15
	v_exp_f32_e32 v14, v14
	v_mul_f32_e32 v16, 0xbfb8aa3b, v16
	v_exp_f32_e32 v15, v15
	v_mul_f32_e32 v17, 0xbfb8aa3b, v17
	v_exp_f32_e32 v16, v16
	v_exp_f32_e32 v17, v17
	v_add_f32_e32 v14, 1.0, v14
	v_add_f32_e32 v15, 1.0, v15
	s_nop 0
	s_waitcnt vmcnt(16)
; __device__ __forceinline__ unsigned cvt_pk_bf16(float lo, float hi) { unsigned r; asm volatile("v_cvt_pk_bf16_f32 %0, %1, %2" : "=v"(r) : "v"(lo), "v"(hi)); return r; }
; __device__ __forceinline__ float bflo(unsigned u) { return __uint_as_float(u << 16); }
; __device__ __forceinline__ float bfhi(unsigned u) { return __uint_as_float(u & 0xffff0000u); }
;     __device__ __forceinline__ void operator()(const f32x4 (&acc)[2][2][4][2], const Unit& u, int wr, int wc, int fr, int fq) const {
;         const int row0 = u.pm * BM + wr * 64 + fr, col0 = u.pn * BM + wc * 32 + 4 * fq;
; #pragma unroll
;         for (int ai = 0; ai < 2; ++ai)
; #pragma unroll
;             for (int m = 0; m < 4; ++m) { const size_t ro = (size_t)(row0 + ai * HALF + m * 16) * ldc + col0;
; #pragma unroll
;                 for (int bj = 0; bj < 2; ++bj)
; #pragma unroll
;                     for (int n = 0; n < 2; ++n) { const f32x4 a = acc[ai][bj][m][n]; const u32x2 yy = *(const u32x2*)(Y + ro + bj * HALF + n * 16);
;                         f32x4 v; v[0] = bflo(yy.x) / (1.0f + __expf(-a[0])); v[1] = bfhi(yy.x) / (1.0f + __expf(-a[1])); v[2] = bflo(yy.y) / (1.0f + __expf(-a[2])); v[3] = bfhi(yy.y) / (1.0f + __expf(-a[3]));
;                         u32x2 o; o.x = cvt_pk_bf16(v[0], v[1]); o.y = cvt_pk_bf16(v[2], v[3]); *(u32x2*)(C + ro + bj * HALF + n * 16) = o; } }
	v_lshlrev_b32_e32 v118, 16, v244
	v_and_b32_e32 v119, 0xffff0000, v244
	v_div_scale_f32 v128, s[6:7], v124, v124, v118
	v_lshlrev_b32_e32 v120, 16, v245
	v_div_scale_f32 v147, s[6:7], v125, v125, v119
	v_rcp_f32_e32 v158, v128
	v_and_b32_e32 v121, 0xffff0000, v245
	v_div_scale_f32 v149, s[8:9], v126, v126, v120
	v_rcp_f32_e32 v159, v147
	v_div_scale_f32 v156, s[10:11], v127, v127, v121
	v_rcp_f32_e32 v160, v149
	v_rcp_f32_e32 v161, v156
	v_fma_f32 v162, -v128, v158, 1.0
	v_div_scale_f32 v129, vcc, v118, v124, v118
	v_fma_f32 v163, -v147, v159, 1.0
	v_fmac_f32_e32 v158, v162, v158
	v_div_scale_f32 v148, s[6:7], v119, v125, v119
	v_fma_f32 v164, -v149, v160, 1.0
	v_fmac_f32_e32 v159, v163, v159
	v_mul_f32_e32 v162, v129, v158
	v_div_scale_f32 v155, s[8:9], v120, v126, v120
	v_fma_f32 v165, -v156, v161, 1.0
	v_fmac_f32_e32 v160, v164, v160
	v_mul_f32_e32 v163, v148, v159
	v_fma_f32 v166, -v128, v162, v129
	v_div_scale_f32 v157, s[10:11], v121, v127, v121
	v_fmac_f32_e32 v161, v165, v161
	v_mul_f32_e32 v164, v155, v160
	v_fma_f32 v167, -v147, v163, v148
	v_fmac_f32_e32 v162, v166, v158
	v_mul_f32_e32 v165, v157, v161
	v_fma_f32 v168, -v149, v164, v155
	v_fmac_f32_e32 v163, v167, v159
	v_fma_f32 v128, -v128, v162, v129
	v_fma_f32 v169, -v156, v165, v157
	v_fmac_f32_e32 v164, v168, v160
	v_fma_f32 v129, -v147, v163, v148
	v_div_fmas_f32 v128, v128, v158, v162
	s_mov_b64 vcc, s[6:7]
	v_fmac_f32_e32 v165, v169, v161
	v_fma_f32 v147, -v149, v164, v155
	v_div_fixup_f32 v118, v128, v124, v118
	v_div_fmas_f32 v124, v129, v159, v163
	s_mov_b64 vcc, s[8:9]
	v_fma_f32 v148, -v156, v165, v157
	v_div_fixup_f32 v119, v124, v125, v119
	v_div_fmas_f32 v124, v147, v160, v164
	s_mov_b64 vcc, s[10:11]
	v_div_fixup_f32 v120, v124, v126, v120
	v_div_fmas_f32 v124, v148, v161, v165
	v_cvt_pk_bf16_f32 v118, v118, v119
	v_div_fixup_f32 v119, v124, v127, v121
	v_cvt_pk_bf16_f32 v119, v120, v119
	global_store_dwordx2 v[122:123], v[118:119], off offset:288
	s_nop 0
	v_add_f32_e32 v16, 1.0, v16
	v_add_f32_e32 v17, 1.0, v17
	v_mul_f32_e32 v10, 0xbfb8aa3b, v10
	v_mul_f32_e32 v11, 0xbfb8aa3b, v11
	v_exp_f32_e32 v10, v10
	v_exp_f32_e32 v11, v11
	v_mul_f32_e32 v12, 0xbfb8aa3b, v12
	v_mul_f32_e32 v13, 0xbfb8aa3b, v13
	v_exp_f32_e32 v12, v12
	v_exp_f32_e32 v13, v13
	v_mul_f32_e32 v6, 0xbfb8aa3b, v6
	v_mul_f32_e32 v7, 0xbfb8aa3b, v7
	v_add_f32_e32 v12, 1.0, v12
	v_add_f32_e32 v13, 1.0, v13
	v_exp_f32_e32 v6, v6
	v_mul_f32_e32 v8, 0xbfb8aa3b, v8
	v_exp_f32_e32 v7, v7
	v_mul_f32_e32 v9, 0xbfb8aa3b, v9
	v_exp_f32_e32 v8, v8
	v_exp_f32_e32 v9, v9
	v_add_f32_e32 v6, 1.0, v6
	v_add_f32_e32 v7, 1.0, v7
	v_add_f32_e32 v8, 1.0, v8
	v_add_f32_e32 v9, 1.0, v9
	v_mul_f32_e32 v2, 0xbfb8aa3b, v2
	v_mul_f32_e32 v3, 0xbfb8aa3b, v3
	v_exp_f32_e32 v2, v2
	v_mul_f32_e32 v4, 0xbfb8aa3b, v4
	v_exp_f32_e32 v3, v3
	v_mul_f32_e32 v5, 0xbfb8aa3b, v5
	v_exp_f32_e32 v4, v4
	v_exp_f32_e32 v5, v5
	v_add_f32_e32 v2, 1.0, v2
	v_add_f32_e32 v3, 1.0, v3
	v_add_f32_e32 v4, 1.0, v4
	v_add_f32_e32 v5, 1.0, v5
	s_nop 0
	s_waitcnt vmcnt(16)
	v_lshlrev_b32_e32 v120, 16, v246
	v_and_b32_e32 v118, 0xffff0000, v246
	v_div_scale_f32 v122, s[6:7], v110, v110, v120
	v_lshlrev_b32_e32 v121, 16, v247
	v_div_scale_f32 v124, s[6:7], v111, v111, v118
	v_rcp_f32_e32 v147, v122
	v_and_b32_e32 v119, 0xffff0000, v247
	v_div_scale_f32 v126, s[8:9], v112, v112, v121
	v_rcp_f32_e32 v148, v124
	v_div_scale_f32 v128, s[10:11], v113, v113, v119
	v_rcp_f32_e32 v149, v126
	v_rcp_f32_e32 v155, v128
	v_fma_f32 v156, -v122, v147, 1.0
	v_div_scale_f32 v123, vcc, v120, v110, v120
	v_fma_f32 v157, -v124, v148, 1.0
	v_fmac_f32_e32 v147, v156, v147
	v_div_scale_f32 v125, s[6:7], v118, v111, v118
	v_fma_f32 v158, -v126, v149, 1.0
	v_fmac_f32_e32 v148, v157, v148
	v_mul_f32_e32 v156, v123, v147
	v_div_scale_f32 v127, s[8:9], v121, v112, v121
	v_fma_f32 v159, -v128, v155, 1.0
	v_fmac_f32_e32 v149, v158, v149
	v_mul_f32_e32 v157, v125, v148
	v_fma_f32 v160, -v122, v156, v123
	v_div_scale_f32 v129, s[10:11], v119, v113, v119
	v_fmac_f32_e32 v155, v159, v155
	v_mul_f32_e32 v158, v127, v149
	v_fma_f32 v161, -v124, v157, v125
	v_fmac_f32_e32 v156, v160, v147
	v_mul_f32_e32 v159, v129, v155
	v_fma_f32 v162, -v126, v158, v127
	v_fmac_f32_e32 v157, v161, v148
	v_fma_f32 v122, -v122, v156, v123
	v_fma_f32 v163, -v128, v159, v129
	v_fmac_f32_e32 v158, v162, v149
	v_fma_f32 v123, -v124, v157, v125
	v_div_fmas_f32 v122, v122, v147, v156
	s_mov_b64 vcc, s[6:7]
	v_fmac_f32_e32 v159, v163, v155
	v_fma_f32 v124, -v126, v158, v127
	v_div_fixup_f32 v110, v122, v110, v120
	v_div_fmas_f32 v120, v123, v148, v157
	s_mov_b64 vcc, s[8:9]
	v_fma_f32 v125, -v128, v159, v129
	v_div_fixup_f32 v111, v120, v111, v118
	v_div_fmas_f32 v118, v124, v149, v158
	s_mov_b64 vcc, s[10:11]
	v_div_fixup_f32 v112, v118, v112, v121
	v_div_fmas_f32 v118, v125, v155, v159
	v_cvt_pk_bf16_f32 v110, v110, v111
	v_div_fixup_f32 v111, v118, v113, v119
	v_cvt_pk_bf16_f32 v111, v112, v111
	s_nop 0
	v_add_f32_e32 v118, 1.0, v106
	v_add_f32_e32 v119, 1.0, v107
	v_lshl_add_u64 v[106:107], s[36:37], 0, v[116:117]
	global_store_dwordx2 v[106:107], v[110:111], off
	s_nop 0
	s_waitcnt vmcnt(16)
; __device__ __forceinline__ unsigned cvt_pk_bf16(float lo, float hi) { unsigned r; asm volatile("v_cvt_pk_bf16_f32 %0, %1, %2" : "=v"(r) : "v"(lo), "v"(hi)); return r; }
; __device__ __forceinline__ float bflo(unsigned u) { return __uint_as_float(u << 16); }
; __device__ __forceinline__ float bfhi(unsigned u) { return __uint_as_float(u & 0xffff0000u); }
;     __device__ __forceinline__ void operator()(const f32x4 (&acc)[2][2][4][2], const Unit& u, int wr, int wc, int fr, int fq) const {
;         const int row0 = u.pm * BM + wr * 64 + fr, col0 = u.pn * BM + wc * 32 + 4 * fq;
; #pragma unroll
;         for (int ai = 0; ai < 2; ++ai)
; #pragma unroll
;             for (int m = 0; m < 4; ++m) { const size_t ro = (size_t)(row0 + ai * HALF + m * 16) * ldc + col0;
; #pragma unroll
;                 for (int bj = 0; bj < 2; ++bj)
; #pragma unroll
;                     for (int n = 0; n < 2; ++n) { const f32x4 a = acc[ai][bj][m][n]; const u32x2 yy = *(const u32x2*)(Y + ro + bj * HALF + n * 16);
;                         f32x4 v; v[0] = bflo(yy.x) / (1.0f + __expf(-a[0])); v[1] = bfhi(yy.x) / (1.0f + __expf(-a[1])); v[2] = bflo(yy.y) / (1.0f + __expf(-a[2])); v[3] = bfhi(yy.y) / (1.0f + __expf(-a[3]));
;                         u32x2 o; o.x = cvt_pk_bf16(v[0], v[1]); o.y = cvt_pk_bf16(v[2], v[3]); *(u32x2*)(C + ro + bj * HALF + n * 16) = o; } }
	v_lshlrev_b32_e32 v110, 16, v240
	v_and_b32_e32 v111, 0xffff0000, v240
	v_div_scale_f32 v116, s[6:7], v118, v118, v110
	v_lshlrev_b32_e32 v112, 16, v241
	v_div_scale_f32 v120, s[6:7], v119, v119, v111
	v_rcp_f32_e32 v126, v116
	v_and_b32_e32 v113, 0xffff0000, v241
	v_div_scale_f32 v122, s[8:9], v108, v108, v112
	v_rcp_f32_e32 v127, v120
	v_div_scale_f32 v124, s[10:11], v109, v109, v113
	v_rcp_f32_e32 v128, v122
	v_rcp_f32_e32 v129, v124
	v_fma_f32 v147, -v116, v126, 1.0
	v_div_scale_f32 v117, vcc, v110, v118, v110
	v_fma_f32 v148, -v120, v127, 1.0
	v_fmac_f32_e32 v126, v147, v126
	v_div_scale_f32 v121, s[6:7], v111, v119, v111
	v_fma_f32 v149, -v122, v128, 1.0
	v_fmac_f32_e32 v127, v148, v127
	v_mul_f32_e32 v147, v117, v126
	v_div_scale_f32 v123, s[8:9], v112, v108, v112
	v_fma_f32 v155, -v124, v129, 1.0
	v_fmac_f32_e32 v128, v149, v128
	v_mul_f32_e32 v148, v121, v127
	v_fma_f32 v156, -v116, v147, v117
	v_div_scale_f32 v125, s[10:11], v113, v109, v113
	v_fmac_f32_e32 v129, v155, v129
	v_mul_f32_e32 v149, v123, v128
	v_fma_f32 v157, -v120, v148, v121
	v_fmac_f32_e32 v147, v156, v126
	v_mul_f32_e32 v155, v125, v129
	v_fma_f32 v158, -v122, v149, v123
	v_fmac_f32_e32 v148, v157, v127
	v_fma_f32 v116, -v116, v147, v117
	v_fma_f32 v159, -v124, v155, v125
	v_fmac_f32_e32 v149, v158, v128
	v_fma_f32 v117, -v120, v148, v121
	v_div_fmas_f32 v116, v116, v126, v147
	s_mov_b64 vcc, s[6:7]
	v_fmac_f32_e32 v155, v159, v129
	v_fma_f32 v120, -v122, v149, v123
	v_div_fixup_f32 v110, v116, v118, v110
	v_div_fmas_f32 v116, v117, v127, v148
	s_mov_b64 vcc, s[8:9]
	v_fma_f32 v121, -v124, v155, v125
	v_div_fixup_f32 v111, v116, v119, v111
	v_div_fmas_f32 v116, v120, v128, v149
	s_mov_b64 vcc, s[10:11]
	v_div_fixup_f32 v112, v116, v108, v112
	v_div_fmas_f32 v116, v121, v129, v155
	v_div_fixup_f32 v109, v116, v109, v113
	v_cvt_pk_bf16_f32 v108, v110, v111
	v_cvt_pk_bf16_f32 v109, v112, v109
	s_nop 0
	s_nop 0
	global_store_dwordx2 v[106:107], v[108:109], off offset:32
	s_nop 0
	s_waitcnt vmcnt(16)
	v_lshlrev_b32_e32 v108, 16, v242
	v_and_b32_e32 v109, 0xffff0000, v242
	v_div_scale_f32 v112, s[6:7], v102, v102, v108
	v_lshlrev_b32_e32 v110, 16, v243
	v_div_scale_f32 v116, s[6:7], v103, v103, v109
	v_rcp_f32_e32 v122, v112
	v_and_b32_e32 v111, 0xffff0000, v243
	v_div_scale_f32 v118, s[8:9], v104, v104, v110
	v_rcp_f32_e32 v123, v116
	v_div_scale_f32 v120, s[10:11], v105, v105, v111
	v_rcp_f32_e32 v124, v118
	v_rcp_f32_e32 v125, v120
	v_fma_f32 v126, -v112, v122, 1.0
	v_div_scale_f32 v113, vcc, v108, v102, v108
	v_fma_f32 v127, -v116, v123, 1.0
	v_fmac_f32_e32 v122, v126, v122
	v_div_scale_f32 v117, s[6:7], v109, v103, v109
	v_fma_f32 v128, -v118, v124, 1.0
	v_fmac_f32_e32 v123, v127, v123
	v_mul_f32_e32 v126, v113, v122
	v_div_scale_f32 v119, s[8:9], v110, v104, v110
	v_fma_f32 v129, -v120, v125, 1.0
	v_fmac_f32_e32 v124, v128, v124
	v_mul_f32_e32 v127, v117, v123
	v_fma_f32 v147, -v112, v126, v113
	v_div_scale_f32 v121, s[10:11], v111, v105, v111
	v_fmac_f32_e32 v125, v129, v125
	v_mul_f32_e32 v128, v119, v124
	v_fma_f32 v148, -v116, v127, v117
	v_fmac_f32_e32 v126, v147, v122
	v_mul_f32_e32 v129, v121, v125
	v_fma_f32 v149, -v118, v128, v119
	v_fmac_f32_e32 v127, v148, v123
	v_fma_f32 v112, -v112, v126, v113
	v_fma_f32 v155, -v120, v129, v121
	v_fmac_f32_e32 v128, v149, v124
	v_fma_f32 v113, -v116, v127, v117
	v_div_fmas_f32 v112, v112, v122, v126
	s_mov_b64 vcc, s[6:7]
	v_fmac_f32_e32 v129, v155, v125
	v_fma_f32 v116, -v118, v128, v119
	v_div_fixup_f32 v102, v112, v102, v108
	v_div_fmas_f32 v108, v113, v123, v127
	s_mov_b64 vcc, s[8:9]
	v_fma_f32 v117, -v120, v129, v121
	v_div_fixup_f32 v103, v108, v103, v109
	v_div_fmas_f32 v108, v116, v124, v128
	s_mov_b64 vcc, s[10:11]
	v_div_fixup_f32 v104, v108, v104, v110
	v_div_fmas_f32 v108, v117, v125, v129
	v_cvt_pk_bf16_f32 v102, v102, v103
	v_div_fixup_f32 v103, v108, v105, v111
	v_cvt_pk_bf16_f32 v103, v104, v103
	s_nop 0
	v_exp_f32_e32 v108, v98
	v_exp_f32_e32 v109, v99
	global_store_dwordx2 v[106:107], v[102:103], off offset:256
	v_add_f32_e32 v110, 1.0, v100
	v_add_f32_e32 v108, 1.0, v108
	v_add_f32_e32 v109, 1.0, v109
	v_add_f32_e32 v111, 1.0, v101
	v_or_b32_e32 v98, 32, v146
	v_ashrrev_i32_e32 v99, 31, v98
	v_lshlrev_b64 v[98:99], 10, v[98:99]
	v_lshl_add_u64 v[98:99], v[98:99], 0, v[144:145]
	v_lshlrev_b64 v[100:101], 1, v[98:99]
	v_lshl_add_u64 v[98:99], s[24:25], 0, v[100:101]
	s_nop 0
	s_waitcnt vmcnt(16)
	v_lshlrev_b32_e32 v102, 16, v236
	v_and_b32_e32 v103, 0xffff0000, v236
	v_div_scale_f32 v112, s[6:7], v108, v108, v102
	v_lshlrev_b32_e32 v104, 16, v237
	v_div_scale_f32 v114, s[6:7], v109, v109, v103
	v_rcp_f32_e32 v120, v112
	v_and_b32_e32 v105, 0xffff0000, v237
	v_div_scale_f32 v116, s[8:9], v110, v110, v104
	v_rcp_f32_e32 v121, v114
	v_div_scale_f32 v118, s[10:11], v111, v111, v105
	v_rcp_f32_e32 v122, v116
	v_rcp_f32_e32 v123, v118
	v_fma_f32 v124, -v112, v120, 1.0
	v_div_scale_f32 v113, vcc, v102, v108, v102
	v_fma_f32 v125, -v114, v121, 1.0
	v_fmac_f32_e32 v120, v124, v120
	v_div_scale_f32 v115, s[6:7], v103, v109, v103
	v_fma_f32 v126, -v116, v122, 1.0
	v_fmac_f32_e32 v121, v125, v121
	v_mul_f32_e32 v124, v113, v120
	v_div_scale_f32 v117, s[8:9], v104, v110, v104
	v_fma_f32 v127, -v118, v123, 1.0
	v_fmac_f32_e32 v122, v126, v122
	v_mul_f32_e32 v125, v115, v121
	v_fma_f32 v128, -v112, v124, v113
	v_div_scale_f32 v119, s[10:11], v105, v111, v105
	v_fmac_f32_e32 v123, v127, v123
	v_mul_f32_e32 v126, v117, v122
	v_fma_f32 v129, -v114, v125, v115
	v_fmac_f32_e32 v124, v128, v120
	v_mul_f32_e32 v127, v119, v123
	v_fma_f32 v147, -v116, v126, v117
	v_fmac_f32_e32 v125, v129, v121
	v_fma_f32 v112, -v112, v124, v113
	v_fma_f32 v148, -v118, v127, v119
	v_fmac_f32_e32 v126, v147, v122
	v_fma_f32 v113, -v114, v125, v115
	v_div_fmas_f32 v112, v112, v120, v124
	s_mov_b64 vcc, s[6:7]
	v_fmac_f32_e32 v127, v148, v123
	v_fma_f32 v114, -v116, v126, v117
	v_div_fixup_f32 v102, v112, v108, v102
	v_div_fmas_f32 v108, v113, v121, v125
	s_mov_b64 vcc, s[8:9]
	v_fma_f32 v115, -v118, v127, v119
	v_div_fixup_f32 v103, v108, v109, v103
	v_div_fmas_f32 v108, v114, v122, v126
	s_mov_b64 vcc, s[10:11]
	v_div_fixup_f32 v104, v108, v110, v104
	v_div_fmas_f32 v108, v115, v123, v127
	v_cvt_pk_bf16_f32 v102, v102, v103
	v_div_fixup_f32 v103, v108, v111, v105
	v_cvt_pk_bf16_f32 v103, v104, v103
	global_store_dwordx2 v[106:107], v[102:103], off offset:288
	s_nop 0
	s_nop 0
	s_waitcnt vmcnt(16)
; __device__ __forceinline__ unsigned cvt_pk_bf16(float lo, float hi) { unsigned r; asm volatile("v_cvt_pk_bf16_f32 %0, %1, %2" : "=v"(r) : "v"(lo), "v"(hi)); return r; }
; __device__ __forceinline__ float bflo(unsigned u) { return __uint_as_float(u << 16); }
; __device__ __forceinline__ float bfhi(unsigned u) { return __uint_as_float(u & 0xffff0000u); }
;     __device__ __forceinline__ void operator()(const f32x4 (&acc)[2][2][4][2], const Unit& u, int wr, int wc, int fr, int fq) const {
;         const int row0 = u.pm * BM + wr * 64 + fr, col0 = u.pn * BM + wc * 32 + 4 * fq;
; #pragma unroll
;         for (int ai = 0; ai < 2; ++ai)
; #pragma unroll
;             for (int m = 0; m < 4; ++m) { const size_t ro = (size_t)(row0 + ai * HALF + m * 16) * ldc + col0;
; #pragma unroll
;                 for (int bj = 0; bj < 2; ++bj)
; #pragma unroll
;                     for (int n = 0; n < 2; ++n) { const f32x4 a = acc[ai][bj][m][n]; const u32x2 yy = *(const u32x2*)(Y + ro + bj * HALF + n * 16);
;                         f32x4 v; v[0] = bflo(yy.x) / (1.0f + __expf(-a[0])); v[1] = bfhi(yy.x) / (1.0f + __expf(-a[1])); v[2] = bflo(yy.y) / (1.0f + __expf(-a[2])); v[3] = bfhi(yy.y) / (1.0f + __expf(-a[3]));
;                         u32x2 o; o.x = cvt_pk_bf16(v[0], v[1]); o.y = cvt_pk_bf16(v[2], v[3]); *(u32x2*)(C + ro + bj * HALF + n * 16) = o; } }
	v_lshlrev_b32_e32 v104, 16, v238
	v_and_b32_e32 v102, 0xffff0000, v238
	v_div_scale_f32 v106, s[6:7], v94, v94, v104
	v_lshlrev_b32_e32 v105, 16, v239
	v_div_scale_f32 v108, s[6:7], v95, v95, v102
	v_rcp_f32_e32 v114, v106
	v_and_b32_e32 v103, 0xffff0000, v239
	v_div_scale_f32 v110, s[8:9], v96, v96, v105
	v_rcp_f32_e32 v115, v108
	v_div_scale_f32 v112, s[10:11], v97, v97, v103
	v_rcp_f32_e32 v116, v110
	v_rcp_f32_e32 v117, v112
	v_fma_f32 v118, -v106, v114, 1.0
	v_div_scale_f32 v107, vcc, v104, v94, v104
	v_fma_f32 v119, -v108, v115, 1.0
	v_fmac_f32_e32 v114, v118, v114
	v_div_scale_f32 v109, s[6:7], v102, v95, v102
	v_fma_f32 v120, -v110, v116, 1.0
	v_fmac_f32_e32 v115, v119, v115
	v_mul_f32_e32 v118, v107, v114
	v_div_scale_f32 v111, s[8:9], v105, v96, v105
	v_fma_f32 v121, -v112, v117, 1.0
	v_fmac_f32_e32 v116, v120, v116
	v_mul_f32_e32 v119, v109, v115
	v_fma_f32 v122, -v106, v118, v107
	v_div_scale_f32 v113, s[10:11], v103, v97, v103
	v_fmac_f32_e32 v117, v121, v117
	v_mul_f32_e32 v120, v111, v116
	v_fma_f32 v123, -v108, v119, v109
	v_fmac_f32_e32 v118, v122, v114
	v_mul_f32_e32 v121, v113, v117
	v_fma_f32 v124, -v110, v120, v111
	v_fmac_f32_e32 v119, v123, v115
	v_fma_f32 v106, -v106, v118, v107
	v_fma_f32 v125, -v112, v121, v113
	v_fmac_f32_e32 v120, v124, v116
	v_fma_f32 v107, -v108, v119, v109
	v_div_fmas_f32 v106, v106, v114, v118
	s_mov_b64 vcc, s[6:7]
	v_fmac_f32_e32 v121, v125, v117
	v_fma_f32 v108, -v110, v120, v111
	v_div_fixup_f32 v94, v106, v94, v104
	v_div_fmas_f32 v104, v107, v115, v119
	s_mov_b64 vcc, s[8:9]
	v_fma_f32 v109, -v112, v121, v113
	v_div_fixup_f32 v95, v104, v95, v102
	v_div_fmas_f32 v102, v108, v116, v120
	s_mov_b64 vcc, s[10:11]
	v_div_fixup_f32 v96, v102, v96, v105
	v_div_fmas_f32 v102, v109, v117, v121
	v_cvt_pk_bf16_f32 v94, v94, v95
	v_div_fixup_f32 v95, v102, v97, v103
	v_cvt_pk_bf16_f32 v95, v96, v95
	v_lshl_add_u64 v[252:253], v[142:143], 0, s[28:29]
	v_lshl_add_u64 v[254:255], s[24:25], 0, v[252:253]
	global_load_dwordx2 v[248:249], v[254:255], off offset:32
	global_load_dwordx2 v[250:251], v[254:255], off offset:256
	global_load_dwordx2 v[244:245], v[254:255], off offset:288
	v_lshl_add_u64 v[178:179], v[142:143], 0, s[42:43]
	v_lshl_add_u64 v[230:231], s[24:25], 0, v[178:179]
	global_load_dwordx2 v[246:247], v[230:231], off
	global_load_dwordx2 v[240:241], v[230:231], off offset:32
	global_load_dwordx2 v[242:243], v[230:231], off offset:256
	global_load_dwordx2 v[236:237], v[230:231], off offset:288
	v_lshl_add_u64 v[252:253], v[142:143], 0, s[46:47]
	v_lshl_add_u64 v[254:255], s[24:25], 0, v[252:253]
	global_load_dwordx2 v[238:239], v[254:255], off
	s_nop 0
	v_add_f32_e32 v102, 1.0, v90
	v_add_f32_e32 v103, 1.0, v91
	v_lshl_add_u64 v[90:91], s[36:37], 0, v[100:101]
	global_store_dwordx2 v[90:91], v[94:95], off
	s_nop 0
	s_waitcnt vmcnt(24)
	v_lshlrev_b32_e32 v94, 16, v232
	v_and_b32_e32 v95, 0xffff0000, v232
	v_div_scale_f32 v100, s[6:7], v102, v102, v94
	v_lshlrev_b32_e32 v96, 16, v233
	v_div_scale_f32 v104, s[6:7], v103, v103, v95
	v_rcp_f32_e32 v110, v100
	v_and_b32_e32 v97, 0xffff0000, v233
	v_div_scale_f32 v106, s[8:9], v92, v92, v96
	v_rcp_f32_e32 v111, v104
	v_div_scale_f32 v108, s[10:11], v93, v93, v97
	v_rcp_f32_e32 v112, v106
	v_rcp_f32_e32 v113, v108
	v_fma_f32 v114, -v100, v110, 1.0
	v_div_scale_f32 v101, vcc, v94, v102, v94
	v_fma_f32 v115, -v104, v111, 1.0
	v_fmac_f32_e32 v110, v114, v110
	v_div_scale_f32 v105, s[6:7], v95, v103, v95
	v_fma_f32 v116, -v106, v112, 1.0
	v_fmac_f32_e32 v111, v115, v111
	v_mul_f32_e32 v114, v101, v110
	v_div_scale_f32 v107, s[8:9], v96, v92, v96
	v_fma_f32 v117, -v108, v113, 1.0
	v_fmac_f32_e32 v112, v116, v112
	v_mul_f32_e32 v115, v105, v111
	v_fma_f32 v118, -v100, v114, v101
	v_div_scale_f32 v109, s[10:11], v97, v93, v97
	v_fmac_f32_e32 v113, v117, v113
	v_mul_f32_e32 v116, v107, v112
	v_fma_f32 v119, -v104, v115, v105
	v_fmac_f32_e32 v114, v118, v110
	v_mul_f32_e32 v117, v109, v113
	v_fma_f32 v120, -v106, v116, v107
	v_fmac_f32_e32 v115, v119, v111
	v_fma_f32 v100, -v100, v114, v101
	v_fma_f32 v121, -v108, v117, v109
	v_fmac_f32_e32 v116, v120, v112
	v_fma_f32 v101, -v104, v115, v105
	v_div_fmas_f32 v100, v100, v110, v114
	s_mov_b64 vcc, s[6:7]
	v_fmac_f32_e32 v117, v121, v113
	v_fma_f32 v104, -v106, v116, v107
	v_div_fixup_f32 v94, v100, v102, v94
	v_div_fmas_f32 v100, v101, v111, v115
	s_mov_b64 vcc, s[8:9]
	v_fma_f32 v105, -v108, v117, v109
	v_div_fixup_f32 v95, v100, v103, v95
	v_div_fmas_f32 v100, v104, v112, v116
	s_mov_b64 vcc, s[10:11]
	v_div_fixup_f32 v96, v100, v92, v96
	v_div_fmas_f32 v100, v105, v113, v117
	v_div_fixup_f32 v93, v100, v93, v97
	v_cvt_pk_bf16_f32 v92, v94, v95
	v_cvt_pk_bf16_f32 v93, v96, v93
	s_nop 0
	s_nop 0
	global_store_dwordx2 v[90:91], v[92:93], off offset:32
	s_nop 0
	s_waitcnt vmcnt(24)
; __device__ __forceinline__ unsigned cvt_pk_bf16(float lo, float hi) { unsigned r; asm volatile("v_cvt_pk_bf16_f32 %0, %1, %2" : "=v"(r) : "v"(lo), "v"(hi)); return r; }
; __device__ __forceinline__ float bflo(unsigned u) { return __uint_as_float(u << 16); }
; __device__ __forceinline__ float bfhi(unsigned u) { return __uint_as_float(u & 0xffff0000u); }
;     __device__ __forceinline__ void operator()(const f32x4 (&acc)[2][2][4][2], const Unit& u, int wr, int wc, int fr, int fq) const {
;         const int row0 = u.pm * BM + wr * 64 + fr, col0 = u.pn * BM + wc * 32 + 4 * fq;
; #pragma unroll
;         for (int ai = 0; ai < 2; ++ai)
; #pragma unroll
;             for (int m = 0; m < 4; ++m) { const size_t ro = (size_t)(row0 + ai * HALF + m * 16) * ldc + col0;
; #pragma unroll
;                 for (int bj = 0; bj < 2; ++bj)
; #pragma unroll
;                     for (int n = 0; n < 2; ++n) { const f32x4 a = acc[ai][bj][m][n]; const u32x2 yy = *(const u32x2*)(Y + ro + bj * HALF + n * 16);
;                         f32x4 v; v[0] = bflo(yy.x) / (1.0f + __expf(-a[0])); v[1] = bfhi(yy.x) / (1.0f + __expf(-a[1])); v[2] = bflo(yy.y) / (1.0f + __expf(-a[2])); v[3] = bfhi(yy.y) / (1.0f + __expf(-a[3]));
;                         u32x2 o; o.x = cvt_pk_bf16(v[0], v[1]); o.y = cvt_pk_bf16(v[2], v[3]); *(u32x2*)(C + ro + bj * HALF + n * 16) = o; } }
	v_lshlrev_b32_e32 v92, 16, v234
	v_and_b32_e32 v93, 0xffff0000, v234
	v_div_scale_f32 v96, s[6:7], v86, v86, v92
	v_lshlrev_b32_e32 v94, 16, v235
	v_div_scale_f32 v100, s[6:7], v87, v87, v93
	v_rcp_f32_e32 v106, v96
	v_and_b32_e32 v95, 0xffff0000, v235
	v_div_scale_f32 v102, s[8:9], v88, v88, v94
	v_rcp_f32_e32 v107, v100
	v_div_scale_f32 v104, s[10:11], v89, v89, v95
	v_rcp_f32_e32 v108, v102
	v_rcp_f32_e32 v109, v104
	v_fma_f32 v110, -v96, v106, 1.0
	v_div_scale_f32 v97, vcc, v92, v86, v92
	v_fma_f32 v111, -v100, v107, 1.0
	v_fmac_f32_e32 v106, v110, v106
	v_div_scale_f32 v101, s[6:7], v93, v87, v93
	v_fma_f32 v112, -v102, v108, 1.0
	v_fmac_f32_e32 v107, v111, v107
	v_mul_f32_e32 v110, v97, v106
	v_div_scale_f32 v103, s[8:9], v94, v88, v94
	v_fma_f32 v113, -v104, v109, 1.0
	v_fmac_f32_e32 v108, v112, v108
	v_mul_f32_e32 v111, v101, v107
	v_fma_f32 v114, -v96, v110, v97
	v_div_scale_f32 v105, s[10:11], v95, v89, v95
	v_fmac_f32_e32 v109, v113, v109
	v_mul_f32_e32 v112, v103, v108
	v_fma_f32 v115, -v100, v111, v101
	v_fmac_f32_e32 v110, v114, v106
	v_mul_f32_e32 v113, v105, v109
	v_fma_f32 v116, -v102, v112, v103
	v_fmac_f32_e32 v111, v115, v107
	v_fma_f32 v96, -v96, v110, v97
	v_fma_f32 v117, -v104, v113, v105
	v_fmac_f32_e32 v112, v116, v108
	v_fma_f32 v97, -v100, v111, v101
	v_div_fmas_f32 v96, v96, v106, v110
	s_mov_b64 vcc, s[6:7]
	v_fmac_f32_e32 v113, v117, v109
	v_fma_f32 v100, -v102, v112, v103
	v_div_fixup_f32 v86, v96, v86, v92
	v_div_fmas_f32 v92, v97, v107, v111
	s_mov_b64 vcc, s[8:9]
	v_fma_f32 v101, -v104, v113, v105
	v_div_fixup_f32 v87, v92, v87, v93
	v_div_fmas_f32 v92, v100, v108, v112
	s_mov_b64 vcc, s[10:11]
	v_div_fixup_f32 v88, v92, v88, v94
	v_div_fmas_f32 v92, v101, v109, v113
	v_cvt_pk_bf16_f32 v86, v86, v87
	v_div_fixup_f32 v87, v92, v89, v95
	v_cvt_pk_bf16_f32 v87, v88, v87
	s_nop 0
	v_exp_f32_e32 v92, v82
	v_exp_f32_e32 v93, v83
	global_store_dwordx2 v[90:91], v[86:87], off offset:256
	v_add_f32_e32 v94, 1.0, v84
	v_add_f32_e32 v92, 1.0, v92
	v_add_f32_e32 v93, 1.0, v93
	v_add_f32_e32 v95, 1.0, v85
	v_or_b32_e32 v82, 48, v146
	v_ashrrev_i32_e32 v83, 31, v82
	v_lshlrev_b64 v[82:83], 10, v[82:83]
	v_lshl_add_u64 v[82:83], v[82:83], 0, v[144:145]
	v_lshlrev_b64 v[84:85], 1, v[82:83]
	v_lshl_add_u64 v[82:83], s[24:25], 0, v[84:85]
	s_nop 0
	s_waitcnt vmcnt(24)
	v_lshlrev_b32_e32 v86, 16, v224
	v_and_b32_e32 v87, 0xffff0000, v224
	v_div_scale_f32 v96, s[6:7], v92, v92, v86
	v_lshlrev_b32_e32 v88, 16, v225
	v_div_scale_f32 v98, s[6:7], v93, v93, v87
	v_rcp_f32_e32 v104, v96
	v_and_b32_e32 v89, 0xffff0000, v225
	v_div_scale_f32 v100, s[8:9], v94, v94, v88
	v_rcp_f32_e32 v105, v98
	v_div_scale_f32 v102, s[10:11], v95, v95, v89
	v_rcp_f32_e32 v106, v100
	v_rcp_f32_e32 v107, v102
	v_fma_f32 v108, -v96, v104, 1.0
	v_div_scale_f32 v97, vcc, v86, v92, v86
	v_fma_f32 v109, -v98, v105, 1.0
	v_fmac_f32_e32 v104, v108, v104
	v_div_scale_f32 v99, s[6:7], v87, v93, v87
	v_fma_f32 v110, -v100, v106, 1.0
	v_fmac_f32_e32 v105, v109, v105
	v_mul_f32_e32 v108, v97, v104
	v_div_scale_f32 v101, s[8:9], v88, v94, v88
	v_fma_f32 v111, -v102, v107, 1.0
	v_fmac_f32_e32 v106, v110, v106
	v_mul_f32_e32 v109, v99, v105
	v_fma_f32 v112, -v96, v108, v97
	v_div_scale_f32 v103, s[10:11], v89, v95, v89
	v_fmac_f32_e32 v107, v111, v107
	v_mul_f32_e32 v110, v101, v106
	v_fma_f32 v113, -v98, v109, v99
	v_fmac_f32_e32 v108, v112, v104
	v_mul_f32_e32 v111, v103, v107
	v_fma_f32 v114, -v100, v110, v101
	v_fmac_f32_e32 v109, v113, v105
	v_fma_f32 v96, -v96, v108, v97
	v_fma_f32 v115, -v102, v111, v103
	v_fmac_f32_e32 v110, v114, v106
	v_fma_f32 v97, -v98, v109, v99
	v_div_fmas_f32 v96, v96, v104, v108
	s_mov_b64 vcc, s[6:7]
	v_fmac_f32_e32 v111, v115, v107
	v_fma_f32 v98, -v100, v110, v101
	v_div_fixup_f32 v86, v96, v92, v86
	v_div_fmas_f32 v92, v97, v105, v109
	s_mov_b64 vcc, s[8:9]
	v_fma_f32 v99, -v102, v111, v103
	v_div_fixup_f32 v87, v92, v93, v87
	v_div_fmas_f32 v92, v98, v106, v110
	s_mov_b64 vcc, s[10:11]
	v_div_fixup_f32 v88, v92, v94, v88
	v_div_fmas_f32 v92, v99, v107, v111
	v_cvt_pk_bf16_f32 v86, v86, v87
	v_div_fixup_f32 v87, v92, v95, v89
	v_cvt_pk_bf16_f32 v87, v88, v87
	global_store_dwordx2 v[90:91], v[86:87], off offset:288
	s_nop 0
	s_nop 0
	s_waitcnt vmcnt(24)
	v_lshlrev_b32_e32 v88, 16, v226
	v_and_b32_e32 v86, 0xffff0000, v226
	v_div_scale_f32 v90, s[6:7], v78, v78, v88
	v_lshlrev_b32_e32 v89, 16, v227
	v_div_scale_f32 v92, s[6:7], v79, v79, v86
	v_rcp_f32_e32 v98, v90
	v_and_b32_e32 v87, 0xffff0000, v227
	v_div_scale_f32 v94, s[8:9], v80, v80, v89
	v_rcp_f32_e32 v99, v92
	v_div_scale_f32 v96, s[10:11], v81, v81, v87
	v_rcp_f32_e32 v100, v94
	v_rcp_f32_e32 v101, v96
	v_fma_f32 v102, -v90, v98, 1.0
	v_div_scale_f32 v91, vcc, v88, v78, v88
	v_fma_f32 v103, -v92, v99, 1.0
	v_fmac_f32_e32 v98, v102, v98
	v_div_scale_f32 v93, s[6:7], v86, v79, v86
	v_fma_f32 v104, -v94, v100, 1.0
	v_fmac_f32_e32 v99, v103, v99
	v_mul_f32_e32 v102, v91, v98
	v_div_scale_f32 v95, s[8:9], v89, v80, v89
	v_fma_f32 v105, -v96, v101, 1.0
	v_fmac_f32_e32 v100, v104, v100
	v_mul_f32_e32 v103, v93, v99
	v_fma_f32 v106, -v90, v102, v91
	v_div_scale_f32 v97, s[10:11], v87, v81, v87
	v_fmac_f32_e32 v101, v105, v101
	v_mul_f32_e32 v104, v95, v100
	v_fma_f32 v107, -v92, v103, v93
	v_fmac_f32_e32 v102, v106, v98
	v_mul_f32_e32 v105, v97, v101
	v_fma_f32 v108, -v94, v104, v95
	v_fmac_f32_e32 v103, v107, v99
	v_fma_f32 v90, -v90, v102, v91
	v_fma_f32 v109, -v96, v105, v97
	v_fmac_f32_e32 v104, v108, v100
	v_fma_f32 v91, -v92, v103, v93
	v_div_fmas_f32 v90, v90, v98, v102
	s_mov_b64 vcc, s[6:7]
	v_fmac_f32_e32 v105, v109, v101
	v_fma_f32 v92, -v94, v104, v95
	v_div_fixup_f32 v78, v90, v78, v88
	v_div_fmas_f32 v88, v91, v99, v103
	s_mov_b64 vcc, s[8:9]
	v_fma_f32 v93, -v96, v105, v97
	v_div_fixup_f32 v79, v88, v79, v86
	v_div_fmas_f32 v86, v92, v100, v104
	s_mov_b64 vcc, s[10:11]
	v_div_fixup_f32 v80, v86, v80, v89
	v_div_fmas_f32 v86, v93, v101, v105
	v_cvt_pk_bf16_f32 v78, v78, v79
	v_div_fixup_f32 v79, v86, v81, v87
	v_cvt_pk_bf16_f32 v79, v80, v79
	s_nop 0
	v_add_f32_e32 v86, 1.0, v74
	v_add_f32_e32 v87, 1.0, v75
	v_lshl_add_u64 v[74:75], s[36:37], 0, v[84:85]
	global_store_dwordx2 v[74:75], v[78:79], off
	s_nop 0
	s_waitcnt vmcnt(24)
; __device__ __forceinline__ unsigned cvt_pk_bf16(float lo, float hi) { unsigned r; asm volatile("v_cvt_pk_bf16_f32 %0, %1, %2" : "=v"(r) : "v"(lo), "v"(hi)); return r; }
; __device__ __forceinline__ float bflo(unsigned u) { return __uint_as_float(u << 16); }
; __device__ __forceinline__ float bfhi(unsigned u) { return __uint_as_float(u & 0xffff0000u); }
;     __device__ __forceinline__ void operator()(const f32x4 (&acc)[2][2][4][2], const Unit& u, int wr, int wc, int fr, int fq) const {
;         const int row0 = u.pm * BM + wr * 64 + fr, col0 = u.pn * BM + wc * 32 + 4 * fq;
; #pragma unroll
;         for (int ai = 0; ai < 2; ++ai)
; #pragma unroll
;             for (int m = 0; m < 4; ++m) { const size_t ro = (size_t)(row0 + ai * HALF + m * 16) * ldc + col0;
; #pragma unroll
;                 for (int bj = 0; bj < 2; ++bj)
; #pragma unroll
;                     for (int n = 0; n < 2; ++n) { const f32x4 a = acc[ai][bj][m][n]; const u32x2 yy = *(const u32x2*)(Y + ro + bj * HALF + n * 16);
;                         f32x4 v; v[0] = bflo(yy.x) / (1.0f + __expf(-a[0])); v[1] = bfhi(yy.x) / (1.0f + __expf(-a[1])); v[2] = bflo(yy.y) / (1.0f + __expf(-a[2])); v[3] = bfhi(yy.y) / (1.0f + __expf(-a[3]));
;                         u32x2 o; o.x = cvt_pk_bf16(v[0], v[1]); o.y = cvt_pk_bf16(v[2], v[3]); *(u32x2*)(C + ro + bj * HALF + n * 16) = o; } }
	v_lshlrev_b32_e32 v78, 16, v220
	v_and_b32_e32 v79, 0xffff0000, v220
	v_div_scale_f32 v84, s[6:7], v86, v86, v78
	v_lshlrev_b32_e32 v80, 16, v221
	v_div_scale_f32 v88, s[6:7], v87, v87, v79
	v_rcp_f32_e32 v94, v84
	v_and_b32_e32 v81, 0xffff0000, v221
	v_div_scale_f32 v90, s[8:9], v76, v76, v80
	v_rcp_f32_e32 v95, v88
	v_div_scale_f32 v92, s[10:11], v77, v77, v81
	v_rcp_f32_e32 v96, v90
	v_rcp_f32_e32 v97, v92
	v_fma_f32 v98, -v84, v94, 1.0
	v_div_scale_f32 v85, vcc, v78, v86, v78
	v_fma_f32 v99, -v88, v95, 1.0
	v_fmac_f32_e32 v94, v98, v94
	v_div_scale_f32 v89, s[6:7], v79, v87, v79
	v_fma_f32 v100, -v90, v96, 1.0
	v_fmac_f32_e32 v95, v99, v95
	v_mul_f32_e32 v98, v85, v94
	v_div_scale_f32 v91, s[8:9], v80, v76, v80
	v_fma_f32 v101, -v92, v97, 1.0
	v_fmac_f32_e32 v96, v100, v96
	v_mul_f32_e32 v99, v89, v95
	v_fma_f32 v102, -v84, v98, v85
	v_div_scale_f32 v93, s[10:11], v81, v77, v81
	v_fmac_f32_e32 v97, v101, v97
	v_mul_f32_e32 v100, v91, v96
	v_fma_f32 v103, -v88, v99, v89
	v_fmac_f32_e32 v98, v102, v94
	v_mul_f32_e32 v101, v93, v97
	v_fma_f32 v104, -v90, v100, v91
	v_fmac_f32_e32 v99, v103, v95
	v_fma_f32 v84, -v84, v98, v85
	v_fma_f32 v105, -v92, v101, v93
	v_fmac_f32_e32 v100, v104, v96
	v_fma_f32 v85, -v88, v99, v89
	v_div_fmas_f32 v84, v84, v94, v98
	s_mov_b64 vcc, s[6:7]
	v_fmac_f32_e32 v101, v105, v97
	v_fma_f32 v88, -v90, v100, v91
	v_div_fixup_f32 v78, v84, v86, v78
	v_div_fmas_f32 v84, v85, v95, v99
	s_mov_b64 vcc, s[8:9]
	v_fma_f32 v89, -v92, v101, v93
	v_div_fixup_f32 v79, v84, v87, v79
	v_div_fmas_f32 v84, v88, v96, v100
	s_mov_b64 vcc, s[10:11]
	v_div_fixup_f32 v80, v84, v76, v80
	v_div_fmas_f32 v84, v89, v97, v101
	v_div_fixup_f32 v77, v84, v77, v81
	v_cvt_pk_bf16_f32 v76, v78, v79
	v_cvt_pk_bf16_f32 v77, v80, v77
	s_nop 0
	s_nop 0
	global_store_dwordx2 v[74:75], v[76:77], off offset:32
	s_nop 0
	s_waitcnt vmcnt(24)
	v_lshlrev_b32_e32 v76, 16, v222
	v_and_b32_e32 v77, 0xffff0000, v222
	v_div_scale_f32 v80, s[6:7], v70, v70, v76
	v_lshlrev_b32_e32 v78, 16, v223
	v_div_scale_f32 v84, s[6:7], v71, v71, v77
	v_rcp_f32_e32 v90, v80
	v_and_b32_e32 v79, 0xffff0000, v223
	v_div_scale_f32 v86, s[8:9], v72, v72, v78
	v_rcp_f32_e32 v91, v84
	v_div_scale_f32 v88, s[10:11], v73, v73, v79
	v_rcp_f32_e32 v92, v86
	v_rcp_f32_e32 v93, v88
	v_fma_f32 v94, -v80, v90, 1.0
	v_div_scale_f32 v81, vcc, v76, v70, v76
	v_fma_f32 v95, -v84, v91, 1.0
	v_fmac_f32_e32 v90, v94, v90
	v_div_scale_f32 v85, s[6:7], v77, v71, v77
	v_fma_f32 v96, -v86, v92, 1.0
	v_fmac_f32_e32 v91, v95, v91
	v_mul_f32_e32 v94, v81, v90
	v_div_scale_f32 v87, s[8:9], v78, v72, v78
	v_fma_f32 v97, -v88, v93, 1.0
	v_fmac_f32_e32 v92, v96, v92
	v_mul_f32_e32 v95, v85, v91
	v_fma_f32 v98, -v80, v94, v81
	v_div_scale_f32 v89, s[10:11], v79, v73, v79
	v_fmac_f32_e32 v93, v97, v93
	v_mul_f32_e32 v96, v87, v92
	v_fma_f32 v99, -v84, v95, v85
	v_fmac_f32_e32 v94, v98, v90
	v_mul_f32_e32 v97, v89, v93
	v_fma_f32 v100, -v86, v96, v87
	v_fmac_f32_e32 v95, v99, v91
	v_fma_f32 v80, -v80, v94, v81
	v_fma_f32 v101, -v88, v97, v89
	v_fmac_f32_e32 v96, v100, v92
	v_fma_f32 v81, -v84, v95, v85
	v_div_fmas_f32 v80, v80, v90, v94
	s_mov_b64 vcc, s[6:7]
	v_fmac_f32_e32 v97, v101, v93
	v_fma_f32 v84, -v86, v96, v87
	v_div_fixup_f32 v70, v80, v70, v76
	v_div_fmas_f32 v76, v81, v91, v95
	s_mov_b64 vcc, s[8:9]
	v_fma_f32 v85, -v88, v97, v89
	v_div_fixup_f32 v71, v76, v71, v77
	v_div_fmas_f32 v76, v84, v92, v96
	s_mov_b64 vcc, s[10:11]
	v_div_fixup_f32 v72, v76, v72, v78
	v_div_fmas_f32 v76, v85, v93, v97
	v_cvt_pk_bf16_f32 v70, v70, v71
	v_div_fixup_f32 v71, v76, v73, v79
	v_cvt_pk_bf16_f32 v71, v72, v71
	s_nop 0
	v_add_f32_e32 v76, 1.0, v66
	global_store_dwordx2 v[74:75], v[70:71], off offset:256
	v_add_f32_e32 v77, 1.0, v67
	v_add_f32_e32 v78, 1.0, v68
	v_add_f32_e32 v79, 1.0, v69
	v_lshl_add_u64 v[68:69], v[142:143], 0, s[28:29]
	v_lshl_add_u64 v[66:67], s[24:25], 0, v[68:69]
	s_nop 0
	s_waitcnt vmcnt(24)
	v_lshlrev_b32_e32 v70, 16, v216
	v_and_b32_e32 v71, 0xffff0000, v216
	v_div_scale_f32 v80, s[6:7], v76, v76, v70
	v_lshlrev_b32_e32 v72, 16, v217
	v_div_scale_f32 v82, s[6:7], v77, v77, v71
	v_rcp_f32_e32 v88, v80
	v_and_b32_e32 v73, 0xffff0000, v217
	v_div_scale_f32 v84, s[8:9], v78, v78, v72
	v_rcp_f32_e32 v89, v82
	v_div_scale_f32 v86, s[10:11], v79, v79, v73
	v_rcp_f32_e32 v90, v84
	v_rcp_f32_e32 v91, v86
	v_fma_f32 v92, -v80, v88, 1.0
	v_div_scale_f32 v81, vcc, v70, v76, v70
	v_fma_f32 v93, -v82, v89, 1.0
	v_fmac_f32_e32 v88, v92, v88
	v_div_scale_f32 v83, s[6:7], v71, v77, v71
	v_fma_f32 v94, -v84, v90, 1.0
	v_fmac_f32_e32 v89, v93, v89
	v_mul_f32_e32 v92, v81, v88
	v_div_scale_f32 v85, s[8:9], v72, v78, v72
	v_fma_f32 v95, -v86, v91, 1.0
	v_fmac_f32_e32 v90, v94, v90
	v_mul_f32_e32 v93, v83, v89
	v_fma_f32 v96, -v80, v92, v81
	v_div_scale_f32 v87, s[10:11], v73, v79, v73
	v_fmac_f32_e32 v91, v95, v91
	v_mul_f32_e32 v94, v85, v90
	v_fma_f32 v97, -v82, v93, v83
	v_fmac_f32_e32 v92, v96, v88
	v_mul_f32_e32 v95, v87, v91
	v_fma_f32 v98, -v84, v94, v85
	v_fmac_f32_e32 v93, v97, v89
	v_fma_f32 v80, -v80, v92, v81
	v_fma_f32 v99, -v86, v95, v87
	v_fmac_f32_e32 v94, v98, v90
	v_fma_f32 v81, -v82, v93, v83
	v_div_fmas_f32 v80, v80, v88, v92
	s_mov_b64 vcc, s[6:7]
	v_fmac_f32_e32 v95, v99, v91
	v_fma_f32 v82, -v84, v94, v85
	v_div_fixup_f32 v70, v80, v76, v70
	v_div_fmas_f32 v76, v81, v89, v93
	s_mov_b64 vcc, s[8:9]
	v_fma_f32 v83, -v86, v95, v87
	v_div_fixup_f32 v71, v76, v77, v71
	v_div_fmas_f32 v76, v82, v90, v94
	s_mov_b64 vcc, s[10:11]
	v_div_fixup_f32 v72, v76, v78, v72
	v_div_fmas_f32 v76, v83, v91, v95
	v_cvt_pk_bf16_f32 v70, v70, v71
	v_div_fixup_f32 v71, v76, v79, v73
	v_cvt_pk_bf16_f32 v71, v72, v71
	global_store_dwordx2 v[74:75], v[70:71], off offset:288
	s_nop 0
	s_nop 0
	s_waitcnt vmcnt(24)
; __device__ __forceinline__ unsigned cvt_pk_bf16(float lo, float hi) { unsigned r; asm volatile("v_cvt_pk_bf16_f32 %0, %1, %2" : "=v"(r) : "v"(lo), "v"(hi)); return r; }
; __device__ __forceinline__ float bflo(unsigned u) { return __uint_as_float(u << 16); }
; __device__ __forceinline__ float bfhi(unsigned u) { return __uint_as_float(u & 0xffff0000u); }
;     __device__ __forceinline__ void operator()(const f32x4 (&acc)[2][2][4][2], const Unit& u, int wr, int wc, int fr, int fq) const {
;         const int row0 = u.pm * BM + wr * 64 + fr, col0 = u.pn * BM + wc * 32 + 4 * fq;
; #pragma unroll
;         for (int ai = 0; ai < 2; ++ai)
; #pragma unroll
;             for (int m = 0; m < 4; ++m) { const size_t ro = (size_t)(row0 + ai * HALF + m * 16) * ldc + col0;
; #pragma unroll
;                 for (int bj = 0; bj < 2; ++bj)
; #pragma unroll
;                     for (int n = 0; n < 2; ++n) { const f32x4 a = acc[ai][bj][m][n]; const u32x2 yy = *(const u32x2*)(Y + ro + bj * HALF + n * 16);
;                         f32x4 v; v[0] = bflo(yy.x) / (1.0f + __expf(-a[0])); v[1] = bfhi(yy.x) / (1.0f + __expf(-a[1])); v[2] = bflo(yy.y) / (1.0f + __expf(-a[2])); v[3] = bfhi(yy.y) / (1.0f + __expf(-a[3]));
;                         u32x2 o; o.x = cvt_pk_bf16(v[0], v[1]); o.y = cvt_pk_bf16(v[2], v[3]); *(u32x2*)(C + ro + bj * HALF + n * 16) = o; } }
	v_lshlrev_b32_e32 v72, 16, v218
	v_and_b32_e32 v70, 0xffff0000, v218
	v_div_scale_f32 v74, s[6:7], v62, v62, v72
	v_lshlrev_b32_e32 v73, 16, v219
	v_div_scale_f32 v76, s[6:7], v63, v63, v70
	v_rcp_f32_e32 v82, v74
	v_and_b32_e32 v71, 0xffff0000, v219
	v_div_scale_f32 v78, s[8:9], v64, v64, v73
	v_rcp_f32_e32 v83, v76
	v_div_scale_f32 v80, s[10:11], v65, v65, v71
	v_rcp_f32_e32 v84, v78
	v_rcp_f32_e32 v85, v80
	v_fma_f32 v86, -v74, v82, 1.0
	v_div_scale_f32 v75, vcc, v72, v62, v72
	v_fma_f32 v87, -v76, v83, 1.0
	v_fmac_f32_e32 v82, v86, v82
	v_div_scale_f32 v77, s[6:7], v70, v63, v70
	v_fma_f32 v88, -v78, v84, 1.0
	v_fmac_f32_e32 v83, v87, v83
	v_mul_f32_e32 v86, v75, v82
	v_div_scale_f32 v79, s[8:9], v73, v64, v73
	v_fma_f32 v89, -v80, v85, 1.0
	v_fmac_f32_e32 v84, v88, v84
	v_mul_f32_e32 v87, v77, v83
	v_fma_f32 v90, -v74, v86, v75
	v_div_scale_f32 v81, s[10:11], v71, v65, v71
	v_fmac_f32_e32 v85, v89, v85
	v_mul_f32_e32 v88, v79, v84
	v_fma_f32 v91, -v76, v87, v77
	v_fmac_f32_e32 v86, v90, v82
	v_mul_f32_e32 v89, v81, v85
	v_fma_f32 v92, -v78, v88, v79
	v_fmac_f32_e32 v87, v91, v83
	v_fma_f32 v74, -v74, v86, v75
	v_fma_f32 v93, -v80, v89, v81
	v_fmac_f32_e32 v88, v92, v84
	v_fma_f32 v75, -v76, v87, v77
	v_div_fmas_f32 v74, v74, v82, v86
	s_mov_b64 vcc, s[6:7]
	v_fmac_f32_e32 v89, v93, v85
	v_fma_f32 v76, -v78, v88, v79
	v_div_fixup_f32 v62, v74, v62, v72
	v_div_fmas_f32 v72, v75, v83, v87
	s_mov_b64 vcc, s[8:9]
	v_fma_f32 v77, -v80, v89, v81
	v_div_fixup_f32 v63, v72, v63, v70
	v_div_fmas_f32 v70, v76, v84, v88
	s_mov_b64 vcc, s[10:11]
	v_div_fixup_f32 v64, v70, v64, v73
	v_div_fmas_f32 v70, v77, v85, v89
	v_cvt_pk_bf16_f32 v62, v62, v63
	v_div_fixup_f32 v63, v70, v65, v71
	v_cvt_pk_bf16_f32 v63, v64, v63
	v_lshl_add_u64 v[178:179], v[142:143], 0, s[46:47]
	v_lshl_add_u64 v[230:231], s[24:25], 0, v[178:179]
	global_load_dwordx2 v[232:233], v[230:231], off offset:32
	global_load_dwordx2 v[234:235], v[230:231], off offset:256
	global_load_dwordx2 v[224:225], v[230:231], off offset:288
	v_lshl_add_u64 v[252:253], v[142:143], 0, s[48:49]
	v_lshl_add_u64 v[254:255], s[24:25], 0, v[252:253]
	global_load_dwordx2 v[226:227], v[254:255], off
	global_load_dwordx2 v[220:221], v[254:255], off offset:32
	global_load_dwordx2 v[222:223], v[254:255], off offset:256
	global_load_dwordx2 v[216:217], v[254:255], off offset:288
	s_nop 0
	v_add_f32_e32 v70, 1.0, v58
	v_add_f32_e32 v71, 1.0, v59
	v_lshl_add_u64 v[58:59], s[36:37], 0, v[68:69]
	global_store_dwordx2 v[58:59], v[62:63], off
	s_nop 0
	s_waitcnt vmcnt(23)
	v_lshlrev_b32_e32 v62, 16, v248
	v_and_b32_e32 v63, 0xffff0000, v248
	v_div_scale_f32 v68, s[6:7], v70, v70, v62
	v_lshlrev_b32_e32 v64, 16, v249
	v_div_scale_f32 v72, s[6:7], v71, v71, v63
	v_rcp_f32_e32 v78, v68
	v_and_b32_e32 v65, 0xffff0000, v249
	v_div_scale_f32 v74, s[8:9], v60, v60, v64
	v_rcp_f32_e32 v79, v72
	v_div_scale_f32 v76, s[10:11], v61, v61, v65
	v_rcp_f32_e32 v80, v74
	v_rcp_f32_e32 v81, v76
	v_fma_f32 v82, -v68, v78, 1.0
	v_div_scale_f32 v69, vcc, v62, v70, v62
	v_fma_f32 v83, -v72, v79, 1.0
	v_fmac_f32_e32 v78, v82, v78
	v_div_scale_f32 v73, s[6:7], v63, v71, v63
	v_fma_f32 v84, -v74, v80, 1.0
	v_fmac_f32_e32 v79, v83, v79
	v_mul_f32_e32 v82, v69, v78
	v_div_scale_f32 v75, s[8:9], v64, v60, v64
	v_fma_f32 v85, -v76, v81, 1.0
	v_fmac_f32_e32 v80, v84, v80
	v_mul_f32_e32 v83, v73, v79
	v_fma_f32 v86, -v68, v82, v69
	v_div_scale_f32 v77, s[10:11], v65, v61, v65
	v_fmac_f32_e32 v81, v85, v81
	v_mul_f32_e32 v84, v75, v80
	v_fma_f32 v87, -v72, v83, v73
	v_fmac_f32_e32 v82, v86, v78
	v_mul_f32_e32 v85, v77, v81
	v_fma_f32 v88, -v74, v84, v75
	v_fmac_f32_e32 v83, v87, v79
	v_fma_f32 v68, -v68, v82, v69
	v_fma_f32 v89, -v76, v85, v77
	v_fmac_f32_e32 v84, v88, v80
	v_fma_f32 v69, -v72, v83, v73
	v_div_fmas_f32 v68, v68, v78, v82
	s_mov_b64 vcc, s[6:7]
	v_fmac_f32_e32 v85, v89, v81
	v_fma_f32 v72, -v74, v84, v75
	v_div_fixup_f32 v62, v68, v70, v62
	v_div_fmas_f32 v68, v69, v79, v83
	s_mov_b64 vcc, s[8:9]
	v_fma_f32 v73, -v76, v85, v77
	v_div_fixup_f32 v63, v68, v71, v63
	v_div_fmas_f32 v68, v72, v80, v84
	s_mov_b64 vcc, s[10:11]
	v_div_fixup_f32 v64, v68, v60, v64
	v_div_fmas_f32 v68, v73, v81, v85
	v_div_fixup_f32 v61, v68, v61, v65
	v_cvt_pk_bf16_f32 v60, v62, v63
	v_cvt_pk_bf16_f32 v61, v64, v61
	s_nop 0
	s_nop 0
	global_store_dwordx2 v[58:59], v[60:61], off offset:32
	s_nop 0
	s_waitcnt vmcnt(23)
	v_lshlrev_b32_e32 v60, 16, v250
	v_and_b32_e32 v61, 0xffff0000, v250
	v_div_scale_f32 v64, s[6:7], v54, v54, v60
	v_lshlrev_b32_e32 v62, 16, v251
	v_div_scale_f32 v68, s[6:7], v55, v55, v61
	v_rcp_f32_e32 v74, v64
	v_and_b32_e32 v63, 0xffff0000, v251
	v_div_scale_f32 v70, s[8:9], v56, v56, v62
	v_rcp_f32_e32 v75, v68
	v_div_scale_f32 v72, s[10:11], v57, v57, v63
	v_rcp_f32_e32 v76, v70
	v_rcp_f32_e32 v77, v72
	v_fma_f32 v78, -v64, v74, 1.0
	v_div_scale_f32 v65, vcc, v60, v54, v60
	v_fma_f32 v79, -v68, v75, 1.0
	v_fmac_f32_e32 v74, v78, v74
	v_div_scale_f32 v69, s[6:7], v61, v55, v61
	v_fma_f32 v80, -v70, v76, 1.0
	v_fmac_f32_e32 v75, v79, v75
	v_mul_f32_e32 v78, v65, v74
	v_div_scale_f32 v71, s[8:9], v62, v56, v62
	v_fma_f32 v81, -v72, v77, 1.0
	v_fmac_f32_e32 v76, v80, v76
	v_mul_f32_e32 v79, v69, v75
	v_fma_f32 v82, -v64, v78, v65
	v_div_scale_f32 v73, s[10:11], v63, v57, v63
	v_fmac_f32_e32 v77, v81, v77
	v_mul_f32_e32 v80, v71, v76
	v_fma_f32 v83, -v68, v79, v69
	v_fmac_f32_e32 v78, v82, v74
	v_mul_f32_e32 v81, v73, v77
	v_fma_f32 v84, -v70, v80, v71
	v_fmac_f32_e32 v79, v83, v75
	v_fma_f32 v64, -v64, v78, v65
	v_fma_f32 v85, -v72, v81, v73
	v_fmac_f32_e32 v80, v84, v76
	v_fma_f32 v65, -v68, v79, v69
	v_div_fmas_f32 v64, v64, v74, v78
	s_mov_b64 vcc, s[6:7]
	v_fmac_f32_e32 v81, v85, v77
	v_fma_f32 v68, -v70, v80, v71
	v_div_fixup_f32 v54, v64, v54, v60
	v_div_fmas_f32 v60, v65, v75, v79
	s_mov_b64 vcc, s[8:9]
	v_fma_f32 v69, -v72, v81, v73
	v_div_fixup_f32 v55, v60, v55, v61
	v_div_fmas_f32 v60, v68, v76, v80
	s_mov_b64 vcc, s[10:11]
	v_div_fixup_f32 v56, v60, v56, v62
	v_div_fmas_f32 v60, v69, v77, v81
	v_cvt_pk_bf16_f32 v54, v54, v55
	v_div_fixup_f32 v55, v60, v57, v63
	v_cvt_pk_bf16_f32 v55, v56, v55
	s_nop 0
	v_add_f32_e32 v60, 1.0, v50
	global_store_dwordx2 v[58:59], v[54:55], off offset:256
	v_add_f32_e32 v61, 1.0, v51
	v_add_f32_e32 v62, 1.0, v52
	v_add_f32_e32 v63, 1.0, v53
	v_lshl_add_u64 v[52:53], v[142:143], 0, s[42:43]
	v_lshl_add_u64 v[50:51], s[24:25], 0, v[52:53]
	s_nop 0
	s_waitcnt vmcnt(23)
; __device__ __forceinline__ unsigned cvt_pk_bf16(float lo, float hi) { unsigned r; asm volatile("v_cvt_pk_bf16_f32 %0, %1, %2" : "=v"(r) : "v"(lo), "v"(hi)); return r; }
; __device__ __forceinline__ float bflo(unsigned u) { return __uint_as_float(u << 16); }
; __device__ __forceinline__ float bfhi(unsigned u) { return __uint_as_float(u & 0xffff0000u); }
;     __device__ __forceinline__ void operator()(const f32x4 (&acc)[2][2][4][2], const Unit& u, int wr, int wc, int fr, int fq) const {
;         const int row0 = u.pm * BM + wr * 64 + fr, col0 = u.pn * BM + wc * 32 + 4 * fq;
; #pragma unroll
;         for (int ai = 0; ai < 2; ++ai)
; #pragma unroll
;             for (int m = 0; m < 4; ++m) { const size_t ro = (size_t)(row0 + ai * HALF + m * 16) * ldc + col0;
; #pragma unroll
;                 for (int bj = 0; bj < 2; ++bj)
; #pragma unroll
;                     for (int n = 0; n < 2; ++n) { const f32x4 a = acc[ai][bj][m][n]; const u32x2 yy = *(const u32x2*)(Y + ro + bj * HALF + n * 16);
;                         f32x4 v; v[0] = bflo(yy.x) / (1.0f + __expf(-a[0])); v[1] = bfhi(yy.x) / (1.0f + __expf(-a[1])); v[2] = bflo(yy.y) / (1.0f + __expf(-a[2])); v[3] = bfhi(yy.y) / (1.0f + __expf(-a[3]));
;                         u32x2 o; o.x = cvt_pk_bf16(v[0], v[1]); o.y = cvt_pk_bf16(v[2], v[3]); *(u32x2*)(C + ro + bj * HALF + n * 16) = o; } }
	v_lshlrev_b32_e32 v54, 16, v244
	v_and_b32_e32 v55, 0xffff0000, v244
	v_div_scale_f32 v64, s[6:7], v60, v60, v54
	v_lshlrev_b32_e32 v56, 16, v245
	v_div_scale_f32 v66, s[6:7], v61, v61, v55
	v_rcp_f32_e32 v72, v64
	v_and_b32_e32 v57, 0xffff0000, v245
	v_div_scale_f32 v68, s[8:9], v62, v62, v56
	v_rcp_f32_e32 v73, v66
	v_div_scale_f32 v70, s[10:11], v63, v63, v57
	v_rcp_f32_e32 v74, v68
	v_rcp_f32_e32 v75, v70
	v_fma_f32 v76, -v64, v72, 1.0
	v_div_scale_f32 v65, vcc, v54, v60, v54
	v_fma_f32 v77, -v66, v73, 1.0
	v_fmac_f32_e32 v72, v76, v72
	v_div_scale_f32 v67, s[6:7], v55, v61, v55
	v_fma_f32 v78, -v68, v74, 1.0
	v_fmac_f32_e32 v73, v77, v73
	v_mul_f32_e32 v76, v65, v72
	v_div_scale_f32 v69, s[8:9], v56, v62, v56
	v_fma_f32 v79, -v70, v75, 1.0
	v_fmac_f32_e32 v74, v78, v74
	v_mul_f32_e32 v77, v67, v73
	v_fma_f32 v80, -v64, v76, v65
	v_div_scale_f32 v71, s[10:11], v57, v63, v57
	v_fmac_f32_e32 v75, v79, v75
	v_mul_f32_e32 v78, v69, v74
	v_fma_f32 v81, -v66, v77, v67
	v_fmac_f32_e32 v76, v80, v72
	v_mul_f32_e32 v79, v71, v75
	v_fma_f32 v82, -v68, v78, v69
	v_fmac_f32_e32 v77, v81, v73
	v_fma_f32 v64, -v64, v76, v65
	v_fma_f32 v83, -v70, v79, v71
	v_fmac_f32_e32 v78, v82, v74
	v_fma_f32 v65, -v66, v77, v67
	v_div_fmas_f32 v64, v64, v72, v76
	s_mov_b64 vcc, s[6:7]
	v_fmac_f32_e32 v79, v83, v75
	v_fma_f32 v66, -v68, v78, v69
	v_div_fixup_f32 v54, v64, v60, v54
	v_div_fmas_f32 v60, v65, v73, v77
	s_mov_b64 vcc, s[8:9]
	v_fma_f32 v67, -v70, v79, v71
	v_div_fixup_f32 v55, v60, v61, v55
	v_div_fmas_f32 v60, v66, v74, v78
	s_mov_b64 vcc, s[10:11]
	v_div_fixup_f32 v56, v60, v62, v56
	v_div_fmas_f32 v60, v67, v75, v79
	v_cvt_pk_bf16_f32 v54, v54, v55
	v_div_fixup_f32 v55, v60, v63, v57
	v_cvt_pk_bf16_f32 v55, v56, v55
	global_store_dwordx2 v[58:59], v[54:55], off offset:288
	s_nop 0
	s_nop 0
	s_waitcnt vmcnt(23)
	v_lshlrev_b32_e32 v56, 16, v246
	v_and_b32_e32 v54, 0xffff0000, v246
	v_div_scale_f32 v58, s[6:7], v46, v46, v56
	v_lshlrev_b32_e32 v57, 16, v247
	v_div_scale_f32 v60, s[6:7], v47, v47, v54
	v_rcp_f32_e32 v66, v58
	v_and_b32_e32 v55, 0xffff0000, v247
	v_div_scale_f32 v62, s[8:9], v48, v48, v57
	v_rcp_f32_e32 v67, v60
	v_div_scale_f32 v64, s[10:11], v49, v49, v55
	v_rcp_f32_e32 v68, v62
	v_rcp_f32_e32 v69, v64
	v_fma_f32 v70, -v58, v66, 1.0
	v_div_scale_f32 v59, vcc, v56, v46, v56
	v_fma_f32 v71, -v60, v67, 1.0
	v_fmac_f32_e32 v66, v70, v66
	v_div_scale_f32 v61, s[6:7], v54, v47, v54
	v_fma_f32 v72, -v62, v68, 1.0
	v_fmac_f32_e32 v67, v71, v67
	v_mul_f32_e32 v70, v59, v66
	v_div_scale_f32 v63, s[8:9], v57, v48, v57
	v_fma_f32 v73, -v64, v69, 1.0
	v_fmac_f32_e32 v68, v72, v68
	v_mul_f32_e32 v71, v61, v67
	v_fma_f32 v74, -v58, v70, v59
	v_div_scale_f32 v65, s[10:11], v55, v49, v55
	v_fmac_f32_e32 v69, v73, v69
	v_mul_f32_e32 v72, v63, v68
	v_fma_f32 v75, -v60, v71, v61
	v_fmac_f32_e32 v70, v74, v66
	v_mul_f32_e32 v73, v65, v69
	v_fma_f32 v76, -v62, v72, v63
	v_fmac_f32_e32 v71, v75, v67
	v_fma_f32 v58, -v58, v70, v59
	v_fma_f32 v77, -v64, v73, v65
	v_fmac_f32_e32 v72, v76, v68
	v_fma_f32 v59, -v60, v71, v61
	v_div_fmas_f32 v58, v58, v66, v70
	s_mov_b64 vcc, s[6:7]
	v_fmac_f32_e32 v73, v77, v69
	v_fma_f32 v60, -v62, v72, v63
	v_div_fixup_f32 v46, v58, v46, v56
	v_div_fmas_f32 v56, v59, v67, v71
	s_mov_b64 vcc, s[8:9]
	v_fma_f32 v61, -v64, v73, v65
	v_div_fixup_f32 v47, v56, v47, v54
	v_div_fmas_f32 v54, v60, v68, v72
	s_mov_b64 vcc, s[10:11]
	v_div_fixup_f32 v48, v54, v48, v57
	v_div_fmas_f32 v54, v61, v69, v73
	v_cvt_pk_bf16_f32 v46, v46, v47
	v_div_fixup_f32 v47, v54, v49, v55
	v_cvt_pk_bf16_f32 v47, v48, v47
	s_nop 0
	v_add_f32_e32 v54, 1.0, v42
	v_add_f32_e32 v55, 1.0, v43
	v_lshl_add_u64 v[42:43], s[36:37], 0, v[52:53]
	global_store_dwordx2 v[42:43], v[46:47], off
	s_nop 0
	s_waitcnt vmcnt(23)
	v_lshlrev_b32_e32 v46, 16, v240
	v_and_b32_e32 v47, 0xffff0000, v240
	v_div_scale_f32 v52, s[6:7], v54, v54, v46
	v_lshlrev_b32_e32 v48, 16, v241
	v_div_scale_f32 v56, s[6:7], v55, v55, v47
	v_rcp_f32_e32 v62, v52
	v_and_b32_e32 v49, 0xffff0000, v241
	v_div_scale_f32 v58, s[8:9], v44, v44, v48
	v_rcp_f32_e32 v63, v56
	v_div_scale_f32 v60, s[10:11], v45, v45, v49
	v_rcp_f32_e32 v64, v58
	v_rcp_f32_e32 v65, v60
	v_fma_f32 v66, -v52, v62, 1.0
	v_div_scale_f32 v53, vcc, v46, v54, v46
	v_fma_f32 v67, -v56, v63, 1.0
	v_fmac_f32_e32 v62, v66, v62
	v_div_scale_f32 v57, s[6:7], v47, v55, v47
	v_fma_f32 v68, -v58, v64, 1.0
	v_fmac_f32_e32 v63, v67, v63
	v_mul_f32_e32 v66, v53, v62
	v_div_scale_f32 v59, s[8:9], v48, v44, v48
	v_fma_f32 v69, -v60, v65, 1.0
	v_fmac_f32_e32 v64, v68, v64
	v_mul_f32_e32 v67, v57, v63
	v_fma_f32 v70, -v52, v66, v53
	v_div_scale_f32 v61, s[10:11], v49, v45, v49
	v_fmac_f32_e32 v65, v69, v65
	v_mul_f32_e32 v68, v59, v64
	v_fma_f32 v71, -v56, v67, v57
	v_fmac_f32_e32 v66, v70, v62
	v_mul_f32_e32 v69, v61, v65
	v_fma_f32 v72, -v58, v68, v59
	v_fmac_f32_e32 v67, v71, v63
	v_fma_f32 v52, -v52, v66, v53
	v_fma_f32 v73, -v60, v69, v61
	v_fmac_f32_e32 v68, v72, v64
	v_fma_f32 v53, -v56, v67, v57
	v_div_fmas_f32 v52, v52, v62, v66
	s_mov_b64 vcc, s[6:7]
	v_fmac_f32_e32 v69, v73, v65
	v_fma_f32 v56, -v58, v68, v59
	v_div_fixup_f32 v46, v52, v54, v46
	v_div_fmas_f32 v52, v53, v63, v67
	s_mov_b64 vcc, s[8:9]
	v_fma_f32 v57, -v60, v69, v61
	v_div_fixup_f32 v47, v52, v55, v47
	v_div_fmas_f32 v52, v56, v64, v68
	s_mov_b64 vcc, s[10:11]
	v_div_fixup_f32 v48, v52, v44, v48
	v_div_fmas_f32 v52, v57, v65, v69
	v_div_fixup_f32 v45, v52, v45, v49
	v_cvt_pk_bf16_f32 v44, v46, v47
	v_cvt_pk_bf16_f32 v45, v48, v45
	s_nop 0
	s_nop 0
	global_store_dwordx2 v[42:43], v[44:45], off offset:32
	s_nop 0
	s_waitcnt vmcnt(23)
; __device__ __forceinline__ unsigned cvt_pk_bf16(float lo, float hi) { unsigned r; asm volatile("v_cvt_pk_bf16_f32 %0, %1, %2" : "=v"(r) : "v"(lo), "v"(hi)); return r; }
; __device__ __forceinline__ float bflo(unsigned u) { return __uint_as_float(u << 16); }
; __device__ __forceinline__ float bfhi(unsigned u) { return __uint_as_float(u & 0xffff0000u); }
;     __device__ __forceinline__ void operator()(const f32x4 (&acc)[2][2][4][2], const Unit& u, int wr, int wc, int fr, int fq) const {
;         const int row0 = u.pm * BM + wr * 64 + fr, col0 = u.pn * BM + wc * 32 + 4 * fq;
; #pragma unroll
;         for (int ai = 0; ai < 2; ++ai)
; #pragma unroll
;             for (int m = 0; m < 4; ++m) { const size_t ro = (size_t)(row0 + ai * HALF + m * 16) * ldc + col0;
; #pragma unroll
;                 for (int bj = 0; bj < 2; ++bj)
; #pragma unroll
;                     for (int n = 0; n < 2; ++n) { const f32x4 a = acc[ai][bj][m][n]; const u32x2 yy = *(const u32x2*)(Y + ro + bj * HALF + n * 16);
;                         f32x4 v; v[0] = bflo(yy.x) / (1.0f + __expf(-a[0])); v[1] = bfhi(yy.x) / (1.0f + __expf(-a[1])); v[2] = bflo(yy.y) / (1.0f + __expf(-a[2])); v[3] = bfhi(yy.y) / (1.0f + __expf(-a[3]));
;                         u32x2 o; o.x = cvt_pk_bf16(v[0], v[1]); o.y = cvt_pk_bf16(v[2], v[3]); *(u32x2*)(C + ro + bj * HALF + n * 16) = o; } }
	v_lshlrev_b32_e32 v44, 16, v242
	v_and_b32_e32 v45, 0xffff0000, v242
	v_div_scale_f32 v48, s[6:7], v38, v38, v44
	v_lshlrev_b32_e32 v46, 16, v243
	v_div_scale_f32 v52, s[6:7], v39, v39, v45
	v_rcp_f32_e32 v58, v48
	v_and_b32_e32 v47, 0xffff0000, v243
	v_div_scale_f32 v54, s[8:9], v40, v40, v46
	v_rcp_f32_e32 v59, v52
	v_div_scale_f32 v56, s[10:11], v41, v41, v47
	v_rcp_f32_e32 v60, v54
	v_rcp_f32_e32 v61, v56
	v_fma_f32 v62, -v48, v58, 1.0
	v_div_scale_f32 v49, vcc, v44, v38, v44
	v_fma_f32 v63, -v52, v59, 1.0
	v_fmac_f32_e32 v58, v62, v58
	v_div_scale_f32 v53, s[6:7], v45, v39, v45
	v_fma_f32 v64, -v54, v60, 1.0
	v_fmac_f32_e32 v59, v63, v59
	v_mul_f32_e32 v62, v49, v58
	v_div_scale_f32 v55, s[8:9], v46, v40, v46
	v_fma_f32 v65, -v56, v61, 1.0
	v_fmac_f32_e32 v60, v64, v60
	v_mul_f32_e32 v63, v53, v59
	v_fma_f32 v66, -v48, v62, v49
	v_div_scale_f32 v57, s[10:11], v47, v41, v47
	v_fmac_f32_e32 v61, v65, v61
	v_mul_f32_e32 v64, v55, v60
	v_fma_f32 v67, -v52, v63, v53
	v_fmac_f32_e32 v62, v66, v58
	v_mul_f32_e32 v65, v57, v61
	v_fma_f32 v68, -v54, v64, v55
	v_fmac_f32_e32 v63, v67, v59
	v_fma_f32 v48, -v48, v62, v49
	v_fma_f32 v69, -v56, v65, v57
	v_fmac_f32_e32 v64, v68, v60
	v_fma_f32 v49, -v52, v63, v53
	v_div_fmas_f32 v48, v48, v58, v62
	s_mov_b64 vcc, s[6:7]
	v_fmac_f32_e32 v65, v69, v61
	v_fma_f32 v52, -v54, v64, v55
	v_div_fixup_f32 v38, v48, v38, v44
	v_div_fmas_f32 v44, v49, v59, v63
	s_mov_b64 vcc, s[8:9]
	v_fma_f32 v53, -v56, v65, v57
	v_div_fixup_f32 v39, v44, v39, v45
	v_div_fmas_f32 v44, v52, v60, v64
	s_mov_b64 vcc, s[10:11]
	v_div_fixup_f32 v40, v44, v40, v46
	v_div_fmas_f32 v44, v53, v61, v65
	v_cvt_pk_bf16_f32 v38, v38, v39
	v_div_fixup_f32 v39, v44, v41, v47
	v_cvt_pk_bf16_f32 v39, v40, v39
	s_nop 0
	v_add_f32_e32 v44, 1.0, v34
	global_store_dwordx2 v[42:43], v[38:39], off offset:256
	v_add_f32_e32 v45, 1.0, v35
	v_add_f32_e32 v46, 1.0, v36
	v_add_f32_e32 v47, 1.0, v37
	v_lshl_add_u64 v[36:37], v[142:143], 0, s[46:47]
	v_lshl_add_u64 v[34:35], s[24:25], 0, v[36:37]
	s_nop 0
	s_waitcnt vmcnt(23)
	v_lshlrev_b32_e32 v38, 16, v236
	v_and_b32_e32 v39, 0xffff0000, v236
	v_div_scale_f32 v48, s[6:7], v44, v44, v38
	v_lshlrev_b32_e32 v40, 16, v237
	v_div_scale_f32 v50, s[6:7], v45, v45, v39
	v_rcp_f32_e32 v56, v48
	v_and_b32_e32 v41, 0xffff0000, v237
	v_div_scale_f32 v52, s[8:9], v46, v46, v40
	v_rcp_f32_e32 v57, v50
	v_div_scale_f32 v54, s[10:11], v47, v47, v41
	v_rcp_f32_e32 v58, v52
	v_rcp_f32_e32 v59, v54
	v_fma_f32 v60, -v48, v56, 1.0
	v_div_scale_f32 v49, vcc, v38, v44, v38
	v_fma_f32 v61, -v50, v57, 1.0
	v_fmac_f32_e32 v56, v60, v56
	v_div_scale_f32 v51, s[6:7], v39, v45, v39
	v_fma_f32 v62, -v52, v58, 1.0
	v_fmac_f32_e32 v57, v61, v57
	v_mul_f32_e32 v60, v49, v56
	v_div_scale_f32 v53, s[8:9], v40, v46, v40
	v_fma_f32 v63, -v54, v59, 1.0
	v_fmac_f32_e32 v58, v62, v58
	v_mul_f32_e32 v61, v51, v57
	v_fma_f32 v64, -v48, v60, v49
	v_div_scale_f32 v55, s[10:11], v41, v47, v41
	v_fmac_f32_e32 v59, v63, v59
	v_mul_f32_e32 v62, v53, v58
	v_fma_f32 v65, -v50, v61, v51
	v_fmac_f32_e32 v60, v64, v56
	v_mul_f32_e32 v63, v55, v59
	v_fma_f32 v66, -v52, v62, v53
	v_fmac_f32_e32 v61, v65, v57
	v_fma_f32 v48, -v48, v60, v49
	v_fma_f32 v67, -v54, v63, v55
	v_fmac_f32_e32 v62, v66, v58
	v_fma_f32 v49, -v50, v61, v51
	v_div_fmas_f32 v48, v48, v56, v60
	s_mov_b64 vcc, s[6:7]
	v_fmac_f32_e32 v63, v67, v59
	v_fma_f32 v50, -v52, v62, v53
	v_div_fixup_f32 v38, v48, v44, v38
	v_div_fmas_f32 v44, v49, v57, v61
	s_mov_b64 vcc, s[8:9]
	v_fma_f32 v51, -v54, v63, v55
	v_div_fixup_f32 v39, v44, v45, v39
	v_div_fmas_f32 v44, v50, v58, v62
	s_mov_b64 vcc, s[10:11]
	v_div_fixup_f32 v40, v44, v46, v40
	v_div_fmas_f32 v44, v51, v59, v63
	v_cvt_pk_bf16_f32 v38, v38, v39
	v_div_fixup_f32 v39, v44, v47, v41
	v_cvt_pk_bf16_f32 v39, v40, v39
	global_store_dwordx2 v[42:43], v[38:39], off offset:288
	s_nop 0
	s_nop 0
	s_waitcnt vmcnt(23)
	v_lshlrev_b32_e32 v40, 16, v238
	v_and_b32_e32 v38, 0xffff0000, v238
	v_div_scale_f32 v42, s[6:7], v30, v30, v40
	v_lshlrev_b32_e32 v41, 16, v239
	v_div_scale_f32 v44, s[6:7], v31, v31, v38
	v_rcp_f32_e32 v50, v42
	v_and_b32_e32 v39, 0xffff0000, v239
	v_div_scale_f32 v46, s[8:9], v32, v32, v41
	v_rcp_f32_e32 v51, v44
	v_div_scale_f32 v48, s[10:11], v33, v33, v39
	v_rcp_f32_e32 v52, v46
	v_rcp_f32_e32 v53, v48
	v_fma_f32 v54, -v42, v50, 1.0
	v_div_scale_f32 v43, vcc, v40, v30, v40
	v_fma_f32 v55, -v44, v51, 1.0
	v_fmac_f32_e32 v50, v54, v50
	v_div_scale_f32 v45, s[6:7], v38, v31, v38
	v_fma_f32 v56, -v46, v52, 1.0
	v_fmac_f32_e32 v51, v55, v51
	v_mul_f32_e32 v54, v43, v50
	v_div_scale_f32 v47, s[8:9], v41, v32, v41
	v_fma_f32 v57, -v48, v53, 1.0
	v_fmac_f32_e32 v52, v56, v52
	v_mul_f32_e32 v55, v45, v51
	v_fma_f32 v58, -v42, v54, v43
	v_div_scale_f32 v49, s[10:11], v39, v33, v39
	v_fmac_f32_e32 v53, v57, v53
	v_mul_f32_e32 v56, v47, v52
	v_fma_f32 v59, -v44, v55, v45
	v_fmac_f32_e32 v54, v58, v50
	v_mul_f32_e32 v57, v49, v53
	v_fma_f32 v60, -v46, v56, v47
	v_fmac_f32_e32 v55, v59, v51
	v_fma_f32 v42, -v42, v54, v43
	v_fma_f32 v61, -v48, v57, v49
	v_fmac_f32_e32 v56, v60, v52
	v_fma_f32 v43, -v44, v55, v45
	v_div_fmas_f32 v42, v42, v50, v54
	s_mov_b64 vcc, s[6:7]
	v_fmac_f32_e32 v57, v61, v53
	v_fma_f32 v44, -v46, v56, v47
	v_div_fixup_f32 v30, v42, v30, v40
	v_div_fmas_f32 v40, v43, v51, v55
	s_mov_b64 vcc, s[8:9]
	v_fma_f32 v45, -v48, v57, v49
	v_div_fixup_f32 v31, v40, v31, v38
	v_div_fmas_f32 v38, v44, v52, v56
	s_mov_b64 vcc, s[10:11]
	v_div_fixup_f32 v32, v38, v32, v41
	v_div_fmas_f32 v38, v45, v53, v57
	v_cvt_pk_bf16_f32 v30, v30, v31
	v_div_fixup_f32 v31, v38, v33, v39
	v_cvt_pk_bf16_f32 v31, v32, v31
	s_nop 0
	v_add_f32_e32 v38, 1.0, v26
	v_add_f32_e32 v39, 1.0, v27
	v_lshl_add_u64 v[26:27], s[36:37], 0, v[36:37]
	global_store_dwordx2 v[26:27], v[30:31], off
	s_nop 0
	s_waitcnt vmcnt(15)
; __device__ __forceinline__ unsigned cvt_pk_bf16(float lo, float hi) { unsigned r; asm volatile("v_cvt_pk_bf16_f32 %0, %1, %2" : "=v"(r) : "v"(lo), "v"(hi)); return r; }
; __device__ __forceinline__ float bflo(unsigned u) { return __uint_as_float(u << 16); }
; __device__ __forceinline__ float bfhi(unsigned u) { return __uint_as_float(u & 0xffff0000u); }
;     __device__ __forceinline__ void operator()(const f32x4 (&acc)[2][2][4][2], const Unit& u, int wr, int wc, int fr, int fq) const {
;         const int row0 = u.pm * BM + wr * 64 + fr, col0 = u.pn * BM + wc * 32 + 4 * fq;
; #pragma unroll
;         for (int ai = 0; ai < 2; ++ai)
; #pragma unroll
;             for (int m = 0; m < 4; ++m) { const size_t ro = (size_t)(row0 + ai * HALF + m * 16) * ldc + col0;
; #pragma unroll
;                 for (int bj = 0; bj < 2; ++bj)
; #pragma unroll
;                     for (int n = 0; n < 2; ++n) { const f32x4 a = acc[ai][bj][m][n]; const u32x2 yy = *(const u32x2*)(Y + ro + bj * HALF + n * 16);
;                         f32x4 v; v[0] = bflo(yy.x) / (1.0f + __expf(-a[0])); v[1] = bfhi(yy.x) / (1.0f + __expf(-a[1])); v[2] = bflo(yy.y) / (1.0f + __expf(-a[2])); v[3] = bfhi(yy.y) / (1.0f + __expf(-a[3]));
;                         u32x2 o; o.x = cvt_pk_bf16(v[0], v[1]); o.y = cvt_pk_bf16(v[2], v[3]); *(u32x2*)(C + ro + bj * HALF + n * 16) = o; } }
	v_lshlrev_b32_e32 v30, 16, v232
	v_and_b32_e32 v31, 0xffff0000, v232
	v_div_scale_f32 v36, s[6:7], v38, v38, v30
	v_lshlrev_b32_e32 v32, 16, v233
	v_div_scale_f32 v40, s[6:7], v39, v39, v31
	v_rcp_f32_e32 v46, v36
	v_and_b32_e32 v33, 0xffff0000, v233
	v_div_scale_f32 v42, s[8:9], v28, v28, v32
	v_rcp_f32_e32 v47, v40
	v_div_scale_f32 v44, s[10:11], v29, v29, v33
	v_rcp_f32_e32 v48, v42
	v_rcp_f32_e32 v49, v44
	v_fma_f32 v50, -v36, v46, 1.0
	v_div_scale_f32 v37, vcc, v30, v38, v30
	v_fma_f32 v51, -v40, v47, 1.0
	v_fmac_f32_e32 v46, v50, v46
	v_div_scale_f32 v41, s[6:7], v31, v39, v31
	v_fma_f32 v52, -v42, v48, 1.0
	v_fmac_f32_e32 v47, v51, v47
	v_mul_f32_e32 v50, v37, v46
	v_div_scale_f32 v43, s[8:9], v32, v28, v32
	v_fma_f32 v53, -v44, v49, 1.0
	v_fmac_f32_e32 v48, v52, v48
	v_mul_f32_e32 v51, v41, v47
	v_fma_f32 v54, -v36, v50, v37
	v_div_scale_f32 v45, s[10:11], v33, v29, v33
	v_fmac_f32_e32 v49, v53, v49
	v_mul_f32_e32 v52, v43, v48
	v_fma_f32 v55, -v40, v51, v41
	v_fmac_f32_e32 v50, v54, v46
	v_mul_f32_e32 v53, v45, v49
	v_fma_f32 v56, -v42, v52, v43
	v_fmac_f32_e32 v51, v55, v47
	v_fma_f32 v36, -v36, v50, v37
	v_fma_f32 v57, -v44, v53, v45
	v_fmac_f32_e32 v52, v56, v48
	v_fma_f32 v37, -v40, v51, v41
	v_div_fmas_f32 v36, v36, v46, v50
	s_mov_b64 vcc, s[6:7]
	v_fmac_f32_e32 v53, v57, v49
	v_fma_f32 v40, -v42, v52, v43
	v_div_fixup_f32 v30, v36, v38, v30
	v_div_fmas_f32 v36, v37, v47, v51
	s_mov_b64 vcc, s[8:9]
	v_fma_f32 v41, -v44, v53, v45
	v_div_fixup_f32 v31, v36, v39, v31
	v_div_fmas_f32 v36, v40, v48, v52
	s_mov_b64 vcc, s[10:11]
	v_div_fixup_f32 v32, v36, v28, v32
	v_div_fmas_f32 v36, v41, v49, v53
	v_div_fixup_f32 v29, v36, v29, v33
	v_cvt_pk_bf16_f32 v28, v30, v31
	v_cvt_pk_bf16_f32 v29, v32, v29
	s_nop 0
	s_nop 0
	global_store_dwordx2 v[26:27], v[28:29], off offset:32
	s_nop 0
	s_waitcnt vmcnt(15)
	v_lshlrev_b32_e32 v28, 16, v234
	v_and_b32_e32 v29, 0xffff0000, v234
	v_div_scale_f32 v32, s[6:7], v22, v22, v28
	v_lshlrev_b32_e32 v30, 16, v235
	v_div_scale_f32 v36, s[6:7], v23, v23, v29
	v_rcp_f32_e32 v42, v32
	v_and_b32_e32 v31, 0xffff0000, v235
	v_div_scale_f32 v38, s[8:9], v24, v24, v30
	v_rcp_f32_e32 v43, v36
	v_div_scale_f32 v40, s[10:11], v25, v25, v31
	v_rcp_f32_e32 v44, v38
	v_rcp_f32_e32 v45, v40
	v_fma_f32 v46, -v32, v42, 1.0
	v_div_scale_f32 v33, vcc, v28, v22, v28
	v_fma_f32 v47, -v36, v43, 1.0
	v_fmac_f32_e32 v42, v46, v42
	v_div_scale_f32 v37, s[6:7], v29, v23, v29
	v_fma_f32 v48, -v38, v44, 1.0
	v_fmac_f32_e32 v43, v47, v43
	v_mul_f32_e32 v46, v33, v42
	v_div_scale_f32 v39, s[8:9], v30, v24, v30
	v_fma_f32 v49, -v40, v45, 1.0
	v_fmac_f32_e32 v44, v48, v44
	v_mul_f32_e32 v47, v37, v43
	v_fma_f32 v50, -v32, v46, v33
	v_div_scale_f32 v41, s[10:11], v31, v25, v31
	v_fmac_f32_e32 v45, v49, v45
	v_mul_f32_e32 v48, v39, v44
	v_fma_f32 v51, -v36, v47, v37
	v_fmac_f32_e32 v46, v50, v42
	v_mul_f32_e32 v49, v41, v45
	v_fma_f32 v52, -v38, v48, v39
	v_fmac_f32_e32 v47, v51, v43
	v_fma_f32 v32, -v32, v46, v33
	v_fma_f32 v53, -v40, v49, v41
	v_fmac_f32_e32 v48, v52, v44
	v_fma_f32 v33, -v36, v47, v37
	v_div_fmas_f32 v32, v32, v42, v46
	s_mov_b64 vcc, s[6:7]
	v_fmac_f32_e32 v49, v53, v45
	v_fma_f32 v36, -v38, v48, v39
	v_div_fixup_f32 v22, v32, v22, v28
	v_div_fmas_f32 v28, v33, v43, v47
	s_mov_b64 vcc, s[8:9]
	v_fma_f32 v37, -v40, v49, v41
	v_div_fixup_f32 v23, v28, v23, v29
	v_div_fmas_f32 v28, v36, v44, v48
	s_mov_b64 vcc, s[10:11]
	v_div_fixup_f32 v24, v28, v24, v30
	v_div_fmas_f32 v28, v37, v45, v49
	v_cvt_pk_bf16_f32 v22, v22, v23
	v_div_fixup_f32 v23, v28, v25, v31
	v_cvt_pk_bf16_f32 v23, v24, v23
	s_nop 0
	v_add_f32_e32 v28, 1.0, v18
	global_store_dwordx2 v[26:27], v[22:23], off offset:256
	v_add_f32_e32 v29, 1.0, v19
	v_add_f32_e32 v30, 1.0, v20
	v_add_f32_e32 v31, 1.0, v21
	v_lshl_add_u64 v[20:21], v[142:143], 0, s[48:49]
	v_lshl_add_u64 v[18:19], s[24:25], 0, v[20:21]
	s_nop 0
	s_waitcnt vmcnt(15)
	v_lshlrev_b32_e32 v22, 16, v224
	v_and_b32_e32 v23, 0xffff0000, v224
	v_div_scale_f32 v32, s[6:7], v28, v28, v22
	v_lshlrev_b32_e32 v24, 16, v225
	v_div_scale_f32 v34, s[6:7], v29, v29, v23
	v_rcp_f32_e32 v40, v32
	v_and_b32_e32 v25, 0xffff0000, v225
	v_div_scale_f32 v36, s[8:9], v30, v30, v24
	v_rcp_f32_e32 v41, v34
	v_div_scale_f32 v38, s[10:11], v31, v31, v25
	v_rcp_f32_e32 v42, v36
	v_rcp_f32_e32 v43, v38
	v_fma_f32 v44, -v32, v40, 1.0
	v_div_scale_f32 v33, vcc, v22, v28, v22
	v_fma_f32 v45, -v34, v41, 1.0
	v_fmac_f32_e32 v40, v44, v40
	v_div_scale_f32 v35, s[6:7], v23, v29, v23
	v_fma_f32 v46, -v36, v42, 1.0
	v_fmac_f32_e32 v41, v45, v41
	v_mul_f32_e32 v44, v33, v40
	v_div_scale_f32 v37, s[8:9], v24, v30, v24
	v_fma_f32 v47, -v38, v43, 1.0
	v_fmac_f32_e32 v42, v46, v42
	v_mul_f32_e32 v45, v35, v41
	v_fma_f32 v48, -v32, v44, v33
	v_div_scale_f32 v39, s[10:11], v25, v31, v25
	v_fmac_f32_e32 v43, v47, v43
	v_mul_f32_e32 v46, v37, v42
	v_fma_f32 v49, -v34, v45, v35
	v_fmac_f32_e32 v44, v48, v40
	v_mul_f32_e32 v47, v39, v43
	v_fma_f32 v50, -v36, v46, v37
	v_fmac_f32_e32 v45, v49, v41
	v_fma_f32 v32, -v32, v44, v33
	v_fma_f32 v51, -v38, v47, v39
	v_fmac_f32_e32 v46, v50, v42
	v_fma_f32 v33, -v34, v45, v35
	v_div_fmas_f32 v32, v32, v40, v44
	s_mov_b64 vcc, s[6:7]
	v_fmac_f32_e32 v47, v51, v43
	v_fma_f32 v34, -v36, v46, v37
	v_div_fixup_f32 v22, v32, v28, v22
	v_div_fmas_f32 v28, v33, v41, v45
	s_mov_b64 vcc, s[8:9]
	v_fma_f32 v35, -v38, v47, v39
	v_div_fixup_f32 v23, v28, v29, v23
	v_div_fmas_f32 v28, v34, v42, v46
	s_mov_b64 vcc, s[10:11]
	v_div_fixup_f32 v24, v28, v30, v24
	v_div_fmas_f32 v28, v35, v43, v47
	v_cvt_pk_bf16_f32 v22, v22, v23
	v_div_fixup_f32 v23, v28, v31, v25
	v_cvt_pk_bf16_f32 v23, v24, v23
	global_store_dwordx2 v[26:27], v[22:23], off offset:288
	s_nop 0
	s_nop 0
	s_waitcnt vmcnt(15)
; __device__ __forceinline__ unsigned cvt_pk_bf16(float lo, float hi) { unsigned r; asm volatile("v_cvt_pk_bf16_f32 %0, %1, %2" : "=v"(r) : "v"(lo), "v"(hi)); return r; }
; __device__ __forceinline__ float bflo(unsigned u) { return __uint_as_float(u << 16); }
; __device__ __forceinline__ float bfhi(unsigned u) { return __uint_as_float(u & 0xffff0000u); }
;     __device__ __forceinline__ void operator()(const f32x4 (&acc)[2][2][4][2], const Unit& u, int wr, int wc, int fr, int fq) const {
;         const int row0 = u.pm * BM + wr * 64 + fr, col0 = u.pn * BM + wc * 32 + 4 * fq;
; #pragma unroll
;         for (int ai = 0; ai < 2; ++ai)
; #pragma unroll
;             for (int m = 0; m < 4; ++m) { const size_t ro = (size_t)(row0 + ai * HALF + m * 16) * ldc + col0;
; #pragma unroll
;                 for (int bj = 0; bj < 2; ++bj)
; #pragma unroll
;                     for (int n = 0; n < 2; ++n) { const f32x4 a = acc[ai][bj][m][n]; const u32x2 yy = *(const u32x2*)(Y + ro + bj * HALF + n * 16);
;                         f32x4 v; v[0] = bflo(yy.x) / (1.0f + __expf(-a[0])); v[1] = bfhi(yy.x) / (1.0f + __expf(-a[1])); v[2] = bflo(yy.y) / (1.0f + __expf(-a[2])); v[3] = bfhi(yy.y) / (1.0f + __expf(-a[3]));
;                         u32x2 o; o.x = cvt_pk_bf16(v[0], v[1]); o.y = cvt_pk_bf16(v[2], v[3]); *(u32x2*)(C + ro + bj * HALF + n * 16) = o; } }
	v_lshlrev_b32_e32 v24, 16, v226
	v_and_b32_e32 v22, 0xffff0000, v226
	v_div_scale_f32 v26, s[6:7], v14, v14, v24
	v_lshlrev_b32_e32 v25, 16, v227
	v_div_scale_f32 v28, s[6:7], v15, v15, v22
	v_rcp_f32_e32 v34, v26
	v_and_b32_e32 v23, 0xffff0000, v227
	v_div_scale_f32 v30, s[8:9], v16, v16, v25
	v_rcp_f32_e32 v35, v28
	v_div_scale_f32 v32, s[10:11], v17, v17, v23
	v_rcp_f32_e32 v36, v30
	v_rcp_f32_e32 v37, v32
	v_fma_f32 v38, -v26, v34, 1.0
	v_div_scale_f32 v27, vcc, v24, v14, v24
	v_fma_f32 v39, -v28, v35, 1.0
	v_fmac_f32_e32 v34, v38, v34
	v_div_scale_f32 v29, s[6:7], v22, v15, v22
	v_fma_f32 v40, -v30, v36, 1.0
	v_fmac_f32_e32 v35, v39, v35
	v_mul_f32_e32 v38, v27, v34
	v_div_scale_f32 v31, s[8:9], v25, v16, v25
	v_fma_f32 v41, -v32, v37, 1.0
	v_fmac_f32_e32 v36, v40, v36
	v_mul_f32_e32 v39, v29, v35
	v_fma_f32 v42, -v26, v38, v27
	v_div_scale_f32 v33, s[10:11], v23, v17, v23
	v_fmac_f32_e32 v37, v41, v37
	v_mul_f32_e32 v40, v31, v36
	v_fma_f32 v43, -v28, v39, v29
	v_fmac_f32_e32 v38, v42, v34
	v_mul_f32_e32 v41, v33, v37
	v_fma_f32 v44, -v30, v40, v31
	v_fmac_f32_e32 v39, v43, v35
	v_fma_f32 v26, -v26, v38, v27
	v_fma_f32 v45, -v32, v41, v33
	v_fmac_f32_e32 v40, v44, v36
	v_fma_f32 v27, -v28, v39, v29
	v_div_fmas_f32 v26, v26, v34, v38
	s_mov_b64 vcc, s[6:7]
	v_fmac_f32_e32 v41, v45, v37
	v_fma_f32 v28, -v30, v40, v31
	v_div_fixup_f32 v14, v26, v14, v24
	v_div_fmas_f32 v24, v27, v35, v39
	s_mov_b64 vcc, s[8:9]
	v_fma_f32 v29, -v32, v41, v33
	v_div_fixup_f32 v15, v24, v15, v22
	v_div_fmas_f32 v22, v28, v36, v40
	s_mov_b64 vcc, s[10:11]
	v_div_fixup_f32 v16, v22, v16, v25
	v_div_fmas_f32 v22, v29, v37, v41
	v_cvt_pk_bf16_f32 v14, v14, v15
	v_div_fixup_f32 v15, v22, v17, v23
	v_cvt_pk_bf16_f32 v15, v16, v15
	s_nop 0
	v_add_f32_e32 v22, 1.0, v10
	v_add_f32_e32 v23, 1.0, v11
	v_lshl_add_u64 v[10:11], s[36:37], 0, v[20:21]
	global_store_dwordx2 v[10:11], v[14:15], off
	s_nop 0
	s_waitcnt vmcnt(15)
	v_lshlrev_b32_e32 v14, 16, v220
	v_and_b32_e32 v15, 0xffff0000, v220
	v_div_scale_f32 v20, s[6:7], v22, v22, v14
	v_lshlrev_b32_e32 v16, 16, v221
	v_div_scale_f32 v24, s[6:7], v23, v23, v15
	v_rcp_f32_e32 v30, v20
	v_and_b32_e32 v17, 0xffff0000, v221
	v_div_scale_f32 v26, s[8:9], v12, v12, v16
	v_rcp_f32_e32 v31, v24
	v_div_scale_f32 v28, s[10:11], v13, v13, v17
	v_rcp_f32_e32 v32, v26
	v_rcp_f32_e32 v33, v28
	v_fma_f32 v34, -v20, v30, 1.0
	v_div_scale_f32 v21, vcc, v14, v22, v14
	v_fma_f32 v35, -v24, v31, 1.0
	v_fmac_f32_e32 v30, v34, v30
	v_div_scale_f32 v25, s[6:7], v15, v23, v15
	v_fma_f32 v36, -v26, v32, 1.0
	v_fmac_f32_e32 v31, v35, v31
	v_mul_f32_e32 v34, v21, v30
	v_div_scale_f32 v27, s[8:9], v16, v12, v16
	v_fma_f32 v37, -v28, v33, 1.0
	v_fmac_f32_e32 v32, v36, v32
	v_mul_f32_e32 v35, v25, v31
	v_fma_f32 v38, -v20, v34, v21
	v_div_scale_f32 v29, s[10:11], v17, v13, v17
	v_fmac_f32_e32 v33, v37, v33
	v_mul_f32_e32 v36, v27, v32
	v_fma_f32 v39, -v24, v35, v25
	v_fmac_f32_e32 v34, v38, v30
	v_mul_f32_e32 v37, v29, v33
	v_fma_f32 v40, -v26, v36, v27
	v_fmac_f32_e32 v35, v39, v31
	v_fma_f32 v20, -v20, v34, v21
	v_fma_f32 v41, -v28, v37, v29
	v_fmac_f32_e32 v36, v40, v32
	v_fma_f32 v21, -v24, v35, v25
	v_div_fmas_f32 v20, v20, v30, v34
	s_mov_b64 vcc, s[6:7]
	v_fmac_f32_e32 v37, v41, v33
	v_fma_f32 v24, -v26, v36, v27
	v_div_fixup_f32 v14, v20, v22, v14
	v_div_fmas_f32 v20, v21, v31, v35
	s_mov_b64 vcc, s[8:9]
	v_fma_f32 v25, -v28, v37, v29
	v_div_fixup_f32 v15, v20, v23, v15
	v_div_fmas_f32 v20, v24, v32, v36
	s_mov_b64 vcc, s[10:11]
	v_div_fixup_f32 v16, v20, v12, v16
	v_div_fmas_f32 v20, v25, v33, v37
	v_div_fixup_f32 v13, v20, v13, v17
	v_cvt_pk_bf16_f32 v12, v14, v15
	v_cvt_pk_bf16_f32 v13, v16, v13
	s_nop 0
	s_nop 0
	global_store_dwordx2 v[10:11], v[12:13], off offset:32
	s_nop 0
	s_waitcnt vmcnt(15)
; __device__ __forceinline__ unsigned cvt_pk_bf16(float lo, float hi) { unsigned r; asm volatile("v_cvt_pk_bf16_f32 %0, %1, %2" : "=v"(r) : "v"(lo), "v"(hi)); return r; }
; __device__ __forceinline__ float bflo(unsigned u) { return __uint_as_float(u << 16); }
; __device__ __forceinline__ float bfhi(unsigned u) { return __uint_as_float(u & 0xffff0000u); }
;     __device__ __forceinline__ void operator()(const f32x4 (&acc)[2][2][4][2], const Unit& u, int wr, int wc, int fr, int fq) const {
;         const int row0 = u.pm * BM + wr * 64 + fr, col0 = u.pn * BM + wc * 32 + 4 * fq;
; #pragma unroll
;         for (int ai = 0; ai < 2; ++ai)
; #pragma unroll
;             for (int m = 0; m < 4; ++m) { const size_t ro = (size_t)(row0 + ai * HALF + m * 16) * ldc + col0;
; #pragma unroll
;                 for (int bj = 0; bj < 2; ++bj)
; #pragma unroll
;                     for (int n = 0; n < 2; ++n) { const f32x4 a = acc[ai][bj][m][n]; const u32x2 yy = *(const u32x2*)(Y + ro + bj * HALF + n * 16);
;                         f32x4 v; v[0] = bflo(yy.x) / (1.0f + __expf(-a[0])); v[1] = bfhi(yy.x) / (1.0f + __expf(-a[1])); v[2] = bflo(yy.y) / (1.0f + __expf(-a[2])); v[3] = bfhi(yy.y) / (1.0f + __expf(-a[3]));
;                         u32x2 o; o.x = cvt_pk_bf16(v[0], v[1]); o.y = cvt_pk_bf16(v[2], v[3]); *(u32x2*)(C + ro + bj * HALF + n * 16) = o; } }
	v_lshlrev_b32_e32 v12, 16, v222
	v_and_b32_e32 v13, 0xffff0000, v222
	v_div_scale_f32 v16, s[6:7], v6, v6, v12
	v_lshlrev_b32_e32 v14, 16, v223
	v_div_scale_f32 v20, s[6:7], v7, v7, v13
	v_rcp_f32_e32 v26, v16
	v_and_b32_e32 v15, 0xffff0000, v223
	v_div_scale_f32 v22, s[8:9], v8, v8, v14
	v_rcp_f32_e32 v27, v20
	v_div_scale_f32 v24, s[10:11], v9, v9, v15
	v_rcp_f32_e32 v28, v22
	v_rcp_f32_e32 v29, v24
	v_fma_f32 v30, -v16, v26, 1.0
	v_div_scale_f32 v17, vcc, v12, v6, v12
	v_fma_f32 v31, -v20, v27, 1.0
	v_fmac_f32_e32 v26, v30, v26
	v_div_scale_f32 v21, s[6:7], v13, v7, v13
	v_fma_f32 v32, -v22, v28, 1.0
	v_fmac_f32_e32 v27, v31, v27
	v_mul_f32_e32 v30, v17, v26
	v_div_scale_f32 v23, s[8:9], v14, v8, v14
	v_fma_f32 v33, -v24, v29, 1.0
	v_fmac_f32_e32 v28, v32, v28
	v_mul_f32_e32 v31, v21, v27
	v_fma_f32 v34, -v16, v30, v17
	v_div_scale_f32 v25, s[10:11], v15, v9, v15
	v_fmac_f32_e32 v29, v33, v29
	v_mul_f32_e32 v32, v23, v28
	v_fma_f32 v35, -v20, v31, v21
	v_fmac_f32_e32 v30, v34, v26
	v_mul_f32_e32 v33, v25, v29
	v_fma_f32 v36, -v22, v32, v23
	v_fmac_f32_e32 v31, v35, v27
	v_fma_f32 v16, -v16, v30, v17
	v_fma_f32 v37, -v24, v33, v25
	v_fmac_f32_e32 v32, v36, v28
	v_fma_f32 v17, -v20, v31, v21
	v_div_fmas_f32 v16, v16, v26, v30
	s_mov_b64 vcc, s[6:7]
	v_fmac_f32_e32 v33, v37, v29
	v_fma_f32 v20, -v22, v32, v23
	v_div_fixup_f32 v6, v16, v6, v12
	v_div_fmas_f32 v12, v17, v27, v31
	s_mov_b64 vcc, s[8:9]
	v_fma_f32 v21, -v24, v33, v25
	v_div_fixup_f32 v7, v12, v7, v13
	v_div_fmas_f32 v12, v20, v28, v32
	s_mov_b64 vcc, s[10:11]
	v_div_fixup_f32 v8, v12, v8, v14
	v_div_fmas_f32 v12, v21, v29, v33
	v_cvt_pk_bf16_f32 v6, v6, v7
	v_div_fixup_f32 v7, v12, v9, v15
	v_cvt_pk_bf16_f32 v7, v8, v7
	s_nop 0
	s_nop 0
	global_store_dwordx2 v[10:11], v[6:7], off offset:256
	s_nop 0
	s_waitcnt vmcnt(15)
	v_lshlrev_b32_e32 v6, 16, v216
	v_and_b32_e32 v7, 0xffff0000, v216
	v_div_scale_f32 v12, s[6:7], v2, v2, v6
	v_lshlrev_b32_e32 v8, 16, v217
	v_div_scale_f32 v14, s[6:7], v3, v3, v7
	v_rcp_f32_e32 v20, v12
	v_and_b32_e32 v9, 0xffff0000, v217
	v_div_scale_f32 v16, s[8:9], v4, v4, v8
	v_rcp_f32_e32 v21, v14
	v_div_scale_f32 v18, s[10:11], v5, v5, v9
	v_rcp_f32_e32 v22, v16
	v_rcp_f32_e32 v23, v18
	v_fma_f32 v24, -v12, v20, 1.0
	v_div_scale_f32 v13, vcc, v6, v2, v6
	v_fma_f32 v25, -v14, v21, 1.0
	v_fmac_f32_e32 v20, v24, v20
	v_div_scale_f32 v15, s[6:7], v7, v3, v7
	v_fma_f32 v26, -v16, v22, 1.0
	v_fmac_f32_e32 v21, v25, v21
	v_mul_f32_e32 v24, v13, v20
	v_div_scale_f32 v17, s[8:9], v8, v4, v8
	v_fma_f32 v27, -v18, v23, 1.0
	v_fmac_f32_e32 v22, v26, v22
	v_mul_f32_e32 v25, v15, v21
	v_fma_f32 v28, -v12, v24, v13
	v_div_scale_f32 v19, s[10:11], v9, v5, v9
	v_fmac_f32_e32 v23, v27, v23
	v_mul_f32_e32 v26, v17, v22
	v_fma_f32 v29, -v14, v25, v15
	v_fmac_f32_e32 v24, v28, v20
	v_mul_f32_e32 v27, v19, v23
	v_fma_f32 v30, -v16, v26, v17
	v_fmac_f32_e32 v25, v29, v21
	v_fma_f32 v12, -v12, v24, v13
	v_fma_f32 v31, -v18, v27, v19
	v_fmac_f32_e32 v26, v30, v22
	v_fma_f32 v13, -v14, v25, v15
	v_div_fmas_f32 v12, v12, v20, v24
	s_mov_b64 vcc, s[6:7]
	v_fmac_f32_e32 v27, v31, v23
	v_fma_f32 v14, -v16, v26, v17
	v_div_fixup_f32 v2, v12, v2, v6
	v_div_fmas_f32 v6, v13, v21, v25
	s_mov_b64 vcc, s[8:9]
	v_fma_f32 v15, -v18, v27, v19
	v_div_fixup_f32 v3, v6, v3, v7
	v_div_fmas_f32 v6, v14, v22, v26
	s_mov_b64 vcc, s[10:11]
	v_div_fixup_f32 v4, v6, v4, v8
	v_div_fmas_f32 v6, v15, v23, v27
	v_cvt_pk_bf16_f32 v2, v2, v3
	s_andn2_b64 vcc, exec, s[4:5]
	v_div_fixup_f32 v3, v6, v5, v9
	s_mov_b64 s[4:5], -1
	v_cvt_pk_bf16_f32 v3, v4, v3
	global_store_dwordx2 v[10:11], v[2:3], off offset:288
	s_cbranch_vccnz .LBB0_675
	s_andn2_b64 vcc, exec, s[30:31]
	s_cbranch_vccnz .LBB0_674
	s_barrier
	s_branch .LBB0_674

; __device__ __forceinline__ unsigned cvt_pk_bf16(float lo, float hi) { unsigned r; asm volatile("v_cvt_pk_bf16_f32 %0, %1, %2" : "=v"(r) : "v"(lo), "v"(hi)); return r; }
;     __device__ __forceinline__ void operator()(const f32x4 (&acc)[2][2][4][2], const Unit& u, int wr, int wc, int fr, int fq) const {
;         const int row0 = u.pm * BM + wr * 64 + fr; const int col0 = u.pn * BM + wc * 32 + 8 * fq;
;         float cs[2][8];
; #pragma unroll
;         for (int bj = 0; bj < 2; ++bj) { const u32x4 c0 = *(const u32x4*)(cmax + col0 + bj * HALF), c1 = *(const u32x4*)(cmax + col0 + bj * HALF + 4);
; #pragma unroll
;             for (int e = 0; e < 4; ++e) { cs[bj][e] = __uint_as_float(c0[e] << 16) * (1.0f / 127.0f); cs[bj][4 + e] = __uint_as_float(c1[e] << 16) * (1.0f / 127.0f); } }
; #pragma unroll
;         for (int ai = 0; ai < 2; ++ai)
; #pragma unroll
;             for (int m = 0; m < 4; ++m) { const int row = row0 + ai * HALF + m * 16; bf16_t* rowp = O + (size_t)row * ldc + col0; const float rs = xs[row];
; #pragma unroll
;                 for (int bj = 0; bj < 2; ++bj) { const i32x4 i0 = __builtin_bit_cast(i32x4, acc[ai][bj][m][0]), i1 = __builtin_bit_cast(i32x4, acc[ai][bj][m][1]);
;                     float v[8];
; #pragma unroll
;                     for (int e = 0; e < 4; ++e) { v[e] = (float)i0[e] * rs * cs[bj][e]; v[4 + e] = (float)i1[e] * rs * cs[bj][4 + e]; }
;                     u32x4 w; w.x = cvt_pk_bf16(v[0], v[1]); w.y = cvt_pk_bf16(v[2], v[3]); w.z = cvt_pk_bf16(v[4], v[5]); w.w = cvt_pk_bf16(v[6], v[7]);
;                     *(u32x4*)(rowp + bj * HALF) = w; } }
.LBB0_722:
	v_lshl_or_b32 v170, s62, 8, v173
	v_ashrrev_i32_e32 v171, 31, v170
	v_lshl_add_u64 v[148:149], v[170:171], 2, s[16:17]
	global_load_dwordx4 v[154:157], v[148:149], off
	global_load_dwordx4 v[158:161], v[148:149], off offset:16
	global_load_dwordx4 v[162:165], v[148:149], off offset:512
	global_load_dwordx4 v[166:169], v[148:149], off offset:528
	v_lshl_add_u32 v148, s36, 8, v1
	v_ashrrev_i32_e32 v149, 31, v148
	v_lshl_add_u64 v[152:153], v[148:149], 2, s[10:11]
	global_load_dword v147, v[152:153], off
	v_cvt_f32_i32_e32 v179, v126
	v_cvt_f32_i32_e32 v127, v127
	v_cvt_f32_i32_e32 v181, v122
	v_cvt_f32_i32_e32 v123, v123
	v_cvt_f32_i32_e32 v183, v128
	v_cvt_f32_i32_e32 v185, v124
	v_cvt_f32_i32_e32 v129, v129
	v_cvt_f32_i32_e32 v187, v125
	v_cvt_f32_i32_e32 v188, v118
	v_cvt_f32_i32_e32 v194, v119
	v_mov_b64_e32 v[150:151], s[8:9]
	v_cvt_f32_i32_e32 v192, v114
	v_cvt_f32_i32_e32 v196, v115
	v_cvt_f32_i32_e32 v198, v120
	v_cvt_f32_i32_e32 v200, v116
	v_cvt_f32_i32_e32 v202, v121
	v_cvt_f32_i32_e32 v204, v117
	v_mad_i64_i32 v[116:117], s[34:35], v148, s61, v[150:151]
	v_lshlrev_b64 v[114:115], 1, v[170:171]
	v_mov_b32_e32 v191, v146
	v_lshl_add_u64 v[206:207], v[116:117], 0, v[114:115]
	v_cvt_f32_i32_e32 v110, v110
	v_cvt_f32_i32_e32 v111, v111
	v_cvt_f32_i32_e32 v112, v112
	v_cvt_f32_i32_e32 v108, v108
	v_cvt_f32_i32_e32 v113, v113
	v_cvt_f32_i32_e32 v109, v109
	v_cvt_f32_i32_e32 v100, v100
	v_cvt_f32_i32_e32 v101, v101
	v_cvt_f32_i32_e32 v94, v94
	v_cvt_f32_i32_e32 v95, v95
	v_cvt_f32_i32_e32 v96, v96
	v_cvt_f32_i32_e32 v92, v92
	v_cvt_f32_i32_e32 v97, v97
	v_cvt_f32_i32_e32 v93, v93
	v_cvt_f32_i32_e32 v84, v84
	v_cvt_f32_i32_e32 v85, v85
	v_cvt_f32_i32_e32 v78, v78
	v_cvt_f32_i32_e32 v74, v74
	v_cvt_f32_i32_e32 v79, v79
	v_cvt_f32_i32_e32 v75, v75
	v_cvt_f32_i32_e32 v80, v80
	v_cvt_f32_i32_e32 v76, v76
	v_cvt_f32_i32_e32 v81, v81
	v_cvt_f32_i32_e32 v77, v77
	v_cvt_f32_i32_e32 v72, v72
	v_cvt_f32_i32_e32 v68, v68
	v_cvt_f32_i32_e32 v73, v73
	v_cvt_f32_i32_e32 v69, v69
	v_cvt_f32_i32_e32 v62, v62
	v_cvt_f32_i32_e32 v58, v58
	v_cvt_f32_i32_e32 v63, v63
	v_cvt_f32_i32_e32 v59, v59
	v_cvt_f32_i32_e32 v64, v64
	v_cvt_f32_i32_e32 v60, v60
	v_cvt_f32_i32_e32 v65, v65
	v_cvt_f32_i32_e32 v61, v61
	v_cvt_f32_i32_e32 v56, v56
	v_cvt_f32_i32_e32 v52, v52
	v_cvt_f32_i32_e32 v57, v57
	v_cvt_f32_i32_e32 v53, v53
	v_cvt_f32_i32_e32 v46, v46
	v_cvt_f32_i32_e32 v42, v42
	v_cvt_f32_i32_e32 v47, v47
	v_cvt_f32_i32_e32 v43, v43
	v_cvt_f32_i32_e32 v48, v48
	v_cvt_f32_i32_e32 v44, v44
	v_cvt_f32_i32_e32 v49, v49
	v_cvt_f32_i32_e32 v45, v45
	v_cvt_f32_i32_e32 v40, v40
	v_cvt_f32_i32_e32 v36, v36
	v_or_b32_e32 v230, 16, v148
	v_ashrrev_i32_e32 v231, 31, v230
	v_lshl_add_u64 v[252:253], v[230:231], 2, s[10:11]
	global_load_dword v250, v[252:253], off
	v_or_b32_e32 v254, 32, v148
	v_ashrrev_i32_e32 v255, 31, v254
	v_lshl_add_u64 v[248:249], v[254:255], 2, s[10:11]
	global_load_dword v244, v[248:249], off
	v_or_b32_e32 v230, 48, v148
	v_ashrrev_i32_e32 v231, 31, v230
	v_lshl_add_u64 v[252:253], v[230:231], 2, s[10:11]
	global_load_dword v246, v[252:253], off
	global_load_dword v240, v[152:153], off offset:512
	global_load_dword v242, v[152:153], off offset:576
	global_load_dword v236, v[152:153], off offset:640
	global_load_dword v238, v[152:153], off offset:704
	s_nop 0
	s_waitcnt vmcnt(11)
	v_lshlrev_b32_e32 v178, 16, v154
	v_lshlrev_b32_e32 v126, 16, v155
	s_waitcnt vmcnt(10)
	v_lshlrev_b32_e32 v180, 16, v158
	v_lshlrev_b32_e32 v122, 16, v159
	v_lshlrev_b32_e32 v182, 16, v156
	v_lshlrev_b32_e32 v184, 16, v160
	v_lshlrev_b32_e32 v128, 16, v157
	v_lshlrev_b32_e32 v186, 16, v161
	s_waitcnt vmcnt(9)
	v_lshlrev_b32_e32 v189, 16, v162
	v_lshlrev_b32_e32 v195, 16, v163
	s_waitcnt vmcnt(7)
	v_mov_b32_e32 v190, v147
	v_pk_mul_f32 v[116:117], v[146:147], v[178:179]
	v_pk_mul_f32 v[120:121], v[146:147], v[126:127]
	v_lshlrev_b32_e32 v193, 16, v166
	v_lshlrev_b32_e32 v197, 16, v167
	v_lshlrev_b32_e32 v199, 16, v164
	v_lshlrev_b32_e32 v201, 16, v168
	v_lshlrev_b32_e32 v203, 16, v165
	v_lshlrev_b32_e32 v205, 16, v169
	v_pk_mul_f32 v[118:119], v[146:147], v[180:181]
	v_pk_mul_f32 v[122:123], v[146:147], v[122:123]
	v_pk_mul_f32 v[124:125], v[146:147], v[182:183]
	v_pk_mul_f32 v[126:127], v[146:147], v[184:185]
	v_pk_mul_f32 v[128:129], v[146:147], v[128:129]
	v_pk_mul_f32 v[154:155], v[146:147], v[186:187]
	v_pk_mul_f32 v[156:157], v[190:191], v[188:189]
	v_pk_mul_f32 v[160:161], v[190:191], v[194:195]
	v_mul_f32_e32 v117, v116, v117
	v_mul_f32_e32 v121, v120, v121
	v_cvt_pk_bf16_f32 v178, v117, v121
	v_pk_mul_f32 v[158:159], v[190:191], v[192:193]
	v_pk_mul_f32 v[162:163], v[190:191], v[196:197]
	v_pk_mul_f32 v[164:165], v[190:191], v[198:199]
	v_pk_mul_f32 v[166:167], v[190:191], v[200:201]
	v_pk_mul_f32 v[168:169], v[190:191], v[202:203]
	v_pk_mul_f32 v[170:171], v[190:191], v[204:205]
	v_mul_f32_e32 v119, v118, v119
	v_mul_f32_e32 v123, v122, v123
	v_mul_f32_e32 v125, v124, v125
	v_mul_f32_e32 v127, v126, v127
	v_mul_f32_e32 v129, v128, v129
	v_mul_f32_e32 v147, v154, v155
	v_mul_f32_e32 v149, v156, v157
	v_mul_f32_e32 v156, v160, v161
	v_cvt_pk_bf16_f32 v179, v125, v129
	v_cvt_pk_bf16_f32 v180, v119, v123
	v_cvt_pk_bf16_f32 v181, v127, v147
	global_store_dwordx4 v[206:207], v[178:181], off
	v_mul_f32_e32 v155, v158, v159
	v_mul_f32_e32 v158, v162, v163
	v_cvt_pk_bf16_f32 v178, v149, v156
	v_mul_f32_e32 v160, v164, v165
	v_mul_f32_e32 v162, v166, v167
	v_mul_f32_e32 v164, v168, v169
	v_mul_f32_e32 v166, v170, v171
	v_cvt_pk_bf16_f32 v179, v160, v164
	v_cvt_pk_bf16_f32 v180, v155, v158
	v_cvt_pk_bf16_f32 v181, v162, v166
	global_store_dwordx4 v[206:207], v[178:181], off offset:256
	v_cvt_f32_i32_e32 v119, v106
	v_cvt_f32_i32_e32 v121, v107
	v_or_b32_e32 v178, 16, v148
	v_ashrrev_i32_e32 v179, 31, v178
	v_lshl_add_u64 v[180:181], v[178:179], 2, s[10:11]
	s_nop 0
	v_cvt_f32_i32_e32 v123, v102
	v_cvt_f32_i32_e32 v125, v98
	v_cvt_f32_i32_e32 v127, v103
	v_cvt_f32_i32_e32 v129, v99
	v_cvt_f32_i32_e32 v147, v104
	v_cvt_f32_i32_e32 v149, v105
	v_or_b32_e32 v102, 32, v148
	v_mad_i64_i32 v[98:99], s[34:35], v178, s61, v[150:151]
	v_ashrrev_i32_e32 v103, 31, v102
	v_lshl_add_u64 v[104:105], v[98:99], 0, v[114:115]
	v_lshl_add_u64 v[106:107], v[102:103], 2, s[10:11]
	v_cvt_f32_i32_e32 v41, v41
	v_cvt_f32_i32_e32 v37, v37
	v_cvt_f32_i32_e32 v30, v30
	v_cvt_f32_i32_e32 v26, v26
	v_cvt_f32_i32_e32 v31, v31
	v_cvt_f32_i32_e32 v27, v27
	v_cvt_f32_i32_e32 v32, v32
	v_cvt_f32_i32_e32 v28, v28
	v_cvt_f32_i32_e32 v33, v33
	v_cvt_f32_i32_e32 v29, v29
	v_cvt_f32_i32_e32 v24, v24
	v_cvt_f32_i32_e32 v20, v20
	v_cvt_f32_i32_e32 v25, v25
	v_cvt_f32_i32_e32 v21, v21
	v_cvt_f32_i32_e32 v14, v14
	v_cvt_f32_i32_e32 v10, v10
	v_cvt_f32_i32_e32 v15, v15
	v_cvt_f32_i32_e32 v11, v11
	v_cvt_f32_i32_e32 v16, v16
	v_cvt_f32_i32_e32 v12, v12
	v_cvt_f32_i32_e32 v17, v17
	v_cvt_f32_i32_e32 v13, v13
	v_cvt_f32_i32_e32 v8, v8
	v_cvt_f32_i32_e32 v4, v4
	v_cvt_f32_i32_e32 v9, v9
	v_cvt_f32_i32_e32 v5, v5
	s_andn2_b64 vcc, exec, s[4:5]
	s_mov_b64 s[4:5], -1
	s_nop 0
	s_waitcnt vmcnt(8)
; __device__ __forceinline__ unsigned cvt_pk_bf16(float lo, float hi) { unsigned r; asm volatile("v_cvt_pk_bf16_f32 %0, %1, %2" : "=v"(r) : "v"(lo), "v"(hi)); return r; }
;     __device__ __forceinline__ void operator()(const f32x4 (&acc)[2][2][4][2], const Unit& u, int wr, int wc, int fr, int fq) const {
;     ...
;             for (int m = 0; m < 4; ++m) { const int row = row0 + ai * HALF + m * 16; bf16_t* rowp = O + (size_t)row * ldc + col0; const float rs = xs[row];
; #pragma unroll
;                 for (int bj = 0; bj < 2; ++bj) { const i32x4 i0 = __builtin_bit_cast(i32x4, acc[ai][bj][m][0]), i1 = __builtin_bit_cast(i32x4, acc[ai][bj][m][1]);
;                     float v[8];
; #pragma unroll
;                     for (int e = 0; e < 4; ++e) { v[e] = (float)i0[e] * rs * cs[bj][e]; v[4 + e] = (float)i1[e] * rs * cs[bj][4 + e]; }
;                     u32x4 w; w.x = cvt_pk_bf16(v[0], v[1]); w.y = cvt_pk_bf16(v[2], v[3]); w.z = cvt_pk_bf16(v[4], v[5]); w.w = cvt_pk_bf16(v[6], v[7]);
;                     *(u32x4*)(rowp + bj * HALF) = w; } }
	v_mul_f32_e32 v98, v250, v110
	v_mul_f32_e32 v99, v250, v119
	v_mul_f32_e32 v103, v250, v111
	v_mul_f32_e32 v110, v250, v121
	v_mul_f32_e32 v111, v250, v112
	v_mul_f32_e32 v108, v250, v108
	v_mul_f32_e32 v112, v250, v113
	v_mul_f32_e32 v109, v250, v109
	v_mul_f32_e32 v113, v250, v123
	v_mul_f32_e32 v119, v250, v125
	v_mul_f32_e32 v121, v250, v127
	v_mul_f32_e32 v123, v250, v129
	v_mul_f32_e32 v125, v250, v147
	v_mul_f32_e32 v100, v250, v100
	v_mul_f32_e32 v127, v250, v149
	v_mul_f32_e32 v101, v250, v101
	v_mul_f32_e32 v98, v116, v98
	v_mul_f32_e32 v117, v118, v99
	v_mul_f32_e32 v99, v120, v103
	v_mul_f32_e32 v103, v122, v110
	v_mul_f32_e32 v110, v124, v111
	v_mul_f32_e32 v108, v126, v108
	v_mul_f32_e32 v111, v128, v112
	v_mul_f32_e32 v109, v154, v109
	v_mul_f32_e32 v112, v157, v113
	v_mul_f32_e32 v113, v159, v119
	v_mul_f32_e32 v119, v161, v121
	v_mul_f32_e32 v121, v163, v123
	v_mul_f32_e32 v123, v165, v125
	v_mul_f32_e32 v125, v167, v100
	v_mul_f32_e32 v129, v171, v101
	v_cvt_pk_bf16_f32 v98, v98, v99
	v_cvt_pk_bf16_f32 v99, v110, v111
	v_cvt_pk_bf16_f32 v100, v117, v103
	v_cvt_pk_bf16_f32 v101, v108, v109
	v_mul_f32_e32 v127, v169, v127
	global_store_dwordx4 v[104:105], v[98:101], off
	v_cvt_f32_i32_e32 v103, v82
	s_nop 0
	v_cvt_pk_bf16_f32 v98, v112, v119
	v_cvt_pk_bf16_f32 v99, v123, v127
	v_cvt_pk_bf16_f32 v100, v113, v121
	v_cvt_pk_bf16_f32 v101, v125, v129
	global_store_dwordx4 v[104:105], v[98:101], off offset:256
	s_nop 0
	v_cvt_f32_i32_e32 v104, v87
	v_cvt_f32_i32_e32 v99, v90
	v_cvt_f32_i32_e32 v100, v91
	v_cvt_f32_i32_e32 v101, v86
	v_cvt_f32_i32_e32 v105, v83
	v_cvt_f32_i32_e32 v106, v88
	v_cvt_f32_i32_e32 v107, v89
	v_or_b32_e32 v86, 48, v148
	v_mad_i64_i32 v[82:83], s[34:35], v102, s61, v[150:151]
	v_ashrrev_i32_e32 v87, 31, v86
	v_lshl_add_u64 v[88:89], v[82:83], 0, v[114:115]
	v_lshl_add_u64 v[90:91], v[86:87], 2, s[10:11]
	s_nop 0
	s_waitcnt vmcnt(9)
	v_mul_f32_e32 v82, v244, v94
	v_mul_f32_e32 v83, v244, v99
	v_mul_f32_e32 v87, v244, v95
	v_mul_f32_e32 v94, v244, v100
	v_mul_f32_e32 v95, v244, v96
	v_mul_f32_e32 v92, v244, v92
	v_mul_f32_e32 v96, v244, v97
	v_mul_f32_e32 v93, v244, v93
	v_mul_f32_e32 v97, v244, v101
	v_mul_f32_e32 v99, v244, v103
	v_mul_f32_e32 v100, v244, v104
	v_mul_f32_e32 v101, v244, v105
	v_mul_f32_e32 v102, v244, v106
	v_mul_f32_e32 v84, v244, v84
	v_mul_f32_e32 v103, v244, v107
	v_mul_f32_e32 v85, v244, v85
	v_mul_f32_e32 v82, v116, v82
	v_mul_f32_e32 v98, v118, v83
	v_mul_f32_e32 v83, v120, v87
	v_mul_f32_e32 v87, v122, v94
	v_mul_f32_e32 v94, v124, v95
	v_mul_f32_e32 v92, v126, v92
	v_mul_f32_e32 v95, v128, v96
	v_mul_f32_e32 v93, v154, v93
	v_mul_f32_e32 v96, v157, v97
	v_mul_f32_e32 v97, v159, v99
	v_mul_f32_e32 v99, v161, v100
	v_mul_f32_e32 v100, v163, v101
	v_mul_f32_e32 v101, v165, v102
	v_mul_f32_e32 v102, v167, v84
	v_mul_f32_e32 v104, v171, v85
	v_cvt_pk_bf16_f32 v82, v82, v83
	v_cvt_pk_bf16_f32 v83, v94, v95
	v_cvt_pk_bf16_f32 v84, v98, v87
	v_cvt_pk_bf16_f32 v85, v92, v93
	v_mul_f32_e32 v103, v169, v103
	global_store_dwordx4 v[88:89], v[82:85], off
	v_cvt_f32_i32_e32 v87, v67
	s_nop 0
	v_cvt_pk_bf16_f32 v82, v96, v99
	v_cvt_pk_bf16_f32 v83, v101, v103
	v_cvt_pk_bf16_f32 v84, v97, v100
	v_cvt_pk_bf16_f32 v85, v102, v104
	global_store_dwordx4 v[88:89], v[82:85], off offset:256
	s_nop 0
	s_nop 0
	s_waitcnt vmcnt(10)
	v_mul_f32_e32 v75, v246, v75
	v_cvt_f32_i32_e32 v83, v70
	v_cvt_f32_i32_e32 v84, v66
	v_cvt_f32_i32_e32 v85, v71
	v_mad_i64_i32 v[66:67], s[34:35], v86, s61, v[150:151]
	v_lshl_add_u64 v[70:71], v[66:67], 0, v[114:115]
	v_mul_f32_e32 v66, v246, v78
	v_mul_f32_e32 v67, v246, v74
	v_mul_f32_e32 v74, v246, v79
	v_mul_f32_e32 v78, v246, v80
	v_mul_f32_e32 v76, v246, v76
	v_mul_f32_e32 v79, v246, v81
	v_mul_f32_e32 v77, v246, v77
	v_mul_f32_e32 v80, v246, v83
	v_mul_f32_e32 v81, v246, v84
	v_mul_f32_e32 v83, v246, v85
	v_mul_f32_e32 v84, v246, v87
	v_mul_f32_e32 v72, v246, v72
	v_mul_f32_e32 v68, v246, v68
	v_mul_f32_e32 v73, v246, v73
	v_mul_f32_e32 v69, v246, v69
	v_mul_f32_e32 v66, v116, v66
	v_mul_f32_e32 v82, v118, v67
	v_mul_f32_e32 v67, v120, v74
	v_mul_f32_e32 v74, v122, v75
	v_mul_f32_e32 v75, v124, v78
	v_mul_f32_e32 v76, v126, v76
	v_mul_f32_e32 v78, v128, v79
	v_mul_f32_e32 v77, v154, v77
	v_mul_f32_e32 v79, v157, v80
	v_mul_f32_e32 v80, v159, v81
	v_mul_f32_e32 v81, v161, v83
	v_mul_f32_e32 v83, v163, v84
	v_mul_f32_e32 v84, v167, v68
	v_mul_f32_e32 v85, v171, v69
	v_cvt_pk_bf16_f32 v66, v66, v67
	v_cvt_pk_bf16_f32 v67, v75, v78
	v_cvt_pk_bf16_f32 v68, v82, v74
	v_cvt_pk_bf16_f32 v69, v76, v77
	v_mul_f32_e32 v72, v165, v72
	v_mul_f32_e32 v73, v169, v73
	global_store_dwordx4 v[70:71], v[66:69], off
	s_nop 1
	v_cvt_pk_bf16_f32 v66, v79, v81
	v_cvt_pk_bf16_f32 v67, v72, v73
	v_cvt_pk_bf16_f32 v68, v80, v83
	v_cvt_pk_bf16_f32 v69, v84, v85
	global_store_dwordx4 v[70:71], v[66:69], off offset:256
	s_nop 0
	v_cvt_f32_i32_e32 v70, v51
	v_cvt_f32_i32_e32 v67, v54
	v_cvt_f32_i32_e32 v68, v50
	v_cvt_f32_i32_e32 v69, v55
	v_add_u32_e32 v50, 0x80, v148
	v_mad_i64_i32 v[50:51], s[34:35], v50, s61, v[150:151]
	v_lshl_add_u64 v[54:55], v[50:51], 0, v[114:115]
	s_nop 0
	s_waitcnt vmcnt(11)
; __device__ __forceinline__ unsigned cvt_pk_bf16(float lo, float hi) { unsigned r; asm volatile("v_cvt_pk_bf16_f32 %0, %1, %2" : "=v"(r) : "v"(lo), "v"(hi)); return r; }
;     __device__ __forceinline__ void operator()(const f32x4 (&acc)[2][2][4][2], const Unit& u, int wr, int wc, int fr, int fq) const {
;     ...
;             for (int m = 0; m < 4; ++m) { const int row = row0 + ai * HALF + m * 16; bf16_t* rowp = O + (size_t)row * ldc + col0; const float rs = xs[row];
; #pragma unroll
;                 for (int bj = 0; bj < 2; ++bj) { const i32x4 i0 = __builtin_bit_cast(i32x4, acc[ai][bj][m][0]), i1 = __builtin_bit_cast(i32x4, acc[ai][bj][m][1]);
;                     float v[8];
; #pragma unroll
;                     for (int e = 0; e < 4; ++e) { v[e] = (float)i0[e] * rs * cs[bj][e]; v[4 + e] = (float)i1[e] * rs * cs[bj][4 + e]; }
;                     u32x4 w; w.x = cvt_pk_bf16(v[0], v[1]); w.y = cvt_pk_bf16(v[2], v[3]); w.z = cvt_pk_bf16(v[4], v[5]); w.w = cvt_pk_bf16(v[6], v[7]);
;                     *(u32x4*)(rowp + bj * HALF) = w; } }
	v_mul_f32_e32 v50, v240, v62
	v_mul_f32_e32 v51, v240, v58
	v_mul_f32_e32 v58, v240, v63
	v_mul_f32_e32 v59, v240, v59
	v_mul_f32_e32 v62, v240, v64
	v_mul_f32_e32 v60, v240, v60
	v_mul_f32_e32 v63, v240, v65
	v_mul_f32_e32 v61, v240, v61
	v_mul_f32_e32 v64, v240, v67
	v_mul_f32_e32 v65, v240, v68
	v_mul_f32_e32 v67, v240, v69
	v_mul_f32_e32 v68, v240, v70
	v_mul_f32_e32 v56, v240, v56
	v_mul_f32_e32 v52, v240, v52
	v_mul_f32_e32 v57, v240, v57
	v_mul_f32_e32 v53, v240, v53
	v_mul_f32_e32 v50, v116, v50
	v_mul_f32_e32 v66, v118, v51
	v_mul_f32_e32 v51, v120, v58
	v_mul_f32_e32 v58, v122, v59
	v_mul_f32_e32 v59, v124, v62
	v_mul_f32_e32 v60, v126, v60
	v_mul_f32_e32 v62, v128, v63
	v_mul_f32_e32 v61, v154, v61
	v_mul_f32_e32 v63, v157, v64
	v_mul_f32_e32 v64, v159, v65
	v_mul_f32_e32 v65, v161, v67
	v_mul_f32_e32 v67, v163, v68
	v_mul_f32_e32 v68, v167, v52
	v_mul_f32_e32 v69, v171, v53
	v_cvt_pk_bf16_f32 v50, v50, v51
	v_cvt_pk_bf16_f32 v51, v59, v62
	v_cvt_pk_bf16_f32 v52, v66, v58
	v_cvt_pk_bf16_f32 v53, v60, v61
	v_mul_f32_e32 v56, v165, v56
	v_mul_f32_e32 v57, v169, v57
	global_store_dwordx4 v[54:55], v[50:53], off
	s_nop 1
	v_cvt_pk_bf16_f32 v50, v63, v65
	v_cvt_pk_bf16_f32 v51, v56, v57
	v_cvt_pk_bf16_f32 v52, v64, v67
	v_cvt_pk_bf16_f32 v53, v68, v69
	global_store_dwordx4 v[54:55], v[50:53], off offset:256
	s_nop 0
	v_cvt_f32_i32_e32 v54, v35
	v_cvt_f32_i32_e32 v51, v38
	v_cvt_f32_i32_e32 v52, v34
	v_cvt_f32_i32_e32 v53, v39
	v_add_u32_e32 v34, 0x90, v148
	v_mad_i64_i32 v[34:35], s[34:35], v34, s61, v[150:151]
	v_lshl_add_u64 v[38:39], v[34:35], 0, v[114:115]
	s_nop 0
	s_waitcnt vmcnt(12)
	v_mul_f32_e32 v34, v242, v46
	v_mul_f32_e32 v35, v242, v42
	v_mul_f32_e32 v42, v242, v47
	v_mul_f32_e32 v43, v242, v43
	v_mul_f32_e32 v46, v242, v48
	v_mul_f32_e32 v44, v242, v44
	v_mul_f32_e32 v47, v242, v49
	v_mul_f32_e32 v45, v242, v45
	v_mul_f32_e32 v48, v242, v51
	v_mul_f32_e32 v49, v242, v52
	v_mul_f32_e32 v51, v242, v53
	v_mul_f32_e32 v52, v242, v54
	v_mul_f32_e32 v40, v242, v40
	v_mul_f32_e32 v36, v242, v36
	v_mul_f32_e32 v41, v242, v41
	v_mul_f32_e32 v37, v242, v37
	v_mul_f32_e32 v34, v116, v34
	v_mul_f32_e32 v50, v118, v35
	v_mul_f32_e32 v35, v120, v42
	v_mul_f32_e32 v42, v122, v43
	v_mul_f32_e32 v43, v124, v46
	v_mul_f32_e32 v44, v126, v44
	v_mul_f32_e32 v46, v128, v47
	v_mul_f32_e32 v45, v154, v45
	v_mul_f32_e32 v47, v157, v48
	v_mul_f32_e32 v48, v159, v49
	v_mul_f32_e32 v49, v161, v51
	v_mul_f32_e32 v51, v163, v52
	v_mul_f32_e32 v52, v167, v36
	v_mul_f32_e32 v53, v171, v37
	v_cvt_pk_bf16_f32 v34, v34, v35
	v_cvt_pk_bf16_f32 v35, v43, v46
	v_cvt_pk_bf16_f32 v36, v50, v42
	v_cvt_pk_bf16_f32 v37, v44, v45
	v_mul_f32_e32 v40, v165, v40
	v_mul_f32_e32 v41, v169, v41
	global_store_dwordx4 v[38:39], v[34:37], off
	s_nop 1
	v_cvt_pk_bf16_f32 v34, v47, v49
	v_cvt_pk_bf16_f32 v35, v40, v41
	v_cvt_pk_bf16_f32 v36, v48, v51
	v_cvt_pk_bf16_f32 v37, v52, v53
	global_store_dwordx4 v[38:39], v[34:37], off offset:256
	s_nop 0
	v_cvt_f32_i32_e32 v38, v19
	v_cvt_f32_i32_e32 v35, v22
	v_cvt_f32_i32_e32 v36, v18
	v_cvt_f32_i32_e32 v37, v23
	v_add_u32_e32 v18, 0xa0, v148
	v_mad_i64_i32 v[18:19], s[34:35], v18, s61, v[150:151]
	v_lshl_add_u64 v[22:23], v[18:19], 0, v[114:115]
	s_nop 0
	s_waitcnt vmcnt(13)
	v_mul_f32_e32 v18, v236, v30
	v_mul_f32_e32 v19, v236, v26
	v_mul_f32_e32 v26, v236, v31
	v_mul_f32_e32 v27, v236, v27
	v_mul_f32_e32 v30, v236, v32
	v_mul_f32_e32 v28, v236, v28
	v_mul_f32_e32 v31, v236, v33
	v_mul_f32_e32 v29, v236, v29
	v_mul_f32_e32 v32, v236, v35
	v_mul_f32_e32 v33, v236, v36
	v_mul_f32_e32 v35, v236, v37
	v_mul_f32_e32 v36, v236, v38
	v_mul_f32_e32 v24, v236, v24
	v_mul_f32_e32 v20, v236, v20
	v_mul_f32_e32 v25, v236, v25
	v_mul_f32_e32 v21, v236, v21
	v_mul_f32_e32 v18, v116, v18
	v_mul_f32_e32 v34, v118, v19
	v_mul_f32_e32 v19, v120, v26
	v_mul_f32_e32 v26, v122, v27
	v_mul_f32_e32 v27, v124, v30
	v_mul_f32_e32 v28, v126, v28
	v_mul_f32_e32 v30, v128, v31
	v_mul_f32_e32 v29, v154, v29
	v_mul_f32_e32 v31, v157, v32
	v_mul_f32_e32 v32, v159, v33
	v_mul_f32_e32 v33, v161, v35
	v_mul_f32_e32 v35, v163, v36
	v_mul_f32_e32 v36, v167, v20
	v_mul_f32_e32 v37, v171, v21
	v_cvt_pk_bf16_f32 v18, v18, v19
	v_cvt_pk_bf16_f32 v19, v27, v30
	v_cvt_pk_bf16_f32 v20, v34, v26
	v_cvt_pk_bf16_f32 v21, v28, v29
	v_mul_f32_e32 v24, v165, v24
	v_mul_f32_e32 v25, v169, v25
	global_store_dwordx4 v[22:23], v[18:21], off
	s_nop 1
	v_cvt_pk_bf16_f32 v18, v31, v33
	v_cvt_pk_bf16_f32 v19, v24, v25
	v_cvt_pk_bf16_f32 v20, v32, v35
	v_cvt_pk_bf16_f32 v21, v36, v37
	global_store_dwordx4 v[22:23], v[18:21], off offset:256
	s_nop 0
	v_cvt_f32_i32_e32 v22, v3
	v_cvt_f32_i32_e32 v19, v6
	v_cvt_f32_i32_e32 v20, v2
	v_cvt_f32_i32_e32 v21, v7
	v_add_u32_e32 v2, 0xb0, v148
	v_mad_i64_i32 v[2:3], s[34:35], v2, s61, v[150:151]
	v_lshl_add_u64 v[6:7], v[2:3], 0, v[114:115]
	s_nop 0
	s_waitcnt vmcnt(14)
	v_mul_f32_e32 v2, v238, v14
	v_mul_f32_e32 v3, v238, v10
	v_mul_f32_e32 v10, v238, v15
	v_mul_f32_e32 v11, v238, v11
	v_mul_f32_e32 v14, v238, v16
	v_mul_f32_e32 v12, v238, v12
	v_mul_f32_e32 v15, v238, v17
	v_mul_f32_e32 v13, v238, v13
	v_mul_f32_e32 v16, v238, v19
	v_mul_f32_e32 v17, v238, v20
	v_mul_f32_e32 v19, v238, v21
	v_mul_f32_e32 v20, v238, v22
	v_mul_f32_e32 v8, v238, v8
	v_mul_f32_e32 v4, v238, v4
	v_mul_f32_e32 v9, v238, v9
	v_mul_f32_e32 v5, v238, v5
	v_mul_f32_e32 v2, v116, v2
	v_mul_f32_e32 v18, v118, v3
	v_mul_f32_e32 v3, v120, v10
	v_mul_f32_e32 v10, v122, v11
	v_mul_f32_e32 v11, v124, v14
	v_mul_f32_e32 v12, v126, v12
	v_mul_f32_e32 v14, v128, v15
	v_mul_f32_e32 v13, v154, v13
	v_mul_f32_e32 v15, v157, v16
	v_mul_f32_e32 v16, v159, v17
	v_mul_f32_e32 v17, v161, v19
	v_mul_f32_e32 v19, v163, v20
	v_mul_f32_e32 v20, v167, v4
	v_mul_f32_e32 v21, v171, v5
	v_cvt_pk_bf16_f32 v2, v2, v3
	v_cvt_pk_bf16_f32 v3, v11, v14
	v_cvt_pk_bf16_f32 v4, v18, v10
	v_cvt_pk_bf16_f32 v5, v12, v13
	v_mul_f32_e32 v8, v165, v8
	v_mul_f32_e32 v9, v169, v9
	global_store_dwordx4 v[6:7], v[2:5], off
	s_nop 1
	v_cvt_pk_bf16_f32 v2, v15, v17
	v_cvt_pk_bf16_f32 v3, v8, v9
	v_cvt_pk_bf16_f32 v4, v16, v19
	v_cvt_pk_bf16_f32 v5, v20, v21
	global_store_dwordx4 v[6:7], v[2:5], off offset:256
	s_cbranch_vccnz .LBB0_711
	s_andn2_b64 vcc, exec, s[6:7]
	s_cbranch_vccnz .LBB0_710
	s_barrier
	s_branch .LBB0_710

; __device__ __forceinline__ unsigned cvt_pk_bf16(float lo, float hi) { unsigned r; asm volatile("v_cvt_pk_bf16_f32 %0, %1, %2" : "=v"(r) : "v"(lo), "v"(hi)); return r; }
;     __device__ __forceinline__ void operator()(const f32x4 (&acc)[2][2][4][2], const Unit& u, int wr, int wc, int fr, int fq) const {
;     ...
;         f32x4 cs[2][2];
; #pragma unroll
;         for (int bj = 0; bj < 2; ++bj)
; #pragma unroll
;             for (int n = 0; n < 2; ++n) { const u32x4 c = *(const u32x4*)(cmax + col0 + bj * HALF + n * 4);
;                 cs[bj][n] = (f32x4){__uint_as_float(c.x << 16), __uint_as_float(c.y << 16), __uint_as_float(c.z << 16), __uint_as_float(c.w << 16)} * (1.0f / 127.0f); }
; #pragma unroll
;         for (int ai = 0; ai < 2; ++ai)
; #pragma unroll
;             for (int m = 0; m < 4; ++m) { const int row = row0 + ai * HALF + m * 16; const size_t ro = (size_t)row * ldc + col0; float ss = 0.f; const float rs = xs[row];
; #pragma unroll
;                 for (int bj = 0; bj < 2; ++bj)
; #pragma unroll
;                     for (int n = 0; n < 2; ++n) { const i32x4 ia = __builtin_bit_cast(i32x4, acc[ai][bj][m][n]);
;                         const f32x4 af = (f32x4){(float)ia[0], (float)ia[1], (float)ia[2], (float)ia[3]} * rs * cs[bj][n];
;                         f32x4 rv; if constexpr (RB16) { const u32x2 rb = *(const u32x2*)((const bf16_t*)R + ro + bj * HALF + n * 4); rv = (f32x4){__uint_as_float(rb.x << 16), __uint_as_float(rb.x & 0xffff0000u), __uint_as_float(rb.y << 16), __uint_as_float(rb.y & 0xffff0000u)}; }
;                         else rv = *(const f32x4*)((const float*)R + ro + bj * HALF + n * 4);
;                         const f32x4 v = af + rv; { u32x2 hb; hb.x = cvt_pk_bf16(v[0], v[1]); hb.y = cvt_pk_bf16(v[2], v[3]); *(u32x2*)(C + ro + bj * HALF + n * 4) = hb; }
;                         const f32x4 g = *(const f32x4*)(gain + col0 + bj * HALF + n * 4);
;                         u32x2 o; o.x = cvt_pk_bf16(v[0] * g[0], v[1] * g[1]); o.y = cvt_pk_bf16(v[2] * g[2], v[3] * g[3]); *(u32x2*)(HG + ro + bj * HALF + n * 4) = o;
;                         ss += (v[0] * v[0] + v[1] * v[1]) + (v[2] * v[2] + v[3] * v[3]); }
.LBB0_881:
	v_lshl_or_b32 v146, s14, 8, v157
	v_ashrrev_i32_e32 v147, 31, v146
	v_lshl_add_u32 v148, s50, 8, v1
	v_lshlrev_b64 v[166:167], 2, v[146:147]
	v_ashrrev_i32_e32 v149, 31, v148
	v_lshl_add_u64 v[174:175], s[28:29], 0, v[166:167]
	v_lshlrev_b64 v[162:163], 12, v[148:149]
	global_load_dwordx4 v[152:155], v[174:175], off
	v_lshl_add_u64 v[150:151], v[148:149], 2, s[24:25]
	v_lshl_add_u64 v[180:181], v[162:163], 0, v[146:147]
	global_load_dword v178, v[150:151], off
	v_lshl_add_u64 v[182:183], v[180:181], 2, s[10:11]
	global_load_dwordx4 v[162:165], v[182:183], off
	v_cvt_f32_i32_e32 v129, v129
	v_cvt_f32_i32_e32 v128, v128
	v_cvt_f32_i32_e32 v185, v127
	v_cvt_f32_i32_e32 v184, v126
	v_lshlrev_b64 v[180:181], 1, v[180:181]
	v_lshl_add_u64 v[186:187], s[18:19], 0, v[180:181]
	v_lshl_add_u64 v[126:127], s[12:13], 0, v[166:167]
	global_load_dwordx4 v[166:169], v[174:175], off offset:528
	global_load_dwordx4 v[170:173], v[174:175], off offset:16
	s_nop 0
	global_load_dwordx4 v[174:177], v[174:175], off offset:512
	v_lshl_add_u64 v[180:181], s[20:21], 0, v[180:181]
	v_cvt_f32_i32_e32 v125, v125
	v_cvt_f32_i32_e32 v124, v124
	v_cvt_f32_i32_e32 v123, v123
	v_cvt_f32_i32_e32 v122, v122
	v_cvt_f32_i32_e32 v121, v121
	v_cvt_f32_i32_e32 v120, v120
	v_cvt_f32_i32_e32 v119, v119
	v_cvt_f32_i32_e32 v118, v118
	v_cvt_f32_i32_e32 v117, v117
	v_cvt_f32_i32_e32 v116, v116
	v_cvt_f32_i32_e32 v115, v115
	v_cvt_f32_i32_e32 v114, v114
	s_lshl_b32 s50, s14, 2
	s_ashr_i32 s51, s50, 31
	global_load_dwordx4 v[192:195], v[126:127], off
	global_load_dwordx4 v[196:199], v[182:183], off offset:16
	global_load_dwordx4 v[200:203], v[126:127], off offset:16
	global_load_dwordx4 v[204:207], v[182:183], off offset:512
	global_load_dwordx4 v[208:211], v[126:127], off offset:512
	global_load_dwordx4 v[212:215], v[182:183], off offset:528
	global_load_dwordx4 v[216:219], v[126:127], off offset:528
	v_or_b32_e32 v230, 16, v148
	v_ashrrev_i32_e32 v231, 31, v230
	v_lshl_add_u64 v[252:253], v[230:231], 2, s[24:25]
	global_load_dword v250, v[252:253], off
	v_or_b32_e32 v254, 16, v148
	v_ashrrev_i32_e32 v255, 31, v254
	v_lshlrev_b64 v[248:249], 12, v[254:255]
	v_lshl_add_u64 v[230:231], v[248:249], 0, v[146:147]
	v_lshl_add_u64 v[252:253], v[230:231], 2, s[10:11]
	global_load_dwordx4 v[220:223], v[252:253], off
	global_load_dwordx4 v[224:227], v[252:253], off offset:16
	global_load_dwordx4 v[232:235], v[252:253], off offset:512
	global_load_dwordx4 v[236:239], v[252:253], off offset:528
	s_nop 0
	s_waitcnt vmcnt(17)
	v_lshlrev_b32_e32 v152, 16, v152
	v_lshlrev_b32_e32 v153, 16, v153
	v_lshlrev_b32_e32 v154, 16, v154
	v_lshlrev_b32_e32 v155, 16, v155
	s_waitcnt vmcnt(16)
	v_pk_mul_f32 v[184:185], v[178:179], v[184:185] op_sel_hi:[0,1]
	v_pk_mul_f32 v[188:189], v[178:179], v[128:129] op_sel_hi:[0,1]
	v_pk_mul_f32 v[128:129], v[154:155], s[38:39] op_sel_hi:[1,0]
	v_pk_mul_f32 v[152:153], v[152:153], s[38:39] op_sel_hi:[1,0]
	s_waitcnt vmcnt(15)
	v_pk_fma_f32 v[154:155], v[188:189], v[128:129], v[164:165]
	v_pk_fma_f32 v[184:185], v[184:185], v[152:153], v[162:163]
	v_pk_mul_f32 v[188:189], v[178:179], v[122:123] op_sel_hi:[0,1]
	v_cvt_pk_bf16_f32 v162, v184, v185
	v_cvt_pk_bf16_f32 v163, v154, v155
	global_store_dwordx2 v[186:187], v[162:163], off
	s_nop 0
	s_waitcnt vmcnt(14)
	v_lshlrev_b32_e32 v170, 16, v170
	v_lshlrev_b32_e32 v171, 16, v171
	v_lshlrev_b32_e32 v172, 16, v172
	v_lshlrev_b32_e32 v173, 16, v173
	v_pk_mul_f32 v[190:191], v[178:179], v[124:125] op_sel_hi:[0,1]
	v_pk_mul_f32 v[122:123], v[172:173], s[38:39] op_sel_hi:[1,0]
	v_pk_mul_f32 v[124:125], v[170:171], s[38:39] op_sel_hi:[1,0]
	s_waitcnt vmcnt(13)
	v_lshlrev_b32_e32 v174, 16, v174
	v_lshlrev_b32_e32 v175, 16, v175
	v_lshlrev_b32_e32 v176, 16, v176
	v_lshlrev_b32_e32 v177, 16, v177
	v_lshlrev_b32_e32 v166, 16, v166
	v_lshlrev_b32_e32 v167, 16, v167
	v_lshlrev_b32_e32 v168, 16, v168
	v_lshlrev_b32_e32 v169, 16, v169
	s_nop 0
	s_waitcnt vmcnt(12)
	v_mul_f32_e32 v162, v192, v184
	v_mul_f32_e32 v163, v193, v185
	v_mul_f32_e32 v164, v194, v154
	v_mul_f32_e32 v165, v195, v155
	v_cvt_pk_bf16_f32 v162, v162, v163
	v_cvt_pk_bf16_f32 v163, v164, v165
	global_store_dwordx2 v[180:181], v[162:163], off
	s_nop 0
	v_mul_f32_e32 v155, v155, v155
	v_fmac_f32_e32 v155, v154, v154
	s_nop 0
	s_waitcnt vmcnt(12)
	v_pk_fma_f32 v[170:171], v[190:191], v[122:123], v[198:199]
	v_pk_fma_f32 v[172:173], v[188:189], v[124:125], v[196:197]
	v_pk_mul_f32 v[188:189], v[178:179], v[118:119] op_sel_hi:[0,1]
	v_cvt_pk_bf16_f32 v162, v172, v173
	v_cvt_pk_bf16_f32 v163, v170, v171
	global_store_dwordx2 v[186:187], v[162:163], off offset:8
	s_nop 0
	v_pk_mul_f32 v[190:191], v[178:179], v[120:121] op_sel_hi:[0,1]
	v_pk_mul_f32 v[118:119], v[176:177], s[38:39] op_sel_hi:[1,0]
	v_pk_mul_f32 v[120:121], v[174:175], s[38:39] op_sel_hi:[1,0]
	s_nop 0
	s_waitcnt vmcnt(12)
	v_mul_f32_e32 v162, v172, v200
	v_mul_f32_e32 v163, v173, v201
	v_mul_f32_e32 v164, v170, v202
	v_mul_f32_e32 v165, v171, v203
	v_cvt_pk_bf16_f32 v162, v162, v163
	v_cvt_pk_bf16_f32 v163, v164, v165
	global_store_dwordx2 v[180:181], v[162:163], off offset:8
	s_nop 0
	v_mul_f32_e32 v171, v171, v171
	v_fmac_f32_e32 v171, v170, v170
	s_nop 0
	s_waitcnt vmcnt(12)
	v_pk_fma_f32 v[174:175], v[190:191], v[118:119], v[206:207]
	v_pk_fma_f32 v[176:177], v[188:189], v[120:121], v[204:205]
	v_mul_f32_e32 v170, v175, v175
	v_cvt_pk_bf16_f32 v162, v176, v177
	v_cvt_pk_bf16_f32 v163, v174, v175
	global_store_dwordx2 v[186:187], v[162:163], off offset:256
	s_nop 0
	v_fmac_f32_e32 v170, v174, v174
	s_nop 0
	s_waitcnt vmcnt(12)
; __device__ __forceinline__ unsigned cvt_pk_bf16(float lo, float hi) { unsigned r; asm volatile("v_cvt_pk_bf16_f32 %0, %1, %2" : "=v"(r) : "v"(lo), "v"(hi)); return r; }
;     __device__ __forceinline__ void operator()(const f32x4 (&acc)[2][2][4][2], const Unit& u, int wr, int wc, int fr, int fq) const {
;     ...
;             for (int m = 0; m < 4; ++m) { const int row = row0 + ai * HALF + m * 16; const size_t ro = (size_t)row * ldc + col0; float ss = 0.f; const float rs = xs[row];
; #pragma unroll
;                 for (int bj = 0; bj < 2; ++bj)
; #pragma unroll
;                     for (int n = 0; n < 2; ++n) { const i32x4 ia = __builtin_bit_cast(i32x4, acc[ai][bj][m][n]);
;                         const f32x4 af = (f32x4){(float)ia[0], (float)ia[1], (float)ia[2], (float)ia[3]} * rs * cs[bj][n];
;                         f32x4 rv; if constexpr (RB16) { const u32x2 rb = *(const u32x2*)((const bf16_t*)R + ro + bj * HALF + n * 4); rv = (f32x4){__uint_as_float(rb.x << 16), __uint_as_float(rb.x & 0xffff0000u), __uint_as_float(rb.y << 16), __uint_as_float(rb.y & 0xffff0000u)}; }
;                         else rv = *(const f32x4*)((const float*)R + ro + bj * HALF + n * 4);
;                         const f32x4 v = af + rv; { u32x2 hb; hb.x = cvt_pk_bf16(v[0], v[1]); hb.y = cvt_pk_bf16(v[2], v[3]); *(u32x2*)(C + ro + bj * HALF + n * 4) = hb; }
;                         const f32x4 g = *(const f32x4*)(gain + col0 + bj * HALF + n * 4);
;                         u32x2 o; o.x = cvt_pk_bf16(v[0] * g[0], v[1] * g[1]); o.y = cvt_pk_bf16(v[2] * g[2], v[3] * g[3]); *(u32x2*)(HG + ro + bj * HALF + n * 4) = o;
;                         ss += (v[0] * v[0] + v[1] * v[1]) + (v[2] * v[2] + v[3] * v[3]); }
;                 ss += __shfl_xor(ss, 16); ss += __shfl_xor(ss, 32);
;                 if (fq == 0) SS[(size_t)row * 64 + u.pn * 4 + wc] = ss; }
	v_mul_f32_e32 v162, v176, v208
	v_mul_f32_e32 v163, v177, v209
	v_mul_f32_e32 v164, v174, v210
	v_mul_f32_e32 v165, v175, v211
	v_cvt_pk_bf16_f32 v162, v162, v163
	v_cvt_pk_bf16_f32 v163, v164, v165
	global_store_dwordx2 v[180:181], v[162:163], off offset:256
	s_nop 0
	v_pk_mul_f32 v[182:183], v[178:179], v[114:115] op_sel_hi:[0,1]
	v_pk_mul_f32 v[178:179], v[178:179], v[116:117] op_sel_hi:[0,1]
	v_pk_mul_f32 v[114:115], v[168:169], s[38:39] op_sel_hi:[1,0]
	v_pk_mul_f32 v[116:117], v[166:167], s[38:39] op_sel_hi:[1,0]
	s_nop 0
	s_waitcnt vmcnt(12)
	v_pk_fma_f32 v[168:169], v[178:179], v[114:115], v[214:215]
	v_pk_fma_f32 v[178:179], v[182:183], v[116:117], v[212:213]
	v_mul_f32_e32 v183, v185, v185
	v_cvt_pk_bf16_f32 v162, v178, v179
	v_cvt_pk_bf16_f32 v163, v168, v169
	global_store_dwordx2 v[186:187], v[162:163], off offset:264
	s_nop 0
	v_fmac_f32_e32 v183, v184, v184
	v_add_f32_e32 v154, v183, v155
	v_mul_f32_e32 v155, v173, v173
	v_fmac_f32_e32 v155, v172, v172
	v_add_f32_e32 v155, v155, v171
	v_add_f32_e32 v154, v154, v155
	v_mul_f32_e32 v155, v177, v177
	v_fmac_f32_e32 v155, v176, v176
	v_and_b32_e32 v163, 64, v161
	v_add_f32_e32 v155, v155, v170
	v_xor_b32_e32 v162, 16, v161
	v_add_u32_e32 v163, 64, v163
	v_add_f32_e32 v154, v154, v155
	v_mul_f32_e32 v155, v179, v179
	v_mul_f32_e32 v170, v169, v169
	v_cmp_lt_i32_e32 vcc, v162, v163
	v_fmac_f32_e32 v155, v178, v178
	v_fmac_f32_e32 v170, v168, v168
	v_cndmask_b32_e32 v162, v161, v162, vcc
	v_add_f32_e32 v155, v155, v170
	v_lshlrev_b32_e32 v162, 2, v162
	v_add_f32_e32 v154, v154, v155
	ds_bpermute_b32 v155, v162, v154
	v_xor_b32_e32 v182, 32, v161
	v_cmp_lt_i32_e32 vcc, v182, v163
	s_waitcnt lgkmcnt(0)
	v_add_f32_e32 v154, v154, v155
	v_cndmask_b32_e32 v163, v161, v182, vcc
	v_lshlrev_b32_e32 v163, 2, v163
	ds_bpermute_b32 v155, v163, v154
	s_nop 0
	s_waitcnt vmcnt(12)
	v_mul_f32_e32 v164, v178, v216
	v_mul_f32_e32 v165, v179, v217
	v_mul_f32_e32 v166, v168, v218
	v_mul_f32_e32 v167, v169, v219
	v_cvt_pk_bf16_f32 v164, v164, v165
	v_cvt_pk_bf16_f32 v165, v166, v167
	global_store_dwordx2 v[180:181], v[164:165], off offset:264
	s_and_saveexec_b64 s[52:53], s[4:5]
	s_cbranch_execz .LBB0_883
	s_waitcnt lgkmcnt(0)
	v_add_f32_e32 v164, v154, v155
	v_lshlrev_b64 v[154:155], 8, v[148:149]
	v_lshl_add_u64 v[154:155], s[22:23], 0, v[154:155]
	v_lshl_add_u64 v[154:155], s[50:51], 2, v[154:155]
	s_lshl_b32 s14, s66, 2
	v_lshl_add_u64 v[154:155], v[154:155], 0, s[14:15]
	global_store_dword v[154:155], v164, off
.LBB0_883:
	s_or_b64 exec, exec, s[52:53]
	v_or_b32_e32 v254, 32, v148
	v_ashrrev_i32_e32 v255, 31, v254
	v_lshl_add_u64 v[248:249], v[254:255], 2, s[24:25]
	global_load_dword v212, v[248:249], off
	v_or_b32_e32 v230, 32, v148
	v_ashrrev_i32_e32 v231, 31, v230
	v_lshlrev_b64 v[252:253], 12, v[230:231]
	v_lshl_add_u64 v[254:255], v[252:253], 0, v[146:147]
	v_lshl_add_u64 v[248:249], v[254:255], 2, s[10:11]
	global_load_dwordx4 v[240:243], v[248:249], off
	global_load_dwordx4 v[244:247], v[248:249], off offset:16
	global_load_dwordx4 v[196:199], v[248:249], off offset:512
	global_load_dwordx4 v[204:207], v[248:249], off offset:528
	v_or_b32_e32 v154, 16, v148
	s_waitcnt lgkmcnt(0)
	v_ashrrev_i32_e32 v155, 31, v154
	v_lshlrev_b64 v[164:165], 12, v[154:155]
	v_lshl_add_u64 v[168:169], v[164:165], 0, v[146:147]
	v_lshl_add_u64 v[164:165], v[154:155], 2, s[24:25]
	s_nop 0
	v_lshl_add_u64 v[172:173], v[168:169], 2, s[10:11]
	s_nop 0
	v_cvt_f32_i32_e32 v113, v113
	v_cvt_f32_i32_e32 v111, v111
	v_cvt_f32_i32_e32 v110, v110
	v_cvt_f32_i32_e32 v112, v112
	v_lshlrev_b64 v[168:169], 1, v[168:169]
	v_lshl_add_u64 v[174:175], s[18:19], 0, v[168:169]
	v_lshl_add_u64 v[168:169], s[20:21], 0, v[168:169]
	v_cvt_f32_i32_e32 v109, v109
	v_cvt_f32_i32_e32 v107, v107
	v_cvt_f32_i32_e32 v106, v106
	v_cvt_f32_i32_e32 v108, v108
	v_cvt_f32_i32_e32 v105, v105
	v_cvt_f32_i32_e32 v103, v103
	v_cvt_f32_i32_e32 v102, v102
	v_cvt_f32_i32_e32 v104, v104
	v_cvt_f32_i32_e32 v101, v101
	v_cvt_f32_i32_e32 v99, v99
	v_cvt_f32_i32_e32 v98, v98
	v_cvt_f32_i32_e32 v100, v100
	s_nop 0
	s_waitcnt vmcnt(17)
	v_pk_mul_f32 v[110:111], v[250:251], v[110:111] op_sel_hi:[0,1]
	v_pk_mul_f32 v[112:113], v[250:251], v[112:113] op_sel_hi:[0,1]
	s_nop 0
	s_waitcnt vmcnt(16)
	v_pk_fma_f32 v[166:167], v[128:129], v[112:113], v[222:223]
	v_pk_fma_f32 v[164:165], v[152:153], v[110:111], v[220:221]
	v_pk_mul_f32 v[106:107], v[250:251], v[106:107] op_sel_hi:[0,1]
	v_cvt_pk_bf16_f32 v110, v164, v165
	v_cvt_pk_bf16_f32 v111, v166, v167
	global_store_dwordx2 v[174:175], v[110:111], off
	s_nop 0
	v_pk_mul_f32 v[108:109], v[250:251], v[108:109] op_sel_hi:[0,1]
	v_pk_mul_f32 v[102:103], v[250:251], v[102:103] op_sel_hi:[0,1]
	v_pk_mul_f32 v[104:105], v[250:251], v[104:105] op_sel_hi:[0,1]
	v_pk_mul_f32 v[98:99], v[250:251], v[98:99] op_sel_hi:[0,1]
	v_pk_mul_f32 v[100:101], v[250:251], v[100:101] op_sel_hi:[0,1]
	s_nop 0
	v_mul_f32_e32 v110, v192, v164
	v_mul_f32_e32 v111, v193, v165
	v_mul_f32_e32 v112, v194, v166
	v_mul_f32_e32 v113, v195, v167
	v_cvt_pk_bf16_f32 v110, v110, v111
	v_cvt_pk_bf16_f32 v111, v112, v113
	global_store_dwordx2 v[168:169], v[110:111], off
	s_nop 0
	s_nop 0
	s_waitcnt vmcnt(17)
	v_pk_fma_f32 v[112:113], v[122:123], v[108:109], v[226:227]
	v_pk_fma_f32 v[110:111], v[124:125], v[106:107], v[224:225]
	s_nop 0
	v_cvt_pk_bf16_f32 v106, v110, v111
	v_cvt_pk_bf16_f32 v107, v112, v113
	global_store_dwordx2 v[174:175], v[106:107], off offset:8
	s_nop 0
	s_nop 0
	v_mul_f32_e32 v106, v110, v200
	v_mul_f32_e32 v107, v111, v201
	v_mul_f32_e32 v108, v112, v202
	v_mul_f32_e32 v109, v113, v203
	v_cvt_pk_bf16_f32 v106, v106, v107
	v_cvt_pk_bf16_f32 v107, v108, v109
	global_store_dwordx2 v[168:169], v[106:107], off offset:8
	s_nop 0
	s_nop 0
	s_waitcnt vmcnt(18)
; __device__ __forceinline__ unsigned cvt_pk_bf16(float lo, float hi) { unsigned r; asm volatile("v_cvt_pk_bf16_f32 %0, %1, %2" : "=v"(r) : "v"(lo), "v"(hi)); return r; }
;     __device__ __forceinline__ void operator()(const f32x4 (&acc)[2][2][4][2], const Unit& u, int wr, int wc, int fr, int fq) const {
;     ...
;             for (int m = 0; m < 4; ++m) { const int row = row0 + ai * HALF + m * 16; const size_t ro = (size_t)row * ldc + col0; float ss = 0.f; const float rs = xs[row];
; #pragma unroll
;                 for (int bj = 0; bj < 2; ++bj)
; #pragma unroll
;                     for (int n = 0; n < 2; ++n) { const i32x4 ia = __builtin_bit_cast(i32x4, acc[ai][bj][m][n]);
;                         const f32x4 af = (f32x4){(float)ia[0], (float)ia[1], (float)ia[2], (float)ia[3]} * rs * cs[bj][n];
;                         f32x4 rv; if constexpr (RB16) { const u32x2 rb = *(const u32x2*)((const bf16_t*)R + ro + bj * HALF + n * 4); rv = (f32x4){__uint_as_float(rb.x << 16), __uint_as_float(rb.x & 0xffff0000u), __uint_as_float(rb.y << 16), __uint_as_float(rb.y & 0xffff0000u)}; }
;                         else rv = *(const f32x4*)((const float*)R + ro + bj * HALF + n * 4);
;                         const f32x4 v = af + rv; { u32x2 hb; hb.x = cvt_pk_bf16(v[0], v[1]); hb.y = cvt_pk_bf16(v[2], v[3]); *(u32x2*)(C + ro + bj * HALF + n * 4) = hb; }
;                         const f32x4 g = *(const f32x4*)(gain + col0 + bj * HALF + n * 4);
;                         u32x2 o; o.x = cvt_pk_bf16(v[0] * g[0], v[1] * g[1]); o.y = cvt_pk_bf16(v[2] * g[2], v[3] * g[3]); *(u32x2*)(HG + ro + bj * HALF + n * 4) = o;
;                         ss += (v[0] * v[0] + v[1] * v[1]) + (v[2] * v[2] + v[3] * v[3]); }
;                 ss += __shfl_xor(ss, 16); ss += __shfl_xor(ss, 32);
;                 if (fq == 0) SS[(size_t)row * 64 + u.pn * 4 + wc] = ss; }
	v_pk_fma_f32 v[108:109], v[118:119], v[104:105], v[234:235]
	v_pk_fma_f32 v[106:107], v[120:121], v[102:103], v[232:233]
	s_nop 0
	v_cvt_pk_bf16_f32 v102, v106, v107
	v_cvt_pk_bf16_f32 v103, v108, v109
	global_store_dwordx2 v[174:175], v[102:103], off offset:256
	s_nop 0
	s_nop 0
	v_mul_f32_e32 v102, v106, v208
	v_mul_f32_e32 v103, v107, v209
	v_mul_f32_e32 v104, v108, v210
	v_mul_f32_e32 v105, v109, v211
	v_cvt_pk_bf16_f32 v102, v102, v103
	v_cvt_pk_bf16_f32 v103, v104, v105
	global_store_dwordx2 v[168:169], v[102:103], off offset:256
	s_nop 0
	s_nop 0
	s_waitcnt vmcnt(19)
	v_pk_fma_f32 v[104:105], v[114:115], v[100:101], v[238:239]
	v_pk_fma_f32 v[170:171], v[116:117], v[98:99], v[236:237]
	s_nop 0
	v_cvt_pk_bf16_f32 v98, v170, v171
	v_cvt_pk_bf16_f32 v99, v104, v105
	global_store_dwordx2 v[174:175], v[98:99], off offset:264
	s_nop 0
	v_mul_f32_e32 v98, v165, v165
	v_mul_f32_e32 v99, v167, v167
	v_fmac_f32_e32 v98, v164, v164
	v_fmac_f32_e32 v99, v166, v166
	v_add_f32_e32 v98, v98, v99
	v_mul_f32_e32 v99, v111, v111
	v_mul_f32_e32 v111, v113, v113
	v_fmac_f32_e32 v99, v110, v110
	v_fmac_f32_e32 v111, v112, v112
	v_add_f32_e32 v99, v99, v111
	v_add_f32_e32 v98, v98, v99
	v_mul_f32_e32 v99, v107, v107
	v_mul_f32_e32 v107, v109, v109
	v_fmac_f32_e32 v99, v106, v106
	v_fmac_f32_e32 v107, v108, v108
	v_add_f32_e32 v99, v99, v107
	v_add_f32_e32 v98, v98, v99
	v_mul_f32_e32 v99, v171, v171
	v_mul_f32_e32 v106, v105, v105
	v_fmac_f32_e32 v99, v170, v170
	v_fmac_f32_e32 v106, v104, v104
	v_add_f32_e32 v99, v99, v106
	v_add_f32_e32 v98, v98, v99
	ds_bpermute_b32 v99, v162, v98
	s_waitcnt lgkmcnt(0)
	v_add_f32_e32 v98, v98, v99
	ds_bpermute_b32 v99, v163, v98
	s_nop 0
	v_mul_f32_e32 v100, v170, v216
	v_mul_f32_e32 v101, v171, v217
	v_mul_f32_e32 v102, v104, v218
	v_mul_f32_e32 v103, v105, v219
	v_cvt_pk_bf16_f32 v100, v100, v101
	v_cvt_pk_bf16_f32 v101, v102, v103
	global_store_dwordx2 v[168:169], v[100:101], off offset:264
	s_and_saveexec_b64 s[52:53], s[4:5]
	s_cbranch_execz .LBB0_885
	s_waitcnt lgkmcnt(0)
	v_add_f32_e32 v100, v98, v99
	v_lshlrev_b64 v[98:99], 8, v[154:155]
	v_lshl_add_u64 v[98:99], s[22:23], 0, v[98:99]
	v_lshl_add_u64 v[98:99], s[50:51], 2, v[98:99]
	s_lshl_b32 s14, s66, 2
	v_lshl_add_u64 v[98:99], v[98:99], 0, s[14:15]
	global_store_dword v[98:99], v100, off
.LBB0_885:
	s_or_b64 exec, exec, s[52:53]
	v_or_b32_e32 v230, 48, v148
	v_ashrrev_i32_e32 v231, 31, v230
	v_lshl_add_u64 v[252:253], v[230:231], 2, s[24:25]
	global_load_dword v214, v[252:253], off
	v_or_b32_e32 v254, 48, v148
	v_ashrrev_i32_e32 v255, 31, v254
	v_lshlrev_b64 v[248:249], 12, v[254:255]
	v_lshl_add_u64 v[230:231], v[248:249], 0, v[146:147]
	v_lshl_add_u64 v[252:253], v[230:231], 2, s[10:11]
	global_load_dwordx4 v[220:223], v[252:253], off
	global_load_dwordx4 v[224:227], v[252:253], off offset:16
	global_load_dwordx4 v[232:235], v[252:253], off offset:512
	global_load_dwordx4 v[236:239], v[252:253], off offset:528
	v_or_b32_e32 v98, 32, v148
	s_waitcnt lgkmcnt(0)
	v_ashrrev_i32_e32 v99, 31, v98
	v_lshlrev_b64 v[100:101], 12, v[98:99]
	v_lshl_add_u64 v[104:105], v[100:101], 0, v[146:147]
	v_lshl_add_u64 v[100:101], v[98:99], 2, s[24:25]
	s_nop 0
	v_lshl_add_u64 v[108:109], v[104:105], 2, s[10:11]
	s_nop 0
	v_cvt_f32_i32_e32 v97, v97
	v_cvt_f32_i32_e32 v95, v95
	v_cvt_f32_i32_e32 v94, v94
	v_cvt_f32_i32_e32 v96, v96
	v_lshlrev_b64 v[104:105], 1, v[104:105]
	v_lshl_add_u64 v[110:111], s[18:19], 0, v[104:105]
	v_lshl_add_u64 v[104:105], s[20:21], 0, v[104:105]
	v_cvt_f32_i32_e32 v93, v93
	v_cvt_f32_i32_e32 v91, v91
	v_cvt_f32_i32_e32 v90, v90
	v_cvt_f32_i32_e32 v92, v92
	v_cvt_f32_i32_e32 v89, v89
	v_cvt_f32_i32_e32 v87, v87
	v_cvt_f32_i32_e32 v86, v86
	v_cvt_f32_i32_e32 v88, v88
	v_cvt_f32_i32_e32 v85, v85
	v_cvt_f32_i32_e32 v83, v83
	v_cvt_f32_i32_e32 v82, v82
	v_cvt_f32_i32_e32 v84, v84
	s_nop 0
	s_waitcnt vmcnt(17)
	v_pk_mul_f32 v[94:95], v[212:213], v[94:95] op_sel_hi:[0,1]
	v_pk_mul_f32 v[96:97], v[212:213], v[96:97] op_sel_hi:[0,1]
	s_nop 0
	s_waitcnt vmcnt(16)
	v_pk_fma_f32 v[102:103], v[128:129], v[96:97], v[242:243]
	v_pk_fma_f32 v[100:101], v[152:153], v[94:95], v[240:241]
	v_pk_mul_f32 v[90:91], v[212:213], v[90:91] op_sel_hi:[0,1]
	v_cvt_pk_bf16_f32 v94, v100, v101
	v_cvt_pk_bf16_f32 v95, v102, v103
	global_store_dwordx2 v[110:111], v[94:95], off
	s_nop 0
	v_pk_mul_f32 v[92:93], v[212:213], v[92:93] op_sel_hi:[0,1]
	v_pk_mul_f32 v[86:87], v[212:213], v[86:87] op_sel_hi:[0,1]
	v_pk_mul_f32 v[88:89], v[212:213], v[88:89] op_sel_hi:[0,1]
	v_pk_mul_f32 v[82:83], v[212:213], v[82:83] op_sel_hi:[0,1]
	v_pk_mul_f32 v[84:85], v[212:213], v[84:85] op_sel_hi:[0,1]
	s_nop 0
	v_mul_f32_e32 v94, v192, v100
	v_mul_f32_e32 v95, v193, v101
	v_mul_f32_e32 v96, v194, v102
	v_mul_f32_e32 v97, v195, v103
	v_cvt_pk_bf16_f32 v94, v94, v95
	v_cvt_pk_bf16_f32 v95, v96, v97
	global_store_dwordx2 v[104:105], v[94:95], off
	s_nop 0
	s_nop 0
	s_waitcnt vmcnt(17)
	v_pk_fma_f32 v[96:97], v[122:123], v[92:93], v[246:247]
	v_pk_fma_f32 v[94:95], v[124:125], v[90:91], v[244:245]
	s_nop 0
	v_cvt_pk_bf16_f32 v90, v94, v95
	v_cvt_pk_bf16_f32 v91, v96, v97
	global_store_dwordx2 v[110:111], v[90:91], off offset:8
	s_nop 0
	s_nop 0
	v_mul_f32_e32 v90, v94, v200
	v_mul_f32_e32 v91, v95, v201
	v_mul_f32_e32 v92, v96, v202
	v_mul_f32_e32 v93, v97, v203
	v_cvt_pk_bf16_f32 v90, v90, v91
	v_cvt_pk_bf16_f32 v91, v92, v93
	global_store_dwordx2 v[104:105], v[90:91], off offset:8
	s_nop 0
	s_nop 0
	s_waitcnt vmcnt(18)
; __device__ __forceinline__ unsigned cvt_pk_bf16(float lo, float hi) { unsigned r; asm volatile("v_cvt_pk_bf16_f32 %0, %1, %2" : "=v"(r) : "v"(lo), "v"(hi)); return r; }
;     __device__ __forceinline__ void operator()(const f32x4 (&acc)[2][2][4][2], const Unit& u, int wr, int wc, int fr, int fq) const {
;     ...
;             for (int m = 0; m < 4; ++m) { const int row = row0 + ai * HALF + m * 16; const size_t ro = (size_t)row * ldc + col0; float ss = 0.f; const float rs = xs[row];
; #pragma unroll
;                 for (int bj = 0; bj < 2; ++bj)
; #pragma unroll
;                     for (int n = 0; n < 2; ++n) { const i32x4 ia = __builtin_bit_cast(i32x4, acc[ai][bj][m][n]);
;                         const f32x4 af = (f32x4){(float)ia[0], (float)ia[1], (float)ia[2], (float)ia[3]} * rs * cs[bj][n];
;                         f32x4 rv; if constexpr (RB16) { const u32x2 rb = *(const u32x2*)((const bf16_t*)R + ro + bj * HALF + n * 4); rv = (f32x4){__uint_as_float(rb.x << 16), __uint_as_float(rb.x & 0xffff0000u), __uint_as_float(rb.y << 16), __uint_as_float(rb.y & 0xffff0000u)}; }
;                         else rv = *(const f32x4*)((const float*)R + ro + bj * HALF + n * 4);
;                         const f32x4 v = af + rv; { u32x2 hb; hb.x = cvt_pk_bf16(v[0], v[1]); hb.y = cvt_pk_bf16(v[2], v[3]); *(u32x2*)(C + ro + bj * HALF + n * 4) = hb; }
;                         const f32x4 g = *(const f32x4*)(gain + col0 + bj * HALF + n * 4);
;                         u32x2 o; o.x = cvt_pk_bf16(v[0] * g[0], v[1] * g[1]); o.y = cvt_pk_bf16(v[2] * g[2], v[3] * g[3]); *(u32x2*)(HG + ro + bj * HALF + n * 4) = o;
;                         ss += (v[0] * v[0] + v[1] * v[1]) + (v[2] * v[2] + v[3] * v[3]); }
;                 ss += __shfl_xor(ss, 16); ss += __shfl_xor(ss, 32);
;                 if (fq == 0) SS[(size_t)row * 64 + u.pn * 4 + wc] = ss; }
	v_pk_fma_f32 v[92:93], v[118:119], v[88:89], v[198:199]
	v_pk_fma_f32 v[90:91], v[120:121], v[86:87], v[196:197]
	s_nop 0
	v_cvt_pk_bf16_f32 v86, v90, v91
	v_cvt_pk_bf16_f32 v87, v92, v93
	global_store_dwordx2 v[110:111], v[86:87], off offset:256
	s_nop 0
	s_nop 0
	v_mul_f32_e32 v86, v90, v208
	v_mul_f32_e32 v87, v91, v209
	v_mul_f32_e32 v88, v92, v210
	v_mul_f32_e32 v89, v93, v211
	v_cvt_pk_bf16_f32 v86, v86, v87
	v_cvt_pk_bf16_f32 v87, v88, v89
	global_store_dwordx2 v[104:105], v[86:87], off offset:256
	s_nop 0
	s_nop 0
	s_waitcnt vmcnt(19)
	v_pk_fma_f32 v[88:89], v[114:115], v[84:85], v[206:207]
	v_pk_fma_f32 v[106:107], v[116:117], v[82:83], v[204:205]
	s_nop 0
	v_cvt_pk_bf16_f32 v82, v106, v107
	v_cvt_pk_bf16_f32 v83, v88, v89
	global_store_dwordx2 v[110:111], v[82:83], off offset:264
	s_nop 0
	v_mul_f32_e32 v82, v101, v101
	v_mul_f32_e32 v83, v103, v103
	v_fmac_f32_e32 v82, v100, v100
	v_fmac_f32_e32 v83, v102, v102
	v_add_f32_e32 v82, v82, v83
	v_mul_f32_e32 v83, v95, v95
	v_mul_f32_e32 v95, v97, v97
	v_fmac_f32_e32 v83, v94, v94
	v_fmac_f32_e32 v95, v96, v96
	v_add_f32_e32 v83, v83, v95
	v_add_f32_e32 v82, v82, v83
	v_mul_f32_e32 v83, v91, v91
	v_mul_f32_e32 v91, v93, v93
	v_fmac_f32_e32 v83, v90, v90
	v_fmac_f32_e32 v91, v92, v92
	v_add_f32_e32 v83, v83, v91
	v_add_f32_e32 v82, v82, v83
	v_mul_f32_e32 v83, v107, v107
	v_mul_f32_e32 v90, v89, v89
	v_fmac_f32_e32 v83, v106, v106
	v_fmac_f32_e32 v90, v88, v88
	v_add_f32_e32 v83, v83, v90
	v_add_f32_e32 v82, v82, v83
	ds_bpermute_b32 v83, v162, v82
	s_waitcnt lgkmcnt(0)
	v_add_f32_e32 v82, v82, v83
	ds_bpermute_b32 v83, v163, v82
	s_nop 0
	v_mul_f32_e32 v84, v106, v216
	v_mul_f32_e32 v85, v107, v217
	v_mul_f32_e32 v86, v88, v218
	v_mul_f32_e32 v87, v89, v219
	v_cvt_pk_bf16_f32 v84, v84, v85
	v_cvt_pk_bf16_f32 v85, v86, v87
	global_store_dwordx2 v[104:105], v[84:85], off offset:264
	s_and_saveexec_b64 s[52:53], s[4:5]
	s_cbranch_execz .LBB0_887
	s_waitcnt lgkmcnt(0)
	v_add_f32_e32 v84, v82, v83
	v_lshlrev_b64 v[82:83], 8, v[98:99]
	v_lshl_add_u64 v[82:83], s[22:23], 0, v[82:83]
	v_lshl_add_u64 v[82:83], s[50:51], 2, v[82:83]
	s_lshl_b32 s14, s66, 2
	v_lshl_add_u64 v[82:83], v[82:83], 0, s[14:15]
	global_store_dword v[82:83], v84, off
.LBB0_887:
	s_or_b64 exec, exec, s[52:53]
	global_load_dword v250, v[150:151], off offset:512
	v_add_u32_e32 v254, 0x80, v148
	v_ashrrev_i32_e32 v255, 31, v254
	v_lshlrev_b64 v[248:249], 12, v[254:255]
	v_lshl_add_u64 v[230:231], v[248:249], 0, v[146:147]
	v_lshl_add_u64 v[252:253], v[230:231], 2, s[10:11]
	global_load_dwordx4 v[240:243], v[252:253], off
	global_load_dwordx4 v[244:247], v[252:253], off offset:16
	global_load_dwordx4 v[196:199], v[252:253], off offset:512
	global_load_dwordx4 v[204:207], v[252:253], off offset:528
	v_or_b32_e32 v82, 48, v148
	s_waitcnt lgkmcnt(0)
	v_ashrrev_i32_e32 v83, 31, v82
	v_lshlrev_b64 v[84:85], 12, v[82:83]
	v_lshl_add_u64 v[88:89], v[84:85], 0, v[146:147]
	v_lshl_add_u64 v[84:85], v[82:83], 2, s[24:25]
	s_nop 0
	v_lshl_add_u64 v[92:93], v[88:89], 2, s[10:11]
	s_nop 0
	v_cvt_f32_i32_e32 v81, v81
	v_cvt_f32_i32_e32 v79, v79
	v_cvt_f32_i32_e32 v78, v78
	v_cvt_f32_i32_e32 v80, v80
	v_lshlrev_b64 v[88:89], 1, v[88:89]
	v_lshl_add_u64 v[94:95], s[18:19], 0, v[88:89]
	v_lshl_add_u64 v[88:89], s[20:21], 0, v[88:89]
	v_cvt_f32_i32_e32 v77, v77
	v_cvt_f32_i32_e32 v75, v75
	v_cvt_f32_i32_e32 v74, v74
	v_cvt_f32_i32_e32 v76, v76
	v_cvt_f32_i32_e32 v73, v73
	v_cvt_f32_i32_e32 v71, v71
	v_cvt_f32_i32_e32 v70, v70
	v_cvt_f32_i32_e32 v72, v72
	v_cvt_f32_i32_e32 v69, v69
	v_cvt_f32_i32_e32 v67, v67
	v_cvt_f32_i32_e32 v66, v66
	v_cvt_f32_i32_e32 v68, v68
	s_nop 0
	s_waitcnt vmcnt(17)
	v_pk_mul_f32 v[78:79], v[214:215], v[78:79] op_sel_hi:[0,1]
	v_pk_mul_f32 v[80:81], v[214:215], v[80:81] op_sel_hi:[0,1]
	s_nop 0
	s_waitcnt vmcnt(16)
	v_pk_fma_f32 v[86:87], v[128:129], v[80:81], v[222:223]
	v_pk_fma_f32 v[84:85], v[152:153], v[78:79], v[220:221]
	v_pk_mul_f32 v[74:75], v[214:215], v[74:75] op_sel_hi:[0,1]
	v_cvt_pk_bf16_f32 v78, v84, v85
	v_cvt_pk_bf16_f32 v79, v86, v87
	global_store_dwordx2 v[94:95], v[78:79], off
	s_nop 0
	v_pk_mul_f32 v[76:77], v[214:215], v[76:77] op_sel_hi:[0,1]
	v_pk_mul_f32 v[70:71], v[214:215], v[70:71] op_sel_hi:[0,1]
	v_pk_mul_f32 v[72:73], v[214:215], v[72:73] op_sel_hi:[0,1]
	v_pk_mul_f32 v[66:67], v[214:215], v[66:67] op_sel_hi:[0,1]
	v_pk_mul_f32 v[68:69], v[214:215], v[68:69] op_sel_hi:[0,1]
	s_nop 0
	v_mul_f32_e32 v78, v192, v84
	v_mul_f32_e32 v79, v193, v85
	v_mul_f32_e32 v80, v194, v86
	v_mul_f32_e32 v81, v195, v87
	v_cvt_pk_bf16_f32 v78, v78, v79
	v_cvt_pk_bf16_f32 v79, v80, v81
	global_store_dwordx2 v[88:89], v[78:79], off
	s_nop 0
	s_nop 0
	s_waitcnt vmcnt(17)
	v_pk_fma_f32 v[80:81], v[122:123], v[76:77], v[226:227]
	v_pk_fma_f32 v[78:79], v[124:125], v[74:75], v[224:225]
	s_nop 0
	v_cvt_pk_bf16_f32 v74, v78, v79
	v_cvt_pk_bf16_f32 v75, v80, v81
	global_store_dwordx2 v[94:95], v[74:75], off offset:8
	s_nop 0
	s_nop 0
	v_mul_f32_e32 v74, v78, v200
	v_mul_f32_e32 v75, v79, v201
	v_mul_f32_e32 v76, v80, v202
	v_mul_f32_e32 v77, v81, v203
	v_cvt_pk_bf16_f32 v74, v74, v75
	v_cvt_pk_bf16_f32 v75, v76, v77
	global_store_dwordx2 v[88:89], v[74:75], off offset:8
	s_nop 0
	s_nop 0
	s_waitcnt vmcnt(18)
	v_pk_fma_f32 v[76:77], v[118:119], v[72:73], v[234:235]
	v_pk_fma_f32 v[74:75], v[120:121], v[70:71], v[232:233]
	s_nop 0
	v_cvt_pk_bf16_f32 v70, v74, v75
	v_cvt_pk_bf16_f32 v71, v76, v77
	global_store_dwordx2 v[94:95], v[70:71], off offset:256
	s_nop 0
	s_nop 0
	v_mul_f32_e32 v70, v74, v208
	v_mul_f32_e32 v71, v75, v209
	v_mul_f32_e32 v72, v76, v210
	v_mul_f32_e32 v73, v77, v211
	v_cvt_pk_bf16_f32 v70, v70, v71
	v_cvt_pk_bf16_f32 v71, v72, v73
	global_store_dwordx2 v[88:89], v[70:71], off offset:256
	s_nop 0
	s_nop 0
	s_waitcnt vmcnt(19)
; __device__ __forceinline__ unsigned cvt_pk_bf16(float lo, float hi) { unsigned r; asm volatile("v_cvt_pk_bf16_f32 %0, %1, %2" : "=v"(r) : "v"(lo), "v"(hi)); return r; }
;     __device__ __forceinline__ void operator()(const f32x4 (&acc)[2][2][4][2], const Unit& u, int wr, int wc, int fr, int fq) const {
;     ...
;             for (int m = 0; m < 4; ++m) { const int row = row0 + ai * HALF + m * 16; const size_t ro = (size_t)row * ldc + col0; float ss = 0.f; const float rs = xs[row];
; #pragma unroll
;                 for (int bj = 0; bj < 2; ++bj)
; #pragma unroll
;                     for (int n = 0; n < 2; ++n) { const i32x4 ia = __builtin_bit_cast(i32x4, acc[ai][bj][m][n]);
;                         const f32x4 af = (f32x4){(float)ia[0], (float)ia[1], (float)ia[2], (float)ia[3]} * rs * cs[bj][n];
;                         f32x4 rv; if constexpr (RB16) { const u32x2 rb = *(const u32x2*)((const bf16_t*)R + ro + bj * HALF + n * 4); rv = (f32x4){__uint_as_float(rb.x << 16), __uint_as_float(rb.x & 0xffff0000u), __uint_as_float(rb.y << 16), __uint_as_float(rb.y & 0xffff0000u)}; }
;                         else rv = *(const f32x4*)((const float*)R + ro + bj * HALF + n * 4);
;                         const f32x4 v = af + rv; { u32x2 hb; hb.x = cvt_pk_bf16(v[0], v[1]); hb.y = cvt_pk_bf16(v[2], v[3]); *(u32x2*)(C + ro + bj * HALF + n * 4) = hb; }
;                         const f32x4 g = *(const f32x4*)(gain + col0 + bj * HALF + n * 4);
;                         u32x2 o; o.x = cvt_pk_bf16(v[0] * g[0], v[1] * g[1]); o.y = cvt_pk_bf16(v[2] * g[2], v[3] * g[3]); *(u32x2*)(HG + ro + bj * HALF + n * 4) = o;
;                         ss += (v[0] * v[0] + v[1] * v[1]) + (v[2] * v[2] + v[3] * v[3]); }
;                 ss += __shfl_xor(ss, 16); ss += __shfl_xor(ss, 32);
;                 if (fq == 0) SS[(size_t)row * 64 + u.pn * 4 + wc] = ss; }
	v_pk_fma_f32 v[72:73], v[114:115], v[68:69], v[238:239]
	v_pk_fma_f32 v[90:91], v[116:117], v[66:67], v[236:237]
	s_nop 0
	v_cvt_pk_bf16_f32 v66, v90, v91
	v_cvt_pk_bf16_f32 v67, v72, v73
	global_store_dwordx2 v[94:95], v[66:67], off offset:264
	s_nop 0
	v_mul_f32_e32 v66, v85, v85
	v_mul_f32_e32 v67, v87, v87
	v_fmac_f32_e32 v66, v84, v84
	v_fmac_f32_e32 v67, v86, v86
	v_add_f32_e32 v66, v66, v67
	v_mul_f32_e32 v67, v79, v79
	v_mul_f32_e32 v79, v81, v81
	v_fmac_f32_e32 v67, v78, v78
	v_fmac_f32_e32 v79, v80, v80
	v_add_f32_e32 v67, v67, v79
	v_add_f32_e32 v66, v66, v67
	v_mul_f32_e32 v67, v75, v75
	v_mul_f32_e32 v75, v77, v77
	v_fmac_f32_e32 v67, v74, v74
	v_fmac_f32_e32 v75, v76, v76
	v_add_f32_e32 v67, v67, v75
	v_add_f32_e32 v66, v66, v67
	v_mul_f32_e32 v67, v91, v91
	v_mul_f32_e32 v74, v73, v73
	v_fmac_f32_e32 v67, v90, v90
	v_fmac_f32_e32 v74, v72, v72
	v_add_f32_e32 v67, v67, v74
	v_add_f32_e32 v66, v66, v67
	ds_bpermute_b32 v67, v162, v66
	s_waitcnt lgkmcnt(0)
	v_add_f32_e32 v66, v66, v67
	ds_bpermute_b32 v67, v163, v66
	s_nop 0
	v_mul_f32_e32 v68, v90, v216
	v_mul_f32_e32 v69, v91, v217
	v_mul_f32_e32 v70, v72, v218
	v_mul_f32_e32 v71, v73, v219
	v_cvt_pk_bf16_f32 v68, v68, v69
	v_cvt_pk_bf16_f32 v69, v70, v71
	global_store_dwordx2 v[88:89], v[68:69], off offset:264
	s_and_saveexec_b64 s[52:53], s[4:5]
	s_cbranch_execz .LBB0_889
	s_waitcnt lgkmcnt(0)
	v_add_f32_e32 v68, v66, v67
	v_lshlrev_b64 v[66:67], 8, v[82:83]
	v_lshl_add_u64 v[66:67], s[22:23], 0, v[66:67]
	v_lshl_add_u64 v[66:67], s[50:51], 2, v[66:67]
	s_lshl_b32 s14, s66, 2
	v_lshl_add_u64 v[66:67], v[66:67], 0, s[14:15]
	global_store_dword v[66:67], v68, off
.LBB0_889:
	s_or_b64 exec, exec, s[52:53]
	global_load_dword v212, v[150:151], off offset:576
	v_add_u32_e32 v254, 0x90, v148
	v_ashrrev_i32_e32 v255, 31, v254
	v_lshlrev_b64 v[248:249], 12, v[254:255]
	v_lshl_add_u64 v[230:231], v[248:249], 0, v[146:147]
	v_lshl_add_u64 v[252:253], v[230:231], 2, s[10:11]
	global_load_dwordx4 v[220:223], v[252:253], off
	global_load_dwordx4 v[224:227], v[252:253], off offset:16
	global_load_dwordx4 v[232:235], v[252:253], off offset:512
	global_load_dwordx4 v[236:239], v[252:253], off offset:528
	v_add_u32_e32 v66, 0x80, v148
	s_waitcnt lgkmcnt(0)
	v_ashrrev_i32_e32 v67, 31, v66
	v_lshlrev_b64 v[68:69], 12, v[66:67]
	v_lshl_add_u64 v[72:73], v[68:69], 0, v[146:147]
	s_nop 0
	v_lshl_add_u64 v[76:77], v[72:73], 2, s[10:11]
	s_nop 0
	v_cvt_f32_i32_e32 v65, v65
	v_cvt_f32_i32_e32 v63, v63
	v_cvt_f32_i32_e32 v62, v62
	v_cvt_f32_i32_e32 v64, v64
	v_lshlrev_b64 v[72:73], 1, v[72:73]
	v_lshl_add_u64 v[78:79], s[18:19], 0, v[72:73]
	v_lshl_add_u64 v[72:73], s[20:21], 0, v[72:73]
	v_cvt_f32_i32_e32 v61, v61
	v_cvt_f32_i32_e32 v59, v59
	v_cvt_f32_i32_e32 v58, v58
	v_cvt_f32_i32_e32 v60, v60
	v_cvt_f32_i32_e32 v57, v57
	v_cvt_f32_i32_e32 v55, v55
	v_cvt_f32_i32_e32 v54, v54
	v_cvt_f32_i32_e32 v56, v56
	v_cvt_f32_i32_e32 v53, v53
	v_cvt_f32_i32_e32 v51, v51
	v_cvt_f32_i32_e32 v50, v50
	v_cvt_f32_i32_e32 v52, v52
	s_nop 0
	s_waitcnt vmcnt(17)
	v_pk_mul_f32 v[62:63], v[250:251], v[62:63] op_sel_hi:[0,1]
	v_pk_mul_f32 v[64:65], v[250:251], v[64:65] op_sel_hi:[0,1]
	s_nop 0
	s_waitcnt vmcnt(16)
	v_pk_fma_f32 v[70:71], v[128:129], v[64:65], v[242:243]
	v_pk_fma_f32 v[68:69], v[152:153], v[62:63], v[240:241]
	v_pk_mul_f32 v[58:59], v[250:251], v[58:59] op_sel_hi:[0,1]
	v_cvt_pk_bf16_f32 v62, v68, v69
	v_cvt_pk_bf16_f32 v63, v70, v71
	global_store_dwordx2 v[78:79], v[62:63], off
	s_nop 0
	v_pk_mul_f32 v[60:61], v[250:251], v[60:61] op_sel_hi:[0,1]
	v_pk_mul_f32 v[54:55], v[250:251], v[54:55] op_sel_hi:[0,1]
	v_pk_mul_f32 v[56:57], v[250:251], v[56:57] op_sel_hi:[0,1]
	v_pk_mul_f32 v[50:51], v[250:251], v[50:51] op_sel_hi:[0,1]
	v_pk_mul_f32 v[52:53], v[250:251], v[52:53] op_sel_hi:[0,1]
	s_nop 0
	v_mul_f32_e32 v62, v192, v68
	v_mul_f32_e32 v63, v193, v69
	v_mul_f32_e32 v64, v194, v70
	v_mul_f32_e32 v65, v195, v71
	v_cvt_pk_bf16_f32 v62, v62, v63
	v_cvt_pk_bf16_f32 v63, v64, v65
	global_store_dwordx2 v[72:73], v[62:63], off
	s_nop 0
	s_nop 0
	s_waitcnt vmcnt(17)
	v_pk_fma_f32 v[64:65], v[122:123], v[60:61], v[246:247]
	v_pk_fma_f32 v[62:63], v[124:125], v[58:59], v[244:245]
	s_nop 0
	v_cvt_pk_bf16_f32 v58, v62, v63
	v_cvt_pk_bf16_f32 v59, v64, v65
	global_store_dwordx2 v[78:79], v[58:59], off offset:8
	s_nop 0
	s_nop 0
	v_mul_f32_e32 v58, v62, v200
	v_mul_f32_e32 v59, v63, v201
	v_mul_f32_e32 v60, v64, v202
	v_mul_f32_e32 v61, v65, v203
	v_cvt_pk_bf16_f32 v58, v58, v59
	v_cvt_pk_bf16_f32 v59, v60, v61
	global_store_dwordx2 v[72:73], v[58:59], off offset:8
	s_nop 0
	s_nop 0
	s_waitcnt vmcnt(18)
	v_pk_fma_f32 v[60:61], v[118:119], v[56:57], v[198:199]
	v_pk_fma_f32 v[58:59], v[120:121], v[54:55], v[196:197]
	s_nop 0
	v_cvt_pk_bf16_f32 v54, v58, v59
	v_cvt_pk_bf16_f32 v55, v60, v61
	global_store_dwordx2 v[78:79], v[54:55], off offset:256
	s_nop 0
	s_nop 0
	v_mul_f32_e32 v54, v58, v208
	v_mul_f32_e32 v55, v59, v209
	v_mul_f32_e32 v56, v60, v210
	v_mul_f32_e32 v57, v61, v211
	v_cvt_pk_bf16_f32 v54, v54, v55
	v_cvt_pk_bf16_f32 v55, v56, v57
	global_store_dwordx2 v[72:73], v[54:55], off offset:256
	s_nop 0
	s_nop 0
	s_waitcnt vmcnt(19)
	v_pk_fma_f32 v[56:57], v[114:115], v[52:53], v[206:207]
	v_pk_fma_f32 v[74:75], v[116:117], v[50:51], v[204:205]
	s_nop 0
	v_cvt_pk_bf16_f32 v50, v74, v75
	v_cvt_pk_bf16_f32 v51, v56, v57
	global_store_dwordx2 v[78:79], v[50:51], off offset:264
	s_nop 0
	v_mul_f32_e32 v50, v69, v69
	v_mul_f32_e32 v51, v71, v71
	v_fmac_f32_e32 v50, v68, v68
	v_fmac_f32_e32 v51, v70, v70
	v_add_f32_e32 v50, v50, v51
	v_mul_f32_e32 v51, v63, v63
	v_mul_f32_e32 v63, v65, v65
	v_fmac_f32_e32 v51, v62, v62
	v_fmac_f32_e32 v63, v64, v64
	v_add_f32_e32 v51, v51, v63
	v_add_f32_e32 v50, v50, v51
	v_mul_f32_e32 v51, v59, v59
	v_mul_f32_e32 v59, v61, v61
	v_fmac_f32_e32 v51, v58, v58
	v_fmac_f32_e32 v59, v60, v60
	v_add_f32_e32 v51, v51, v59
	v_add_f32_e32 v50, v50, v51
	v_mul_f32_e32 v51, v75, v75
	v_mul_f32_e32 v58, v57, v57
	v_fmac_f32_e32 v51, v74, v74
	v_fmac_f32_e32 v58, v56, v56
	v_add_f32_e32 v51, v51, v58
	v_add_f32_e32 v50, v50, v51
	ds_bpermute_b32 v51, v162, v50
	s_waitcnt lgkmcnt(0)
	v_add_f32_e32 v50, v50, v51
	ds_bpermute_b32 v51, v163, v50
	s_nop 0
	v_mul_f32_e32 v52, v74, v216
	v_mul_f32_e32 v53, v75, v217
	v_mul_f32_e32 v54, v56, v218
	v_mul_f32_e32 v55, v57, v219
	v_cvt_pk_bf16_f32 v52, v52, v53
	v_cvt_pk_bf16_f32 v53, v54, v55
	global_store_dwordx2 v[72:73], v[52:53], off offset:264
	s_and_saveexec_b64 s[52:53], s[4:5]
	s_cbranch_execz .LBB0_891
	s_waitcnt lgkmcnt(0)
	v_add_f32_e32 v52, v50, v51
	v_lshlrev_b64 v[50:51], 8, v[66:67]
	v_lshl_add_u64 v[50:51], s[22:23], 0, v[50:51]
	v_lshl_add_u64 v[50:51], s[50:51], 2, v[50:51]
	s_lshl_b32 s14, s66, 2
	v_lshl_add_u64 v[50:51], v[50:51], 0, s[14:15]
	global_store_dword v[50:51], v52, off
; __device__ __forceinline__ unsigned cvt_pk_bf16(float lo, float hi) { unsigned r; asm volatile("v_cvt_pk_bf16_f32 %0, %1, %2" : "=v"(r) : "v"(lo), "v"(hi)); return r; }
;     __device__ __forceinline__ void operator()(const f32x4 (&acc)[2][2][4][2], const Unit& u, int wr, int wc, int fr, int fq) const {
;     ...
;             for (int m = 0; m < 4; ++m) { const int row = row0 + ai * HALF + m * 16; const size_t ro = (size_t)row * ldc + col0; float ss = 0.f; const float rs = xs[row];
; #pragma unroll
;                 for (int bj = 0; bj < 2; ++bj)
; #pragma unroll
;                     for (int n = 0; n < 2; ++n) { const i32x4 ia = __builtin_bit_cast(i32x4, acc[ai][bj][m][n]);
;                         const f32x4 af = (f32x4){(float)ia[0], (float)ia[1], (float)ia[2], (float)ia[3]} * rs * cs[bj][n];
;                         f32x4 rv; if constexpr (RB16) { const u32x2 rb = *(const u32x2*)((const bf16_t*)R + ro + bj * HALF + n * 4); rv = (f32x4){__uint_as_float(rb.x << 16), __uint_as_float(rb.x & 0xffff0000u), __uint_as_float(rb.y << 16), __uint_as_float(rb.y & 0xffff0000u)}; }
;                         else rv = *(const f32x4*)((const float*)R + ro + bj * HALF + n * 4);
;                         const f32x4 v = af + rv; { u32x2 hb; hb.x = cvt_pk_bf16(v[0], v[1]); hb.y = cvt_pk_bf16(v[2], v[3]); *(u32x2*)(C + ro + bj * HALF + n * 4) = hb; }
;                         const f32x4 g = *(const f32x4*)(gain + col0 + bj * HALF + n * 4);
;                         u32x2 o; o.x = cvt_pk_bf16(v[0] * g[0], v[1] * g[1]); o.y = cvt_pk_bf16(v[2] * g[2], v[3] * g[3]); *(u32x2*)(HG + ro + bj * HALF + n * 4) = o;
;                         ss += (v[0] * v[0] + v[1] * v[1]) + (v[2] * v[2] + v[3] * v[3]); }
;                 ss += __shfl_xor(ss, 16); ss += __shfl_xor(ss, 32);
;                 if (fq == 0) SS[(size_t)row * 64 + u.pn * 4 + wc] = ss; }
.LBB0_891:
	s_or_b64 exec, exec, s[52:53]
	global_load_dword v214, v[150:151], off offset:640
	v_add_u32_e32 v254, 0xa0, v148
	v_ashrrev_i32_e32 v255, 31, v254
	v_lshlrev_b64 v[248:249], 12, v[254:255]
	v_lshl_add_u64 v[230:231], v[248:249], 0, v[146:147]
	v_lshl_add_u64 v[252:253], v[230:231], 2, s[10:11]
	global_load_dwordx4 v[240:243], v[252:253], off
	global_load_dwordx4 v[244:247], v[252:253], off offset:16
	global_load_dwordx4 v[196:199], v[252:253], off offset:512
	global_load_dwordx4 v[204:207], v[252:253], off offset:528
	v_add_u32_e32 v50, 0x90, v148
	s_waitcnt lgkmcnt(0)
	v_ashrrev_i32_e32 v51, 31, v50
	v_lshlrev_b64 v[52:53], 12, v[50:51]
	v_lshl_add_u64 v[56:57], v[52:53], 0, v[146:147]
	s_nop 0
	v_lshl_add_u64 v[60:61], v[56:57], 2, s[10:11]
	s_nop 0
	v_cvt_f32_i32_e32 v49, v49
	v_cvt_f32_i32_e32 v47, v47
	v_cvt_f32_i32_e32 v46, v46
	v_cvt_f32_i32_e32 v48, v48
	v_lshlrev_b64 v[56:57], 1, v[56:57]
	v_lshl_add_u64 v[62:63], s[18:19], 0, v[56:57]
	v_lshl_add_u64 v[56:57], s[20:21], 0, v[56:57]
	v_cvt_f32_i32_e32 v45, v45
	v_cvt_f32_i32_e32 v43, v43
	v_cvt_f32_i32_e32 v42, v42
	v_cvt_f32_i32_e32 v44, v44
	v_cvt_f32_i32_e32 v41, v41
	v_cvt_f32_i32_e32 v39, v39
	v_cvt_f32_i32_e32 v38, v38
	v_cvt_f32_i32_e32 v40, v40
	v_cvt_f32_i32_e32 v37, v37
	v_cvt_f32_i32_e32 v35, v35
	v_cvt_f32_i32_e32 v34, v34
	v_cvt_f32_i32_e32 v36, v36
	s_nop 0
	s_waitcnt vmcnt(17)
	v_pk_mul_f32 v[46:47], v[212:213], v[46:47] op_sel_hi:[0,1]
	v_pk_mul_f32 v[48:49], v[212:213], v[48:49] op_sel_hi:[0,1]
	s_nop 0
	s_waitcnt vmcnt(16)
	v_pk_fma_f32 v[54:55], v[128:129], v[48:49], v[222:223]
	v_pk_fma_f32 v[52:53], v[152:153], v[46:47], v[220:221]
	v_pk_mul_f32 v[42:43], v[212:213], v[42:43] op_sel_hi:[0,1]
	v_cvt_pk_bf16_f32 v46, v52, v53
	v_cvt_pk_bf16_f32 v47, v54, v55
	global_store_dwordx2 v[62:63], v[46:47], off
	s_nop 0
	v_pk_mul_f32 v[44:45], v[212:213], v[44:45] op_sel_hi:[0,1]
	v_pk_mul_f32 v[38:39], v[212:213], v[38:39] op_sel_hi:[0,1]
	v_pk_mul_f32 v[40:41], v[212:213], v[40:41] op_sel_hi:[0,1]
	v_pk_mul_f32 v[34:35], v[212:213], v[34:35] op_sel_hi:[0,1]
	v_pk_mul_f32 v[36:37], v[212:213], v[36:37] op_sel_hi:[0,1]
	s_nop 0
	v_mul_f32_e32 v46, v192, v52
	v_mul_f32_e32 v47, v193, v53
	v_mul_f32_e32 v48, v194, v54
	v_mul_f32_e32 v49, v195, v55
	v_cvt_pk_bf16_f32 v46, v46, v47
	v_cvt_pk_bf16_f32 v47, v48, v49
	global_store_dwordx2 v[56:57], v[46:47], off
	s_nop 0
	s_nop 0
	s_waitcnt vmcnt(17)
	v_pk_fma_f32 v[48:49], v[122:123], v[44:45], v[226:227]
	v_pk_fma_f32 v[46:47], v[124:125], v[42:43], v[224:225]
	s_nop 0
	v_cvt_pk_bf16_f32 v42, v46, v47
	v_cvt_pk_bf16_f32 v43, v48, v49
	global_store_dwordx2 v[62:63], v[42:43], off offset:8
	s_nop 0
	s_nop 0
	v_mul_f32_e32 v42, v46, v200
	v_mul_f32_e32 v43, v47, v201
	v_mul_f32_e32 v44, v48, v202
	v_mul_f32_e32 v45, v49, v203
	v_cvt_pk_bf16_f32 v42, v42, v43
	v_cvt_pk_bf16_f32 v43, v44, v45
	global_store_dwordx2 v[56:57], v[42:43], off offset:8
	s_nop 0
	s_nop 0
	s_waitcnt vmcnt(18)
	v_pk_fma_f32 v[44:45], v[118:119], v[40:41], v[234:235]
	v_pk_fma_f32 v[42:43], v[120:121], v[38:39], v[232:233]
	s_nop 0
	v_cvt_pk_bf16_f32 v38, v42, v43
	v_cvt_pk_bf16_f32 v39, v44, v45
	global_store_dwordx2 v[62:63], v[38:39], off offset:256
	s_nop 0
	s_nop 0
	v_mul_f32_e32 v38, v42, v208
	v_mul_f32_e32 v39, v43, v209
	v_mul_f32_e32 v40, v44, v210
	v_mul_f32_e32 v41, v45, v211
	v_cvt_pk_bf16_f32 v38, v38, v39
	v_cvt_pk_bf16_f32 v39, v40, v41
	global_store_dwordx2 v[56:57], v[38:39], off offset:256
	s_nop 0
	s_nop 0
	s_waitcnt vmcnt(19)
	v_pk_fma_f32 v[40:41], v[114:115], v[36:37], v[238:239]
	v_pk_fma_f32 v[58:59], v[116:117], v[34:35], v[236:237]
	s_nop 0
	v_cvt_pk_bf16_f32 v34, v58, v59
	v_cvt_pk_bf16_f32 v35, v40, v41
	global_store_dwordx2 v[62:63], v[34:35], off offset:264
	s_nop 0
	v_mul_f32_e32 v34, v53, v53
	v_mul_f32_e32 v35, v55, v55
	v_fmac_f32_e32 v34, v52, v52
	v_fmac_f32_e32 v35, v54, v54
	v_add_f32_e32 v34, v34, v35
	v_mul_f32_e32 v35, v47, v47
	v_mul_f32_e32 v47, v49, v49
	v_fmac_f32_e32 v35, v46, v46
	v_fmac_f32_e32 v47, v48, v48
	v_add_f32_e32 v35, v35, v47
	v_add_f32_e32 v34, v34, v35
	v_mul_f32_e32 v35, v43, v43
	v_mul_f32_e32 v43, v45, v45
	v_fmac_f32_e32 v35, v42, v42
	v_fmac_f32_e32 v43, v44, v44
	v_add_f32_e32 v35, v35, v43
	v_add_f32_e32 v34, v34, v35
	v_mul_f32_e32 v35, v59, v59
	v_mul_f32_e32 v42, v41, v41
	v_fmac_f32_e32 v35, v58, v58
	v_fmac_f32_e32 v42, v40, v40
	v_add_f32_e32 v35, v35, v42
	v_add_f32_e32 v34, v34, v35
	ds_bpermute_b32 v35, v162, v34
	s_waitcnt lgkmcnt(0)
	v_add_f32_e32 v34, v34, v35
	ds_bpermute_b32 v35, v163, v34
	s_nop 0
	v_mul_f32_e32 v36, v58, v216
	v_mul_f32_e32 v37, v59, v217
	v_mul_f32_e32 v38, v40, v218
	v_mul_f32_e32 v39, v41, v219
	v_cvt_pk_bf16_f32 v36, v36, v37
	v_cvt_pk_bf16_f32 v37, v38, v39
	global_store_dwordx2 v[56:57], v[36:37], off offset:264
	s_and_saveexec_b64 s[52:53], s[4:5]
	s_cbranch_execz .LBB0_893
	s_waitcnt lgkmcnt(0)
	v_add_f32_e32 v36, v34, v35
	v_lshlrev_b64 v[34:35], 8, v[50:51]
	v_lshl_add_u64 v[34:35], s[22:23], 0, v[34:35]
	v_lshl_add_u64 v[34:35], s[50:51], 2, v[34:35]
	s_lshl_b32 s14, s66, 2
	v_lshl_add_u64 v[34:35], v[34:35], 0, s[14:15]
	global_store_dword v[34:35], v36, off
; __device__ __forceinline__ unsigned cvt_pk_bf16(float lo, float hi) { unsigned r; asm volatile("v_cvt_pk_bf16_f32 %0, %1, %2" : "=v"(r) : "v"(lo), "v"(hi)); return r; }
;     __device__ __forceinline__ void operator()(const f32x4 (&acc)[2][2][4][2], const Unit& u, int wr, int wc, int fr, int fq) const {
;     ...
;             for (int m = 0; m < 4; ++m) { const int row = row0 + ai * HALF + m * 16; const size_t ro = (size_t)row * ldc + col0; float ss = 0.f; const float rs = xs[row];
; #pragma unroll
;                 for (int bj = 0; bj < 2; ++bj)
; #pragma unroll
;                     for (int n = 0; n < 2; ++n) { const i32x4 ia = __builtin_bit_cast(i32x4, acc[ai][bj][m][n]);
;                         const f32x4 af = (f32x4){(float)ia[0], (float)ia[1], (float)ia[2], (float)ia[3]} * rs * cs[bj][n];
;                         f32x4 rv; if constexpr (RB16) { const u32x2 rb = *(const u32x2*)((const bf16_t*)R + ro + bj * HALF + n * 4); rv = (f32x4){__uint_as_float(rb.x << 16), __uint_as_float(rb.x & 0xffff0000u), __uint_as_float(rb.y << 16), __uint_as_float(rb.y & 0xffff0000u)}; }
;                         else rv = *(const f32x4*)((const float*)R + ro + bj * HALF + n * 4);
;                         const f32x4 v = af + rv; { u32x2 hb; hb.x = cvt_pk_bf16(v[0], v[1]); hb.y = cvt_pk_bf16(v[2], v[3]); *(u32x2*)(C + ro + bj * HALF + n * 4) = hb; }
;                         const f32x4 g = *(const f32x4*)(gain + col0 + bj * HALF + n * 4);
;                         u32x2 o; o.x = cvt_pk_bf16(v[0] * g[0], v[1] * g[1]); o.y = cvt_pk_bf16(v[2] * g[2], v[3] * g[3]); *(u32x2*)(HG + ro + bj * HALF + n * 4) = o;
;                         ss += (v[0] * v[0] + v[1] * v[1]) + (v[2] * v[2] + v[3] * v[3]); }
;                 ss += __shfl_xor(ss, 16); ss += __shfl_xor(ss, 32);
;                 if (fq == 0) SS[(size_t)row * 64 + u.pn * 4 + wc] = ss; }
.LBB0_893:
	s_or_b64 exec, exec, s[52:53]
	global_load_dword v250, v[150:151], off offset:704
	v_add_u32_e32 v254, 0xb0, v148
	v_ashrrev_i32_e32 v255, 31, v254
	v_lshlrev_b64 v[248:249], 12, v[254:255]
	v_lshl_add_u64 v[230:231], v[248:249], 0, v[146:147]
	v_lshl_add_u64 v[252:253], v[230:231], 2, s[10:11]
	global_load_dwordx4 v[220:223], v[252:253], off
	global_load_dwordx4 v[224:227], v[252:253], off offset:16
	global_load_dwordx4 v[232:235], v[252:253], off offset:512
	global_load_dwordx4 v[236:239], v[252:253], off offset:528
	v_add_u32_e32 v34, 0xa0, v148
	s_waitcnt lgkmcnt(0)
	v_ashrrev_i32_e32 v35, 31, v34
	v_lshlrev_b64 v[36:37], 12, v[34:35]
	v_lshl_add_u64 v[40:41], v[36:37], 0, v[146:147]
	s_nop 0
	v_lshl_add_u64 v[44:45], v[40:41], 2, s[10:11]
	s_nop 0
	v_cvt_f32_i32_e32 v33, v33
	v_cvt_f32_i32_e32 v31, v31
	v_cvt_f32_i32_e32 v30, v30
	v_cvt_f32_i32_e32 v32, v32
	v_lshlrev_b64 v[40:41], 1, v[40:41]
	v_lshl_add_u64 v[46:47], s[18:19], 0, v[40:41]
	v_lshl_add_u64 v[40:41], s[20:21], 0, v[40:41]
	v_cvt_f32_i32_e32 v29, v29
	v_cvt_f32_i32_e32 v27, v27
	v_cvt_f32_i32_e32 v26, v26
	v_cvt_f32_i32_e32 v28, v28
	v_cvt_f32_i32_e32 v25, v25
	v_cvt_f32_i32_e32 v23, v23
	v_cvt_f32_i32_e32 v22, v22
	v_cvt_f32_i32_e32 v24, v24
	v_cvt_f32_i32_e32 v21, v21
	v_cvt_f32_i32_e32 v19, v19
	v_cvt_f32_i32_e32 v18, v18
	v_cvt_f32_i32_e32 v20, v20
	s_nop 0
	s_waitcnt vmcnt(17)
	v_pk_mul_f32 v[30:31], v[214:215], v[30:31] op_sel_hi:[0,1]
	v_pk_mul_f32 v[32:33], v[214:215], v[32:33] op_sel_hi:[0,1]
	s_nop 0
	s_waitcnt vmcnt(16)
	v_pk_fma_f32 v[38:39], v[128:129], v[32:33], v[242:243]
	v_pk_fma_f32 v[36:37], v[152:153], v[30:31], v[240:241]
	v_pk_mul_f32 v[26:27], v[214:215], v[26:27] op_sel_hi:[0,1]
	v_cvt_pk_bf16_f32 v30, v36, v37
	v_cvt_pk_bf16_f32 v31, v38, v39
	global_store_dwordx2 v[46:47], v[30:31], off
	s_nop 0
	v_pk_mul_f32 v[28:29], v[214:215], v[28:29] op_sel_hi:[0,1]
	v_pk_mul_f32 v[22:23], v[214:215], v[22:23] op_sel_hi:[0,1]
	v_pk_mul_f32 v[24:25], v[214:215], v[24:25] op_sel_hi:[0,1]
	v_pk_mul_f32 v[18:19], v[214:215], v[18:19] op_sel_hi:[0,1]
	v_pk_mul_f32 v[20:21], v[214:215], v[20:21] op_sel_hi:[0,1]
	s_nop 0
	v_mul_f32_e32 v30, v192, v36
	v_mul_f32_e32 v31, v193, v37
	v_mul_f32_e32 v32, v194, v38
	v_mul_f32_e32 v33, v195, v39
	v_cvt_pk_bf16_f32 v30, v30, v31
	v_cvt_pk_bf16_f32 v31, v32, v33
	global_store_dwordx2 v[40:41], v[30:31], off
	s_nop 0
	s_nop 0
	s_waitcnt vmcnt(17)
	v_pk_fma_f32 v[32:33], v[122:123], v[28:29], v[246:247]
	v_pk_fma_f32 v[30:31], v[124:125], v[26:27], v[244:245]
	s_nop 0
	v_cvt_pk_bf16_f32 v26, v30, v31
	v_cvt_pk_bf16_f32 v27, v32, v33
	global_store_dwordx2 v[46:47], v[26:27], off offset:8
	s_nop 0
	s_nop 0
	v_mul_f32_e32 v26, v30, v200
	v_mul_f32_e32 v27, v31, v201
	v_mul_f32_e32 v28, v32, v202
	v_mul_f32_e32 v29, v33, v203
	v_cvt_pk_bf16_f32 v26, v26, v27
	v_cvt_pk_bf16_f32 v27, v28, v29
	global_store_dwordx2 v[40:41], v[26:27], off offset:8
	s_nop 0
	s_nop 0
	s_waitcnt vmcnt(18)
	v_pk_fma_f32 v[28:29], v[118:119], v[24:25], v[198:199]
	v_pk_fma_f32 v[26:27], v[120:121], v[22:23], v[196:197]
	s_nop 0
	v_cvt_pk_bf16_f32 v22, v26, v27
	v_cvt_pk_bf16_f32 v23, v28, v29
	global_store_dwordx2 v[46:47], v[22:23], off offset:256
	s_nop 0
	s_nop 0
	v_mul_f32_e32 v22, v26, v208
	v_mul_f32_e32 v23, v27, v209
	v_mul_f32_e32 v24, v28, v210
	v_mul_f32_e32 v25, v29, v211
	v_cvt_pk_bf16_f32 v22, v22, v23
	v_cvt_pk_bf16_f32 v23, v24, v25
	global_store_dwordx2 v[40:41], v[22:23], off offset:256
	s_nop 0
	s_nop 0
	s_waitcnt vmcnt(19)
	v_pk_fma_f32 v[24:25], v[114:115], v[20:21], v[206:207]
	v_pk_fma_f32 v[42:43], v[116:117], v[18:19], v[204:205]
	s_nop 0
	v_cvt_pk_bf16_f32 v18, v42, v43
	v_cvt_pk_bf16_f32 v19, v24, v25
	global_store_dwordx2 v[46:47], v[18:19], off offset:264
	s_nop 0
	v_mul_f32_e32 v18, v37, v37
	v_mul_f32_e32 v19, v39, v39
	v_fmac_f32_e32 v18, v36, v36
	v_fmac_f32_e32 v19, v38, v38
	v_add_f32_e32 v18, v18, v19
	v_mul_f32_e32 v19, v31, v31
	v_mul_f32_e32 v31, v33, v33
	v_fmac_f32_e32 v19, v30, v30
	v_fmac_f32_e32 v31, v32, v32
	v_add_f32_e32 v19, v19, v31
	v_add_f32_e32 v18, v18, v19
	v_mul_f32_e32 v19, v27, v27
	v_mul_f32_e32 v27, v29, v29
	v_fmac_f32_e32 v19, v26, v26
	v_fmac_f32_e32 v27, v28, v28
	v_add_f32_e32 v19, v19, v27
	v_add_f32_e32 v18, v18, v19
	v_mul_f32_e32 v19, v43, v43
	v_mul_f32_e32 v26, v25, v25
	v_fmac_f32_e32 v19, v42, v42
	v_fmac_f32_e32 v26, v24, v24
	v_add_f32_e32 v19, v19, v26
	v_add_f32_e32 v18, v18, v19
	ds_bpermute_b32 v19, v162, v18
	s_waitcnt lgkmcnt(0)
	v_add_f32_e32 v18, v18, v19
	ds_bpermute_b32 v19, v163, v18
	s_nop 0
	v_mul_f32_e32 v20, v42, v216
	v_mul_f32_e32 v21, v43, v217
	v_mul_f32_e32 v22, v24, v218
	v_mul_f32_e32 v23, v25, v219
	v_cvt_pk_bf16_f32 v20, v20, v21
	v_cvt_pk_bf16_f32 v21, v22, v23
	global_store_dwordx2 v[40:41], v[20:21], off offset:264
	s_and_saveexec_b64 s[52:53], s[4:5]
	s_cbranch_execz .LBB0_895
	s_waitcnt lgkmcnt(0)
	v_add_f32_e32 v20, v18, v19
	v_lshlrev_b64 v[18:19], 8, v[34:35]
	v_lshl_add_u64 v[18:19], s[22:23], 0, v[18:19]
	v_lshl_add_u64 v[18:19], s[50:51], 2, v[18:19]
	s_lshl_b32 s14, s66, 2
	v_lshl_add_u64 v[18:19], v[18:19], 0, s[14:15]
	global_store_dword v[18:19], v20, off
; __device__ __forceinline__ unsigned cvt_pk_bf16(float lo, float hi) { unsigned r; asm volatile("v_cvt_pk_bf16_f32 %0, %1, %2" : "=v"(r) : "v"(lo), "v"(hi)); return r; }
;     __device__ __forceinline__ void operator()(const f32x4 (&acc)[2][2][4][2], const Unit& u, int wr, int wc, int fr, int fq) const {
;     ...
;             for (int m = 0; m < 4; ++m) { const int row = row0 + ai * HALF + m * 16; const size_t ro = (size_t)row * ldc + col0; float ss = 0.f; const float rs = xs[row];
; #pragma unroll
;                 for (int bj = 0; bj < 2; ++bj)
; #pragma unroll
;                     for (int n = 0; n < 2; ++n) { const i32x4 ia = __builtin_bit_cast(i32x4, acc[ai][bj][m][n]);
;                         const f32x4 af = (f32x4){(float)ia[0], (float)ia[1], (float)ia[2], (float)ia[3]} * rs * cs[bj][n];
;                         f32x4 rv; if constexpr (RB16) { const u32x2 rb = *(const u32x2*)((const bf16_t*)R + ro + bj * HALF + n * 4); rv = (f32x4){__uint_as_float(rb.x << 16), __uint_as_float(rb.x & 0xffff0000u), __uint_as_float(rb.y << 16), __uint_as_float(rb.y & 0xffff0000u)}; }
;                         else rv = *(const f32x4*)((const float*)R + ro + bj * HALF + n * 4);
;                         const f32x4 v = af + rv; { u32x2 hb; hb.x = cvt_pk_bf16(v[0], v[1]); hb.y = cvt_pk_bf16(v[2], v[3]); *(u32x2*)(C + ro + bj * HALF + n * 4) = hb; }
;                         const f32x4 g = *(const f32x4*)(gain + col0 + bj * HALF + n * 4);
;                         u32x2 o; o.x = cvt_pk_bf16(v[0] * g[0], v[1] * g[1]); o.y = cvt_pk_bf16(v[2] * g[2], v[3] * g[3]); *(u32x2*)(HG + ro + bj * HALF + n * 4) = o;
;                         ss += (v[0] * v[0] + v[1] * v[1]) + (v[2] * v[2] + v[3] * v[3]); }
;                 ss += __shfl_xor(ss, 16); ss += __shfl_xor(ss, 32);
;                 if (fq == 0) SS[(size_t)row * 64 + u.pn * 4 + wc] = ss; }
.LBB0_895:
	s_or_b64 exec, exec, s[52:53]
	v_add_u32_e32 v18, 0xb0, v148
	s_waitcnt lgkmcnt(0)
	v_ashrrev_i32_e32 v19, 31, v18
	v_lshlrev_b64 v[20:21], 12, v[18:19]
	v_lshl_add_u64 v[24:25], v[20:21], 0, v[146:147]
	s_nop 0
	v_lshl_add_u64 v[28:29], v[24:25], 2, s[10:11]
	s_nop 0
	v_cvt_f32_i32_e32 v17, v17
	v_cvt_f32_i32_e32 v15, v15
	v_cvt_f32_i32_e32 v14, v14
	v_cvt_f32_i32_e32 v16, v16
	v_lshlrev_b64 v[24:25], 1, v[24:25]
	v_lshl_add_u64 v[30:31], s[18:19], 0, v[24:25]
	v_lshl_add_u64 v[24:25], s[20:21], 0, v[24:25]
	v_cvt_f32_i32_e32 v13, v13
	v_cvt_f32_i32_e32 v11, v11
	v_cvt_f32_i32_e32 v10, v10
	v_cvt_f32_i32_e32 v12, v12
	v_cvt_f32_i32_e32 v9, v9
	v_cvt_f32_i32_e32 v7, v7
	v_cvt_f32_i32_e32 v6, v6
	v_cvt_f32_i32_e32 v8, v8
	v_cvt_f32_i32_e32 v5, v5
	v_cvt_f32_i32_e32 v3, v3
	v_cvt_f32_i32_e32 v2, v2
	v_cvt_f32_i32_e32 v4, v4
	s_nop 0
	s_waitcnt vmcnt(12)
	v_pk_mul_f32 v[14:15], v[250:251], v[14:15] op_sel_hi:[0,1]
	v_pk_mul_f32 v[16:17], v[250:251], v[16:17] op_sel_hi:[0,1]
	s_nop 0
	s_waitcnt vmcnt(11)
	v_pk_fma_f32 v[22:23], v[128:129], v[16:17], v[222:223]
	v_pk_fma_f32 v[20:21], v[152:153], v[14:15], v[220:221]
	v_pk_mul_f32 v[10:11], v[250:251], v[10:11] op_sel_hi:[0,1]
	v_cvt_pk_bf16_f32 v14, v20, v21
	v_cvt_pk_bf16_f32 v15, v22, v23
	global_store_dwordx2 v[30:31], v[14:15], off
	s_nop 0
	v_pk_mul_f32 v[12:13], v[250:251], v[12:13] op_sel_hi:[0,1]
	v_pk_mul_f32 v[6:7], v[250:251], v[6:7] op_sel_hi:[0,1]
	v_pk_mul_f32 v[8:9], v[250:251], v[8:9] op_sel_hi:[0,1]
	v_pk_mul_f32 v[2:3], v[250:251], v[2:3] op_sel_hi:[0,1]
	v_pk_mul_f32 v[4:5], v[250:251], v[4:5] op_sel_hi:[0,1]
	s_nop 0
	v_mul_f32_e32 v14, v192, v20
	v_mul_f32_e32 v15, v193, v21
	v_mul_f32_e32 v16, v194, v22
	v_mul_f32_e32 v17, v195, v23
	v_cvt_pk_bf16_f32 v14, v14, v15
	v_cvt_pk_bf16_f32 v15, v16, v17
	global_store_dwordx2 v[24:25], v[14:15], off
	s_nop 0
	s_nop 0
	s_waitcnt vmcnt(12)
	v_pk_fma_f32 v[16:17], v[122:123], v[12:13], v[226:227]
	v_pk_fma_f32 v[14:15], v[124:125], v[10:11], v[224:225]
	s_nop 0
	v_cvt_pk_bf16_f32 v10, v14, v15
	v_cvt_pk_bf16_f32 v11, v16, v17
	global_store_dwordx2 v[30:31], v[10:11], off offset:8
	s_nop 0
	s_nop 0
	v_mul_f32_e32 v10, v14, v200
	v_mul_f32_e32 v11, v15, v201
	v_mul_f32_e32 v12, v16, v202
	v_mul_f32_e32 v13, v17, v203
	v_cvt_pk_bf16_f32 v10, v10, v11
	v_cvt_pk_bf16_f32 v11, v12, v13
	global_store_dwordx2 v[24:25], v[10:11], off offset:8
	s_nop 0
	s_nop 0
	s_waitcnt vmcnt(13)
	v_pk_fma_f32 v[12:13], v[118:119], v[8:9], v[234:235]
	v_pk_fma_f32 v[10:11], v[120:121], v[6:7], v[232:233]
	s_nop 0
	v_cvt_pk_bf16_f32 v6, v10, v11
	v_cvt_pk_bf16_f32 v7, v12, v13
	global_store_dwordx2 v[30:31], v[6:7], off offset:256
	s_nop 0
	s_nop 0
	v_mul_f32_e32 v6, v10, v208
	v_mul_f32_e32 v7, v11, v209
	v_mul_f32_e32 v8, v12, v210
	v_mul_f32_e32 v9, v13, v211
	v_cvt_pk_bf16_f32 v6, v6, v7
	v_cvt_pk_bf16_f32 v7, v8, v9
	global_store_dwordx2 v[24:25], v[6:7], off offset:256
	s_nop 0
	s_nop 0
	s_waitcnt vmcnt(14)
	v_pk_fma_f32 v[8:9], v[114:115], v[4:5], v[238:239]
	v_pk_fma_f32 v[26:27], v[116:117], v[2:3], v[236:237]
	s_nop 0
	v_cvt_pk_bf16_f32 v2, v26, v27
	v_cvt_pk_bf16_f32 v3, v8, v9
	global_store_dwordx2 v[30:31], v[2:3], off offset:264
	s_nop 0
	v_mul_f32_e32 v2, v21, v21
	v_mul_f32_e32 v3, v23, v23
	v_fmac_f32_e32 v2, v20, v20
	v_fmac_f32_e32 v3, v22, v22
	v_add_f32_e32 v2, v2, v3
	v_mul_f32_e32 v3, v15, v15
	v_mul_f32_e32 v15, v17, v17
	v_fmac_f32_e32 v3, v14, v14
	v_fmac_f32_e32 v15, v16, v16
	v_add_f32_e32 v3, v3, v15
	v_add_f32_e32 v2, v2, v3
	v_mul_f32_e32 v3, v11, v11
	v_mul_f32_e32 v11, v13, v13
	v_fmac_f32_e32 v3, v10, v10
	v_fmac_f32_e32 v11, v12, v12
	v_add_f32_e32 v3, v3, v11
	v_add_f32_e32 v2, v2, v3
	v_mul_f32_e32 v3, v27, v27
	v_mul_f32_e32 v10, v9, v9
	v_fmac_f32_e32 v3, v26, v26
	v_fmac_f32_e32 v10, v8, v8
	v_add_f32_e32 v3, v3, v10
	v_add_f32_e32 v2, v2, v3
	ds_bpermute_b32 v3, v162, v2
	s_waitcnt lgkmcnt(0)
	v_add_f32_e32 v2, v2, v3
	ds_bpermute_b32 v3, v163, v2
	s_nop 0
	v_mul_f32_e32 v4, v26, v216
	v_mul_f32_e32 v5, v27, v217
	v_mul_f32_e32 v6, v8, v218
	v_mul_f32_e32 v7, v9, v219
	v_cvt_pk_bf16_f32 v4, v4, v5
	v_cvt_pk_bf16_f32 v5, v6, v7
	global_store_dwordx2 v[24:25], v[4:5], off offset:264
	s_and_saveexec_b64 s[52:53], s[4:5]
	s_cbranch_execz .LBB0_897
	s_waitcnt lgkmcnt(0)
	v_add_f32_e32 v4, v2, v3
	v_lshlrev_b64 v[2:3], 8, v[18:19]
	v_lshl_add_u64 v[2:3], s[22:23], 0, v[2:3]
	v_lshl_add_u64 v[2:3], s[50:51], 2, v[2:3]
	s_lshl_b32 s14, s66, 2
	v_lshl_add_u64 v[2:3], v[2:3], 0, s[14:15]
	global_store_dword v[2:3], v4, off

; __device__ __forceinline__ unsigned cvt_pk_bf16(float lo, float hi) { unsigned r; asm volatile("v_cvt_pk_bf16_f32 %0, %1, %2" : "=v"(r) : "v"(lo), "v"(hi)); return r; }
;     __device__ __forceinline__ void operator()(const f32x4 (&acc)[2][2][4][2], const Unit& u, int wr, int wc, int fr, int fq) const {
;     ...
;         f32x4 cs[2][2];
; #pragma unroll
;         for (int bj = 0; bj < 2; ++bj)
; #pragma unroll
;             for (int n = 0; n < 2; ++n) { const u32x4 c = *(const u32x4*)(cmax + col0 + bj * HALF + n * 4);
;                 cs[bj][n] = (f32x4){__uint_as_float(c.x << 16), __uint_as_float(c.y << 16), __uint_as_float(c.z << 16), __uint_as_float(c.w << 16)} * (1.0f / 127.0f); }
; #pragma unroll
;         for (int ai = 0; ai < 2; ++ai)
; #pragma unroll
;             for (int m = 0; m < 4; ++m) { const int row = row0 + ai * HALF + m * 16; const size_t ro = (size_t)row * ldc + col0; float ss = 0.f; const float rs = xs[row];
; #pragma unroll
;                 for (int bj = 0; bj < 2; ++bj)
; #pragma unroll
;                     for (int n = 0; n < 2; ++n) { const i32x4 ia = __builtin_bit_cast(i32x4, acc[ai][bj][m][n]);
;                         const f32x4 af = (f32x4){(float)ia[0], (float)ia[1], (float)ia[2], (float)ia[3]} * rs * cs[bj][n];
;                         f32x4 rv; if constexpr (RB16) { const u32x2 rb = *(const u32x2*)((const bf16_t*)R + ro + bj * HALF + n * 4); rv = (f32x4){__uint_as_float(rb.x << 16), __uint_as_float(rb.x & 0xffff0000u), __uint_as_float(rb.y << 16), __uint_as_float(rb.y & 0xffff0000u)}; }
;                         else rv = *(const f32x4*)((const float*)R + ro + bj * HALF + n * 4);
;                         const f32x4 v = af + rv; { u32x2 hb; hb.x = cvt_pk_bf16(v[0], v[1]); hb.y = cvt_pk_bf16(v[2], v[3]); *(u32x2*)(C + ro + bj * HALF + n * 4) = hb; }
;                         const f32x4 g = *(const f32x4*)(gain + col0 + bj * HALF + n * 4);
;                         u32x2 o; o.x = cvt_pk_bf16(v[0] * g[0], v[1] * g[1]); o.y = cvt_pk_bf16(v[2] * g[2], v[3] * g[3]); *(u32x2*)(HG + ro + bj * HALF + n * 4) = o;
;                         ss += (v[0] * v[0] + v[1] * v[1]) + (v[2] * v[2] + v[3] * v[3]); }
.LBB0_1942:
	v_lshl_or_b32 v146, s10, 8, v157
	v_lshl_add_u32 v148, s48, 8, v1
	v_ashrrev_i32_e32 v147, 31, v146
	v_ashrrev_i32_e32 v149, 31, v148
	v_lshlrev_b64 v[166:167], 2, v[146:147]
	v_lshlrev_b64 v[162:163], 12, v[148:149]
	v_lshl_add_u64 v[170:171], s[24:25], 0, v[166:167]
	v_lshl_add_u64 v[162:163], v[162:163], 0, v[146:147]
	global_load_dwordx4 v[152:155], v[170:171], off
	v_lshl_add_u64 v[150:151], v[148:149], 2, s[22:23]
	v_lshlrev_b64 v[180:181], 1, v[162:163]
	global_load_dword v178, v[150:151], off
	v_lshl_add_u64 v[182:183], s[14:15], 0, v[180:181]
	global_load_dwordx2 v[174:175], v[182:183], off
	global_load_dwordx4 v[162:165], v[170:171], off offset:528
	v_cvt_f32_i32_e32 v129, v129
	v_cvt_f32_i32_e32 v128, v128
	v_cvt_f32_i32_e32 v177, v127
	v_cvt_f32_i32_e32 v176, v126
	v_lshl_add_u64 v[126:127], s[18:19], 0, v[166:167]
	global_load_dwordx4 v[166:169], v[170:171], off offset:16
	s_nop 0
	global_load_dwordx4 v[170:173], v[170:171], off offset:512
	v_cvt_f32_i32_e32 v125, v125
	v_cvt_f32_i32_e32 v124, v124
	v_cvt_f32_i32_e32 v123, v123
	v_cvt_f32_i32_e32 v122, v122
	v_lshl_add_u64 v[180:181], s[16:17], 0, v[180:181]
	v_cvt_f32_i32_e32 v121, v121
	v_cvt_f32_i32_e32 v120, v120
	v_cvt_f32_i32_e32 v119, v119
	v_cvt_f32_i32_e32 v118, v118
	v_cvt_f32_i32_e32 v117, v117
	v_cvt_f32_i32_e32 v116, v116
	v_cvt_f32_i32_e32 v115, v115
	v_cvt_f32_i32_e32 v114, v114
	s_lshl_b32 s48, s10, 2
	s_ashr_i32 s49, s48, 31
	global_load_dwordx4 v[192:195], v[126:127], off
	global_load_dwordx2 v[248:249], v[182:183], off offset:8
	global_load_dwordx4 v[196:199], v[126:127], off offset:16
	global_load_dwordx2 v[250:251], v[182:183], off offset:256
	global_load_dwordx4 v[200:203], v[126:127], off offset:512
	global_load_dwordx2 v[244:245], v[182:183], off offset:264
	global_load_dwordx4 v[204:207], v[126:127], off offset:528
	v_or_b32_e32 v190, 16, v148
	v_ashrrev_i32_e32 v191, 31, v190
	v_lshl_add_u64 v[230:231], v[190:191], 2, s[22:23]
	global_load_dword v246, v[230:231], off
	v_or_b32_e32 v252, 16, v148
	v_ashrrev_i32_e32 v253, 31, v252
	v_lshlrev_b64 v[254:255], 12, v[252:253]
	v_lshl_add_u64 v[254:255], v[254:255], 0, v[146:147]
	v_lshlrev_b64 v[254:255], 1, v[254:255]
	v_lshl_add_u64 v[190:191], s[14:15], 0, v[254:255]
	global_load_dwordx2 v[240:241], v[190:191], off
	global_load_dwordx2 v[242:243], v[190:191], off offset:8
	global_load_dwordx2 v[236:237], v[190:191], off offset:256
	global_load_dwordx2 v[238:239], v[190:191], off offset:264
	s_nop 0
	s_waitcnt vmcnt(17)
	v_lshlrev_b32_e32 v184, 16, v152
	v_lshlrev_b32_e32 v185, 16, v153
	v_lshlrev_b32_e32 v152, 16, v154
	v_lshlrev_b32_e32 v153, 16, v155
	s_waitcnt vmcnt(16)
	v_pk_mul_f32 v[154:155], v[178:179], v[176:177] op_sel_hi:[0,1]
	v_pk_mul_f32 v[176:177], v[178:179], v[128:129] op_sel_hi:[0,1]
	v_pk_mul_f32 v[152:153], v[152:153], s[36:37] op_sel_hi:[1,0]
	v_pk_mul_f32 v[128:129], v[184:185], s[36:37] op_sel_hi:[1,0]
	s_waitcnt vmcnt(15)
	v_lshlrev_b32_e32 v184, 16, v174
	v_and_b32_e32 v185, 0xffff0000, v174
	v_lshlrev_b32_e32 v174, 16, v175
	v_and_b32_e32 v175, 0xffff0000, v175
	v_pk_fma_f32 v[186:187], v[176:177], v[152:153], v[174:175]
	v_pk_fma_f32 v[154:155], v[154:155], v[128:129], v[184:185]
	s_waitcnt vmcnt(13)
	v_lshlrev_b32_e32 v166, 16, v166
	v_cvt_pk_bf16_f32 v174, v154, v155
	v_cvt_pk_bf16_f32 v175, v186, v187
	global_store_dwordx2 v[182:183], v[174:175], off
	s_nop 0
	v_lshlrev_b32_e32 v167, 16, v167
	v_lshlrev_b32_e32 v168, 16, v168
	v_lshlrev_b32_e32 v169, 16, v169
	v_pk_mul_f32 v[184:185], v[178:179], v[122:123] op_sel_hi:[0,1]
	v_pk_mul_f32 v[188:189], v[178:179], v[124:125] op_sel_hi:[0,1]
	v_pk_mul_f32 v[124:125], v[168:169], s[36:37] op_sel_hi:[1,0]
	v_pk_mul_f32 v[122:123], v[166:167], s[36:37] op_sel_hi:[1,0]
	s_waitcnt vmcnt(13)
	v_lshlrev_b32_e32 v170, 16, v170
	v_lshlrev_b32_e32 v171, 16, v171
	v_lshlrev_b32_e32 v172, 16, v172
	v_lshlrev_b32_e32 v173, 16, v173
	v_lshlrev_b32_e32 v162, 16, v162
	v_lshlrev_b32_e32 v163, 16, v163
	v_lshlrev_b32_e32 v164, 16, v164
	v_lshlrev_b32_e32 v165, 16, v165
	s_nop 0
	s_waitcnt vmcnt(12)
	v_mul_f32_e32 v174, v192, v154
	v_mul_f32_e32 v175, v193, v155
	v_mul_f32_e32 v176, v194, v186
	v_mul_f32_e32 v177, v195, v187
	v_cvt_pk_bf16_f32 v174, v174, v175
	v_cvt_pk_bf16_f32 v175, v176, v177
	s_nop 0
	v_mul_f32_e32 v155, v155, v155
	global_store_dwordx2 v[180:181], v[174:175], off
	v_fmac_f32_e32 v155, v154, v154
	s_nop 0
	s_waitcnt vmcnt(12)
	v_lshlrev_b32_e32 v166, 16, v248
	v_and_b32_e32 v167, 0xffff0000, v248
	v_lshlrev_b32_e32 v168, 16, v249
	v_and_b32_e32 v169, 0xffff0000, v249
	v_pk_fma_f32 v[174:175], v[188:189], v[124:125], v[168:169]
	v_pk_fma_f32 v[176:177], v[184:185], v[122:123], v[166:167]
	v_pk_mul_f32 v[184:185], v[178:179], v[118:119] op_sel_hi:[0,1]
	v_cvt_pk_bf16_f32 v166, v176, v177
	v_cvt_pk_bf16_f32 v167, v174, v175
	global_store_dwordx2 v[182:183], v[166:167], off offset:8
	s_nop 0
	v_pk_mul_f32 v[188:189], v[178:179], v[120:121] op_sel_hi:[0,1]
	v_pk_mul_f32 v[120:121], v[172:173], s[36:37] op_sel_hi:[1,0]
	v_pk_mul_f32 v[118:119], v[170:171], s[36:37] op_sel_hi:[1,0]
	s_nop 0
	s_waitcnt vmcnt(12)
	v_mul_f32_e32 v166, v196, v176
	v_mul_f32_e32 v167, v197, v177
	v_mul_f32_e32 v168, v198, v174
	v_mul_f32_e32 v169, v199, v175
	v_cvt_pk_bf16_f32 v166, v166, v167
	v_cvt_pk_bf16_f32 v167, v168, v169
	s_nop 0
	v_mul_f32_e32 v175, v175, v175
	global_store_dwordx2 v[180:181], v[166:167], off offset:8
	v_fmac_f32_e32 v175, v174, v174
	s_nop 0
	s_waitcnt vmcnt(12)
; __device__ __forceinline__ unsigned cvt_pk_bf16(float lo, float hi) { unsigned r; asm volatile("v_cvt_pk_bf16_f32 %0, %1, %2" : "=v"(r) : "v"(lo), "v"(hi)); return r; }
;     __device__ __forceinline__ void operator()(const f32x4 (&acc)[2][2][4][2], const Unit& u, int wr, int wc, int fr, int fq) const {
;     ...
;             for (int m = 0; m < 4; ++m) { const int row = row0 + ai * HALF + m * 16; const size_t ro = (size_t)row * ldc + col0; float ss = 0.f; const float rs = xs[row];
; #pragma unroll
;                 for (int bj = 0; bj < 2; ++bj)
; #pragma unroll
;                     for (int n = 0; n < 2; ++n) { const i32x4 ia = __builtin_bit_cast(i32x4, acc[ai][bj][m][n]);
;                         const f32x4 af = (f32x4){(float)ia[0], (float)ia[1], (float)ia[2], (float)ia[3]} * rs * cs[bj][n];
;                         f32x4 rv; if constexpr (RB16) { const u32x2 rb = *(const u32x2*)((const bf16_t*)R + ro + bj * HALF + n * 4); rv = (f32x4){__uint_as_float(rb.x << 16), __uint_as_float(rb.x & 0xffff0000u), __uint_as_float(rb.y << 16), __uint_as_float(rb.y & 0xffff0000u)}; }
;                         else rv = *(const f32x4*)((const float*)R + ro + bj * HALF + n * 4);
;                         const f32x4 v = af + rv; { u32x2 hb; hb.x = cvt_pk_bf16(v[0], v[1]); hb.y = cvt_pk_bf16(v[2], v[3]); *(u32x2*)(C + ro + bj * HALF + n * 4) = hb; }
;                         const f32x4 g = *(const f32x4*)(gain + col0 + bj * HALF + n * 4);
;                         u32x2 o; o.x = cvt_pk_bf16(v[0] * g[0], v[1] * g[1]); o.y = cvt_pk_bf16(v[2] * g[2], v[3] * g[3]); *(u32x2*)(HG + ro + bj * HALF + n * 4) = o;
;                         ss += (v[0] * v[0] + v[1] * v[1]) + (v[2] * v[2] + v[3] * v[3]); }
;                 ss += __shfl_xor(ss, 16); ss += __shfl_xor(ss, 32);
;                 if (fq == 0) SS[(size_t)row * 64 + u.pn * 4 + wc] = ss; }
	v_lshlrev_b32_e32 v166, 16, v250
	v_and_b32_e32 v167, 0xffff0000, v250
	v_lshlrev_b32_e32 v168, 16, v251
	v_and_b32_e32 v169, 0xffff0000, v251
	v_pk_fma_f32 v[170:171], v[188:189], v[120:121], v[168:169]
	v_pk_fma_f32 v[172:173], v[184:185], v[118:119], v[166:167]
	v_pk_mul_f32 v[184:185], v[178:179], v[114:115] op_sel_hi:[0,1]
	v_cvt_pk_bf16_f32 v166, v172, v173
	v_cvt_pk_bf16_f32 v167, v170, v171
	global_store_dwordx2 v[182:183], v[166:167], off offset:256
	s_nop 0
	v_pk_mul_f32 v[178:179], v[178:179], v[116:117] op_sel_hi:[0,1]
	v_pk_mul_f32 v[116:117], v[164:165], s[36:37] op_sel_hi:[1,0]
	v_pk_mul_f32 v[114:115], v[162:163], s[36:37] op_sel_hi:[1,0]
	s_nop 0
	s_waitcnt vmcnt(12)
	v_mul_f32_e32 v166, v200, v172
	v_mul_f32_e32 v167, v201, v173
	v_mul_f32_e32 v168, v202, v170
	v_mul_f32_e32 v169, v203, v171
	v_cvt_pk_bf16_f32 v166, v166, v167
	v_cvt_pk_bf16_f32 v167, v168, v169
	s_nop 0
	v_mul_f32_e32 v171, v171, v171
	global_store_dwordx2 v[180:181], v[166:167], off offset:256
	v_fmac_f32_e32 v171, v170, v170
	s_nop 0
	s_waitcnt vmcnt(12)
	v_lshlrev_b32_e32 v162, 16, v244
	v_and_b32_e32 v163, 0xffff0000, v244
	v_lshlrev_b32_e32 v164, 16, v245
	v_and_b32_e32 v165, 0xffff0000, v245
	v_pk_fma_f32 v[168:169], v[178:179], v[116:117], v[164:165]
	v_pk_fma_f32 v[178:179], v[184:185], v[114:115], v[162:163]
	v_mul_f32_e32 v170, v169, v169
	v_cvt_pk_bf16_f32 v162, v178, v179
	v_cvt_pk_bf16_f32 v163, v168, v169
	global_store_dwordx2 v[182:183], v[162:163], off offset:264
	s_nop 0
	v_mul_f32_e32 v183, v187, v187
	v_fmac_f32_e32 v183, v186, v186
	v_add_f32_e32 v154, v155, v183
	v_mul_f32_e32 v155, v177, v177
	v_fmac_f32_e32 v155, v176, v176
	v_add_f32_e32 v155, v155, v175
	v_add_f32_e32 v154, v154, v155
	v_mul_f32_e32 v155, v173, v173
	v_fmac_f32_e32 v155, v172, v172
	v_and_b32_e32 v163, 64, v161
	v_add_f32_e32 v155, v155, v171
	v_xor_b32_e32 v162, 16, v161
	v_add_u32_e32 v163, 64, v163
	v_add_f32_e32 v154, v154, v155
	v_mul_f32_e32 v155, v179, v179
	v_cmp_lt_i32_e32 vcc, v162, v163
	v_fmac_f32_e32 v155, v178, v178
	v_fmac_f32_e32 v170, v168, v168
	v_cndmask_b32_e32 v162, v161, v162, vcc
	v_add_f32_e32 v155, v155, v170
	v_lshlrev_b32_e32 v162, 2, v162
	v_add_f32_e32 v154, v154, v155
	ds_bpermute_b32 v155, v162, v154
	v_xor_b32_e32 v182, 32, v161
	v_cmp_lt_i32_e32 vcc, v182, v163
	s_waitcnt lgkmcnt(0)
	v_add_f32_e32 v154, v154, v155
	v_cndmask_b32_e32 v163, v161, v182, vcc
	v_lshlrev_b32_e32 v163, 2, v163
	ds_bpermute_b32 v155, v163, v154
	s_nop 0
	s_waitcnt vmcnt(12)
	v_mul_f32_e32 v164, v204, v178
	v_mul_f32_e32 v165, v205, v179
	v_mul_f32_e32 v166, v206, v168
	v_mul_f32_e32 v167, v207, v169
	v_cvt_pk_bf16_f32 v164, v164, v165
	v_cvt_pk_bf16_f32 v165, v166, v167
	global_store_dwordx2 v[180:181], v[164:165], off offset:264
	s_and_saveexec_b64 s[50:51], s[4:5]
	s_cbranch_execz .LBB0_1944
	s_waitcnt lgkmcnt(0)
	v_add_f32_e32 v164, v154, v155
	v_lshlrev_b64 v[154:155], 8, v[148:149]
	v_lshl_add_u64 v[154:155], s[20:21], 0, v[154:155]
	v_lshl_add_u64 v[154:155], s[48:49], 2, v[154:155]
	s_lshl_b32 s10, s64, 2
	v_lshl_add_u64 v[154:155], v[154:155], 0, s[10:11]
	global_store_dword v[154:155], v164, off
.LBB0_1944:
	s_or_b64 exec, exec, s[50:51]
	v_or_b32_e32 v230, 32, v148
	v_ashrrev_i32_e32 v231, 31, v230
	v_lshl_add_u64 v[252:253], v[230:231], 2, s[22:23]
	global_load_dword v248, v[252:253], off
	v_or_b32_e32 v254, 32, v148
	v_ashrrev_i32_e32 v255, 31, v254
	v_lshlrev_b64 v[190:191], 12, v[254:255]
	v_lshl_add_u64 v[190:191], v[190:191], 0, v[146:147]
	v_lshlrev_b64 v[190:191], 1, v[190:191]
	v_lshl_add_u64 v[230:231], s[14:15], 0, v[190:191]
	global_load_dwordx2 v[250:251], v[230:231], off
	global_load_dwordx2 v[244:245], v[230:231], off offset:8
	global_load_dwordx2 v[232:233], v[230:231], off offset:256
	global_load_dwordx2 v[234:235], v[230:231], off offset:264
	v_or_b32_e32 v154, 16, v148
	s_waitcnt lgkmcnt(0)
	v_ashrrev_i32_e32 v155, 31, v154
	v_lshlrev_b64 v[164:165], 12, v[154:155]
	v_lshl_add_u64 v[164:165], v[164:165], 0, v[146:147]
	v_lshlrev_b64 v[164:165], 1, v[164:165]
	v_lshl_add_u64 v[166:167], v[154:155], 2, s[22:23]
	v_lshl_add_u64 v[168:169], s[14:15], 0, v[164:165]
	s_nop 0
	v_cvt_f32_i32_e32 v113, v113
	s_nop 0
	v_cvt_f32_i32_e32 v111, v111
	v_cvt_f32_i32_e32 v110, v110
	v_cvt_f32_i32_e32 v112, v112
	v_cvt_f32_i32_e32 v109, v109
	v_cvt_f32_i32_e32 v107, v107
	v_cvt_f32_i32_e32 v106, v106
	v_cvt_f32_i32_e32 v108, v108
	v_lshl_add_u64 v[164:165], s[16:17], 0, v[164:165]
	v_cvt_f32_i32_e32 v105, v105
	v_cvt_f32_i32_e32 v103, v103
	v_cvt_f32_i32_e32 v102, v102
	v_cvt_f32_i32_e32 v104, v104
	v_cvt_f32_i32_e32 v101, v101
	v_cvt_f32_i32_e32 v99, v99
	v_cvt_f32_i32_e32 v98, v98
	v_cvt_f32_i32_e32 v100, v100
	s_nop 0
	s_waitcnt vmcnt(17)
	v_pk_mul_f32 v[110:111], v[246:247], v[110:111] op_sel_hi:[0,1]
	v_pk_mul_f32 v[112:113], v[246:247], v[112:113] op_sel_hi:[0,1]
	s_nop 0
	s_waitcnt vmcnt(16)
	v_lshlrev_b32_e32 v172, 16, v240
	v_and_b32_e32 v173, 0xffff0000, v240
	v_lshlrev_b32_e32 v170, 16, v241
	v_and_b32_e32 v171, 0xffff0000, v241
	v_pk_fma_f32 v[170:171], v[152:153], v[112:113], v[170:171]
	v_pk_fma_f32 v[172:173], v[128:129], v[110:111], v[172:173]
	v_pk_mul_f32 v[106:107], v[246:247], v[106:107] op_sel_hi:[0,1]
	v_cvt_pk_bf16_f32 v110, v172, v173
	v_cvt_pk_bf16_f32 v111, v170, v171
	global_store_dwordx2 v[168:169], v[110:111], off
	s_nop 0
	v_pk_mul_f32 v[108:109], v[246:247], v[108:109] op_sel_hi:[0,1]
	v_pk_mul_f32 v[102:103], v[246:247], v[102:103] op_sel_hi:[0,1]
	v_pk_mul_f32 v[104:105], v[246:247], v[104:105] op_sel_hi:[0,1]
	v_pk_mul_f32 v[98:99], v[246:247], v[98:99] op_sel_hi:[0,1]
	v_pk_mul_f32 v[100:101], v[246:247], v[100:101] op_sel_hi:[0,1]
	s_nop 0
	v_mul_f32_e32 v110, v192, v172
	v_mul_f32_e32 v111, v193, v173
	v_mul_f32_e32 v112, v194, v170
	v_mul_f32_e32 v113, v195, v171
	v_cvt_pk_bf16_f32 v110, v110, v111
	v_cvt_pk_bf16_f32 v111, v112, v113
	s_nop 0
	s_nop 0
	global_store_dwordx2 v[164:165], v[110:111], off
	s_nop 0
	s_waitcnt vmcnt(17)
; __device__ __forceinline__ unsigned cvt_pk_bf16(float lo, float hi) { unsigned r; asm volatile("v_cvt_pk_bf16_f32 %0, %1, %2" : "=v"(r) : "v"(lo), "v"(hi)); return r; }
;     __device__ __forceinline__ void operator()(const f32x4 (&acc)[2][2][4][2], const Unit& u, int wr, int wc, int fr, int fq) const {
;     ...
;             for (int m = 0; m < 4; ++m) { const int row = row0 + ai * HALF + m * 16; const size_t ro = (size_t)row * ldc + col0; float ss = 0.f; const float rs = xs[row];
; #pragma unroll
;                 for (int bj = 0; bj < 2; ++bj)
; #pragma unroll
;                     for (int n = 0; n < 2; ++n) { const i32x4 ia = __builtin_bit_cast(i32x4, acc[ai][bj][m][n]);
;                         const f32x4 af = (f32x4){(float)ia[0], (float)ia[1], (float)ia[2], (float)ia[3]} * rs * cs[bj][n];
;                         f32x4 rv; if constexpr (RB16) { const u32x2 rb = *(const u32x2*)((const bf16_t*)R + ro + bj * HALF + n * 4); rv = (f32x4){__uint_as_float(rb.x << 16), __uint_as_float(rb.x & 0xffff0000u), __uint_as_float(rb.y << 16), __uint_as_float(rb.y & 0xffff0000u)}; }
;                         else rv = *(const f32x4*)((const float*)R + ro + bj * HALF + n * 4);
;                         const f32x4 v = af + rv; { u32x2 hb; hb.x = cvt_pk_bf16(v[0], v[1]); hb.y = cvt_pk_bf16(v[2], v[3]); *(u32x2*)(C + ro + bj * HALF + n * 4) = hb; }
;                         const f32x4 g = *(const f32x4*)(gain + col0 + bj * HALF + n * 4);
;                         u32x2 o; o.x = cvt_pk_bf16(v[0] * g[0], v[1] * g[1]); o.y = cvt_pk_bf16(v[2] * g[2], v[3] * g[3]); *(u32x2*)(HG + ro + bj * HALF + n * 4) = o;
;                         ss += (v[0] * v[0] + v[1] * v[1]) + (v[2] * v[2] + v[3] * v[3]); }
;                 ss += __shfl_xor(ss, 16); ss += __shfl_xor(ss, 32);
;                 if (fq == 0) SS[(size_t)row * 64 + u.pn * 4 + wc] = ss; }
	v_lshlrev_b32_e32 v110, 16, v242
	v_and_b32_e32 v111, 0xffff0000, v242
	v_lshlrev_b32_e32 v112, 16, v243
	v_and_b32_e32 v113, 0xffff0000, v243
	v_pk_fma_f32 v[112:113], v[124:125], v[108:109], v[112:113]
	v_pk_fma_f32 v[110:111], v[122:123], v[106:107], v[110:111]
	s_nop 0
	v_cvt_pk_bf16_f32 v106, v110, v111
	v_cvt_pk_bf16_f32 v107, v112, v113
	global_store_dwordx2 v[168:169], v[106:107], off offset:8
	s_nop 0
	s_nop 0
	v_mul_f32_e32 v106, v196, v110
	v_mul_f32_e32 v107, v197, v111
	v_mul_f32_e32 v108, v198, v112
	v_mul_f32_e32 v109, v199, v113
	v_cvt_pk_bf16_f32 v106, v106, v107
	v_cvt_pk_bf16_f32 v107, v108, v109
	s_nop 0
	s_nop 0
	global_store_dwordx2 v[164:165], v[106:107], off offset:8
	s_nop 0
	s_waitcnt vmcnt(18)
	v_lshlrev_b32_e32 v106, 16, v236
	v_and_b32_e32 v107, 0xffff0000, v236
	v_lshlrev_b32_e32 v108, 16, v237
	v_and_b32_e32 v109, 0xffff0000, v237
	v_pk_fma_f32 v[108:109], v[120:121], v[104:105], v[108:109]
	v_pk_fma_f32 v[106:107], v[118:119], v[102:103], v[106:107]
	s_nop 0
	v_cvt_pk_bf16_f32 v102, v106, v107
	v_cvt_pk_bf16_f32 v103, v108, v109
	global_store_dwordx2 v[168:169], v[102:103], off offset:256
	s_nop 0
	s_nop 0
	v_mul_f32_e32 v102, v200, v106
	v_mul_f32_e32 v103, v201, v107
	v_mul_f32_e32 v104, v202, v108
	v_mul_f32_e32 v105, v203, v109
	v_cvt_pk_bf16_f32 v102, v102, v103
	v_cvt_pk_bf16_f32 v103, v104, v105
	s_nop 0
	s_nop 0
	global_store_dwordx2 v[164:165], v[102:103], off offset:256
	s_nop 0
	s_waitcnt vmcnt(19)
	v_lshlrev_b32_e32 v102, 16, v238
	v_and_b32_e32 v103, 0xffff0000, v238
	v_lshlrev_b32_e32 v104, 16, v239
	v_and_b32_e32 v105, 0xffff0000, v239
	v_pk_fma_f32 v[104:105], v[116:117], v[100:101], v[104:105]
	v_pk_fma_f32 v[166:167], v[114:115], v[98:99], v[102:103]
	s_nop 0
	v_cvt_pk_bf16_f32 v98, v166, v167
	v_cvt_pk_bf16_f32 v99, v104, v105
	global_store_dwordx2 v[168:169], v[98:99], off offset:264
	s_nop 0
	v_mul_f32_e32 v98, v173, v173
	v_mul_f32_e32 v99, v171, v171
	v_fmac_f32_e32 v98, v172, v172
	v_fmac_f32_e32 v99, v170, v170
	v_add_f32_e32 v98, v98, v99
	v_mul_f32_e32 v99, v111, v111
	v_mul_f32_e32 v111, v113, v113
	v_fmac_f32_e32 v99, v110, v110
	v_fmac_f32_e32 v111, v112, v112
	v_add_f32_e32 v99, v99, v111
	v_add_f32_e32 v98, v98, v99
	v_mul_f32_e32 v99, v107, v107
	v_mul_f32_e32 v107, v109, v109
	v_fmac_f32_e32 v99, v106, v106
	v_fmac_f32_e32 v107, v108, v108
	v_add_f32_e32 v99, v99, v107
	v_add_f32_e32 v98, v98, v99
	v_mul_f32_e32 v99, v167, v167
	v_mul_f32_e32 v106, v105, v105
	v_fmac_f32_e32 v99, v166, v166
	v_fmac_f32_e32 v106, v104, v104
	v_add_f32_e32 v99, v99, v106
	v_add_f32_e32 v98, v98, v99
	ds_bpermute_b32 v99, v162, v98
	s_waitcnt lgkmcnt(0)
	v_add_f32_e32 v98, v98, v99
	ds_bpermute_b32 v99, v163, v98
	s_nop 0
	v_mul_f32_e32 v100, v204, v166
	v_mul_f32_e32 v101, v205, v167
	v_mul_f32_e32 v102, v206, v104
	v_mul_f32_e32 v103, v207, v105
	v_cvt_pk_bf16_f32 v100, v100, v101
	v_cvt_pk_bf16_f32 v101, v102, v103
	global_store_dwordx2 v[164:165], v[100:101], off offset:264
	s_and_saveexec_b64 s[50:51], s[4:5]
	s_cbranch_execz .LBB0_1946
	s_waitcnt lgkmcnt(0)
	v_add_f32_e32 v100, v98, v99
	v_lshlrev_b64 v[98:99], 8, v[154:155]
	v_lshl_add_u64 v[98:99], s[20:21], 0, v[98:99]
	v_lshl_add_u64 v[98:99], s[48:49], 2, v[98:99]
	s_lshl_b32 s10, s64, 2
	v_lshl_add_u64 v[98:99], v[98:99], 0, s[10:11]
	global_store_dword v[98:99], v100, off
.LBB0_1946:
	s_or_b64 exec, exec, s[50:51]
	v_or_b32_e32 v252, 48, v148
	v_ashrrev_i32_e32 v253, 31, v252
	v_lshl_add_u64 v[254:255], v[252:253], 2, s[22:23]
	global_load_dword v246, v[254:255], off
	v_or_b32_e32 v190, 48, v148
	v_ashrrev_i32_e32 v191, 31, v190
	v_lshlrev_b64 v[230:231], 12, v[190:191]
	v_lshl_add_u64 v[230:231], v[230:231], 0, v[146:147]
	v_lshlrev_b64 v[230:231], 1, v[230:231]
	v_lshl_add_u64 v[252:253], s[14:15], 0, v[230:231]
	global_load_dwordx2 v[240:241], v[252:253], off
	global_load_dwordx2 v[242:243], v[252:253], off offset:8
	global_load_dwordx2 v[236:237], v[252:253], off offset:256
	global_load_dwordx2 v[238:239], v[252:253], off offset:264
	v_or_b32_e32 v98, 32, v148
	s_waitcnt lgkmcnt(0)
	v_ashrrev_i32_e32 v99, 31, v98
	v_lshlrev_b64 v[100:101], 12, v[98:99]
	v_lshl_add_u64 v[100:101], v[100:101], 0, v[146:147]
	v_lshlrev_b64 v[100:101], 1, v[100:101]
	v_lshl_add_u64 v[102:103], v[98:99], 2, s[22:23]
	v_lshl_add_u64 v[104:105], s[14:15], 0, v[100:101]
	s_nop 0
	v_cvt_f32_i32_e32 v97, v97
	s_nop 0
	v_cvt_f32_i32_e32 v95, v95
	v_cvt_f32_i32_e32 v94, v94
	v_cvt_f32_i32_e32 v96, v96
	v_cvt_f32_i32_e32 v93, v93
	v_cvt_f32_i32_e32 v91, v91
	v_cvt_f32_i32_e32 v90, v90
	v_cvt_f32_i32_e32 v92, v92
	v_lshl_add_u64 v[100:101], s[16:17], 0, v[100:101]
	v_cvt_f32_i32_e32 v89, v89
	v_cvt_f32_i32_e32 v87, v87
	v_cvt_f32_i32_e32 v86, v86
	v_cvt_f32_i32_e32 v88, v88
	v_cvt_f32_i32_e32 v85, v85
	v_cvt_f32_i32_e32 v83, v83
	v_cvt_f32_i32_e32 v82, v82
	v_cvt_f32_i32_e32 v84, v84
	s_nop 0
	s_waitcnt vmcnt(17)
	v_pk_mul_f32 v[94:95], v[248:249], v[94:95] op_sel_hi:[0,1]
	v_pk_mul_f32 v[96:97], v[248:249], v[96:97] op_sel_hi:[0,1]
	s_nop 0
	s_waitcnt vmcnt(16)
	v_lshlrev_b32_e32 v108, 16, v250
	v_and_b32_e32 v109, 0xffff0000, v250
	v_lshlrev_b32_e32 v106, 16, v251
	v_and_b32_e32 v107, 0xffff0000, v251
	v_pk_fma_f32 v[106:107], v[152:153], v[96:97], v[106:107]
	v_pk_fma_f32 v[108:109], v[128:129], v[94:95], v[108:109]
	v_pk_mul_f32 v[90:91], v[248:249], v[90:91] op_sel_hi:[0,1]
	v_cvt_pk_bf16_f32 v94, v108, v109
	v_cvt_pk_bf16_f32 v95, v106, v107
	global_store_dwordx2 v[104:105], v[94:95], off
	s_nop 0
	v_pk_mul_f32 v[92:93], v[248:249], v[92:93] op_sel_hi:[0,1]
	v_pk_mul_f32 v[86:87], v[248:249], v[86:87] op_sel_hi:[0,1]
	v_pk_mul_f32 v[88:89], v[248:249], v[88:89] op_sel_hi:[0,1]
	v_pk_mul_f32 v[82:83], v[248:249], v[82:83] op_sel_hi:[0,1]
	v_pk_mul_f32 v[84:85], v[248:249], v[84:85] op_sel_hi:[0,1]
	s_nop 0
	v_mul_f32_e32 v94, v192, v108
	v_mul_f32_e32 v95, v193, v109
	v_mul_f32_e32 v96, v194, v106
	v_mul_f32_e32 v97, v195, v107
	v_cvt_pk_bf16_f32 v94, v94, v95
	v_cvt_pk_bf16_f32 v95, v96, v97
	s_nop 0
	s_nop 0
	global_store_dwordx2 v[100:101], v[94:95], off
	s_nop 0
	s_waitcnt vmcnt(17)
; __device__ __forceinline__ unsigned cvt_pk_bf16(float lo, float hi) { unsigned r; asm volatile("v_cvt_pk_bf16_f32 %0, %1, %2" : "=v"(r) : "v"(lo), "v"(hi)); return r; }
;     __device__ __forceinline__ void operator()(const f32x4 (&acc)[2][2][4][2], const Unit& u, int wr, int wc, int fr, int fq) const {
;     ...
;             for (int m = 0; m < 4; ++m) { const int row = row0 + ai * HALF + m * 16; const size_t ro = (size_t)row * ldc + col0; float ss = 0.f; const float rs = xs[row];
; #pragma unroll
;                 for (int bj = 0; bj < 2; ++bj)
; #pragma unroll
;                     for (int n = 0; n < 2; ++n) { const i32x4 ia = __builtin_bit_cast(i32x4, acc[ai][bj][m][n]);
;                         const f32x4 af = (f32x4){(float)ia[0], (float)ia[1], (float)ia[2], (float)ia[3]} * rs * cs[bj][n];
;                         f32x4 rv; if constexpr (RB16) { const u32x2 rb = *(const u32x2*)((const bf16_t*)R + ro + bj * HALF + n * 4); rv = (f32x4){__uint_as_float(rb.x << 16), __uint_as_float(rb.x & 0xffff0000u), __uint_as_float(rb.y << 16), __uint_as_float(rb.y & 0xffff0000u)}; }
;                         else rv = *(const f32x4*)((const float*)R + ro + bj * HALF + n * 4);
;                         const f32x4 v = af + rv; { u32x2 hb; hb.x = cvt_pk_bf16(v[0], v[1]); hb.y = cvt_pk_bf16(v[2], v[3]); *(u32x2*)(C + ro + bj * HALF + n * 4) = hb; }
;                         const f32x4 g = *(const f32x4*)(gain + col0 + bj * HALF + n * 4);
;                         u32x2 o; o.x = cvt_pk_bf16(v[0] * g[0], v[1] * g[1]); o.y = cvt_pk_bf16(v[2] * g[2], v[3] * g[3]); *(u32x2*)(HG + ro + bj * HALF + n * 4) = o;
;                         ss += (v[0] * v[0] + v[1] * v[1]) + (v[2] * v[2] + v[3] * v[3]); }
;                 ss += __shfl_xor(ss, 16); ss += __shfl_xor(ss, 32);
;                 if (fq == 0) SS[(size_t)row * 64 + u.pn * 4 + wc] = ss; }
	v_lshlrev_b32_e32 v94, 16, v244
	v_and_b32_e32 v95, 0xffff0000, v244
	v_lshlrev_b32_e32 v96, 16, v245
	v_and_b32_e32 v97, 0xffff0000, v245
	v_pk_fma_f32 v[96:97], v[124:125], v[92:93], v[96:97]
	v_pk_fma_f32 v[94:95], v[122:123], v[90:91], v[94:95]
	s_nop 0
	v_cvt_pk_bf16_f32 v90, v94, v95
	v_cvt_pk_bf16_f32 v91, v96, v97
	global_store_dwordx2 v[104:105], v[90:91], off offset:8
	s_nop 0
	s_nop 0
	v_mul_f32_e32 v90, v196, v94
	v_mul_f32_e32 v91, v197, v95
	v_mul_f32_e32 v92, v198, v96
	v_mul_f32_e32 v93, v199, v97
	v_cvt_pk_bf16_f32 v90, v90, v91
	v_cvt_pk_bf16_f32 v91, v92, v93
	s_nop 0
	s_nop 0
	global_store_dwordx2 v[100:101], v[90:91], off offset:8
	s_nop 0
	s_waitcnt vmcnt(18)
	v_lshlrev_b32_e32 v90, 16, v232
	v_and_b32_e32 v91, 0xffff0000, v232
	v_lshlrev_b32_e32 v92, 16, v233
	v_and_b32_e32 v93, 0xffff0000, v233
	v_pk_fma_f32 v[92:93], v[120:121], v[88:89], v[92:93]
	v_pk_fma_f32 v[90:91], v[118:119], v[86:87], v[90:91]
	s_nop 0
	v_cvt_pk_bf16_f32 v86, v90, v91
	v_cvt_pk_bf16_f32 v87, v92, v93
	global_store_dwordx2 v[104:105], v[86:87], off offset:256
	s_nop 0
	s_nop 0
	v_mul_f32_e32 v86, v200, v90
	v_mul_f32_e32 v87, v201, v91
	v_mul_f32_e32 v88, v202, v92
	v_mul_f32_e32 v89, v203, v93
	v_cvt_pk_bf16_f32 v86, v86, v87
	v_cvt_pk_bf16_f32 v87, v88, v89
	s_nop 0
	s_nop 0
	global_store_dwordx2 v[100:101], v[86:87], off offset:256
	s_nop 0
	s_waitcnt vmcnt(19)
	v_lshlrev_b32_e32 v86, 16, v234
	v_and_b32_e32 v87, 0xffff0000, v234
	v_lshlrev_b32_e32 v88, 16, v235
	v_and_b32_e32 v89, 0xffff0000, v235
	v_pk_fma_f32 v[88:89], v[116:117], v[84:85], v[88:89]
	v_pk_fma_f32 v[102:103], v[114:115], v[82:83], v[86:87]
	s_nop 0
	v_cvt_pk_bf16_f32 v82, v102, v103
	v_cvt_pk_bf16_f32 v83, v88, v89
	global_store_dwordx2 v[104:105], v[82:83], off offset:264
	s_nop 0
	v_mul_f32_e32 v82, v109, v109
	v_mul_f32_e32 v83, v107, v107
	v_fmac_f32_e32 v82, v108, v108
	v_fmac_f32_e32 v83, v106, v106
	v_add_f32_e32 v82, v82, v83
	v_mul_f32_e32 v83, v95, v95
	v_mul_f32_e32 v95, v97, v97
	v_fmac_f32_e32 v83, v94, v94
	v_fmac_f32_e32 v95, v96, v96
	v_add_f32_e32 v83, v83, v95
	v_add_f32_e32 v82, v82, v83
	v_mul_f32_e32 v83, v91, v91
	v_mul_f32_e32 v91, v93, v93
	v_fmac_f32_e32 v83, v90, v90
	v_fmac_f32_e32 v91, v92, v92
	v_add_f32_e32 v83, v83, v91
	v_add_f32_e32 v82, v82, v83
	v_mul_f32_e32 v83, v103, v103
	v_mul_f32_e32 v90, v89, v89
	v_fmac_f32_e32 v83, v102, v102
	v_fmac_f32_e32 v90, v88, v88
	v_add_f32_e32 v83, v83, v90
	v_add_f32_e32 v82, v82, v83
	ds_bpermute_b32 v83, v162, v82
	s_waitcnt lgkmcnt(0)
	v_add_f32_e32 v82, v82, v83
	ds_bpermute_b32 v83, v163, v82
	s_nop 0
	v_mul_f32_e32 v84, v204, v102
	v_mul_f32_e32 v85, v205, v103
	v_mul_f32_e32 v86, v206, v88
	v_mul_f32_e32 v87, v207, v89
	v_cvt_pk_bf16_f32 v84, v84, v85
	v_cvt_pk_bf16_f32 v85, v86, v87
	global_store_dwordx2 v[100:101], v[84:85], off offset:264
	s_and_saveexec_b64 s[50:51], s[4:5]
	s_cbranch_execz .LBB0_1948
	s_waitcnt lgkmcnt(0)
	v_add_f32_e32 v84, v82, v83
	v_lshlrev_b64 v[82:83], 8, v[98:99]
	v_lshl_add_u64 v[82:83], s[20:21], 0, v[82:83]
	v_lshl_add_u64 v[82:83], s[48:49], 2, v[82:83]
	s_lshl_b32 s10, s64, 2
	v_lshl_add_u64 v[82:83], v[82:83], 0, s[10:11]
	global_store_dword v[82:83], v84, off
.LBB0_1948:
	s_or_b64 exec, exec, s[50:51]
	global_load_dword v248, v[150:151], off offset:512
	v_add_u32_e32 v254, 0x80, v148
	v_ashrrev_i32_e32 v255, 31, v254
	v_lshlrev_b64 v[190:191], 12, v[254:255]
	v_lshl_add_u64 v[190:191], v[190:191], 0, v[146:147]
	v_lshlrev_b64 v[190:191], 1, v[190:191]
	v_lshl_add_u64 v[230:231], s[14:15], 0, v[190:191]
	global_load_dwordx2 v[250:251], v[230:231], off
	global_load_dwordx2 v[244:245], v[230:231], off offset:8
	global_load_dwordx2 v[232:233], v[230:231], off offset:256
	global_load_dwordx2 v[234:235], v[230:231], off offset:264
	v_or_b32_e32 v82, 48, v148
	s_waitcnt lgkmcnt(0)
	v_ashrrev_i32_e32 v83, 31, v82
	v_lshlrev_b64 v[84:85], 12, v[82:83]
	v_lshl_add_u64 v[84:85], v[84:85], 0, v[146:147]
	v_lshlrev_b64 v[84:85], 1, v[84:85]
	v_lshl_add_u64 v[86:87], v[82:83], 2, s[22:23]
	v_lshl_add_u64 v[88:89], s[14:15], 0, v[84:85]
	s_nop 0
	v_cvt_f32_i32_e32 v81, v81
	s_nop 0
	v_cvt_f32_i32_e32 v79, v79
	v_cvt_f32_i32_e32 v78, v78
	v_cvt_f32_i32_e32 v80, v80
	v_cvt_f32_i32_e32 v77, v77
	v_cvt_f32_i32_e32 v75, v75
	v_cvt_f32_i32_e32 v74, v74
	v_cvt_f32_i32_e32 v76, v76
	v_lshl_add_u64 v[84:85], s[16:17], 0, v[84:85]
	v_cvt_f32_i32_e32 v73, v73
	v_cvt_f32_i32_e32 v71, v71
	v_cvt_f32_i32_e32 v70, v70
	v_cvt_f32_i32_e32 v72, v72
	v_cvt_f32_i32_e32 v69, v69
	v_cvt_f32_i32_e32 v67, v67
	v_cvt_f32_i32_e32 v66, v66
	v_cvt_f32_i32_e32 v68, v68
	s_nop 0
	s_waitcnt vmcnt(17)
	v_pk_mul_f32 v[78:79], v[246:247], v[78:79] op_sel_hi:[0,1]
	v_pk_mul_f32 v[80:81], v[246:247], v[80:81] op_sel_hi:[0,1]
	s_nop 0
	s_waitcnt vmcnt(16)
	v_lshlrev_b32_e32 v92, 16, v240
	v_and_b32_e32 v93, 0xffff0000, v240
	v_lshlrev_b32_e32 v90, 16, v241
	v_and_b32_e32 v91, 0xffff0000, v241
	v_pk_fma_f32 v[90:91], v[152:153], v[80:81], v[90:91]
	v_pk_fma_f32 v[92:93], v[128:129], v[78:79], v[92:93]
	v_pk_mul_f32 v[74:75], v[246:247], v[74:75] op_sel_hi:[0,1]
	v_cvt_pk_bf16_f32 v78, v92, v93
	v_cvt_pk_bf16_f32 v79, v90, v91
	global_store_dwordx2 v[88:89], v[78:79], off
	s_nop 0
	v_pk_mul_f32 v[76:77], v[246:247], v[76:77] op_sel_hi:[0,1]
	v_pk_mul_f32 v[70:71], v[246:247], v[70:71] op_sel_hi:[0,1]
	v_pk_mul_f32 v[72:73], v[246:247], v[72:73] op_sel_hi:[0,1]
	v_pk_mul_f32 v[66:67], v[246:247], v[66:67] op_sel_hi:[0,1]
	v_pk_mul_f32 v[68:69], v[246:247], v[68:69] op_sel_hi:[0,1]
	s_nop 0
	v_mul_f32_e32 v78, v192, v92
	v_mul_f32_e32 v79, v193, v93
	v_mul_f32_e32 v80, v194, v90
	v_mul_f32_e32 v81, v195, v91
	v_cvt_pk_bf16_f32 v78, v78, v79
	v_cvt_pk_bf16_f32 v79, v80, v81
	s_nop 0
	s_nop 0
	global_store_dwordx2 v[84:85], v[78:79], off
	s_nop 0
	s_waitcnt vmcnt(17)
; __device__ __forceinline__ unsigned cvt_pk_bf16(float lo, float hi) { unsigned r; asm volatile("v_cvt_pk_bf16_f32 %0, %1, %2" : "=v"(r) : "v"(lo), "v"(hi)); return r; }
;     __device__ __forceinline__ void operator()(const f32x4 (&acc)[2][2][4][2], const Unit& u, int wr, int wc, int fr, int fq) const {
;     ...
;             for (int m = 0; m < 4; ++m) { const int row = row0 + ai * HALF + m * 16; const size_t ro = (size_t)row * ldc + col0; float ss = 0.f; const float rs = xs[row];
; #pragma unroll
;                 for (int bj = 0; bj < 2; ++bj)
; #pragma unroll
;                     for (int n = 0; n < 2; ++n) { const i32x4 ia = __builtin_bit_cast(i32x4, acc[ai][bj][m][n]);
;                         const f32x4 af = (f32x4){(float)ia[0], (float)ia[1], (float)ia[2], (float)ia[3]} * rs * cs[bj][n];
;                         f32x4 rv; if constexpr (RB16) { const u32x2 rb = *(const u32x2*)((const bf16_t*)R + ro + bj * HALF + n * 4); rv = (f32x4){__uint_as_float(rb.x << 16), __uint_as_float(rb.x & 0xffff0000u), __uint_as_float(rb.y << 16), __uint_as_float(rb.y & 0xffff0000u)}; }
;                         else rv = *(const f32x4*)((const float*)R + ro + bj * HALF + n * 4);
;                         const f32x4 v = af + rv; { u32x2 hb; hb.x = cvt_pk_bf16(v[0], v[1]); hb.y = cvt_pk_bf16(v[2], v[3]); *(u32x2*)(C + ro + bj * HALF + n * 4) = hb; }
;                         const f32x4 g = *(const f32x4*)(gain + col0 + bj * HALF + n * 4);
;                         u32x2 o; o.x = cvt_pk_bf16(v[0] * g[0], v[1] * g[1]); o.y = cvt_pk_bf16(v[2] * g[2], v[3] * g[3]); *(u32x2*)(HG + ro + bj * HALF + n * 4) = o;
;                         ss += (v[0] * v[0] + v[1] * v[1]) + (v[2] * v[2] + v[3] * v[3]); }
;                 ss += __shfl_xor(ss, 16); ss += __shfl_xor(ss, 32);
;                 if (fq == 0) SS[(size_t)row * 64 + u.pn * 4 + wc] = ss; }
	v_lshlrev_b32_e32 v78, 16, v242
	v_and_b32_e32 v79, 0xffff0000, v242
	v_lshlrev_b32_e32 v80, 16, v243
	v_and_b32_e32 v81, 0xffff0000, v243
	v_pk_fma_f32 v[80:81], v[124:125], v[76:77], v[80:81]
	v_pk_fma_f32 v[78:79], v[122:123], v[74:75], v[78:79]
	s_nop 0
	v_cvt_pk_bf16_f32 v74, v78, v79
	v_cvt_pk_bf16_f32 v75, v80, v81
	global_store_dwordx2 v[88:89], v[74:75], off offset:8
	s_nop 0
	s_nop 0
	v_mul_f32_e32 v74, v196, v78
	v_mul_f32_e32 v75, v197, v79
	v_mul_f32_e32 v76, v198, v80
	v_mul_f32_e32 v77, v199, v81
	v_cvt_pk_bf16_f32 v74, v74, v75
	v_cvt_pk_bf16_f32 v75, v76, v77
	s_nop 0
	s_nop 0
	global_store_dwordx2 v[84:85], v[74:75], off offset:8
	s_nop 0
	s_waitcnt vmcnt(18)
	v_lshlrev_b32_e32 v74, 16, v236
	v_and_b32_e32 v75, 0xffff0000, v236
	v_lshlrev_b32_e32 v76, 16, v237
	v_and_b32_e32 v77, 0xffff0000, v237
	v_pk_fma_f32 v[76:77], v[120:121], v[72:73], v[76:77]
	v_pk_fma_f32 v[74:75], v[118:119], v[70:71], v[74:75]
	s_nop 0
	v_cvt_pk_bf16_f32 v70, v74, v75
	v_cvt_pk_bf16_f32 v71, v76, v77
	global_store_dwordx2 v[88:89], v[70:71], off offset:256
	s_nop 0
	s_nop 0
	v_mul_f32_e32 v70, v200, v74
	v_mul_f32_e32 v71, v201, v75
	v_mul_f32_e32 v72, v202, v76
	v_mul_f32_e32 v73, v203, v77
	v_cvt_pk_bf16_f32 v70, v70, v71
	v_cvt_pk_bf16_f32 v71, v72, v73
	s_nop 0
	s_nop 0
	global_store_dwordx2 v[84:85], v[70:71], off offset:256
	s_nop 0
	s_waitcnt vmcnt(19)
	v_lshlrev_b32_e32 v70, 16, v238
	v_and_b32_e32 v71, 0xffff0000, v238
	v_lshlrev_b32_e32 v72, 16, v239
	v_and_b32_e32 v73, 0xffff0000, v239
	v_pk_fma_f32 v[72:73], v[116:117], v[68:69], v[72:73]
	v_pk_fma_f32 v[86:87], v[114:115], v[66:67], v[70:71]
	s_nop 0
	v_cvt_pk_bf16_f32 v66, v86, v87
	v_cvt_pk_bf16_f32 v67, v72, v73
	global_store_dwordx2 v[88:89], v[66:67], off offset:264
	s_nop 0
	v_mul_f32_e32 v66, v93, v93
	v_mul_f32_e32 v67, v91, v91
	v_fmac_f32_e32 v66, v92, v92
	v_fmac_f32_e32 v67, v90, v90
	v_add_f32_e32 v66, v66, v67
	v_mul_f32_e32 v67, v79, v79
	v_mul_f32_e32 v79, v81, v81
	v_fmac_f32_e32 v67, v78, v78
	v_fmac_f32_e32 v79, v80, v80
	v_add_f32_e32 v67, v67, v79
	v_add_f32_e32 v66, v66, v67
	v_mul_f32_e32 v67, v75, v75
	v_mul_f32_e32 v75, v77, v77
	v_fmac_f32_e32 v67, v74, v74
	v_fmac_f32_e32 v75, v76, v76
	v_add_f32_e32 v67, v67, v75
	v_add_f32_e32 v66, v66, v67
	v_mul_f32_e32 v67, v87, v87
	v_mul_f32_e32 v74, v73, v73
	v_fmac_f32_e32 v67, v86, v86
	v_fmac_f32_e32 v74, v72, v72
	v_add_f32_e32 v67, v67, v74
	v_add_f32_e32 v66, v66, v67
	ds_bpermute_b32 v67, v162, v66
	s_waitcnt lgkmcnt(0)
	v_add_f32_e32 v66, v66, v67
	ds_bpermute_b32 v67, v163, v66
	s_nop 0
	v_mul_f32_e32 v68, v204, v86
	v_mul_f32_e32 v69, v205, v87
	v_mul_f32_e32 v70, v206, v72
	v_mul_f32_e32 v71, v207, v73
	v_cvt_pk_bf16_f32 v68, v68, v69
	v_cvt_pk_bf16_f32 v69, v70, v71
	global_store_dwordx2 v[84:85], v[68:69], off offset:264
	s_and_saveexec_b64 s[50:51], s[4:5]
	s_cbranch_execz .LBB0_1950
	s_waitcnt lgkmcnt(0)
	v_add_f32_e32 v68, v66, v67
	v_lshlrev_b64 v[66:67], 8, v[82:83]
	v_lshl_add_u64 v[66:67], s[20:21], 0, v[66:67]
	v_lshl_add_u64 v[66:67], s[48:49], 2, v[66:67]
	s_lshl_b32 s10, s64, 2
	v_lshl_add_u64 v[66:67], v[66:67], 0, s[10:11]
	global_store_dword v[66:67], v68, off
.LBB0_1950:
	s_or_b64 exec, exec, s[50:51]
	global_load_dword v246, v[150:151], off offset:576
	v_add_u32_e32 v252, 0x90, v148
	v_ashrrev_i32_e32 v253, 31, v252
	v_lshlrev_b64 v[254:255], 12, v[252:253]
	v_lshl_add_u64 v[254:255], v[254:255], 0, v[146:147]
	v_lshlrev_b64 v[254:255], 1, v[254:255]
	v_lshl_add_u64 v[190:191], s[14:15], 0, v[254:255]
	global_load_dwordx2 v[240:241], v[190:191], off
	global_load_dwordx2 v[242:243], v[190:191], off offset:8
	global_load_dwordx2 v[236:237], v[190:191], off offset:256
	global_load_dwordx2 v[238:239], v[190:191], off offset:264
	v_add_u32_e32 v66, 0x80, v148
	s_waitcnt lgkmcnt(0)
	v_ashrrev_i32_e32 v67, 31, v66
	v_lshlrev_b64 v[68:69], 12, v[66:67]
	v_lshl_add_u64 v[68:69], v[68:69], 0, v[146:147]
	v_lshlrev_b64 v[68:69], 1, v[68:69]
	v_lshl_add_u64 v[72:73], s[14:15], 0, v[68:69]
	s_nop 0
	s_nop 0
	v_cvt_f32_i32_e32 v65, v65
	v_cvt_f32_i32_e32 v63, v63
	v_cvt_f32_i32_e32 v62, v62
	v_cvt_f32_i32_e32 v64, v64
	v_cvt_f32_i32_e32 v61, v61
	v_cvt_f32_i32_e32 v59, v59
	v_cvt_f32_i32_e32 v58, v58
	v_cvt_f32_i32_e32 v60, v60
	v_lshl_add_u64 v[68:69], s[16:17], 0, v[68:69]
	v_cvt_f32_i32_e32 v57, v57
	v_cvt_f32_i32_e32 v55, v55
	v_cvt_f32_i32_e32 v54, v54
	v_cvt_f32_i32_e32 v56, v56
	v_cvt_f32_i32_e32 v53, v53
	v_cvt_f32_i32_e32 v51, v51
	v_cvt_f32_i32_e32 v50, v50
	v_cvt_f32_i32_e32 v52, v52
	s_nop 0
	s_waitcnt vmcnt(17)
	v_pk_mul_f32 v[62:63], v[248:249], v[62:63] op_sel_hi:[0,1]
	v_pk_mul_f32 v[64:65], v[248:249], v[64:65] op_sel_hi:[0,1]
	s_nop 0
	s_waitcnt vmcnt(16)
	v_lshlrev_b32_e32 v76, 16, v250
	v_and_b32_e32 v77, 0xffff0000, v250
	v_lshlrev_b32_e32 v74, 16, v251
	v_and_b32_e32 v75, 0xffff0000, v251
	v_pk_fma_f32 v[74:75], v[152:153], v[64:65], v[74:75]
	v_pk_fma_f32 v[76:77], v[128:129], v[62:63], v[76:77]
	v_pk_mul_f32 v[58:59], v[248:249], v[58:59] op_sel_hi:[0,1]
	v_cvt_pk_bf16_f32 v62, v76, v77
	v_cvt_pk_bf16_f32 v63, v74, v75
	global_store_dwordx2 v[72:73], v[62:63], off
	s_nop 0
	v_pk_mul_f32 v[60:61], v[248:249], v[60:61] op_sel_hi:[0,1]
	v_pk_mul_f32 v[54:55], v[248:249], v[54:55] op_sel_hi:[0,1]
	v_pk_mul_f32 v[56:57], v[248:249], v[56:57] op_sel_hi:[0,1]
	v_pk_mul_f32 v[50:51], v[248:249], v[50:51] op_sel_hi:[0,1]
	v_pk_mul_f32 v[52:53], v[248:249], v[52:53] op_sel_hi:[0,1]
	s_nop 0
	v_mul_f32_e32 v62, v192, v76
	v_mul_f32_e32 v63, v193, v77
	v_mul_f32_e32 v64, v194, v74
	v_mul_f32_e32 v65, v195, v75
	v_cvt_pk_bf16_f32 v62, v62, v63
	v_cvt_pk_bf16_f32 v63, v64, v65
	s_nop 0
	s_nop 0
	global_store_dwordx2 v[68:69], v[62:63], off
	s_nop 0
	s_waitcnt vmcnt(17)
; __device__ __forceinline__ unsigned cvt_pk_bf16(float lo, float hi) { unsigned r; asm volatile("v_cvt_pk_bf16_f32 %0, %1, %2" : "=v"(r) : "v"(lo), "v"(hi)); return r; }
;     __device__ __forceinline__ void operator()(const f32x4 (&acc)[2][2][4][2], const Unit& u, int wr, int wc, int fr, int fq) const {
;     ...
;             for (int m = 0; m < 4; ++m) { const int row = row0 + ai * HALF + m * 16; const size_t ro = (size_t)row * ldc + col0; float ss = 0.f; const float rs = xs[row];
; #pragma unroll
;                 for (int bj = 0; bj < 2; ++bj)
; #pragma unroll
;                     for (int n = 0; n < 2; ++n) { const i32x4 ia = __builtin_bit_cast(i32x4, acc[ai][bj][m][n]);
;                         const f32x4 af = (f32x4){(float)ia[0], (float)ia[1], (float)ia[2], (float)ia[3]} * rs * cs[bj][n];
;                         f32x4 rv; if constexpr (RB16) { const u32x2 rb = *(const u32x2*)((const bf16_t*)R + ro + bj * HALF + n * 4); rv = (f32x4){__uint_as_float(rb.x << 16), __uint_as_float(rb.x & 0xffff0000u), __uint_as_float(rb.y << 16), __uint_as_float(rb.y & 0xffff0000u)}; }
;                         else rv = *(const f32x4*)((const float*)R + ro + bj * HALF + n * 4);
;                         const f32x4 v = af + rv; { u32x2 hb; hb.x = cvt_pk_bf16(v[0], v[1]); hb.y = cvt_pk_bf16(v[2], v[3]); *(u32x2*)(C + ro + bj * HALF + n * 4) = hb; }
;                         const f32x4 g = *(const f32x4*)(gain + col0 + bj * HALF + n * 4);
;                         u32x2 o; o.x = cvt_pk_bf16(v[0] * g[0], v[1] * g[1]); o.y = cvt_pk_bf16(v[2] * g[2], v[3] * g[3]); *(u32x2*)(HG + ro + bj * HALF + n * 4) = o;
;                         ss += (v[0] * v[0] + v[1] * v[1]) + (v[2] * v[2] + v[3] * v[3]); }
;                 ss += __shfl_xor(ss, 16); ss += __shfl_xor(ss, 32);
;                 if (fq == 0) SS[(size_t)row * 64 + u.pn * 4 + wc] = ss; }
	v_lshlrev_b32_e32 v62, 16, v244
	v_and_b32_e32 v63, 0xffff0000, v244
	v_lshlrev_b32_e32 v64, 16, v245
	v_and_b32_e32 v65, 0xffff0000, v245
	v_pk_fma_f32 v[64:65], v[124:125], v[60:61], v[64:65]
	v_pk_fma_f32 v[62:63], v[122:123], v[58:59], v[62:63]
	s_nop 0
	v_cvt_pk_bf16_f32 v58, v62, v63
	v_cvt_pk_bf16_f32 v59, v64, v65
	global_store_dwordx2 v[72:73], v[58:59], off offset:8
	s_nop 0
	s_nop 0
	v_mul_f32_e32 v58, v196, v62
	v_mul_f32_e32 v59, v197, v63
	v_mul_f32_e32 v60, v198, v64
	v_mul_f32_e32 v61, v199, v65
	v_cvt_pk_bf16_f32 v58, v58, v59
	v_cvt_pk_bf16_f32 v59, v60, v61
	s_nop 0
	s_nop 0
	global_store_dwordx2 v[68:69], v[58:59], off offset:8
	s_nop 0
	s_waitcnt vmcnt(18)
	v_lshlrev_b32_e32 v58, 16, v232
	v_and_b32_e32 v59, 0xffff0000, v232
	v_lshlrev_b32_e32 v60, 16, v233
	v_and_b32_e32 v61, 0xffff0000, v233
	v_pk_fma_f32 v[60:61], v[120:121], v[56:57], v[60:61]
	v_pk_fma_f32 v[58:59], v[118:119], v[54:55], v[58:59]
	s_nop 0
	v_cvt_pk_bf16_f32 v54, v58, v59
	v_cvt_pk_bf16_f32 v55, v60, v61
	global_store_dwordx2 v[72:73], v[54:55], off offset:256
	s_nop 0
	s_nop 0
	v_mul_f32_e32 v54, v200, v58
	v_mul_f32_e32 v55, v201, v59
	v_mul_f32_e32 v56, v202, v60
	v_mul_f32_e32 v57, v203, v61
	v_cvt_pk_bf16_f32 v54, v54, v55
	v_cvt_pk_bf16_f32 v55, v56, v57
	s_nop 0
	s_nop 0
	global_store_dwordx2 v[68:69], v[54:55], off offset:256
	s_nop 0
	s_waitcnt vmcnt(19)
	v_lshlrev_b32_e32 v54, 16, v234
	v_and_b32_e32 v55, 0xffff0000, v234
	v_lshlrev_b32_e32 v56, 16, v235
	v_and_b32_e32 v57, 0xffff0000, v235
	v_pk_fma_f32 v[56:57], v[116:117], v[52:53], v[56:57]
	v_pk_fma_f32 v[70:71], v[114:115], v[50:51], v[54:55]
	s_nop 0
	v_cvt_pk_bf16_f32 v50, v70, v71
	v_cvt_pk_bf16_f32 v51, v56, v57
	global_store_dwordx2 v[72:73], v[50:51], off offset:264
	s_nop 0
	v_mul_f32_e32 v50, v77, v77
	v_mul_f32_e32 v51, v75, v75
	v_fmac_f32_e32 v50, v76, v76
	v_fmac_f32_e32 v51, v74, v74
	v_add_f32_e32 v50, v50, v51
	v_mul_f32_e32 v51, v63, v63
	v_mul_f32_e32 v63, v65, v65
	v_fmac_f32_e32 v51, v62, v62
	v_fmac_f32_e32 v63, v64, v64
	v_add_f32_e32 v51, v51, v63
	v_add_f32_e32 v50, v50, v51
	v_mul_f32_e32 v51, v59, v59
	v_mul_f32_e32 v59, v61, v61
	v_fmac_f32_e32 v51, v58, v58
	v_fmac_f32_e32 v59, v60, v60
	v_add_f32_e32 v51, v51, v59
	v_add_f32_e32 v50, v50, v51
	v_mul_f32_e32 v51, v71, v71
	v_mul_f32_e32 v58, v57, v57
	v_fmac_f32_e32 v51, v70, v70
	v_fmac_f32_e32 v58, v56, v56
	v_add_f32_e32 v51, v51, v58
	v_add_f32_e32 v50, v50, v51
	ds_bpermute_b32 v51, v162, v50
	s_waitcnt lgkmcnt(0)
	v_add_f32_e32 v50, v50, v51
	ds_bpermute_b32 v51, v163, v50
	s_nop 0
	v_mul_f32_e32 v52, v204, v70
	v_mul_f32_e32 v53, v205, v71
	v_mul_f32_e32 v54, v206, v56
	v_mul_f32_e32 v55, v207, v57
	v_cvt_pk_bf16_f32 v52, v52, v53
	v_cvt_pk_bf16_f32 v53, v54, v55
	global_store_dwordx2 v[68:69], v[52:53], off offset:264
	s_and_saveexec_b64 s[50:51], s[4:5]
	s_cbranch_execz .LBB0_1952
	s_waitcnt lgkmcnt(0)
	v_add_f32_e32 v52, v50, v51
	v_lshlrev_b64 v[50:51], 8, v[66:67]
	v_lshl_add_u64 v[50:51], s[20:21], 0, v[50:51]
	v_lshl_add_u64 v[50:51], s[48:49], 2, v[50:51]
	s_lshl_b32 s10, s64, 2
	v_lshl_add_u64 v[50:51], v[50:51], 0, s[10:11]
	global_store_dword v[50:51], v52, off
.LBB0_1952:
	s_or_b64 exec, exec, s[50:51]
	global_load_dword v248, v[150:151], off offset:640
	v_add_u32_e32 v230, 0xa0, v148
	v_ashrrev_i32_e32 v231, 31, v230
	v_lshlrev_b64 v[252:253], 12, v[230:231]
	v_lshl_add_u64 v[252:253], v[252:253], 0, v[146:147]
	v_lshlrev_b64 v[252:253], 1, v[252:253]
	v_lshl_add_u64 v[254:255], s[14:15], 0, v[252:253]
	global_load_dwordx2 v[250:251], v[254:255], off
	global_load_dwordx2 v[244:245], v[254:255], off offset:8
	global_load_dwordx2 v[232:233], v[254:255], off offset:256
	global_load_dwordx2 v[234:235], v[254:255], off offset:264
	v_add_u32_e32 v50, 0x90, v148
	s_waitcnt lgkmcnt(0)
	v_ashrrev_i32_e32 v51, 31, v50
	v_lshlrev_b64 v[52:53], 12, v[50:51]
	v_lshl_add_u64 v[52:53], v[52:53], 0, v[146:147]
	v_lshlrev_b64 v[52:53], 1, v[52:53]
	v_lshl_add_u64 v[56:57], s[14:15], 0, v[52:53]
	s_nop 0
	s_nop 0
	v_cvt_f32_i32_e32 v49, v49
	v_cvt_f32_i32_e32 v47, v47
	v_cvt_f32_i32_e32 v46, v46
	v_cvt_f32_i32_e32 v48, v48
	v_cvt_f32_i32_e32 v45, v45
	v_cvt_f32_i32_e32 v43, v43
	v_cvt_f32_i32_e32 v42, v42
	v_cvt_f32_i32_e32 v44, v44
	v_lshl_add_u64 v[52:53], s[16:17], 0, v[52:53]
	v_cvt_f32_i32_e32 v41, v41
	v_cvt_f32_i32_e32 v39, v39
	v_cvt_f32_i32_e32 v38, v38
	v_cvt_f32_i32_e32 v40, v40
	v_cvt_f32_i32_e32 v37, v37
	v_cvt_f32_i32_e32 v35, v35
	v_cvt_f32_i32_e32 v34, v34
	v_cvt_f32_i32_e32 v36, v36
	s_nop 0
	s_waitcnt vmcnt(17)
	v_pk_mul_f32 v[46:47], v[246:247], v[46:47] op_sel_hi:[0,1]
	v_pk_mul_f32 v[48:49], v[246:247], v[48:49] op_sel_hi:[0,1]
	s_nop 0
	s_waitcnt vmcnt(16)
	v_lshlrev_b32_e32 v60, 16, v240
	v_and_b32_e32 v61, 0xffff0000, v240
	v_lshlrev_b32_e32 v58, 16, v241
	v_and_b32_e32 v59, 0xffff0000, v241
	v_pk_fma_f32 v[58:59], v[152:153], v[48:49], v[58:59]
	v_pk_fma_f32 v[60:61], v[128:129], v[46:47], v[60:61]
	v_pk_mul_f32 v[42:43], v[246:247], v[42:43] op_sel_hi:[0,1]
	v_cvt_pk_bf16_f32 v46, v60, v61
	v_cvt_pk_bf16_f32 v47, v58, v59
	global_store_dwordx2 v[56:57], v[46:47], off
	s_nop 0
	v_pk_mul_f32 v[44:45], v[246:247], v[44:45] op_sel_hi:[0,1]
	v_pk_mul_f32 v[38:39], v[246:247], v[38:39] op_sel_hi:[0,1]
	v_pk_mul_f32 v[40:41], v[246:247], v[40:41] op_sel_hi:[0,1]
	v_pk_mul_f32 v[34:35], v[246:247], v[34:35] op_sel_hi:[0,1]
	v_pk_mul_f32 v[36:37], v[246:247], v[36:37] op_sel_hi:[0,1]
	s_nop 0
	v_mul_f32_e32 v46, v192, v60
	v_mul_f32_e32 v47, v193, v61
	v_mul_f32_e32 v48, v194, v58
	v_mul_f32_e32 v49, v195, v59
	v_cvt_pk_bf16_f32 v46, v46, v47
	v_cvt_pk_bf16_f32 v47, v48, v49
	s_nop 0
	s_nop 0
	global_store_dwordx2 v[52:53], v[46:47], off
	s_nop 0
	s_waitcnt vmcnt(17)
; __device__ __forceinline__ unsigned cvt_pk_bf16(float lo, float hi) { unsigned r; asm volatile("v_cvt_pk_bf16_f32 %0, %1, %2" : "=v"(r) : "v"(lo), "v"(hi)); return r; }
;     __device__ __forceinline__ void operator()(const f32x4 (&acc)[2][2][4][2], const Unit& u, int wr, int wc, int fr, int fq) const {
;     ...
;             for (int m = 0; m < 4; ++m) { const int row = row0 + ai * HALF + m * 16; const size_t ro = (size_t)row * ldc + col0; float ss = 0.f; const float rs = xs[row];
; #pragma unroll
;                 for (int bj = 0; bj < 2; ++bj)
; #pragma unroll
;                     for (int n = 0; n < 2; ++n) { const i32x4 ia = __builtin_bit_cast(i32x4, acc[ai][bj][m][n]);
;                         const f32x4 af = (f32x4){(float)ia[0], (float)ia[1], (float)ia[2], (float)ia[3]} * rs * cs[bj][n];
;                         f32x4 rv; if constexpr (RB16) { const u32x2 rb = *(const u32x2*)((const bf16_t*)R + ro + bj * HALF + n * 4); rv = (f32x4){__uint_as_float(rb.x << 16), __uint_as_float(rb.x & 0xffff0000u), __uint_as_float(rb.y << 16), __uint_as_float(rb.y & 0xffff0000u)}; }
;                         else rv = *(const f32x4*)((const float*)R + ro + bj * HALF + n * 4);
;                         const f32x4 v = af + rv; { u32x2 hb; hb.x = cvt_pk_bf16(v[0], v[1]); hb.y = cvt_pk_bf16(v[2], v[3]); *(u32x2*)(C + ro + bj * HALF + n * 4) = hb; }
;                         const f32x4 g = *(const f32x4*)(gain + col0 + bj * HALF + n * 4);
;                         u32x2 o; o.x = cvt_pk_bf16(v[0] * g[0], v[1] * g[1]); o.y = cvt_pk_bf16(v[2] * g[2], v[3] * g[3]); *(u32x2*)(HG + ro + bj * HALF + n * 4) = o;
;                         ss += (v[0] * v[0] + v[1] * v[1]) + (v[2] * v[2] + v[3] * v[3]); }
;                 ss += __shfl_xor(ss, 16); ss += __shfl_xor(ss, 32);
;                 if (fq == 0) SS[(size_t)row * 64 + u.pn * 4 + wc] = ss; }
	v_lshlrev_b32_e32 v46, 16, v242
	v_and_b32_e32 v47, 0xffff0000, v242
	v_lshlrev_b32_e32 v48, 16, v243
	v_and_b32_e32 v49, 0xffff0000, v243
	v_pk_fma_f32 v[48:49], v[124:125], v[44:45], v[48:49]
	v_pk_fma_f32 v[46:47], v[122:123], v[42:43], v[46:47]
	s_nop 0
	v_cvt_pk_bf16_f32 v42, v46, v47
	v_cvt_pk_bf16_f32 v43, v48, v49
	global_store_dwordx2 v[56:57], v[42:43], off offset:8
	s_nop 0
	s_nop 0
	v_mul_f32_e32 v42, v196, v46
	v_mul_f32_e32 v43, v197, v47
	v_mul_f32_e32 v44, v198, v48
	v_mul_f32_e32 v45, v199, v49
	v_cvt_pk_bf16_f32 v42, v42, v43
	v_cvt_pk_bf16_f32 v43, v44, v45
	s_nop 0
	s_nop 0
	global_store_dwordx2 v[52:53], v[42:43], off offset:8
	s_nop 0
	s_waitcnt vmcnt(18)
	v_lshlrev_b32_e32 v42, 16, v236
	v_and_b32_e32 v43, 0xffff0000, v236
	v_lshlrev_b32_e32 v44, 16, v237
	v_and_b32_e32 v45, 0xffff0000, v237
	v_pk_fma_f32 v[44:45], v[120:121], v[40:41], v[44:45]
	v_pk_fma_f32 v[42:43], v[118:119], v[38:39], v[42:43]
	s_nop 0
	v_cvt_pk_bf16_f32 v38, v42, v43
	v_cvt_pk_bf16_f32 v39, v44, v45
	global_store_dwordx2 v[56:57], v[38:39], off offset:256
	s_nop 0
	s_nop 0
	v_mul_f32_e32 v38, v200, v42
	v_mul_f32_e32 v39, v201, v43
	v_mul_f32_e32 v40, v202, v44
	v_mul_f32_e32 v41, v203, v45
	v_cvt_pk_bf16_f32 v38, v38, v39
	v_cvt_pk_bf16_f32 v39, v40, v41
	s_nop 0
	s_nop 0
	global_store_dwordx2 v[52:53], v[38:39], off offset:256
	s_nop 0
	s_waitcnt vmcnt(19)
	v_lshlrev_b32_e32 v38, 16, v238
	v_and_b32_e32 v39, 0xffff0000, v238
	v_lshlrev_b32_e32 v40, 16, v239
	v_and_b32_e32 v41, 0xffff0000, v239
	v_pk_fma_f32 v[40:41], v[116:117], v[36:37], v[40:41]
	v_pk_fma_f32 v[54:55], v[114:115], v[34:35], v[38:39]
	s_nop 0
	v_cvt_pk_bf16_f32 v34, v54, v55
	v_cvt_pk_bf16_f32 v35, v40, v41
	global_store_dwordx2 v[56:57], v[34:35], off offset:264
	s_nop 0
	v_mul_f32_e32 v34, v61, v61
	v_mul_f32_e32 v35, v59, v59
	v_fmac_f32_e32 v34, v60, v60
	v_fmac_f32_e32 v35, v58, v58
	v_add_f32_e32 v34, v34, v35
	v_mul_f32_e32 v35, v47, v47
	v_mul_f32_e32 v47, v49, v49
	v_fmac_f32_e32 v35, v46, v46
	v_fmac_f32_e32 v47, v48, v48
	v_add_f32_e32 v35, v35, v47
	v_add_f32_e32 v34, v34, v35
	v_mul_f32_e32 v35, v43, v43
	v_mul_f32_e32 v43, v45, v45
	v_fmac_f32_e32 v35, v42, v42
	v_fmac_f32_e32 v43, v44, v44
	v_add_f32_e32 v35, v35, v43
	v_add_f32_e32 v34, v34, v35
	v_mul_f32_e32 v35, v55, v55
	v_mul_f32_e32 v42, v41, v41
	v_fmac_f32_e32 v35, v54, v54
	v_fmac_f32_e32 v42, v40, v40
	v_add_f32_e32 v35, v35, v42
	v_add_f32_e32 v34, v34, v35
	ds_bpermute_b32 v35, v162, v34
	s_waitcnt lgkmcnt(0)
	v_add_f32_e32 v34, v34, v35
	ds_bpermute_b32 v35, v163, v34
	s_nop 0
	v_mul_f32_e32 v36, v204, v54
	v_mul_f32_e32 v37, v205, v55
	v_mul_f32_e32 v38, v206, v40
	v_mul_f32_e32 v39, v207, v41
	v_cvt_pk_bf16_f32 v36, v36, v37
	v_cvt_pk_bf16_f32 v37, v38, v39
	global_store_dwordx2 v[52:53], v[36:37], off offset:264
	s_and_saveexec_b64 s[50:51], s[4:5]
	s_cbranch_execz .LBB0_1954
	s_waitcnt lgkmcnt(0)
	v_add_f32_e32 v36, v34, v35
	v_lshlrev_b64 v[34:35], 8, v[50:51]
	v_lshl_add_u64 v[34:35], s[20:21], 0, v[34:35]
	v_lshl_add_u64 v[34:35], s[48:49], 2, v[34:35]
	s_lshl_b32 s10, s64, 2
	v_lshl_add_u64 v[34:35], v[34:35], 0, s[10:11]
	global_store_dword v[34:35], v36, off
.LBB0_1954:
	s_or_b64 exec, exec, s[50:51]
	global_load_dword v246, v[150:151], off offset:704
	v_add_u32_e32 v190, 0xb0, v148
	v_ashrrev_i32_e32 v191, 31, v190
	v_lshlrev_b64 v[230:231], 12, v[190:191]
	v_lshl_add_u64 v[230:231], v[230:231], 0, v[146:147]
	v_lshlrev_b64 v[230:231], 1, v[230:231]
	v_lshl_add_u64 v[252:253], s[14:15], 0, v[230:231]
	global_load_dwordx2 v[240:241], v[252:253], off
	global_load_dwordx2 v[242:243], v[252:253], off offset:8
	global_load_dwordx2 v[236:237], v[252:253], off offset:256
	global_load_dwordx2 v[238:239], v[252:253], off offset:264
	v_add_u32_e32 v34, 0xa0, v148
	s_waitcnt lgkmcnt(0)
	v_ashrrev_i32_e32 v35, 31, v34
	v_lshlrev_b64 v[36:37], 12, v[34:35]
	v_lshl_add_u64 v[36:37], v[36:37], 0, v[146:147]
	v_lshlrev_b64 v[36:37], 1, v[36:37]
	v_lshl_add_u64 v[40:41], s[14:15], 0, v[36:37]
	s_nop 0
	s_nop 0
	v_cvt_f32_i32_e32 v33, v33
	v_cvt_f32_i32_e32 v31, v31
	v_cvt_f32_i32_e32 v30, v30
	v_cvt_f32_i32_e32 v32, v32
	v_cvt_f32_i32_e32 v29, v29
	v_cvt_f32_i32_e32 v27, v27
	v_cvt_f32_i32_e32 v26, v26
	v_cvt_f32_i32_e32 v28, v28
	v_lshl_add_u64 v[36:37], s[16:17], 0, v[36:37]
	v_cvt_f32_i32_e32 v25, v25
	v_cvt_f32_i32_e32 v23, v23
	v_cvt_f32_i32_e32 v22, v22
	v_cvt_f32_i32_e32 v24, v24
	v_cvt_f32_i32_e32 v21, v21
	v_cvt_f32_i32_e32 v19, v19
	v_cvt_f32_i32_e32 v18, v18
	v_cvt_f32_i32_e32 v20, v20
	s_nop 0
	s_waitcnt vmcnt(17)
	v_pk_mul_f32 v[30:31], v[248:249], v[30:31] op_sel_hi:[0,1]
	v_pk_mul_f32 v[32:33], v[248:249], v[32:33] op_sel_hi:[0,1]
	s_nop 0
	s_waitcnt vmcnt(16)
	v_lshlrev_b32_e32 v44, 16, v250
	v_and_b32_e32 v45, 0xffff0000, v250
	v_lshlrev_b32_e32 v42, 16, v251
	v_and_b32_e32 v43, 0xffff0000, v251
	v_pk_fma_f32 v[42:43], v[152:153], v[32:33], v[42:43]
	v_pk_fma_f32 v[44:45], v[128:129], v[30:31], v[44:45]
	v_pk_mul_f32 v[26:27], v[248:249], v[26:27] op_sel_hi:[0,1]
	v_cvt_pk_bf16_f32 v30, v44, v45
	v_cvt_pk_bf16_f32 v31, v42, v43
	global_store_dwordx2 v[40:41], v[30:31], off
	s_nop 0
	v_pk_mul_f32 v[28:29], v[248:249], v[28:29] op_sel_hi:[0,1]
	v_pk_mul_f32 v[22:23], v[248:249], v[22:23] op_sel_hi:[0,1]
	v_pk_mul_f32 v[24:25], v[248:249], v[24:25] op_sel_hi:[0,1]
	v_pk_mul_f32 v[18:19], v[248:249], v[18:19] op_sel_hi:[0,1]
	v_pk_mul_f32 v[20:21], v[248:249], v[20:21] op_sel_hi:[0,1]
	s_nop 0
	v_mul_f32_e32 v30, v192, v44
	v_mul_f32_e32 v31, v193, v45
	v_mul_f32_e32 v32, v194, v42
	v_mul_f32_e32 v33, v195, v43
	v_cvt_pk_bf16_f32 v30, v30, v31
	v_cvt_pk_bf16_f32 v31, v32, v33
	s_nop 0
	s_nop 0
	global_store_dwordx2 v[36:37], v[30:31], off
	s_nop 0
	s_waitcnt vmcnt(17)
; __device__ __forceinline__ unsigned cvt_pk_bf16(float lo, float hi) { unsigned r; asm volatile("v_cvt_pk_bf16_f32 %0, %1, %2" : "=v"(r) : "v"(lo), "v"(hi)); return r; }
;     __device__ __forceinline__ void operator()(const f32x4 (&acc)[2][2][4][2], const Unit& u, int wr, int wc, int fr, int fq) const {
;     ...
;             for (int m = 0; m < 4; ++m) { const int row = row0 + ai * HALF + m * 16; const size_t ro = (size_t)row * ldc + col0; float ss = 0.f; const float rs = xs[row];
; #pragma unroll
;                 for (int bj = 0; bj < 2; ++bj)
; #pragma unroll
;                     for (int n = 0; n < 2; ++n) { const i32x4 ia = __builtin_bit_cast(i32x4, acc[ai][bj][m][n]);
;                         const f32x4 af = (f32x4){(float)ia[0], (float)ia[1], (float)ia[2], (float)ia[3]} * rs * cs[bj][n];
;                         f32x4 rv; if constexpr (RB16) { const u32x2 rb = *(const u32x2*)((const bf16_t*)R + ro + bj * HALF + n * 4); rv = (f32x4){__uint_as_float(rb.x << 16), __uint_as_float(rb.x & 0xffff0000u), __uint_as_float(rb.y << 16), __uint_as_float(rb.y & 0xffff0000u)}; }
;                         else rv = *(const f32x4*)((const float*)R + ro + bj * HALF + n * 4);
;                         const f32x4 v = af + rv; { u32x2 hb; hb.x = cvt_pk_bf16(v[0], v[1]); hb.y = cvt_pk_bf16(v[2], v[3]); *(u32x2*)(C + ro + bj * HALF + n * 4) = hb; }
;                         const f32x4 g = *(const f32x4*)(gain + col0 + bj * HALF + n * 4);
;                         u32x2 o; o.x = cvt_pk_bf16(v[0] * g[0], v[1] * g[1]); o.y = cvt_pk_bf16(v[2] * g[2], v[3] * g[3]); *(u32x2*)(HG + ro + bj * HALF + n * 4) = o;
;                         ss += (v[0] * v[0] + v[1] * v[1]) + (v[2] * v[2] + v[3] * v[3]); }
;                 ss += __shfl_xor(ss, 16); ss += __shfl_xor(ss, 32);
;                 if (fq == 0) SS[(size_t)row * 64 + u.pn * 4 + wc] = ss; }
	v_lshlrev_b32_e32 v30, 16, v244
	v_and_b32_e32 v31, 0xffff0000, v244
	v_lshlrev_b32_e32 v32, 16, v245
	v_and_b32_e32 v33, 0xffff0000, v245
	v_pk_fma_f32 v[32:33], v[124:125], v[28:29], v[32:33]
	v_pk_fma_f32 v[30:31], v[122:123], v[26:27], v[30:31]
	s_nop 0
	v_cvt_pk_bf16_f32 v26, v30, v31
	v_cvt_pk_bf16_f32 v27, v32, v33
	global_store_dwordx2 v[40:41], v[26:27], off offset:8
	s_nop 0
	s_nop 0
	v_mul_f32_e32 v26, v196, v30
	v_mul_f32_e32 v27, v197, v31
	v_mul_f32_e32 v28, v198, v32
	v_mul_f32_e32 v29, v199, v33
	v_cvt_pk_bf16_f32 v26, v26, v27
	v_cvt_pk_bf16_f32 v27, v28, v29
	s_nop 0
	s_nop 0
	global_store_dwordx2 v[36:37], v[26:27], off offset:8
	s_nop 0
	s_waitcnt vmcnt(18)
	v_lshlrev_b32_e32 v26, 16, v232
	v_and_b32_e32 v27, 0xffff0000, v232
	v_lshlrev_b32_e32 v28, 16, v233
	v_and_b32_e32 v29, 0xffff0000, v233
	v_pk_fma_f32 v[28:29], v[120:121], v[24:25], v[28:29]
	v_pk_fma_f32 v[26:27], v[118:119], v[22:23], v[26:27]
	s_nop 0
	v_cvt_pk_bf16_f32 v22, v26, v27
	v_cvt_pk_bf16_f32 v23, v28, v29
	global_store_dwordx2 v[40:41], v[22:23], off offset:256
	s_nop 0
	s_nop 0
	v_mul_f32_e32 v22, v200, v26
	v_mul_f32_e32 v23, v201, v27
	v_mul_f32_e32 v24, v202, v28
	v_mul_f32_e32 v25, v203, v29
	v_cvt_pk_bf16_f32 v22, v22, v23
	v_cvt_pk_bf16_f32 v23, v24, v25
	s_nop 0
	s_nop 0
	global_store_dwordx2 v[36:37], v[22:23], off offset:256
	s_nop 0
	s_waitcnt vmcnt(19)
	v_lshlrev_b32_e32 v22, 16, v234
	v_and_b32_e32 v23, 0xffff0000, v234
	v_lshlrev_b32_e32 v24, 16, v235
	v_and_b32_e32 v25, 0xffff0000, v235
	v_pk_fma_f32 v[24:25], v[116:117], v[20:21], v[24:25]
	v_pk_fma_f32 v[38:39], v[114:115], v[18:19], v[22:23]
	s_nop 0
	v_cvt_pk_bf16_f32 v18, v38, v39
	v_cvt_pk_bf16_f32 v19, v24, v25
	global_store_dwordx2 v[40:41], v[18:19], off offset:264
	s_nop 0
	v_mul_f32_e32 v18, v45, v45
	v_mul_f32_e32 v19, v43, v43
	v_fmac_f32_e32 v18, v44, v44
	v_fmac_f32_e32 v19, v42, v42
	v_add_f32_e32 v18, v18, v19
	v_mul_f32_e32 v19, v31, v31
	v_mul_f32_e32 v31, v33, v33
	v_fmac_f32_e32 v19, v30, v30
	v_fmac_f32_e32 v31, v32, v32
	v_add_f32_e32 v19, v19, v31
	v_add_f32_e32 v18, v18, v19
	v_mul_f32_e32 v19, v27, v27
	v_mul_f32_e32 v27, v29, v29
	v_fmac_f32_e32 v19, v26, v26
	v_fmac_f32_e32 v27, v28, v28
	v_add_f32_e32 v19, v19, v27
	v_add_f32_e32 v18, v18, v19
	v_mul_f32_e32 v19, v39, v39
	v_mul_f32_e32 v26, v25, v25
	v_fmac_f32_e32 v19, v38, v38
	v_fmac_f32_e32 v26, v24, v24
	v_add_f32_e32 v19, v19, v26
	v_add_f32_e32 v18, v18, v19
	ds_bpermute_b32 v19, v162, v18
	s_waitcnt lgkmcnt(0)
	v_add_f32_e32 v18, v18, v19
	ds_bpermute_b32 v19, v163, v18
	s_nop 0
	v_mul_f32_e32 v20, v204, v38
	v_mul_f32_e32 v21, v205, v39
	v_mul_f32_e32 v22, v206, v24
	v_mul_f32_e32 v23, v207, v25
	v_cvt_pk_bf16_f32 v20, v20, v21
	v_cvt_pk_bf16_f32 v21, v22, v23
	global_store_dwordx2 v[36:37], v[20:21], off offset:264
	s_and_saveexec_b64 s[50:51], s[4:5]
	s_cbranch_execz .LBB0_1956
	s_waitcnt lgkmcnt(0)
	v_add_f32_e32 v20, v18, v19
	v_lshlrev_b64 v[18:19], 8, v[34:35]
	v_lshl_add_u64 v[18:19], s[20:21], 0, v[18:19]
	v_lshl_add_u64 v[18:19], s[48:49], 2, v[18:19]
	s_lshl_b32 s10, s64, 2
	v_lshl_add_u64 v[18:19], v[18:19], 0, s[10:11]
	global_store_dword v[18:19], v20, off
; __device__ __forceinline__ unsigned cvt_pk_bf16(float lo, float hi) { unsigned r; asm volatile("v_cvt_pk_bf16_f32 %0, %1, %2" : "=v"(r) : "v"(lo), "v"(hi)); return r; }
;     __device__ __forceinline__ void operator()(const f32x4 (&acc)[2][2][4][2], const Unit& u, int wr, int wc, int fr, int fq) const {
;     ...
;             for (int m = 0; m < 4; ++m) { const int row = row0 + ai * HALF + m * 16; const size_t ro = (size_t)row * ldc + col0; float ss = 0.f; const float rs = xs[row];
; #pragma unroll
;                 for (int bj = 0; bj < 2; ++bj)
; #pragma unroll
;                     for (int n = 0; n < 2; ++n) { const i32x4 ia = __builtin_bit_cast(i32x4, acc[ai][bj][m][n]);
;                         const f32x4 af = (f32x4){(float)ia[0], (float)ia[1], (float)ia[2], (float)ia[3]} * rs * cs[bj][n];
;                         f32x4 rv; if constexpr (RB16) { const u32x2 rb = *(const u32x2*)((const bf16_t*)R + ro + bj * HALF + n * 4); rv = (f32x4){__uint_as_float(rb.x << 16), __uint_as_float(rb.x & 0xffff0000u), __uint_as_float(rb.y << 16), __uint_as_float(rb.y & 0xffff0000u)}; }
;                         else rv = *(const f32x4*)((const float*)R + ro + bj * HALF + n * 4);
;                         const f32x4 v = af + rv; { u32x2 hb; hb.x = cvt_pk_bf16(v[0], v[1]); hb.y = cvt_pk_bf16(v[2], v[3]); *(u32x2*)(C + ro + bj * HALF + n * 4) = hb; }
;                         const f32x4 g = *(const f32x4*)(gain + col0 + bj * HALF + n * 4);
;                         u32x2 o; o.x = cvt_pk_bf16(v[0] * g[0], v[1] * g[1]); o.y = cvt_pk_bf16(v[2] * g[2], v[3] * g[3]); *(u32x2*)(HG + ro + bj * HALF + n * 4) = o;
;                         ss += (v[0] * v[0] + v[1] * v[1]) + (v[2] * v[2] + v[3] * v[3]); }
;                 ss += __shfl_xor(ss, 16); ss += __shfl_xor(ss, 32);
;                 if (fq == 0) SS[(size_t)row * 64 + u.pn * 4 + wc] = ss; }
.LBB0_1956:
	s_or_b64 exec, exec, s[50:51]
	v_add_u32_e32 v18, 0xb0, v148
	s_waitcnt lgkmcnt(0)
	v_ashrrev_i32_e32 v19, 31, v18
	v_lshlrev_b64 v[20:21], 12, v[18:19]
	v_lshl_add_u64 v[20:21], v[20:21], 0, v[146:147]
	v_lshlrev_b64 v[20:21], 1, v[20:21]
	v_lshl_add_u64 v[24:25], s[14:15], 0, v[20:21]
	s_nop 0
	s_nop 0
	v_cvt_f32_i32_e32 v17, v17
	v_cvt_f32_i32_e32 v15, v15
	v_cvt_f32_i32_e32 v14, v14
	v_cvt_f32_i32_e32 v16, v16
	v_cvt_f32_i32_e32 v13, v13
	v_cvt_f32_i32_e32 v11, v11
	v_cvt_f32_i32_e32 v10, v10
	v_cvt_f32_i32_e32 v12, v12
	v_lshl_add_u64 v[20:21], s[16:17], 0, v[20:21]
	v_cvt_f32_i32_e32 v9, v9
	v_cvt_f32_i32_e32 v7, v7
	v_cvt_f32_i32_e32 v6, v6
	v_cvt_f32_i32_e32 v8, v8
	v_cvt_f32_i32_e32 v5, v5
	v_cvt_f32_i32_e32 v3, v3
	v_cvt_f32_i32_e32 v2, v2
	v_cvt_f32_i32_e32 v4, v4
	s_nop 0
	s_waitcnt vmcnt(12)
	v_pk_mul_f32 v[14:15], v[246:247], v[14:15] op_sel_hi:[0,1]
	v_pk_mul_f32 v[16:17], v[246:247], v[16:17] op_sel_hi:[0,1]
	s_nop 0
	s_waitcnt vmcnt(11)
	v_lshlrev_b32_e32 v28, 16, v240
	v_and_b32_e32 v29, 0xffff0000, v240
	v_lshlrev_b32_e32 v26, 16, v241
	v_and_b32_e32 v27, 0xffff0000, v241
	v_pk_fma_f32 v[26:27], v[152:153], v[16:17], v[26:27]
	v_pk_fma_f32 v[28:29], v[128:129], v[14:15], v[28:29]
	v_pk_mul_f32 v[10:11], v[246:247], v[10:11] op_sel_hi:[0,1]
	v_cvt_pk_bf16_f32 v14, v28, v29
	v_cvt_pk_bf16_f32 v15, v26, v27
	global_store_dwordx2 v[24:25], v[14:15], off
	s_nop 0
	v_pk_mul_f32 v[12:13], v[246:247], v[12:13] op_sel_hi:[0,1]
	v_pk_mul_f32 v[6:7], v[246:247], v[6:7] op_sel_hi:[0,1]
	v_pk_mul_f32 v[8:9], v[246:247], v[8:9] op_sel_hi:[0,1]
	v_pk_mul_f32 v[2:3], v[246:247], v[2:3] op_sel_hi:[0,1]
	v_pk_mul_f32 v[4:5], v[246:247], v[4:5] op_sel_hi:[0,1]
	s_nop 0
	v_mul_f32_e32 v14, v192, v28
	v_mul_f32_e32 v15, v193, v29
	v_mul_f32_e32 v16, v194, v26
	v_mul_f32_e32 v17, v195, v27
	v_cvt_pk_bf16_f32 v14, v14, v15
	v_cvt_pk_bf16_f32 v15, v16, v17
	s_nop 0
	s_nop 0
	global_store_dwordx2 v[20:21], v[14:15], off
	s_nop 0
	s_waitcnt vmcnt(12)
	v_lshlrev_b32_e32 v14, 16, v242
	v_and_b32_e32 v15, 0xffff0000, v242
	v_lshlrev_b32_e32 v16, 16, v243
	v_and_b32_e32 v17, 0xffff0000, v243
	v_pk_fma_f32 v[16:17], v[124:125], v[12:13], v[16:17]
	v_pk_fma_f32 v[14:15], v[122:123], v[10:11], v[14:15]
	s_nop 0
	v_cvt_pk_bf16_f32 v10, v14, v15
	v_cvt_pk_bf16_f32 v11, v16, v17
	global_store_dwordx2 v[24:25], v[10:11], off offset:8
	s_nop 0
	s_nop 0
	v_mul_f32_e32 v10, v196, v14
	v_mul_f32_e32 v11, v197, v15
	v_mul_f32_e32 v12, v198, v16
	v_mul_f32_e32 v13, v199, v17
	v_cvt_pk_bf16_f32 v10, v10, v11
	v_cvt_pk_bf16_f32 v11, v12, v13
	s_nop 0
	s_nop 0
	global_store_dwordx2 v[20:21], v[10:11], off offset:8
	s_nop 0
	s_waitcnt vmcnt(13)
	v_lshlrev_b32_e32 v10, 16, v236
	v_and_b32_e32 v11, 0xffff0000, v236
	v_lshlrev_b32_e32 v12, 16, v237
	v_and_b32_e32 v13, 0xffff0000, v237
	v_pk_fma_f32 v[12:13], v[120:121], v[8:9], v[12:13]
	v_pk_fma_f32 v[10:11], v[118:119], v[6:7], v[10:11]
	s_nop 0
	v_cvt_pk_bf16_f32 v6, v10, v11
	v_cvt_pk_bf16_f32 v7, v12, v13
	global_store_dwordx2 v[24:25], v[6:7], off offset:256
	s_nop 0
	s_nop 0
	v_mul_f32_e32 v6, v200, v10
	v_mul_f32_e32 v7, v201, v11
	v_mul_f32_e32 v8, v202, v12
	v_mul_f32_e32 v9, v203, v13
	v_cvt_pk_bf16_f32 v6, v6, v7
	v_cvt_pk_bf16_f32 v7, v8, v9
	s_nop 0
	s_nop 0
	global_store_dwordx2 v[20:21], v[6:7], off offset:256
	s_nop 0
	s_waitcnt vmcnt(14)
	v_lshlrev_b32_e32 v6, 16, v238
	v_and_b32_e32 v7, 0xffff0000, v238
	v_lshlrev_b32_e32 v8, 16, v239
	v_and_b32_e32 v9, 0xffff0000, v239
	v_pk_fma_f32 v[8:9], v[116:117], v[4:5], v[8:9]
	v_pk_fma_f32 v[22:23], v[114:115], v[2:3], v[6:7]
	s_nop 0
	v_cvt_pk_bf16_f32 v2, v22, v23
	v_cvt_pk_bf16_f32 v3, v8, v9
	global_store_dwordx2 v[24:25], v[2:3], off offset:264
	s_nop 0
	v_mul_f32_e32 v2, v29, v29
	v_mul_f32_e32 v3, v27, v27
	v_fmac_f32_e32 v2, v28, v28
	v_fmac_f32_e32 v3, v26, v26
	v_add_f32_e32 v2, v2, v3
	v_mul_f32_e32 v3, v15, v15
	v_mul_f32_e32 v15, v17, v17
	v_fmac_f32_e32 v3, v14, v14
	v_fmac_f32_e32 v15, v16, v16
	v_add_f32_e32 v3, v3, v15
	v_add_f32_e32 v2, v2, v3
	v_mul_f32_e32 v3, v11, v11
	v_mul_f32_e32 v11, v13, v13
	v_fmac_f32_e32 v3, v10, v10
	v_fmac_f32_e32 v11, v12, v12
	v_add_f32_e32 v3, v3, v11
	v_add_f32_e32 v2, v2, v3
	v_mul_f32_e32 v3, v23, v23
	v_mul_f32_e32 v10, v9, v9
	v_fmac_f32_e32 v3, v22, v22
	v_fmac_f32_e32 v10, v8, v8
	v_add_f32_e32 v3, v3, v10
	v_add_f32_e32 v2, v2, v3
	ds_bpermute_b32 v3, v162, v2
	s_waitcnt lgkmcnt(0)
	v_add_f32_e32 v2, v2, v3
	ds_bpermute_b32 v3, v163, v2
	s_nop 0
	v_mul_f32_e32 v4, v204, v22
	v_mul_f32_e32 v5, v205, v23
	v_mul_f32_e32 v6, v206, v8
	v_mul_f32_e32 v7, v207, v9
	v_cvt_pk_bf16_f32 v4, v4, v5
	v_cvt_pk_bf16_f32 v5, v6, v7
	global_store_dwordx2 v[20:21], v[4:5], off offset:264
	s_and_saveexec_b64 s[50:51], s[4:5]
	s_cbranch_execz .LBB0_1958
	s_waitcnt lgkmcnt(0)
	v_add_f32_e32 v4, v2, v3
	v_lshlrev_b64 v[2:3], 8, v[18:19]
	v_lshl_add_u64 v[2:3], s[20:21], 0, v[2:3]
	v_lshl_add_u64 v[2:3], s[48:49], 2, v[2:3]
	s_lshl_b32 s10, s64, 2
	v_lshl_add_u64 v[2:3], v[2:3], 0, s[10:11]
	global_store_dword v[2:3], v4, off
